# LDS-DMA wrappers: s_nop 2 -> s_nop 0 between the m0 write and global_load_lds (1 wait state is the documented requirement), 392 sites
# baseline (speedup 1.0000x reference)
.LBB0_132:
	s_cmp_lt_i32 s94, 2
	s_cselect_b64 s[0:1], -1, 0
	s_cmp_gt_i32 s95, 1
	v_writelane_b32 v253, s90, 26
	s_cselect_b64 s[2:3], -1, 0
	v_writelane_b32 v253, s94, 27
	s_and_b64 s[0:1], s[0:1], s[2:3]
	s_andn2_b64 vcc, exec, s[0:1]
	v_writelane_b32 v253, s95, 28
	s_mov_b64 s[4:5], -1
	v_writelane_b32 v253, s96, 29
	v_writelane_b32 v253, s88, 30
	s_cbranch_vccnz .LBB0_283
	s_add_u32 s2, s74, 0xd000000
	s_addc_u32 s3, s75, 0
	s_add_u32 s24, s74, 0x200000
	s_addc_u32 s25, s75, 0
	s_add_u32 s26, s74, 0xf000000
	s_addc_u32 s27, s75, 0
	s_add_u32 s0, s74, 0x10000000
	v_writelane_b32 v253, s0, 31
	s_addc_u32 s0, s75, 0
	s_add_u32 s6, s74, 0x11000000
	s_addc_u32 s7, s75, 0
	v_writelane_b32 v253, s0, 33
	s_add_u32 s0, s74, 0x11800000
	v_writelane_b32 v253, s0, 35
	s_addc_u32 s0, s75, 0
	v_writelane_b32 v253, s0, 37
	s_add_u32 s0, s74, 0x13800000
	v_writelane_b32 v253, s0, 39
	s_addc_u32 s0, s75, 0
	s_cmpk_lg_i32 s90, 0x100
	v_writelane_b32 v253, s0, 41
	s_cselect_b64 s[0:1], -1, 0
	s_and_b64 vcc, exec, s[0:1]
	s_cbranch_vccz .LBB0_165
	s_cmpk_gt_i32 s93, 0xbf
	v_readfirstlane_b32 s5, v0
	s_cbranch_scc1 .LBB0_164
	v_lshlrev_b32_e32 v2, 4, v0
	v_and_b32_e32 v3, 32, v0
	v_bitop3_b32 v2, v2, v3, 48 bitop3:0x6c
	v_lshrrev_b32_e32 v3, 1, v0
	v_bfe_u32 v5, v0, 2, 2
	v_bfe_u32 v4, v0, 2, 4
	v_and_or_b32 v3, v3, 24, v5
	v_lshrrev_b32_e32 v5, 3, v0
	v_lshrrev_b32_e32 v7, 5, v0
	v_and_or_b32 v6, v5, 48, v4
	v_and_or_b32 v5, v5, 32, v7
	v_and_or_b32 v5, v5, 36, v3
	v_and_or_b32 v2, v0, 64, v2
	v_lshl_or_b32 v137, v5, 11, v2
	v_bfe_u32 v5, v0, 3, 25
	v_or_b32_e32 v5, 64, v5
	s_movk_i32 s4, 0x70
	v_and_or_b32 v4, v5, s4, v4
	s_movk_i32 s4, 0x60
	v_and_or_b32 v5, v5, s4, v7
	s_movk_i32 s4, 0x64
	s_ashr_i32 s28, s93, 31
	v_and_or_b32 v3, v5, s4, v3
	s_lshr_b32 s4, s28, 29
	s_add_i32 s4, s93, s4
	s_lshr_b32 s11, s5, 6
	s_ashr_i32 s8, s4, 3
	s_and_b32 s4, s4, -8
	s_lshr_b32 s10, s5, 8
	s_lshl_b32 s14, s11, 10
	s_sub_i32 s4, s93, s4
	s_cmp_lt_i32 s4, 0
	s_cselect_b32 s9, 25, 24
	s_mul_i32 s4, s4, s9
	s_add_i32 s4, s4, s8
	s_mul_hi_i32 s8, s4, 0x2aaaaaab
	s_lshr_b32 s9, s8, 31
	s_ashr_i32 s8, s8, 2
	s_add_i32 s8, s8, s9
	s_lshl_b32 s9, s8, 3
	s_mul_i32 s8, s8, 24
	s_sub_i32 s4, s4, s8
	s_bfe_i32 s8, s4, 0x80000
	s_bfe_u32 s8, s8, 0x3000c
	s_add_i32 s8, s4, s8
	s_bfe_i32 s12, s8, 0x80000
	s_and_b32 s8, s8, 0xf8
	s_sub_i32 s8, s4, s8
	s_sext_i32_i16 s12, s12
	s_sext_i32_i8 s8, s8
	s_ashr_i32 s12, s12, 3
	s_add_i32 s20, s9, s8
	s_and_b32 s4, s4, 0xf8
	s_cmp_lg_u32 s4, 16
	s_cselect_b32 s4, s12, 4
	s_ashr_i32 s21, s20, 31
	s_bfe_i64 s[12:13], s[4:5], 0x100000
	s_lshl_b64 s[8:9], s[20:21], 19
	s_lshl_b64 s[12:13], s[12:13], 19
	s_add_u32 s40, s24, s12
	s_addc_u32 s41, s25, s13
	s_add_i32 s21, s14, 0
	s_add_i32 s30, s21, 0x10000
	s_mov_b32 s12, m0
	s_mov_b32 m0, s30
	s_nop 0
	global_load_lds_dwordx4 v137, s[40:41]
	s_mov_b32 m0, s12
	v_lshl_or_b32 v139, v3, 11, v2
	s_add_i32 s31, s21, 0x12000
	s_mov_b32 s12, m0
	s_mov_b32 m0, s31
	s_nop 0
	global_load_lds_dwordx4 v139, s[40:41]
	s_mov_b32 m0, s12
	s_add_u32 s12, s40, 0x40000
	s_addc_u32 s13, s41, 0
	s_add_i32 s34, s21, 0x14000
	s_mov_b32 s14, m0
	s_mov_b32 m0, s34
	s_nop 0
	global_load_lds_dwordx4 v137, s[12:13]
	s_mov_b32 m0, s14
	s_add_i32 s35, s21, 0x16000
	s_mov_b32 s14, m0
	s_mov_b32 m0, s35
	s_nop 0
	global_load_lds_dwordx4 v139, s[12:13]
	s_mov_b32 m0, s14
	s_add_u32 s22, s2, s8
	v_lshl_or_b32 v136, v6, 11, v2
	s_addc_u32 s23, s3, s9
	s_mov_b32 s8, m0
	s_mov_b32 m0, s21
	s_nop 0
	global_load_lds_dwordx4 v136, s[22:23]
	s_mov_b32 m0, s8
	s_add_i32 s36, s21, 0x2000
	v_lshl_or_b32 v138, v4, 11, v2
	s_mov_b32 s8, m0
	s_mov_b32 m0, s36
	s_nop 0
	global_load_lds_dwordx4 v138, s[22:23]
	s_mov_b32 m0, s8
	s_add_u32 s12, s22, 0x40000
	s_addc_u32 s13, s23, 0
	s_add_i32 s37, s21, 0x4000
	s_mov_b32 s8, m0
	s_mov_b32 m0, s37
	s_nop 0
	global_load_lds_dwordx4 v136, s[12:13]
	s_mov_b32 m0, s8
	s_add_i32 s52, s21, 0x6000
	s_mov_b32 s14, m0
	s_mov_b32 m0, s52
	s_nop 0
	global_load_lds_dwordx4 v138, s[12:13]
	s_mov_b32 m0, s14
	s_cmp_eq_u32 s10, 1
	s_mov_b32 s29, 0
	s_cselect_b64 s[8:9], -1, 0
	s_cmp_lg_u32 s10, 1
	s_cbranch_scc1 .LBB0_137
	s_barrier
.LBB0_137:
	v_bfe_u32 v141, v0, 4, 2
	v_and_b32_e32 v140, 15, v0
	v_lshlrev_b32_e32 v2, 4, v141
	v_lshlrev_b32_e32 v4, 2, v0
	s_sext_i32_i16 s78, s4
	v_lshl_or_b32 v3, v140, 6, v2
	s_lshl_b32 s4, s10, 13
	v_and_b32_e32 v4, 32, v4
	v_bitop3_b32 v3, v3, s4, v4 bitop3:0xde
	s_lshl_b32 s4, s11, 5
	s_and_b32 s60, s4, 0x60
	v_lshlrev_b32_e32 v5, 6, v0
	s_movk_i32 s4, 0x3c0
	s_lshl_b32 s53, s10, 6
	v_and_or_b32 v2, v5, s4, v2
	s_lshl_b32 s4, s60, 7
	s_add_u32 s10, s40, 0x80
	v_bitop3_b32 v2, s4, v2, v4 bitop3:0xf6
	s_waitcnt vmcnt(2)
	s_barrier
	s_addc_u32 s11, s41, 0
	s_add_i32 s61, s21, 0x18000
	s_mov_b32 s4, m0
	s_mov_b32 m0, s61
	s_nop 0
	global_load_lds_dwordx4 v137, s[10:11]
	s_mov_b32 m0, s4
	s_add_i32 s62, s21, 0x1a000
	s_mov_b32 s4, m0
	s_mov_b32 m0, s62
	s_nop 0
	global_load_lds_dwordx4 v139, s[10:11]
	s_mov_b32 m0, s4
	s_add_u32 s10, s22, 0x80
	s_addc_u32 s11, s23, 0
	s_add_i32 s63, s21, 0x8000
	s_mov_b32 s4, m0
	s_mov_b32 m0, s63
	s_nop 0
	global_load_lds_dwordx4 v136, s[10:11]
	s_mov_b32 m0, s4
	s_add_i32 s64, s21, 0xa000
	s_mov_b32 s4, m0
	s_mov_b32 m0, s64
	s_nop 0
	global_load_lds_dwordx4 v138, s[10:11]
	s_mov_b32 m0, s4
	s_add_u32 s10, s40, 0x40080
	s_addc_u32 s11, s41, 0
	s_add_i32 s65, s21, 0x1c000
	s_mov_b32 s4, m0
	s_mov_b32 m0, s65
	s_nop 0
	global_load_lds_dwordx4 v137, s[10:11]
	s_mov_b32 m0, s4
	s_add_i32 s66, s21, 0x1e000
	s_mov_b32 s4, m0
	s_mov_b32 m0, s66
	s_nop 0
	global_load_lds_dwordx4 v139, s[10:11]
	s_mov_b32 m0, s4
	s_waitcnt vmcnt(6)
	s_add_i32 s67, s21, 0xc000
	s_cmpk_lt_u32 s5, 0x100
	v_add_u32_e32 v2, 0, v2
	s_cselect_b64 s[10:11], -1, 0
	s_add_i32 s76, s21, 0xe000
	s_ashr_i32 s77, s90, 31
	v_mov_b64_e32 v[130:131], 0xc0
	v_mov_b64_e32 v[132:133], 0xbf
	v_add_u32_e32 v142, 0x10000, v2
	v_add_u32_e32 v143, 0x14000, v2
	v_add_u32_e32 v144, 0, v3
	v_add_u32_e32 v145, 0x18000, v2
	v_add_u32_e32 v146, 0x1c000, v2
	s_barrier
	s_branch .LBB0_140

.LBB0_143:
	ds_read_b128 v[148:151], v142
	ds_read_b128 v[152:155], v142 offset:1024
	ds_read_b128 v[156:159], v142 offset:2048
	ds_read_b128 v[160:163], v142 offset:3072
	ds_read_b128 v[164:167], v143
	ds_read_b128 v[174:177], v143 offset:1024
	ds_read_b128 v[178:181], v143 offset:2048
	ds_read_b128 v[182:185], v143 offset:3072
	s_add_u32 s40, s22, 0x100
	s_addc_u32 s41, s23, 0
	s_cmp_eq_u32 s82, 12
	s_cselect_b32 s58, s33, s40
	s_cselect_b32 s59, s13, s41
	s_cselect_b32 s56, s79, s80
	s_cselect_b32 s57, s15, s81
	s_add_u32 s54, s58, 0x80
	s_addc_u32 s55, s59, 0
	ds_read_b128 v[186:189], v144
	ds_read_b128 v[190:193], v144 offset:1024
	ds_read_b128 v[194:197], v144 offset:2048
	ds_read_b128 v[198:201], v144 offset:3072
	ds_read_b128 v[202:205], v144 offset:4096
	ds_read_b128 v[206:209], v144 offset:5120
	ds_read_b128 v[210:213], v144 offset:6144
	ds_read_b128 v[214:217], v144 offset:7168
	s_add_u32 s22, s22, 0x40080
	s_addc_u32 s23, s23, 0
	s_mov_b32 s83, m0
	s_mov_b32 m0, s67
	s_nop 0
	global_load_lds_dwordx4 v136, s[22:23]
	s_mov_b32 m0, s83
	s_nop 0
	s_mov_b32 s83, m0
	s_mov_b32 m0, s76
	s_nop 0
	global_load_lds_dwordx4 v138, s[22:23]
	s_mov_b32 m0, s83
	s_waitcnt vmcnt(8)
	s_waitcnt lgkmcnt(0)
	s_barrier
	s_setprio 1
	s_waitcnt lgkmcnt(7)
	v_mfma_f32_16x16x32_bf16 v[126:129], v[148:151], v[186:189], v[126:129]
	v_mfma_f32_16x16x32_bf16 v[122:125], v[156:159], v[186:189], v[122:125]
	s_waitcnt lgkmcnt(5)
	v_mfma_f32_16x16x32_bf16 v[110:113], v[148:151], v[194:197], v[110:113]
	v_mfma_f32_16x16x32_bf16 v[106:109], v[156:159], v[194:197], v[106:109]
	s_waitcnt lgkmcnt(3)
	v_mfma_f32_16x16x32_bf16 v[94:97], v[148:151], v[202:205], v[94:97]
	v_mfma_f32_16x16x32_bf16 v[90:93], v[156:159], v[202:205], v[90:93]
	s_waitcnt lgkmcnt(1)
	v_mfma_f32_16x16x32_bf16 v[78:81], v[148:151], v[210:213], v[78:81]
	v_mfma_f32_16x16x32_bf16 v[74:77], v[156:159], v[210:213], v[74:77]
	v_mfma_f32_16x16x32_bf16 v[126:129], v[152:155], v[190:193], v[126:129]
	v_mfma_f32_16x16x32_bf16 v[122:125], v[160:163], v[190:193], v[122:125]
	v_mfma_f32_16x16x32_bf16 v[110:113], v[152:155], v[198:201], v[110:113]
	v_mfma_f32_16x16x32_bf16 v[106:109], v[160:163], v[198:201], v[106:109]
	v_mfma_f32_16x16x32_bf16 v[94:97], v[152:155], v[206:209], v[94:97]
	v_mfma_f32_16x16x32_bf16 v[90:93], v[160:163], v[206:209], v[90:93]
	s_waitcnt lgkmcnt(0)
	v_mfma_f32_16x16x32_bf16 v[78:81], v[152:155], v[214:217], v[78:81]
	v_mfma_f32_16x16x32_bf16 v[74:77], v[160:163], v[214:217], v[74:77]
	s_setprio 0
	s_setprio 1
	v_mfma_f32_16x16x32_bf16 v[118:121], v[164:167], v[186:189], v[118:121]
	v_mfma_f32_16x16x32_bf16 v[114:117], v[178:181], v[186:189], v[114:117]
	v_mfma_f32_16x16x32_bf16 v[102:105], v[164:167], v[194:197], v[102:105]
	v_mfma_f32_16x16x32_bf16 v[98:101], v[178:181], v[194:197], v[98:101]
	v_mfma_f32_16x16x32_bf16 v[86:89], v[164:167], v[202:205], v[86:89]
	v_mfma_f32_16x16x32_bf16 v[82:85], v[178:181], v[202:205], v[82:85]
	v_mfma_f32_16x16x32_bf16 v[70:73], v[164:167], v[210:213], v[70:73]
	v_mfma_f32_16x16x32_bf16 v[66:69], v[178:181], v[210:213], v[66:69]
	v_mfma_f32_16x16x32_bf16 v[118:121], v[174:177], v[190:193], v[118:121]
	v_mfma_f32_16x16x32_bf16 v[114:117], v[182:185], v[190:193], v[114:117]
	v_mfma_f32_16x16x32_bf16 v[102:105], v[174:177], v[198:201], v[102:105]
	v_mfma_f32_16x16x32_bf16 v[98:101], v[182:185], v[198:201], v[98:101]
	v_mfma_f32_16x16x32_bf16 v[86:89], v[174:177], v[206:209], v[86:89]
	v_mfma_f32_16x16x32_bf16 v[82:85], v[182:185], v[206:209], v[82:85]
	v_mfma_f32_16x16x32_bf16 v[70:73], v[174:177], v[214:217], v[70:73]
	v_mfma_f32_16x16x32_bf16 v[66:69], v[182:185], v[214:217], v[66:69]
	s_setprio 0
	s_barrier
	ds_read_b128 v[186:189], v144 offset:16384
	ds_read_b128 v[190:193], v144 offset:17408
	ds_read_b128 v[194:197], v144 offset:18432
	ds_read_b128 v[198:201], v144 offset:19456
	ds_read_b128 v[202:205], v144 offset:20480
	ds_read_b128 v[206:209], v144 offset:21504
	ds_read_b128 v[210:213], v144 offset:22528
	ds_read_b128 v[214:217], v144 offset:23552
	s_mov_b32 s22, m0
	s_mov_b32 m0, s30
	s_nop 0
	global_load_lds_dwordx4 v137, s[56:57]
	s_mov_b32 m0, s22
	s_nop 0
	s_mov_b32 s22, m0
	s_mov_b32 m0, s31
	s_nop 0
	global_load_lds_dwordx4 v139, s[56:57]
	s_mov_b32 m0, s22
	s_add_u32 s22, s56, 0x40000
	s_addc_u32 s23, s57, 0
	s_mov_b32 s83, m0
	s_mov_b32 m0, s34
	s_nop 0
	global_load_lds_dwordx4 v137, s[22:23]
	s_mov_b32 m0, s83
	s_nop 0
	s_mov_b32 s83, m0
	s_mov_b32 m0, s35
	s_nop 0
	global_load_lds_dwordx4 v139, s[22:23]
	s_mov_b32 m0, s83
	s_mov_b32 s22, m0
	s_mov_b32 m0, s21
	s_nop 0
	global_load_lds_dwordx4 v136, s[58:59]
	s_mov_b32 m0, s22
	s_nop 0
	s_mov_b32 s22, m0
	s_mov_b32 m0, s36
	s_nop 0
	global_load_lds_dwordx4 v138, s[58:59]
	s_mov_b32 m0, s22
	s_waitcnt vmcnt(8)
	s_waitcnt lgkmcnt(0)
	s_barrier
	s_setprio 1
	s_waitcnt lgkmcnt(7)
	v_mfma_f32_16x16x32_bf16 v[62:65], v[148:151], v[186:189], v[62:65]
	v_mfma_f32_16x16x32_bf16 v[58:61], v[156:159], v[186:189], v[58:61]
	s_waitcnt lgkmcnt(5)
	v_mfma_f32_16x16x32_bf16 v[46:49], v[148:151], v[194:197], v[46:49]
	v_mfma_f32_16x16x32_bf16 v[42:45], v[156:159], v[194:197], v[42:45]
	s_waitcnt lgkmcnt(3)
	v_mfma_f32_16x16x32_bf16 v[30:33], v[148:151], v[202:205], v[30:33]
	v_mfma_f32_16x16x32_bf16 v[26:29], v[156:159], v[202:205], v[26:29]
	s_waitcnt lgkmcnt(1)
	v_mfma_f32_16x16x32_bf16 v[14:17], v[148:151], v[210:213], v[14:17]
	v_mfma_f32_16x16x32_bf16 v[10:13], v[156:159], v[210:213], v[10:13]
	v_mfma_f32_16x16x32_bf16 v[62:65], v[152:155], v[190:193], v[62:65]
	v_mfma_f32_16x16x32_bf16 v[58:61], v[160:163], v[190:193], v[58:61]
	v_mfma_f32_16x16x32_bf16 v[46:49], v[152:155], v[198:201], v[46:49]
	v_mfma_f32_16x16x32_bf16 v[42:45], v[160:163], v[198:201], v[42:45]
	v_mfma_f32_16x16x32_bf16 v[30:33], v[152:155], v[206:209], v[30:33]
	v_mfma_f32_16x16x32_bf16 v[26:29], v[160:163], v[206:209], v[26:29]
	s_waitcnt lgkmcnt(0)
	v_mfma_f32_16x16x32_bf16 v[14:17], v[152:155], v[214:217], v[14:17]
	v_mfma_f32_16x16x32_bf16 v[10:13], v[160:163], v[214:217], v[10:13]
	s_setprio 0
	s_setprio 1
	v_mfma_f32_16x16x32_bf16 v[54:57], v[164:167], v[186:189], v[54:57]
	v_mfma_f32_16x16x32_bf16 v[50:53], v[178:181], v[186:189], v[50:53]
	v_mfma_f32_16x16x32_bf16 v[38:41], v[164:167], v[194:197], v[38:41]
	v_mfma_f32_16x16x32_bf16 v[34:37], v[178:181], v[194:197], v[34:37]
	v_mfma_f32_16x16x32_bf16 v[22:25], v[164:167], v[202:205], v[22:25]
	v_mfma_f32_16x16x32_bf16 v[18:21], v[178:181], v[202:205], v[18:21]
	v_mfma_f32_16x16x32_bf16 v[6:9], v[164:167], v[210:213], v[6:9]
	v_mfma_f32_16x16x32_bf16 v[2:5], v[178:181], v[210:213], v[2:5]
	v_mfma_f32_16x16x32_bf16 v[54:57], v[174:177], v[190:193], v[54:57]
	v_mfma_f32_16x16x32_bf16 v[50:53], v[182:185], v[190:193], v[50:53]
	v_mfma_f32_16x16x32_bf16 v[38:41], v[174:177], v[198:201], v[38:41]
	v_mfma_f32_16x16x32_bf16 v[34:37], v[182:185], v[198:201], v[34:37]
	v_mfma_f32_16x16x32_bf16 v[22:25], v[174:177], v[206:209], v[22:25]
	v_mfma_f32_16x16x32_bf16 v[18:21], v[182:185], v[206:209], v[18:21]
	v_mfma_f32_16x16x32_bf16 v[6:9], v[174:177], v[214:217], v[6:9]
	v_mfma_f32_16x16x32_bf16 v[2:5], v[182:185], v[214:217], v[2:5]
	s_setprio 0
	s_barrier
	ds_read_b128 v[148:151], v145
	ds_read_b128 v[152:155], v145 offset:1024
	ds_read_b128 v[156:159], v145 offset:2048
	ds_read_b128 v[160:163], v145 offset:3072
	ds_read_b128 v[164:167], v146
	ds_read_b128 v[174:177], v146 offset:1024
	ds_read_b128 v[178:181], v146 offset:2048
	ds_read_b128 v[182:185], v146 offset:3072
	ds_read_b128 v[186:189], v144 offset:32768
	ds_read_b128 v[190:193], v144 offset:33792
	ds_read_b128 v[194:197], v144 offset:34816
	ds_read_b128 v[198:201], v144 offset:35840
	ds_read_b128 v[202:205], v144 offset:36864
	ds_read_b128 v[206:209], v144 offset:37888
	ds_read_b128 v[210:213], v144 offset:38912
	ds_read_b128 v[214:217], v144 offset:39936
	s_add_u32 s22, s58, 0x40000
	s_addc_u32 s23, s59, 0
	s_mov_b32 s58, m0
	s_mov_b32 m0, s37
	s_nop 0
	global_load_lds_dwordx4 v136, s[22:23]
	s_mov_b32 m0, s58
	s_nop 0
	s_mov_b32 s58, m0
	s_mov_b32 m0, s52
	s_nop 0
	global_load_lds_dwordx4 v138, s[22:23]
	s_mov_b32 m0, s58
	s_waitcnt vmcnt(8)
	s_waitcnt lgkmcnt(0)
	s_barrier
	s_setprio 1
	s_waitcnt lgkmcnt(7)
	v_mfma_f32_16x16x32_bf16 v[126:129], v[148:151], v[186:189], v[126:129]
	v_mfma_f32_16x16x32_bf16 v[122:125], v[156:159], v[186:189], v[122:125]
	s_waitcnt lgkmcnt(5)
	v_mfma_f32_16x16x32_bf16 v[110:113], v[148:151], v[194:197], v[110:113]
	v_mfma_f32_16x16x32_bf16 v[106:109], v[156:159], v[194:197], v[106:109]
	s_waitcnt lgkmcnt(3)
	v_mfma_f32_16x16x32_bf16 v[94:97], v[148:151], v[202:205], v[94:97]
	v_mfma_f32_16x16x32_bf16 v[90:93], v[156:159], v[202:205], v[90:93]
	s_waitcnt lgkmcnt(1)
	v_mfma_f32_16x16x32_bf16 v[78:81], v[148:151], v[210:213], v[78:81]
	v_mfma_f32_16x16x32_bf16 v[74:77], v[156:159], v[210:213], v[74:77]
	v_mfma_f32_16x16x32_bf16 v[126:129], v[152:155], v[190:193], v[126:129]
	v_mfma_f32_16x16x32_bf16 v[122:125], v[160:163], v[190:193], v[122:125]
	v_mfma_f32_16x16x32_bf16 v[110:113], v[152:155], v[198:201], v[110:113]
	v_mfma_f32_16x16x32_bf16 v[106:109], v[160:163], v[198:201], v[106:109]
	v_mfma_f32_16x16x32_bf16 v[94:97], v[152:155], v[206:209], v[94:97]
	v_mfma_f32_16x16x32_bf16 v[90:93], v[160:163], v[206:209], v[90:93]
	s_waitcnt lgkmcnt(0)
	v_mfma_f32_16x16x32_bf16 v[78:81], v[152:155], v[214:217], v[78:81]
	v_mfma_f32_16x16x32_bf16 v[74:77], v[160:163], v[214:217], v[74:77]
	s_setprio 0
	s_setprio 1
	v_mfma_f32_16x16x32_bf16 v[118:121], v[164:167], v[186:189], v[118:121]
	v_mfma_f32_16x16x32_bf16 v[114:117], v[178:181], v[186:189], v[114:117]
	v_mfma_f32_16x16x32_bf16 v[102:105], v[164:167], v[194:197], v[102:105]
	v_mfma_f32_16x16x32_bf16 v[98:101], v[178:181], v[194:197], v[98:101]
	v_mfma_f32_16x16x32_bf16 v[86:89], v[164:167], v[202:205], v[86:89]
	v_mfma_f32_16x16x32_bf16 v[82:85], v[178:181], v[202:205], v[82:85]
	v_mfma_f32_16x16x32_bf16 v[70:73], v[164:167], v[210:213], v[70:73]
	v_mfma_f32_16x16x32_bf16 v[66:69], v[178:181], v[210:213], v[66:69]
	v_mfma_f32_16x16x32_bf16 v[118:121], v[174:177], v[190:193], v[118:121]
	v_mfma_f32_16x16x32_bf16 v[114:117], v[182:185], v[190:193], v[114:117]
	v_mfma_f32_16x16x32_bf16 v[102:105], v[174:177], v[198:201], v[102:105]
	v_mfma_f32_16x16x32_bf16 v[98:101], v[182:185], v[198:201], v[98:101]
	v_mfma_f32_16x16x32_bf16 v[86:89], v[174:177], v[206:209], v[86:89]
	v_mfma_f32_16x16x32_bf16 v[82:85], v[182:185], v[206:209], v[82:85]
	v_mfma_f32_16x16x32_bf16 v[70:73], v[174:177], v[214:217], v[70:73]
	v_mfma_f32_16x16x32_bf16 v[66:69], v[182:185], v[214:217], v[66:69]
	s_setprio 0
	s_barrier
	ds_read_b128 v[186:189], v144 offset:49152
	ds_read_b128 v[190:193], v144 offset:50176
	ds_read_b128 v[194:197], v144 offset:51200
	ds_read_b128 v[198:201], v144 offset:52224
	ds_read_b128 v[202:205], v144 offset:53248
	ds_read_b128 v[206:209], v144 offset:54272
	ds_read_b128 v[210:213], v144 offset:55296
	ds_read_b128 v[214:217], v144 offset:56320
	s_add_u32 s22, s56, 0x80
	s_addc_u32 s23, s57, 0
	s_mov_b32 s58, m0
	s_mov_b32 m0, s61
	s_nop 0
	global_load_lds_dwordx4 v137, s[22:23]
	s_mov_b32 m0, s58
	s_nop 0
	s_mov_b32 s58, m0
	s_mov_b32 m0, s62
	s_nop 0
	global_load_lds_dwordx4 v139, s[22:23]
	s_mov_b32 m0, s58
	s_add_u32 s22, s56, 0x40080
	s_addc_u32 s23, s57, 0
	s_mov_b32 s56, m0
	s_mov_b32 m0, s65
	s_nop 0
	global_load_lds_dwordx4 v137, s[22:23]
	s_mov_b32 m0, s56
	s_nop 0
	s_mov_b32 s56, m0
	s_mov_b32 m0, s66
	s_nop 0
	global_load_lds_dwordx4 v139, s[22:23]
	s_mov_b32 m0, s56
	s_mov_b32 s22, m0
	s_mov_b32 m0, s63
	s_nop 0
	global_load_lds_dwordx4 v136, s[54:55]
	s_mov_b32 m0, s22
	s_nop 0
	s_mov_b32 s22, m0
	s_mov_b32 m0, s64
	s_nop 0
	global_load_lds_dwordx4 v138, s[54:55]
	s_mov_b32 m0, s22
	s_waitcnt vmcnt(8)
	s_waitcnt lgkmcnt(0)
	s_barrier
	s_setprio 1
	s_waitcnt lgkmcnt(7)
	v_mfma_f32_16x16x32_bf16 v[62:65], v[148:151], v[186:189], v[62:65]
	v_mfma_f32_16x16x32_bf16 v[58:61], v[156:159], v[186:189], v[58:61]
	s_waitcnt lgkmcnt(5)
	v_mfma_f32_16x16x32_bf16 v[46:49], v[148:151], v[194:197], v[46:49]
	v_mfma_f32_16x16x32_bf16 v[42:45], v[156:159], v[194:197], v[42:45]
	s_waitcnt lgkmcnt(3)
	v_mfma_f32_16x16x32_bf16 v[30:33], v[148:151], v[202:205], v[30:33]
	v_mfma_f32_16x16x32_bf16 v[26:29], v[156:159], v[202:205], v[26:29]
	s_waitcnt lgkmcnt(1)
	v_mfma_f32_16x16x32_bf16 v[14:17], v[148:151], v[210:213], v[14:17]
	v_mfma_f32_16x16x32_bf16 v[10:13], v[156:159], v[210:213], v[10:13]
	v_mfma_f32_16x16x32_bf16 v[62:65], v[152:155], v[190:193], v[62:65]
	v_mfma_f32_16x16x32_bf16 v[58:61], v[160:163], v[190:193], v[58:61]
	v_mfma_f32_16x16x32_bf16 v[46:49], v[152:155], v[198:201], v[46:49]
	v_mfma_f32_16x16x32_bf16 v[42:45], v[160:163], v[198:201], v[42:45]
	v_mfma_f32_16x16x32_bf16 v[30:33], v[152:155], v[206:209], v[30:33]
	v_mfma_f32_16x16x32_bf16 v[26:29], v[160:163], v[206:209], v[26:29]
	s_waitcnt lgkmcnt(0)
	v_mfma_f32_16x16x32_bf16 v[14:17], v[152:155], v[214:217], v[14:17]
	v_mfma_f32_16x16x32_bf16 v[10:13], v[160:163], v[214:217], v[10:13]
	s_setprio 0
	s_setprio 1
	v_mfma_f32_16x16x32_bf16 v[54:57], v[164:167], v[186:189], v[54:57]
	v_mfma_f32_16x16x32_bf16 v[50:53], v[178:181], v[186:189], v[50:53]
	v_mfma_f32_16x16x32_bf16 v[38:41], v[164:167], v[194:197], v[38:41]
	v_mfma_f32_16x16x32_bf16 v[34:37], v[178:181], v[194:197], v[34:37]
	v_mfma_f32_16x16x32_bf16 v[22:25], v[164:167], v[202:205], v[22:25]
	v_mfma_f32_16x16x32_bf16 v[18:21], v[178:181], v[202:205], v[18:21]
	v_mfma_f32_16x16x32_bf16 v[6:9], v[164:167], v[210:213], v[6:9]
	v_mfma_f32_16x16x32_bf16 v[2:5], v[178:181], v[210:213], v[2:5]
	v_mfma_f32_16x16x32_bf16 v[54:57], v[174:177], v[190:193], v[54:57]
	v_mfma_f32_16x16x32_bf16 v[50:53], v[182:185], v[190:193], v[50:53]
	v_mfma_f32_16x16x32_bf16 v[38:41], v[174:177], v[198:201], v[38:41]
	v_mfma_f32_16x16x32_bf16 v[34:37], v[182:185], v[198:201], v[34:37]
	v_mfma_f32_16x16x32_bf16 v[22:25], v[174:177], v[206:209], v[22:25]
	v_mfma_f32_16x16x32_bf16 v[18:21], v[182:185], v[206:209], v[18:21]
	v_mfma_f32_16x16x32_bf16 v[6:9], v[174:177], v[214:217], v[6:9]
	v_mfma_f32_16x16x32_bf16 v[2:5], v[182:185], v[214:217], v[2:5]
	s_setprio 0
	s_barrier
	s_add_i32 s82, s82, 2
	s_add_u32 s80, s80, 0x100
	s_addc_u32 s81, s81, 0
	s_cmp_gt_u32 s82, 13
	s_mov_b64 s[22:23], s[40:41]
	s_cbranch_scc0 .LBB0_143
	s_and_b64 vcc, exec, s[10:11]
	s_cbranch_vccz .LBB0_146
	s_barrier

.LBB0_165:
	s_andn2_b64 vcc, exec, s[4:5]
	s_cbranch_vccnz .LBB0_180
	s_ashr_i32 s4, s93, 3
	s_cmp_gt_i32 s4, 23
	v_readfirstlane_b32 s23, v0
	s_cbranch_scc1 .LBB0_180
	v_lshlrev_b32_e32 v2, 4, v0
	v_and_b32_e32 v3, 32, v0
	v_bitop3_b32 v2, v2, v3, 48 bitop3:0x6c
	v_lshrrev_b32_e32 v3, 1, v0
	v_bfe_u32 v5, v0, 2, 2
	v_bfe_u32 v4, v0, 2, 4
	v_and_or_b32 v3, v3, 24, v5
	v_lshrrev_b32_e32 v5, 3, v0
	v_lshrrev_b32_e32 v7, 5, v0
	v_and_or_b32 v6, v5, 48, v4
	v_and_or_b32 v5, v5, 32, v7
	v_and_or_b32 v5, v5, 36, v3
	v_and_or_b32 v2, v0, 64, v2
	v_lshl_or_b32 v133, v5, 11, v2
	v_bfe_u32 v5, v0, 3, 25
	v_or_b32_e32 v5, 64, v5
	s_movk_i32 s5, 0x70
	s_lshr_b32 s16, s23, 6
	s_lshr_b32 s13, s23, 8
	v_and_or_b32 v4, v5, s5, v4
	s_movk_i32 s5, 0x60
	s_lshl_b32 s10, s16, 10
	v_and_or_b32 v5, v5, s5, v7
	s_movk_i32 s5, 0x64
	s_cmp_lt_i32 s4, 16
	v_and_or_b32 v3, v5, s5, v3
	s_cselect_b32 s5, 0, 16
	s_add_i32 s5, s5, s4
	s_lshl_b32 s4, s93, 3
	s_and_b32 s4, s4, 56
	s_bfe_u32 s12, s93, 0x30003
	s_or_b32 s22, s4, s12
	s_ashr_i32 s4, s5, 3
	s_ashr_i32 s5, s4, 31
	s_lshl_b32 s17, s22, 19
	s_lshl_b64 s[14:15], s[4:5], 19
	s_add_u32 s8, s24, s14
	s_addc_u32 s9, s25, s15
	s_add_i32 s5, s10, 0
	s_add_i32 s24, s5, 0x10000
	s_mov_b32 s10, m0
	s_mov_b32 m0, s24
	s_nop 0
	global_load_lds_dwordx4 v133, s[8:9]
	s_mov_b32 m0, s10
	v_lshl_or_b32 v135, v3, 11, v2
	s_add_i32 s25, s5, 0x12000
	s_mov_b32 s10, m0
	s_mov_b32 m0, s25
	s_nop 0
	global_load_lds_dwordx4 v135, s[8:9]
	s_mov_b32 m0, s10
	s_add_u32 s10, s8, 0x40000
	s_addc_u32 s11, s9, 0
	s_add_i32 s28, s5, 0x14000
	s_mov_b32 s18, m0
	s_mov_b32 m0, s28
	s_nop 0
	global_load_lds_dwordx4 v133, s[10:11]
	s_mov_b32 m0, s18
	s_add_i32 s29, s5, 0x16000
	s_mov_b32 s18, m0
	s_mov_b32 m0, s29
	s_nop 0
	global_load_lds_dwordx4 v135, s[10:11]
	s_mov_b32 m0, s18
	s_add_u32 s10, s2, s17
	v_lshl_or_b32 v132, v6, 11, v2
	s_addc_u32 s11, s3, 0
	s_mov_b32 s2, m0
	s_mov_b32 m0, s5
	s_nop 0
	global_load_lds_dwordx4 v132, s[10:11]
	s_mov_b32 m0, s2
	v_lshl_or_b32 v134, v4, 11, v2
	s_add_i32 s30, s5, 0x2000
	s_mov_b32 s2, m0
	s_mov_b32 m0, s30
	s_nop 0
	global_load_lds_dwordx4 v134, s[10:11]
	s_mov_b32 m0, s2
	s_add_u32 s2, s10, 0x40000
	s_addc_u32 s3, s11, 0
	s_add_i32 s31, s5, 0x4000
	s_mov_b32 s17, m0
	s_mov_b32 m0, s31
	s_nop 0
	global_load_lds_dwordx4 v132, s[2:3]
	s_mov_b32 m0, s17
	s_add_i32 s33, s5, 0x6000
	s_mov_b32 s17, m0
	s_mov_b32 m0, s33
	s_nop 0
	global_load_lds_dwordx4 v134, s[2:3]
	s_mov_b32 m0, s17
	s_cmp_lg_u32 s13, 1
	s_cbranch_scc1 .LBB0_169
	s_barrier
.LBB0_169:
	v_bfe_u32 v131, v0, 4, 2
	v_and_b32_e32 v130, 15, v0
	v_lshlrev_b32_e32 v2, 4, v131
	v_lshlrev_b32_e32 v4, 2, v0
	v_lshl_or_b32 v3, v130, 6, v2
	s_lshl_b32 s3, s13, 13
	v_and_b32_e32 v4, 32, v4
	v_bitop3_b32 v3, v3, s3, v4 bitop3:0xde
	s_lshl_b32 s3, s16, 5
	s_lshl_b32 s2, s13, 6
	s_and_b32 s3, s3, 0x60
	v_lshlrev_b32_e32 v5, 6, v0
	s_movk_i32 s13, 0x3c0
	v_and_or_b32 v2, v5, s13, v2
	s_lshl_b32 s13, s3, 7
	s_add_u32 s16, s8, 0x80
	v_bitop3_b32 v4, s13, v2, v4 bitop3:0xf6
	s_waitcnt vmcnt(2)
	s_barrier
	s_addc_u32 s17, s9, 0
	s_add_i32 s34, s5, 0x18000
	s_mov_b32 s13, m0
	s_mov_b32 m0, s34
	s_nop 0
	global_load_lds_dwordx4 v133, s[16:17]
	s_mov_b32 m0, s13
	s_add_i32 s35, s5, 0x1a000
	s_mov_b32 s13, m0
	s_mov_b32 m0, s35
	s_nop 0
	global_load_lds_dwordx4 v135, s[16:17]
	s_mov_b32 m0, s13
	s_add_u32 s16, s10, 0x80
	s_addc_u32 s17, s11, 0
	s_add_i32 s36, s5, 0x8000
	s_mov_b32 s13, m0
	s_mov_b32 m0, s36
	s_nop 0
	global_load_lds_dwordx4 v132, s[16:17]
	s_mov_b32 m0, s13
	s_add_i32 s37, s5, 0xa000
	s_mov_b32 s13, m0
	s_mov_b32 m0, s37
	s_nop 0
	global_load_lds_dwordx4 v134, s[16:17]
	s_mov_b32 m0, s13
	s_add_u32 s16, s8, 0x40080
	s_addc_u32 s17, s9, 0
	s_add_i32 s40, s5, 0x1c000
	s_mov_b32 s13, m0
	s_mov_b32 m0, s40
	s_nop 0
	global_load_lds_dwordx4 v133, s[16:17]
	s_mov_b32 m0, s13
	s_add_i32 s41, s5, 0x1e000
	s_mov_b32 s13, m0
	s_mov_b32 m0, s41
	s_nop 0
	global_load_lds_dwordx4 v135, s[16:17]
	s_mov_b32 m0, s13
	s_and_b32 s13, s93, 7
	s_lshl_b32 s13, s13, 22
	s_lshl_b32 s12, s12, 19
	s_add_i32 s52, s5, 0xc000
	s_add_i32 s53, s5, 0xe000
	s_or_b32 s12, s13, s12
	s_add_u32 s12, s74, s12
	s_addc_u32 s13, s75, 0
	s_add_u32 s12, s12, 0xd000000
	s_addc_u32 s13, s13, 0
	s_add_u32 s14, s74, s14
	s_waitcnt vmcnt(6)
	s_addc_u32 s15, s75, s15
	s_add_u32 s54, s14, 0x200100
	v_add_u32_e32 v4, 0, v4
	s_addc_u32 s55, s15, 0
	s_mov_b32 s56, -2
	v_add_u32_e32 v136, 0x10000, v4
	v_add_u32_e32 v137, 0x14000, v4
	v_add_u32_e32 v138, 0, v3
	v_add_u32_e32 v139, 0x18000, v4
	v_add_u32_e32 v140, 0x1c000, v4
	s_barrier
.Lpeel170:
	ds_read_b128 v[142:145], v136
	ds_read_b128 v[146:149], v136 offset:1024
	ds_read_b128 v[150:153], v136 offset:2048
	ds_read_b128 v[154:157], v136 offset:3072
	ds_read_b128 v[158:161], v137
	ds_read_b128 v[162:165], v137 offset:1024
	ds_read_b128 v[166:169], v137 offset:2048
	ds_read_b128 v[174:177], v137 offset:3072
	s_add_u32 s14, s12, 0x100
	s_addc_u32 s15, s13, 0
	s_cmp_eq_u32 s56, 12
	s_cselect_b32 s20, s10, s14
	s_cselect_b32 s21, s11, s15
	s_cselect_b32 s18, s8, s54
	s_cselect_b32 s19, s9, s55
	s_add_u32 s16, s20, 0x80
	s_addc_u32 s17, s21, 0
	ds_read_b128 v[178:181], v138
	ds_read_b128 v[182:185], v138 offset:1024
	ds_read_b128 v[186:189], v138 offset:2048
	ds_read_b128 v[190:193], v138 offset:3072
	ds_read_b128 v[194:197], v138 offset:4096
	ds_read_b128 v[198:201], v138 offset:5120
	ds_read_b128 v[202:205], v138 offset:6144
	ds_read_b128 v[206:209], v138 offset:7168
	s_add_u32 s12, s12, 0x40080
	s_addc_u32 s13, s13, 0
	s_mov_b32 s57, m0
	s_mov_b32 m0, s52
	s_nop 0
	global_load_lds_dwordx4 v132, s[12:13]
	s_mov_b32 m0, s57
	s_nop 0
	s_mov_b32 s57, m0
	s_mov_b32 m0, s53
	s_nop 0
	global_load_lds_dwordx4 v134, s[12:13]
	s_mov_b32 m0, s57
	s_waitcnt vmcnt(8)
	s_waitcnt lgkmcnt(0)
	s_barrier
	s_setprio 1
	s_waitcnt lgkmcnt(7)
	v_mfma_f32_16x16x32_bf16 v[126:129], v[142:145], v[178:181], 0
	v_mfma_f32_16x16x32_bf16 v[122:125], v[150:153], v[178:181], 0
	s_waitcnt lgkmcnt(5)
	v_mfma_f32_16x16x32_bf16 v[110:113], v[142:145], v[186:189], 0
	v_mfma_f32_16x16x32_bf16 v[106:109], v[150:153], v[186:189], 0
	s_waitcnt lgkmcnt(3)
	v_mfma_f32_16x16x32_bf16 v[94:97], v[142:145], v[194:197], 0
	v_mfma_f32_16x16x32_bf16 v[90:93], v[150:153], v[194:197], 0
	s_waitcnt lgkmcnt(1)
	v_mfma_f32_16x16x32_bf16 v[78:81], v[142:145], v[202:205], 0
	v_mfma_f32_16x16x32_bf16 v[74:77], v[150:153], v[202:205], 0
	v_mfma_f32_16x16x32_bf16 v[126:129], v[146:149], v[182:185], v[126:129]
	v_mfma_f32_16x16x32_bf16 v[122:125], v[154:157], v[182:185], v[122:125]
	v_mfma_f32_16x16x32_bf16 v[110:113], v[146:149], v[190:193], v[110:113]
	v_mfma_f32_16x16x32_bf16 v[106:109], v[154:157], v[190:193], v[106:109]
	v_mfma_f32_16x16x32_bf16 v[94:97], v[146:149], v[198:201], v[94:97]
	v_mfma_f32_16x16x32_bf16 v[90:93], v[154:157], v[198:201], v[90:93]
	s_waitcnt lgkmcnt(0)
	v_mfma_f32_16x16x32_bf16 v[78:81], v[146:149], v[206:209], v[78:81]
	v_mfma_f32_16x16x32_bf16 v[74:77], v[154:157], v[206:209], v[74:77]
	s_setprio 0
	s_setprio 1
	v_mfma_f32_16x16x32_bf16 v[118:121], v[158:161], v[178:181], 0
	v_mfma_f32_16x16x32_bf16 v[114:117], v[166:169], v[178:181], 0
	v_mfma_f32_16x16x32_bf16 v[102:105], v[158:161], v[186:189], 0
	v_mfma_f32_16x16x32_bf16 v[98:101], v[166:169], v[186:189], 0
	v_mfma_f32_16x16x32_bf16 v[86:89], v[158:161], v[194:197], 0
	v_mfma_f32_16x16x32_bf16 v[82:85], v[166:169], v[194:197], 0
	v_mfma_f32_16x16x32_bf16 v[70:73], v[158:161], v[202:205], 0
	v_mfma_f32_16x16x32_bf16 v[66:69], v[166:169], v[202:205], 0
	v_mfma_f32_16x16x32_bf16 v[118:121], v[162:165], v[182:185], v[118:121]
	v_mfma_f32_16x16x32_bf16 v[114:117], v[174:177], v[182:185], v[114:117]
	v_mfma_f32_16x16x32_bf16 v[102:105], v[162:165], v[190:193], v[102:105]
	v_mfma_f32_16x16x32_bf16 v[98:101], v[174:177], v[190:193], v[98:101]
	v_mfma_f32_16x16x32_bf16 v[86:89], v[162:165], v[198:201], v[86:89]
	v_mfma_f32_16x16x32_bf16 v[82:85], v[174:177], v[198:201], v[82:85]
	v_mfma_f32_16x16x32_bf16 v[70:73], v[162:165], v[206:209], v[70:73]
	v_mfma_f32_16x16x32_bf16 v[66:69], v[174:177], v[206:209], v[66:69]
	s_setprio 0
	s_barrier
	ds_read_b128 v[178:181], v138 offset:16384
	ds_read_b128 v[182:185], v138 offset:17408
	ds_read_b128 v[186:189], v138 offset:18432
	ds_read_b128 v[190:193], v138 offset:19456
	ds_read_b128 v[194:197], v138 offset:20480
	ds_read_b128 v[198:201], v138 offset:21504
	ds_read_b128 v[202:205], v138 offset:22528
	ds_read_b128 v[206:209], v138 offset:23552
	s_mov_b32 s12, m0
	s_mov_b32 m0, s24
	s_nop 0
	global_load_lds_dwordx4 v133, s[18:19]
	s_mov_b32 m0, s12
	s_nop 0
	s_mov_b32 s12, m0
	s_mov_b32 m0, s25
	s_nop 0
	global_load_lds_dwordx4 v135, s[18:19]
	s_mov_b32 m0, s12
	s_add_u32 s12, s18, 0x40000
	s_addc_u32 s13, s19, 0
	s_mov_b32 s57, m0
	s_mov_b32 m0, s28
	s_nop 0
	global_load_lds_dwordx4 v133, s[12:13]
	s_mov_b32 m0, s57
	s_nop 0
	s_mov_b32 s57, m0
	s_mov_b32 m0, s29
	s_nop 0
	global_load_lds_dwordx4 v135, s[12:13]
	s_mov_b32 m0, s57
	s_mov_b32 s12, m0
	s_mov_b32 m0, s5
	s_nop 0
	global_load_lds_dwordx4 v132, s[20:21]
	s_mov_b32 m0, s12
	s_nop 0
	s_mov_b32 s12, m0
	s_mov_b32 m0, s30
	s_nop 0
	global_load_lds_dwordx4 v134, s[20:21]
	s_mov_b32 m0, s12
	s_waitcnt vmcnt(8)
	s_waitcnt lgkmcnt(0)
	s_barrier
	s_setprio 1
	s_waitcnt lgkmcnt(7)
	v_mfma_f32_16x16x32_bf16 v[62:65], v[142:145], v[178:181], 0
	v_mfma_f32_16x16x32_bf16 v[58:61], v[150:153], v[178:181], 0
	s_waitcnt lgkmcnt(5)
	v_mfma_f32_16x16x32_bf16 v[46:49], v[142:145], v[186:189], 0
	v_mfma_f32_16x16x32_bf16 v[42:45], v[150:153], v[186:189], 0
	s_waitcnt lgkmcnt(3)
	v_mfma_f32_16x16x32_bf16 v[30:33], v[142:145], v[194:197], 0
	v_mfma_f32_16x16x32_bf16 v[26:29], v[150:153], v[194:197], 0
	s_waitcnt lgkmcnt(1)
	v_mfma_f32_16x16x32_bf16 v[14:17], v[142:145], v[202:205], 0
	v_mfma_f32_16x16x32_bf16 v[10:13], v[150:153], v[202:205], 0
	v_mfma_f32_16x16x32_bf16 v[62:65], v[146:149], v[182:185], v[62:65]
	v_mfma_f32_16x16x32_bf16 v[58:61], v[154:157], v[182:185], v[58:61]
	v_mfma_f32_16x16x32_bf16 v[46:49], v[146:149], v[190:193], v[46:49]
	v_mfma_f32_16x16x32_bf16 v[42:45], v[154:157], v[190:193], v[42:45]
	v_mfma_f32_16x16x32_bf16 v[30:33], v[146:149], v[198:201], v[30:33]
	v_mfma_f32_16x16x32_bf16 v[26:29], v[154:157], v[198:201], v[26:29]
	s_waitcnt lgkmcnt(0)
	v_mfma_f32_16x16x32_bf16 v[14:17], v[146:149], v[206:209], v[14:17]
	v_mfma_f32_16x16x32_bf16 v[10:13], v[154:157], v[206:209], v[10:13]
	s_setprio 0
	s_setprio 1
	v_mfma_f32_16x16x32_bf16 v[54:57], v[158:161], v[178:181], 0
	v_mfma_f32_16x16x32_bf16 v[50:53], v[166:169], v[178:181], 0
	v_mfma_f32_16x16x32_bf16 v[38:41], v[158:161], v[186:189], 0
	v_mfma_f32_16x16x32_bf16 v[34:37], v[166:169], v[186:189], 0
	v_mfma_f32_16x16x32_bf16 v[22:25], v[158:161], v[194:197], 0
	v_mfma_f32_16x16x32_bf16 v[18:21], v[166:169], v[194:197], 0
	v_mfma_f32_16x16x32_bf16 v[6:9], v[158:161], v[202:205], 0
	v_mfma_f32_16x16x32_bf16 v[2:5], v[166:169], v[202:205], 0
	v_mfma_f32_16x16x32_bf16 v[54:57], v[162:165], v[182:185], v[54:57]
	v_mfma_f32_16x16x32_bf16 v[50:53], v[174:177], v[182:185], v[50:53]
	v_mfma_f32_16x16x32_bf16 v[38:41], v[162:165], v[190:193], v[38:41]
	v_mfma_f32_16x16x32_bf16 v[34:37], v[174:177], v[190:193], v[34:37]
	v_mfma_f32_16x16x32_bf16 v[22:25], v[162:165], v[198:201], v[22:25]
	v_mfma_f32_16x16x32_bf16 v[18:21], v[174:177], v[198:201], v[18:21]
	v_mfma_f32_16x16x32_bf16 v[6:9], v[162:165], v[206:209], v[6:9]
	v_mfma_f32_16x16x32_bf16 v[2:5], v[174:177], v[206:209], v[2:5]
	s_setprio 0
	s_barrier
	s_branch .Lmid170
.LBB0_170:
	ds_read_b128 v[142:145], v136
	ds_read_b128 v[146:149], v136 offset:1024
	ds_read_b128 v[150:153], v136 offset:2048
	ds_read_b128 v[154:157], v136 offset:3072
	ds_read_b128 v[158:161], v137
	ds_read_b128 v[162:165], v137 offset:1024
	ds_read_b128 v[166:169], v137 offset:2048
	ds_read_b128 v[174:177], v137 offset:3072
	s_add_u32 s14, s12, 0x100
	s_addc_u32 s15, s13, 0
	s_cmp_eq_u32 s56, 12
	s_cselect_b32 s20, s10, s14
	s_cselect_b32 s21, s11, s15
	s_cselect_b32 s18, s8, s54
	s_cselect_b32 s19, s9, s55
	s_add_u32 s16, s20, 0x80
	s_addc_u32 s17, s21, 0
	ds_read_b128 v[178:181], v138
	ds_read_b128 v[182:185], v138 offset:1024
	ds_read_b128 v[186:189], v138 offset:2048
	ds_read_b128 v[190:193], v138 offset:3072
	ds_read_b128 v[194:197], v138 offset:4096
	ds_read_b128 v[198:201], v138 offset:5120
	ds_read_b128 v[202:205], v138 offset:6144
	ds_read_b128 v[206:209], v138 offset:7168
	s_add_u32 s12, s12, 0x40080
	s_addc_u32 s13, s13, 0
	s_mov_b32 s57, m0
	s_mov_b32 m0, s52
	s_nop 0
	global_load_lds_dwordx4 v132, s[12:13]
	s_mov_b32 m0, s57
	s_nop 0
	s_mov_b32 s57, m0
	s_mov_b32 m0, s53
	s_nop 0
	global_load_lds_dwordx4 v134, s[12:13]
	s_mov_b32 m0, s57
	s_waitcnt vmcnt(8)
	s_waitcnt lgkmcnt(0)
	s_barrier
	s_setprio 1
	s_waitcnt lgkmcnt(7)
	v_mfma_f32_16x16x32_bf16 v[126:129], v[142:145], v[178:181], v[126:129]
	v_mfma_f32_16x16x32_bf16 v[122:125], v[150:153], v[178:181], v[122:125]
	s_waitcnt lgkmcnt(5)
	v_mfma_f32_16x16x32_bf16 v[110:113], v[142:145], v[186:189], v[110:113]
	v_mfma_f32_16x16x32_bf16 v[106:109], v[150:153], v[186:189], v[106:109]
	s_waitcnt lgkmcnt(3)
	v_mfma_f32_16x16x32_bf16 v[94:97], v[142:145], v[194:197], v[94:97]
	v_mfma_f32_16x16x32_bf16 v[90:93], v[150:153], v[194:197], v[90:93]
	s_waitcnt lgkmcnt(1)
	v_mfma_f32_16x16x32_bf16 v[78:81], v[142:145], v[202:205], v[78:81]
	v_mfma_f32_16x16x32_bf16 v[74:77], v[150:153], v[202:205], v[74:77]
	v_mfma_f32_16x16x32_bf16 v[126:129], v[146:149], v[182:185], v[126:129]
	v_mfma_f32_16x16x32_bf16 v[122:125], v[154:157], v[182:185], v[122:125]
	v_mfma_f32_16x16x32_bf16 v[110:113], v[146:149], v[190:193], v[110:113]
	v_mfma_f32_16x16x32_bf16 v[106:109], v[154:157], v[190:193], v[106:109]
	v_mfma_f32_16x16x32_bf16 v[94:97], v[146:149], v[198:201], v[94:97]
	v_mfma_f32_16x16x32_bf16 v[90:93], v[154:157], v[198:201], v[90:93]
	s_waitcnt lgkmcnt(0)
	v_mfma_f32_16x16x32_bf16 v[78:81], v[146:149], v[206:209], v[78:81]
	v_mfma_f32_16x16x32_bf16 v[74:77], v[154:157], v[206:209], v[74:77]
	s_setprio 0
	s_setprio 1
	v_mfma_f32_16x16x32_bf16 v[118:121], v[158:161], v[178:181], v[118:121]
	v_mfma_f32_16x16x32_bf16 v[114:117], v[166:169], v[178:181], v[114:117]
	v_mfma_f32_16x16x32_bf16 v[102:105], v[158:161], v[186:189], v[102:105]
	v_mfma_f32_16x16x32_bf16 v[98:101], v[166:169], v[186:189], v[98:101]
	v_mfma_f32_16x16x32_bf16 v[86:89], v[158:161], v[194:197], v[86:89]
	v_mfma_f32_16x16x32_bf16 v[82:85], v[166:169], v[194:197], v[82:85]
	v_mfma_f32_16x16x32_bf16 v[70:73], v[158:161], v[202:205], v[70:73]
	v_mfma_f32_16x16x32_bf16 v[66:69], v[166:169], v[202:205], v[66:69]
	v_mfma_f32_16x16x32_bf16 v[118:121], v[162:165], v[182:185], v[118:121]
	v_mfma_f32_16x16x32_bf16 v[114:117], v[174:177], v[182:185], v[114:117]
	v_mfma_f32_16x16x32_bf16 v[102:105], v[162:165], v[190:193], v[102:105]
	v_mfma_f32_16x16x32_bf16 v[98:101], v[174:177], v[190:193], v[98:101]
	v_mfma_f32_16x16x32_bf16 v[86:89], v[162:165], v[198:201], v[86:89]
	v_mfma_f32_16x16x32_bf16 v[82:85], v[174:177], v[198:201], v[82:85]
	v_mfma_f32_16x16x32_bf16 v[70:73], v[162:165], v[206:209], v[70:73]
	v_mfma_f32_16x16x32_bf16 v[66:69], v[174:177], v[206:209], v[66:69]
	s_setprio 0
	s_barrier
	ds_read_b128 v[178:181], v138 offset:16384
	ds_read_b128 v[182:185], v138 offset:17408
	ds_read_b128 v[186:189], v138 offset:18432
	ds_read_b128 v[190:193], v138 offset:19456
	ds_read_b128 v[194:197], v138 offset:20480
	ds_read_b128 v[198:201], v138 offset:21504
	ds_read_b128 v[202:205], v138 offset:22528
	ds_read_b128 v[206:209], v138 offset:23552
	s_mov_b32 s12, m0
	s_mov_b32 m0, s24
	s_nop 0
	global_load_lds_dwordx4 v133, s[18:19]
	s_mov_b32 m0, s12
	s_nop 0
	s_mov_b32 s12, m0
	s_mov_b32 m0, s25
	s_nop 0
	global_load_lds_dwordx4 v135, s[18:19]
	s_mov_b32 m0, s12
	s_add_u32 s12, s18, 0x40000
	s_addc_u32 s13, s19, 0
	s_mov_b32 s57, m0
	s_mov_b32 m0, s28
	s_nop 0
	global_load_lds_dwordx4 v133, s[12:13]
	s_mov_b32 m0, s57
	s_nop 0
	s_mov_b32 s57, m0
	s_mov_b32 m0, s29
	s_nop 0
	global_load_lds_dwordx4 v135, s[12:13]
	s_mov_b32 m0, s57
	s_mov_b32 s12, m0
	s_mov_b32 m0, s5
	s_nop 0
	global_load_lds_dwordx4 v132, s[20:21]
	s_mov_b32 m0, s12
	s_nop 0
	s_mov_b32 s12, m0
	s_mov_b32 m0, s30
	s_nop 0
	global_load_lds_dwordx4 v134, s[20:21]
	s_mov_b32 m0, s12
	s_waitcnt vmcnt(8)
	s_waitcnt lgkmcnt(0)
	s_barrier
	s_setprio 1
	s_waitcnt lgkmcnt(7)
	v_mfma_f32_16x16x32_bf16 v[62:65], v[142:145], v[178:181], v[62:65]
	v_mfma_f32_16x16x32_bf16 v[58:61], v[150:153], v[178:181], v[58:61]
	s_waitcnt lgkmcnt(5)
	v_mfma_f32_16x16x32_bf16 v[46:49], v[142:145], v[186:189], v[46:49]
	v_mfma_f32_16x16x32_bf16 v[42:45], v[150:153], v[186:189], v[42:45]
	s_waitcnt lgkmcnt(3)
	v_mfma_f32_16x16x32_bf16 v[30:33], v[142:145], v[194:197], v[30:33]
	v_mfma_f32_16x16x32_bf16 v[26:29], v[150:153], v[194:197], v[26:29]
	s_waitcnt lgkmcnt(1)
	v_mfma_f32_16x16x32_bf16 v[14:17], v[142:145], v[202:205], v[14:17]
	v_mfma_f32_16x16x32_bf16 v[10:13], v[150:153], v[202:205], v[10:13]
	v_mfma_f32_16x16x32_bf16 v[62:65], v[146:149], v[182:185], v[62:65]
	v_mfma_f32_16x16x32_bf16 v[58:61], v[154:157], v[182:185], v[58:61]
	v_mfma_f32_16x16x32_bf16 v[46:49], v[146:149], v[190:193], v[46:49]
	v_mfma_f32_16x16x32_bf16 v[42:45], v[154:157], v[190:193], v[42:45]
	v_mfma_f32_16x16x32_bf16 v[30:33], v[146:149], v[198:201], v[30:33]
	v_mfma_f32_16x16x32_bf16 v[26:29], v[154:157], v[198:201], v[26:29]
	s_waitcnt lgkmcnt(0)
	v_mfma_f32_16x16x32_bf16 v[14:17], v[146:149], v[206:209], v[14:17]
	v_mfma_f32_16x16x32_bf16 v[10:13], v[154:157], v[206:209], v[10:13]
	s_setprio 0
	s_setprio 1
	v_mfma_f32_16x16x32_bf16 v[54:57], v[158:161], v[178:181], v[54:57]
	v_mfma_f32_16x16x32_bf16 v[50:53], v[166:169], v[178:181], v[50:53]
	v_mfma_f32_16x16x32_bf16 v[38:41], v[158:161], v[186:189], v[38:41]
	v_mfma_f32_16x16x32_bf16 v[34:37], v[166:169], v[186:189], v[34:37]
	v_mfma_f32_16x16x32_bf16 v[22:25], v[158:161], v[194:197], v[22:25]
	v_mfma_f32_16x16x32_bf16 v[18:21], v[166:169], v[194:197], v[18:21]
	v_mfma_f32_16x16x32_bf16 v[6:9], v[158:161], v[202:205], v[6:9]
	v_mfma_f32_16x16x32_bf16 v[2:5], v[166:169], v[202:205], v[2:5]
	v_mfma_f32_16x16x32_bf16 v[54:57], v[162:165], v[182:185], v[54:57]
	v_mfma_f32_16x16x32_bf16 v[50:53], v[174:177], v[182:185], v[50:53]
	v_mfma_f32_16x16x32_bf16 v[38:41], v[162:165], v[190:193], v[38:41]
	v_mfma_f32_16x16x32_bf16 v[34:37], v[174:177], v[190:193], v[34:37]
	v_mfma_f32_16x16x32_bf16 v[22:25], v[162:165], v[198:201], v[22:25]
	v_mfma_f32_16x16x32_bf16 v[18:21], v[174:177], v[198:201], v[18:21]
	v_mfma_f32_16x16x32_bf16 v[6:9], v[162:165], v[206:209], v[6:9]
	v_mfma_f32_16x16x32_bf16 v[2:5], v[174:177], v[206:209], v[2:5]
	s_setprio 0
	s_barrier
.Lmid170:
	ds_read_b128 v[142:145], v139
	ds_read_b128 v[146:149], v139 offset:1024
	ds_read_b128 v[150:153], v139 offset:2048
	ds_read_b128 v[154:157], v139 offset:3072
	ds_read_b128 v[158:161], v140
	ds_read_b128 v[162:165], v140 offset:1024
	ds_read_b128 v[166:169], v140 offset:2048
	ds_read_b128 v[174:177], v140 offset:3072
	ds_read_b128 v[178:181], v138 offset:32768
	ds_read_b128 v[182:185], v138 offset:33792
	ds_read_b128 v[186:189], v138 offset:34816
	ds_read_b128 v[190:193], v138 offset:35840
	ds_read_b128 v[194:197], v138 offset:36864
	ds_read_b128 v[198:201], v138 offset:37888
	ds_read_b128 v[202:205], v138 offset:38912
	ds_read_b128 v[206:209], v138 offset:39936
	s_add_u32 s12, s20, 0x40000
	s_addc_u32 s13, s21, 0
	s_mov_b32 s20, m0
	s_mov_b32 m0, s31
	s_nop 0
	global_load_lds_dwordx4 v132, s[12:13]
	s_mov_b32 m0, s20
	s_nop 0
	s_mov_b32 s20, m0
	s_mov_b32 m0, s33
	s_nop 0
	global_load_lds_dwordx4 v134, s[12:13]
	s_mov_b32 m0, s20
	s_waitcnt vmcnt(8)
	s_waitcnt lgkmcnt(0)
	s_barrier
	s_setprio 1
	s_waitcnt lgkmcnt(7)
	v_mfma_f32_16x16x32_bf16 v[126:129], v[142:145], v[178:181], v[126:129]
	v_mfma_f32_16x16x32_bf16 v[122:125], v[150:153], v[178:181], v[122:125]
	s_waitcnt lgkmcnt(5)
	v_mfma_f32_16x16x32_bf16 v[110:113], v[142:145], v[186:189], v[110:113]
	v_mfma_f32_16x16x32_bf16 v[106:109], v[150:153], v[186:189], v[106:109]
	s_waitcnt lgkmcnt(3)
	v_mfma_f32_16x16x32_bf16 v[94:97], v[142:145], v[194:197], v[94:97]
	v_mfma_f32_16x16x32_bf16 v[90:93], v[150:153], v[194:197], v[90:93]
	s_waitcnt lgkmcnt(1)
	v_mfma_f32_16x16x32_bf16 v[78:81], v[142:145], v[202:205], v[78:81]
	v_mfma_f32_16x16x32_bf16 v[74:77], v[150:153], v[202:205], v[74:77]
	v_mfma_f32_16x16x32_bf16 v[126:129], v[146:149], v[182:185], v[126:129]
	v_mfma_f32_16x16x32_bf16 v[122:125], v[154:157], v[182:185], v[122:125]
	v_mfma_f32_16x16x32_bf16 v[110:113], v[146:149], v[190:193], v[110:113]
	v_mfma_f32_16x16x32_bf16 v[106:109], v[154:157], v[190:193], v[106:109]
	v_mfma_f32_16x16x32_bf16 v[94:97], v[146:149], v[198:201], v[94:97]
	v_mfma_f32_16x16x32_bf16 v[90:93], v[154:157], v[198:201], v[90:93]
	s_waitcnt lgkmcnt(0)
	v_mfma_f32_16x16x32_bf16 v[78:81], v[146:149], v[206:209], v[78:81]
	v_mfma_f32_16x16x32_bf16 v[74:77], v[154:157], v[206:209], v[74:77]
	s_setprio 0
	s_setprio 1
	v_mfma_f32_16x16x32_bf16 v[118:121], v[158:161], v[178:181], v[118:121]
	v_mfma_f32_16x16x32_bf16 v[114:117], v[166:169], v[178:181], v[114:117]
	v_mfma_f32_16x16x32_bf16 v[102:105], v[158:161], v[186:189], v[102:105]
	v_mfma_f32_16x16x32_bf16 v[98:101], v[166:169], v[186:189], v[98:101]
	v_mfma_f32_16x16x32_bf16 v[86:89], v[158:161], v[194:197], v[86:89]
	v_mfma_f32_16x16x32_bf16 v[82:85], v[166:169], v[194:197], v[82:85]
	v_mfma_f32_16x16x32_bf16 v[70:73], v[158:161], v[202:205], v[70:73]
	v_mfma_f32_16x16x32_bf16 v[66:69], v[166:169], v[202:205], v[66:69]
	v_mfma_f32_16x16x32_bf16 v[118:121], v[162:165], v[182:185], v[118:121]
	v_mfma_f32_16x16x32_bf16 v[114:117], v[174:177], v[182:185], v[114:117]
	v_mfma_f32_16x16x32_bf16 v[102:105], v[162:165], v[190:193], v[102:105]
	v_mfma_f32_16x16x32_bf16 v[98:101], v[174:177], v[190:193], v[98:101]
	v_mfma_f32_16x16x32_bf16 v[86:89], v[162:165], v[198:201], v[86:89]
	v_mfma_f32_16x16x32_bf16 v[82:85], v[174:177], v[198:201], v[82:85]
	v_mfma_f32_16x16x32_bf16 v[70:73], v[162:165], v[206:209], v[70:73]
	v_mfma_f32_16x16x32_bf16 v[66:69], v[174:177], v[206:209], v[66:69]
	s_setprio 0
	s_barrier
	ds_read_b128 v[178:181], v138 offset:49152
	ds_read_b128 v[182:185], v138 offset:50176
	ds_read_b128 v[186:189], v138 offset:51200
	ds_read_b128 v[190:193], v138 offset:52224
	ds_read_b128 v[194:197], v138 offset:53248
	ds_read_b128 v[198:201], v138 offset:54272
	ds_read_b128 v[202:205], v138 offset:55296
	ds_read_b128 v[206:209], v138 offset:56320
	s_add_u32 s12, s18, 0x80
	s_addc_u32 s13, s19, 0
	s_mov_b32 s20, m0
	s_mov_b32 m0, s34
	s_nop 0
	global_load_lds_dwordx4 v133, s[12:13]
	s_mov_b32 m0, s20
	s_nop 0
	s_mov_b32 s20, m0
	s_mov_b32 m0, s35
	s_nop 0
	global_load_lds_dwordx4 v135, s[12:13]
	s_mov_b32 m0, s20
	s_add_u32 s12, s18, 0x40080
	s_addc_u32 s13, s19, 0
	s_mov_b32 s18, m0
	s_mov_b32 m0, s40
	s_nop 0
	global_load_lds_dwordx4 v133, s[12:13]
	s_mov_b32 m0, s18
	s_nop 0
	s_mov_b32 s18, m0
	s_mov_b32 m0, s41
	s_nop 0
	global_load_lds_dwordx4 v135, s[12:13]
	s_mov_b32 m0, s18
	s_mov_b32 s12, m0
	s_mov_b32 m0, s36
	s_nop 0
	global_load_lds_dwordx4 v132, s[16:17]
	s_mov_b32 m0, s12
	s_nop 0
	s_mov_b32 s12, m0
	s_mov_b32 m0, s37
	s_nop 0
	global_load_lds_dwordx4 v134, s[16:17]
	s_mov_b32 m0, s12
	s_waitcnt vmcnt(8)
	s_waitcnt lgkmcnt(0)
	s_barrier
	s_setprio 1
	s_waitcnt lgkmcnt(7)
	v_mfma_f32_16x16x32_bf16 v[62:65], v[142:145], v[178:181], v[62:65]
	v_mfma_f32_16x16x32_bf16 v[58:61], v[150:153], v[178:181], v[58:61]
	s_waitcnt lgkmcnt(5)
	v_mfma_f32_16x16x32_bf16 v[46:49], v[142:145], v[186:189], v[46:49]
	v_mfma_f32_16x16x32_bf16 v[42:45], v[150:153], v[186:189], v[42:45]
	s_waitcnt lgkmcnt(3)
	v_mfma_f32_16x16x32_bf16 v[30:33], v[142:145], v[194:197], v[30:33]
	v_mfma_f32_16x16x32_bf16 v[26:29], v[150:153], v[194:197], v[26:29]
	s_waitcnt lgkmcnt(1)
	v_mfma_f32_16x16x32_bf16 v[14:17], v[142:145], v[202:205], v[14:17]
	v_mfma_f32_16x16x32_bf16 v[10:13], v[150:153], v[202:205], v[10:13]
	v_mfma_f32_16x16x32_bf16 v[62:65], v[146:149], v[182:185], v[62:65]
	v_mfma_f32_16x16x32_bf16 v[58:61], v[154:157], v[182:185], v[58:61]
	v_mfma_f32_16x16x32_bf16 v[46:49], v[146:149], v[190:193], v[46:49]
	v_mfma_f32_16x16x32_bf16 v[42:45], v[154:157], v[190:193], v[42:45]
	v_mfma_f32_16x16x32_bf16 v[30:33], v[146:149], v[198:201], v[30:33]
	v_mfma_f32_16x16x32_bf16 v[26:29], v[154:157], v[198:201], v[26:29]
	s_waitcnt lgkmcnt(0)
	v_mfma_f32_16x16x32_bf16 v[14:17], v[146:149], v[206:209], v[14:17]
	v_mfma_f32_16x16x32_bf16 v[10:13], v[154:157], v[206:209], v[10:13]
	s_setprio 0
	s_setprio 1
	v_mfma_f32_16x16x32_bf16 v[54:57], v[158:161], v[178:181], v[54:57]
	v_mfma_f32_16x16x32_bf16 v[50:53], v[166:169], v[178:181], v[50:53]
	v_mfma_f32_16x16x32_bf16 v[38:41], v[158:161], v[186:189], v[38:41]
	v_mfma_f32_16x16x32_bf16 v[34:37], v[166:169], v[186:189], v[34:37]
	v_mfma_f32_16x16x32_bf16 v[22:25], v[158:161], v[194:197], v[22:25]
	v_mfma_f32_16x16x32_bf16 v[18:21], v[166:169], v[194:197], v[18:21]
	v_mfma_f32_16x16x32_bf16 v[6:9], v[158:161], v[202:205], v[6:9]
	v_mfma_f32_16x16x32_bf16 v[2:5], v[166:169], v[202:205], v[2:5]
	v_mfma_f32_16x16x32_bf16 v[54:57], v[162:165], v[182:185], v[54:57]
	v_mfma_f32_16x16x32_bf16 v[50:53], v[174:177], v[182:185], v[50:53]
	v_mfma_f32_16x16x32_bf16 v[38:41], v[162:165], v[190:193], v[38:41]
	v_mfma_f32_16x16x32_bf16 v[34:37], v[174:177], v[190:193], v[34:37]
	v_mfma_f32_16x16x32_bf16 v[22:25], v[162:165], v[198:201], v[22:25]
	v_mfma_f32_16x16x32_bf16 v[18:21], v[174:177], v[198:201], v[18:21]
	v_mfma_f32_16x16x32_bf16 v[6:9], v[162:165], v[206:209], v[6:9]
	v_mfma_f32_16x16x32_bf16 v[2:5], v[174:177], v[206:209], v[2:5]
	s_setprio 0
	s_barrier
	s_add_i32 s56, s56, 2
	s_add_u32 s54, s54, 0x100
	s_addc_u32 s55, s55, 0
	s_cmp_gt_u32 s56, 13
	s_mov_b64 s[12:13], s[14:15]
	s_cbranch_scc0 .LBB0_170
	s_cmpk_lt_u32 s23, 0x100
	s_cbranch_scc0 .LBB0_173
	s_barrier

.LBB0_180:
	s_add_u32 s13, s74, 0x32000000
	s_addc_u32 s26, s75, 0
	s_add_u32 s27, s74, 0x33000000
	s_addc_u32 s34, s75, 0
	s_mov_b64 s[4:5], -1
	s_and_b64 vcc, exec, s[0:1]
	s_cbranch_vccz .LBB0_202
	s_cmpk_gt_i32 s93, 0x27f
	v_readfirstlane_b32 s4, v0
	s_cbranch_scc1 .LBB0_201
	v_lshlrev_b32_e32 v2, 4, v0
	v_and_b32_e32 v3, 32, v0
	v_bitop3_b32 v2, v2, v3, 48 bitop3:0x6c
	v_lshrrev_b32_e32 v3, 1, v0
	v_bfe_u32 v5, v0, 2, 2
	v_bfe_u32 v4, v0, 2, 4
	v_and_or_b32 v3, v3, 24, v5
	v_lshrrev_b32_e32 v5, 3, v0
	v_lshrrev_b32_e32 v7, 5, v0
	v_and_or_b32 v6, v5, 48, v4
	v_and_or_b32 v5, v5, 32, v7
	v_and_or_b32 v5, v5, 36, v3
	v_and_or_b32 v2, v0, 64, v2
	v_lshl_or_b32 v167, v5, 10, v2
	v_bfe_u32 v5, v0, 3, 25
	v_or_b32_e32 v5, 64, v5
	s_movk_i32 s0, 0x70
	v_and_or_b32 v4, v5, s0, v4
	s_movk_i32 s0, 0x60
	v_and_or_b32 v5, v5, s0, v7
	s_movk_i32 s0, 0x64
	s_ashr_i32 s30, s93, 31
	v_and_or_b32 v3, v5, s0, v3
	s_lshr_b32 s0, s30, 29
	s_add_i32 s0, s93, s0
	s_lshr_b32 s5, s4, 6
	s_ashr_i32 s3, s0, 3
	s_and_b32 s0, s0, -8
	s_lshr_b32 s2, s4, 8
	s_lshl_b32 s35, s5, 10
	s_sub_i32 s0, s93, s0
	s_cmp_lt_i32 s0, 0
	s_movk_i32 s6, 0x51
	s_cselect_b32 s6, s6, 0x50
	s_mul_i32 s0, s0, s6
	s_add_i32 s0, s0, s3
	s_mul_hi_i32 s3, s0, 0x66666667
	s_lshr_b32 s6, s3, 31
	s_ashr_i32 s3, s3, 5
	s_add_i32 s3, s3, s6
	s_lshl_b32 s6, s3, 3
	s_mulk_i32 s3, 0x50
	s_sub_i32 s3, s0, s3
	s_bfe_i32 s0, s3, 0x80000
	s_bfe_u32 s0, s0, 0x3000c
	s_add_i32 s7, s3, s0
	s_bfe_i32 s0, s7, 0x80000
	s_and_b32 s7, s7, 0xf8
	s_sub_i32 s3, s3, s7
	s_sext_i32_i16 s0, s0
	s_sext_i32_i8 s3, s3
	s_mov_b32 s1, 0
	s_lshr_b32 s0, s0, 3
	s_add_i32 s66, s6, s3
	s_ashr_i32 s67, s66, 31
	s_bfe_i64 s[8:9], s[0:1], 0x100000
	s_lshl_b64 s[6:7], s[66:67], 18
	s_lshl_b64 s[8:9], s[8:9], 18
	s_add_u32 s76, s27, s8
	s_addc_u32 s77, s34, s9
	s_add_i32 s35, s35, 0
	s_add_i32 s36, s35, 0x10000
	s_mov_b32 s3, m0
	s_mov_b32 m0, s36
	s_nop 0
	global_load_lds_dwordx4 v167, s[76:77]
	s_mov_b32 m0, s3
	s_add_i32 s37, s35, 0x12000
	v_lshl_or_b32 v169, v3, 10, v2
	s_mov_b32 s3, m0
	s_mov_b32 m0, s37
	s_nop 0
	global_load_lds_dwordx4 v169, s[76:77]
	s_mov_b32 m0, s3
	s_add_u32 s8, s76, 0x20000
	s_addc_u32 s9, s77, 0
	s_add_i32 s55, s35, 0x14000
	s_mov_b32 s3, m0
	s_mov_b32 m0, s55
	s_nop 0
	global_load_lds_dwordx4 v167, s[8:9]
	s_mov_b32 m0, s3
	s_add_i32 s86, s35, 0x16000
	s_mov_b32 s3, m0
	s_mov_b32 m0, s86
	s_nop 0
	global_load_lds_dwordx4 v169, s[8:9]
	s_mov_b32 m0, s3
	s_add_u32 s78, s13, s6
	v_lshl_or_b32 v166, v6, 10, v2
	s_addc_u32 s79, s26, s7
	s_mov_b32 s3, m0
	s_mov_b32 m0, s35
	s_nop 0
	global_load_lds_dwordx4 v166, s[78:79]
	s_mov_b32 m0, s3
	s_add_i32 s87, s35, 0x2000
	v_lshl_or_b32 v168, v4, 10, v2
	s_mov_b32 s3, m0
	s_mov_b32 m0, s87
	s_nop 0
	global_load_lds_dwordx4 v168, s[78:79]
	s_mov_b32 m0, s3
	s_add_u32 s6, s78, 0x20000
	s_addc_u32 s7, s79, 0
	s_add_i32 s89, s35, 0x4000
	s_mov_b32 s3, m0
	s_mov_b32 m0, s89
	s_nop 0
	global_load_lds_dwordx4 v166, s[6:7]
	s_mov_b32 m0, s3
	s_add_i32 s3, s35, 0x6000
	s_mov_b32 s10, m0
	s_mov_b32 m0, s3
	s_nop 0
	global_load_lds_dwordx4 v168, s[6:7]
	s_mov_b32 m0, s10
	s_cmp_eq_u32 s2, 1
	v_writelane_b32 v253, s92, 43
	s_mov_b32 s29, s93
	s_cselect_b64 s[8:9], -1, 0
	s_cmp_lg_u32 s2, 1
	v_writelane_b32 v253, s97, 44
	s_cbranch_scc1 .LBB0_184
	s_barrier
.LBB0_184:
	v_bfe_u32 v172, v0, 4, 2
	v_and_b32_e32 v170, 15, v0
	v_lshlrev_b32_e32 v2, 4, v172
	v_lshlrev_b32_e32 v4, 2, v0
	s_lshl_b32 s24, s2, 6
	v_lshl_or_b32 v3, v170, 6, v2
	s_lshl_b32 s2, s2, 13
	v_and_b32_e32 v4, 32, v4
	v_bitop3_b32 v3, v3, s2, v4 bitop3:0xde
	s_lshl_b32 s2, s5, 5
	s_and_b32 s25, s2, 0x60
	v_lshlrev_b32_e32 v5, 6, v0
	s_movk_i32 s2, 0x3c0
	v_and_or_b32 v2, v5, s2, v2
	s_lshl_b32 s2, s25, 7
	s_add_u32 s6, s76, 0x80
	v_bitop3_b32 v2, s2, v2, v4 bitop3:0xf6
	s_waitcnt vmcnt(2)
	s_barrier
	s_addc_u32 s7, s77, 0
	s_add_i32 s90, s35, 0x18000
	s_mov_b32 s2, m0
	s_mov_b32 m0, s90
	s_nop 0
	global_load_lds_dwordx4 v167, s[6:7]
	s_mov_b32 m0, s2
	s_add_i32 s28, s35, 0x1a000
	s_mov_b32 s2, m0
	s_mov_b32 m0, s28
	s_nop 0
	global_load_lds_dwordx4 v169, s[6:7]
	s_mov_b32 m0, s2
	s_add_u32 s6, s78, 0x80
	s_addc_u32 s7, s79, 0
	s_add_i32 s93, s35, 0x8000
	s_mov_b32 s2, m0
	s_mov_b32 m0, s93
	s_nop 0
	global_load_lds_dwordx4 v166, s[6:7]
	s_mov_b32 m0, s2
	s_add_i32 s2, s35, 0xa000
	s_mov_b32 s5, m0
	s_mov_b32 m0, s2
	s_nop 0
	global_load_lds_dwordx4 v168, s[6:7]
	s_mov_b32 m0, s5
	s_add_u32 s6, s76, 0x20080
	s_addc_u32 s7, s77, 0
	s_add_i32 s94, s35, 0x1c000
	s_mov_b32 s5, m0
	s_mov_b32 m0, s94
	s_nop 0
	global_load_lds_dwordx4 v167, s[6:7]
	s_mov_b32 m0, s5
	s_add_i32 s95, s35, 0x1e000
	s_mov_b32 s5, m0
	s_mov_b32 m0, s95
	s_nop 0
	global_load_lds_dwordx4 v169, s[6:7]
	s_mov_b32 m0, s5
	s_waitcnt vmcnt(6)
	s_add_i32 s96, s35, 0xc000
	s_cmpk_lt_u32 s4, 0x100
	v_readlane_b32 s4, v253, 26
	v_add_u32_e32 v2, 0, v2
	s_sext_i32_i8 s0, s0
	s_mov_b32 s91, 0xc000
	s_cselect_b64 s[10:11], -1, 0
	s_add_i32 s92, s35, 0xe000
	s_ashr_i32 s97, s4, 31
	v_mov_b64_e32 v[162:163], 0x280
	v_mov_b64_e32 v[164:165], 0x27f
	v_add_u32_e32 v174, 0x10000, v2
	v_add_u32_e32 v175, 0x14000, v2
	v_add_u32_e32 v176, 0, v3
	v_add_u32_e32 v177, 0x18000, v2
	v_add_u32_e32 v178, 0x1c000, v2
	s_mov_b32 s12, 0x3b800000
	s_mov_b32 s52, 0xc3e00000
	s_mov_b64 s[14:15], 0x4000
	s_mov_b64 s[16:17], 0x8000
	s_mov_b64 s[18:19], 0xc000
	s_mov_b32 s53, 0x20000
	s_mov_b64 s[20:21], 0x24000
	s_mov_b32 s64, 0x24000
	s_mov_b64 s[22:23], 0x28000
	s_mov_b32 s65, 0x28000
	s_mov_b64 s[40:41], 0x2c000
	s_mov_b32 s31, 0x2c000
	s_mov_b32 s54, 0x3a000000
	v_mov_b32_e32 v179, 0x43e00000
	s_mov_b32 s6, 0
	s_barrier
	s_branch .LBB0_187

.LBB0_190:
	ds_read_b128 v[18:21], v174
	ds_read_b128 v[22:25], v174 offset:1024
	ds_read_b128 v[26:29], v174 offset:2048
	ds_read_b128 v[30:33], v174 offset:3072
	ds_read_b128 v[2:5], v175
	ds_read_b128 v[6:9], v175 offset:1024
	ds_read_b128 v[10:13], v175 offset:2048
	ds_read_b128 v[14:17], v175 offset:3072
	s_add_u32 s76, s78, 0x100
	s_addc_u32 s77, s79, 0
	s_cmp_eq_u32 s33, 4
	s_cselect_b32 s84, s59, s76
	s_cselect_b32 s85, s7, s77
	s_cselect_b32 s82, s67, vcc_lo
	s_cselect_b32 s83, s57, vcc_hi
	s_add_u32 s80, s84, 0x80
	s_addc_u32 s81, s85, 0
	ds_read_b128 v[180:183], v176
	ds_read_b128 v[184:187], v176 offset:1024
	ds_read_b128 v[188:191], v176 offset:2048
	ds_read_b128 v[192:195], v176 offset:3072
	ds_read_b128 v[196:199], v176 offset:4096
	ds_read_b128 v[200:203], v176 offset:5120
	ds_read_b128 v[204:207], v176 offset:6144
	ds_read_b128 v[208:211], v176 offset:7168
	s_add_u32 s78, s78, 0x20080
	s_addc_u32 s79, s79, 0
	s_mov_b32 s88, m0
	s_mov_b32 m0, s96
	s_nop 0
	global_load_lds_dwordx4 v166, s[78:79]
	s_mov_b32 m0, s88
	s_nop 0
	s_mov_b32 s88, m0
	s_mov_b32 m0, s92
	s_nop 0
	global_load_lds_dwordx4 v168, s[78:79]
	s_mov_b32 m0, s88
	s_waitcnt vmcnt(8)
	s_waitcnt lgkmcnt(0)
	s_barrier
	s_setprio 1
	s_waitcnt lgkmcnt(6)
	v_mfma_f32_16x16x128_f8f6f4 v[158:161], v[18:25], v[180:187], v[158:161]
	v_mfma_f32_16x16x128_f8f6f4 v[154:157], v[26:33], v[180:187], v[154:157]
	s_waitcnt lgkmcnt(4)
	v_mfma_f32_16x16x128_f8f6f4 v[146:149], v[18:25], v[188:195], v[146:149]
	v_mfma_f32_16x16x128_f8f6f4 v[138:141], v[26:33], v[188:195], v[138:141]
	s_waitcnt lgkmcnt(2)
	v_mfma_f32_16x16x128_f8f6f4 v[130:133], v[18:25], v[196:203], v[130:133]
	v_mfma_f32_16x16x128_f8f6f4 v[122:125], v[26:33], v[196:203], v[122:125]
	s_waitcnt lgkmcnt(0)
	v_mfma_f32_16x16x128_f8f6f4 v[114:117], v[18:25], v[204:211], v[114:117]
	v_mfma_f32_16x16x128_f8f6f4 v[106:109], v[26:33], v[204:211], v[106:109]
	s_setprio 0
	s_setprio 1
	v_mfma_f32_16x16x128_f8f6f4 v[150:153], v[2:9], v[180:187], v[150:153]
	v_mfma_f32_16x16x128_f8f6f4 v[142:145], v[10:17], v[180:187], v[142:145]
	v_mfma_f32_16x16x128_f8f6f4 v[134:137], v[2:9], v[188:195], v[134:137]
	v_mfma_f32_16x16x128_f8f6f4 v[126:129], v[10:17], v[188:195], v[126:129]
	v_mfma_f32_16x16x128_f8f6f4 v[118:121], v[2:9], v[196:203], v[118:121]
	v_mfma_f32_16x16x128_f8f6f4 v[110:113], v[10:17], v[196:203], v[110:113]
	v_mfma_f32_16x16x128_f8f6f4 v[102:105], v[2:9], v[204:211], v[102:105]
	v_mfma_f32_16x16x128_f8f6f4 v[98:101], v[10:17], v[204:211], v[98:101]
	s_setprio 0
	s_barrier
	ds_read_b128 v[180:183], v176 offset:16384
	ds_read_b128 v[184:187], v176 offset:17408
	ds_read_b128 v[188:191], v176 offset:18432
	ds_read_b128 v[192:195], v176 offset:19456
	ds_read_b128 v[196:199], v176 offset:20480
	ds_read_b128 v[200:203], v176 offset:21504
	ds_read_b128 v[204:207], v176 offset:22528
	ds_read_b128 v[208:211], v176 offset:23552
	s_mov_b32 s78, m0
	s_mov_b32 m0, s36
	s_nop 0
	global_load_lds_dwordx4 v167, s[82:83]
	s_mov_b32 m0, s78
	s_nop 0
	s_mov_b32 s78, m0
	s_mov_b32 m0, s37
	s_nop 0
	global_load_lds_dwordx4 v169, s[82:83]
	s_mov_b32 m0, s78
	s_add_u32 s78, s82, 0x20000
	s_addc_u32 s79, s83, 0
	s_mov_b32 s88, m0
	s_mov_b32 m0, s55
	s_nop 0
	global_load_lds_dwordx4 v167, s[78:79]
	s_mov_b32 m0, s88
	s_nop 0
	s_mov_b32 s88, m0
	s_mov_b32 m0, s86
	s_nop 0
	global_load_lds_dwordx4 v169, s[78:79]
	s_mov_b32 m0, s88
	s_mov_b32 s78, m0
	s_mov_b32 m0, s35
	s_nop 0
	global_load_lds_dwordx4 v166, s[84:85]
	s_mov_b32 m0, s78
	s_nop 0
	s_mov_b32 s78, m0
	s_mov_b32 m0, s87
	s_nop 0
	global_load_lds_dwordx4 v168, s[84:85]
	s_mov_b32 m0, s78
	s_waitcnt vmcnt(8)
	s_waitcnt lgkmcnt(0)
	s_barrier
	s_setprio 1
	s_waitcnt lgkmcnt(6)
	v_mfma_f32_16x16x128_f8f6f4 v[94:97], v[18:25], v[180:187], v[94:97]
	v_mfma_f32_16x16x128_f8f6f4 v[90:93], v[26:33], v[180:187], v[90:93]
	s_waitcnt lgkmcnt(4)
	v_mfma_f32_16x16x128_f8f6f4 v[82:85], v[18:25], v[188:195], v[82:85]
	v_mfma_f32_16x16x128_f8f6f4 v[74:77], v[26:33], v[188:195], v[74:77]
	s_waitcnt lgkmcnt(2)
	v_mfma_f32_16x16x128_f8f6f4 v[66:69], v[18:25], v[196:203], v[66:69]
	v_mfma_f32_16x16x128_f8f6f4 v[58:61], v[26:33], v[196:203], v[58:61]
	s_waitcnt lgkmcnt(0)
	v_mfma_f32_16x16x128_f8f6f4 v[50:53], v[18:25], v[204:211], v[50:53]
	v_mfma_f32_16x16x128_f8f6f4 v[42:45], v[26:33], v[204:211], v[42:45]
	s_setprio 0
	s_setprio 1
	v_mfma_f32_16x16x128_f8f6f4 v[86:89], v[2:9], v[180:187], v[86:89]
	v_mfma_f32_16x16x128_f8f6f4 v[78:81], v[10:17], v[180:187], v[78:81]
	v_mfma_f32_16x16x128_f8f6f4 v[70:73], v[2:9], v[188:195], v[70:73]
	v_mfma_f32_16x16x128_f8f6f4 v[62:65], v[10:17], v[188:195], v[62:65]
	v_mfma_f32_16x16x128_f8f6f4 v[54:57], v[2:9], v[196:203], v[54:57]
	v_mfma_f32_16x16x128_f8f6f4 v[46:49], v[10:17], v[196:203], v[46:49]
	v_mfma_f32_16x16x128_f8f6f4 v[38:41], v[2:9], v[204:211], v[38:41]
	v_mfma_f32_16x16x128_f8f6f4 v[34:37], v[10:17], v[204:211], v[34:37]
	s_setprio 0
	s_barrier
	ds_read_b128 v[2:5], v177
	ds_read_b128 v[6:9], v177 offset:1024
	ds_read_b128 v[10:13], v177 offset:2048
	ds_read_b128 v[14:17], v177 offset:3072
	ds_read_b128 v[18:21], v178
	ds_read_b128 v[22:25], v178 offset:1024
	ds_read_b128 v[26:29], v178 offset:2048
	ds_read_b128 v[30:33], v178 offset:3072
	ds_read_b128 v[180:183], v176 offset:32768
	ds_read_b128 v[184:187], v176 offset:33792
	ds_read_b128 v[188:191], v176 offset:34816
	ds_read_b128 v[192:195], v176 offset:35840
	ds_read_b128 v[196:199], v176 offset:36864
	ds_read_b128 v[200:203], v176 offset:37888
	ds_read_b128 v[204:207], v176 offset:38912
	ds_read_b128 v[208:211], v176 offset:39936
	s_add_u32 s78, s84, 0x20000
	s_addc_u32 s79, s85, 0
	s_mov_b32 s84, m0
	s_mov_b32 m0, s89
	s_nop 0
	global_load_lds_dwordx4 v166, s[78:79]
	s_mov_b32 m0, s84
	s_nop 0
	s_mov_b32 s84, m0
	s_mov_b32 m0, s3
	s_nop 0
	global_load_lds_dwordx4 v168, s[78:79]
	s_mov_b32 m0, s84
	s_waitcnt vmcnt(8)
	s_waitcnt lgkmcnt(0)
	s_barrier
	s_setprio 1
	s_waitcnt lgkmcnt(6)
	v_mfma_f32_16x16x128_f8f6f4 v[158:161], v[2:9], v[180:187], v[158:161]
	v_mfma_f32_16x16x128_f8f6f4 v[154:157], v[10:17], v[180:187], v[154:157]
	s_waitcnt lgkmcnt(4)
	v_mfma_f32_16x16x128_f8f6f4 v[146:149], v[2:9], v[188:195], v[146:149]
	v_mfma_f32_16x16x128_f8f6f4 v[138:141], v[10:17], v[188:195], v[138:141]
	s_waitcnt lgkmcnt(2)
	v_mfma_f32_16x16x128_f8f6f4 v[130:133], v[2:9], v[196:203], v[130:133]
	v_mfma_f32_16x16x128_f8f6f4 v[122:125], v[10:17], v[196:203], v[122:125]
	s_waitcnt lgkmcnt(0)
	v_mfma_f32_16x16x128_f8f6f4 v[114:117], v[2:9], v[204:211], v[114:117]
	v_mfma_f32_16x16x128_f8f6f4 v[106:109], v[10:17], v[204:211], v[106:109]
	s_setprio 0
	s_setprio 1
	v_mfma_f32_16x16x128_f8f6f4 v[150:153], v[18:25], v[180:187], v[150:153]
	v_mfma_f32_16x16x128_f8f6f4 v[142:145], v[26:33], v[180:187], v[142:145]
	v_mfma_f32_16x16x128_f8f6f4 v[134:137], v[18:25], v[188:195], v[134:137]
	v_mfma_f32_16x16x128_f8f6f4 v[126:129], v[26:33], v[188:195], v[126:129]
	v_mfma_f32_16x16x128_f8f6f4 v[118:121], v[18:25], v[196:203], v[118:121]
	v_mfma_f32_16x16x128_f8f6f4 v[110:113], v[26:33], v[196:203], v[110:113]
	v_mfma_f32_16x16x128_f8f6f4 v[102:105], v[18:25], v[204:211], v[102:105]
	v_mfma_f32_16x16x128_f8f6f4 v[98:101], v[26:33], v[204:211], v[98:101]
	s_setprio 0
	s_barrier
	ds_read_b128 v[180:183], v176 offset:49152
	ds_read_b128 v[184:187], v176 offset:50176
	ds_read_b128 v[188:191], v176 offset:51200
	ds_read_b128 v[192:195], v176 offset:52224
	ds_read_b128 v[196:199], v176 offset:53248
	ds_read_b128 v[200:203], v176 offset:54272
	ds_read_b128 v[204:207], v176 offset:55296
	ds_read_b128 v[208:211], v176 offset:56320
	s_add_u32 s78, s82, 0x80
	s_addc_u32 s79, s83, 0
	s_mov_b32 s84, m0
	s_mov_b32 m0, s90
	s_nop 0
	global_load_lds_dwordx4 v167, s[78:79]
	s_mov_b32 m0, s84
	s_nop 0
	s_mov_b32 s84, m0
	s_mov_b32 m0, s28
	s_nop 0
	global_load_lds_dwordx4 v169, s[78:79]
	s_mov_b32 m0, s84
	s_add_u32 s78, s82, 0x20080
	s_addc_u32 s79, s83, 0
	s_mov_b32 s82, m0
	s_mov_b32 m0, s94
	s_nop 0
	global_load_lds_dwordx4 v167, s[78:79]
	s_mov_b32 m0, s82
	s_nop 0
	s_mov_b32 s82, m0
	s_mov_b32 m0, s95
	s_nop 0
	global_load_lds_dwordx4 v169, s[78:79]
	s_mov_b32 m0, s82
	s_mov_b32 s78, m0
	s_mov_b32 m0, s93
	s_nop 0
	global_load_lds_dwordx4 v166, s[80:81]
	s_mov_b32 m0, s78
	s_nop 0
	s_mov_b32 s78, m0
	s_mov_b32 m0, s2
	s_nop 0
	global_load_lds_dwordx4 v168, s[80:81]
	s_mov_b32 m0, s78
	s_waitcnt vmcnt(8)
	s_waitcnt lgkmcnt(0)
	s_barrier
	s_setprio 1
	s_waitcnt lgkmcnt(6)
	v_mfma_f32_16x16x128_f8f6f4 v[94:97], v[2:9], v[180:187], v[94:97]
	v_mfma_f32_16x16x128_f8f6f4 v[90:93], v[10:17], v[180:187], v[90:93]
	s_waitcnt lgkmcnt(4)
	v_mfma_f32_16x16x128_f8f6f4 v[82:85], v[2:9], v[188:195], v[82:85]
	v_mfma_f32_16x16x128_f8f6f4 v[74:77], v[10:17], v[188:195], v[74:77]
	s_waitcnt lgkmcnt(2)
	v_mfma_f32_16x16x128_f8f6f4 v[66:69], v[2:9], v[196:203], v[66:69]
	v_mfma_f32_16x16x128_f8f6f4 v[58:61], v[10:17], v[196:203], v[58:61]
	s_waitcnt lgkmcnt(0)
	v_mfma_f32_16x16x128_f8f6f4 v[50:53], v[2:9], v[204:211], v[50:53]
	v_mfma_f32_16x16x128_f8f6f4 v[42:45], v[10:17], v[204:211], v[42:45]
	s_setprio 0
	s_setprio 1
	v_mfma_f32_16x16x128_f8f6f4 v[86:89], v[18:25], v[180:187], v[86:89]
	v_mfma_f32_16x16x128_f8f6f4 v[78:81], v[26:33], v[180:187], v[78:81]
	v_mfma_f32_16x16x128_f8f6f4 v[70:73], v[18:25], v[188:195], v[70:73]
	v_mfma_f32_16x16x128_f8f6f4 v[62:65], v[26:33], v[188:195], v[62:65]
	v_mfma_f32_16x16x128_f8f6f4 v[54:57], v[18:25], v[196:203], v[54:57]
	v_mfma_f32_16x16x128_f8f6f4 v[46:49], v[26:33], v[196:203], v[46:49]
	v_mfma_f32_16x16x128_f8f6f4 v[38:41], v[18:25], v[204:211], v[38:41]
	v_mfma_f32_16x16x128_f8f6f4 v[34:37], v[26:33], v[204:211], v[34:37]
	s_setprio 0
	s_barrier
	s_add_i32 s33, s33, 2
	s_add_u32 vcc_lo, vcc_lo, 0x100
	s_addc_u32 vcc_hi, vcc_hi, 0
	s_cmp_gt_u32 s33, 5
	s_mov_b64 s[78:79], s[76:77]
	s_cbranch_scc0 .LBB0_190
	s_and_b64 vcc, exec, s[10:11]
	s_cbranch_vccz .LBB0_193
	s_barrier

.LBB0_202:
	s_andn2_b64 vcc, exec, s[4:5]
	s_cbranch_vccnz .LBB0_229
	v_lshlrev_b32_e32 v2, 4, v0
	v_and_b32_e32 v3, 32, v0
	v_bitop3_b32 v2, v2, v3, 48 bitop3:0x6c
	v_lshrrev_b32_e32 v3, 1, v0
	v_bfe_u32 v5, v0, 2, 2
	v_bfe_u32 v4, v0, 2, 4
	v_and_or_b32 v3, v3, 24, v5
	v_lshrrev_b32_e32 v5, 3, v0
	v_lshrrev_b32_e32 v7, 5, v0
	v_and_or_b32 v6, v5, 48, v4
	v_and_or_b32 v5, v5, 32, v7
	v_and_or_b32 v5, v5, 36, v3
	v_and_or_b32 v2, v0, 64, v2
	v_readfirstlane_b32 s6, v0
	v_lshl_or_b32 v163, v5, 10, v2
	v_bfe_u32 v5, v0, 3, 25
	v_or_b32_e32 v5, 64, v5
	s_movk_i32 s0, 0x70
	s_lshr_b32 s7, s6, 6
	s_ashr_i32 s9, s93, 3
	s_lshr_b32 s2, s6, 8
	v_and_or_b32 v4, v5, s0, v4
	s_movk_i32 s0, 0x60
	s_lshl_b32 s3, s7, 10
	v_and_or_b32 v5, v5, s0, v7
	s_movk_i32 s0, 0x64
	s_cmp_gt_i32 s9, 23
	v_and_or_b32 v3, v5, s0, v3
	s_cselect_b64 s[0:1], -1, 0
	s_cmp_lt_i32 s9, 24
	s_cselect_b32 s4, 0, 24
	v_writelane_b32 v253, s92, 43
	s_add_i32 s8, s4, s9
	s_lshl_b32 s4, s93, 3
	v_writelane_b32 v253, s97, 44
	s_and_b32 s31, s4, 56
	s_and_b32 s4, s9, 7
	s_ashr_i32 s76, s8, 3
	v_writelane_b32 v253, s93, 45
	s_or_b32 s4, s31, s4
	s_ashr_i32 s77, s76, 31
	v_writelane_b32 v253, s9, 46
	s_lshl_b32 s10, s4, 18
	s_lshl_b64 s[8:9], s[76:77], 18
	s_add_u32 s78, s27, s8
	s_addc_u32 s79, s34, s9
	s_add_i32 s35, s3, 0
	s_add_i32 s36, s35, 0x10000
	s_mov_b32 s3, m0
	s_mov_b32 m0, s36
	s_nop 0
	global_load_lds_dwordx4 v163, s[78:79]
	s_mov_b32 m0, s3
	s_add_i32 s37, s35, 0x12000
	v_lshl_or_b32 v165, v3, 10, v2
	s_mov_b32 s3, m0
	s_mov_b32 m0, s37
	s_nop 0
	global_load_lds_dwordx4 v165, s[78:79]
	s_mov_b32 m0, s3
	s_add_u32 s8, s78, 0x20000
	s_addc_u32 s9, s79, 0
	s_add_i32 s55, s35, 0x14000
	s_mov_b32 s3, m0
	s_mov_b32 m0, s55
	s_nop 0
	global_load_lds_dwordx4 v163, s[8:9]
	s_mov_b32 m0, s3
	s_add_i32 s77, s35, 0x16000
	s_mov_b32 s3, m0
	s_mov_b32 m0, s77
	s_nop 0
	global_load_lds_dwordx4 v165, s[8:9]
	s_mov_b32 m0, s3
	s_add_u32 s80, s13, s10
	v_lshl_or_b32 v162, v6, 10, v2
	s_addc_u32 s81, s26, 0
	s_mov_b32 s3, m0
	s_mov_b32 m0, s35
	s_nop 0
	global_load_lds_dwordx4 v162, s[80:81]
	s_mov_b32 m0, s3
	s_add_i32 s88, s35, 0x2000
	v_lshl_or_b32 v164, v4, 10, v2
	s_mov_b32 s3, m0
	s_mov_b32 m0, s88
	s_nop 0
	global_load_lds_dwordx4 v164, s[80:81]
	s_mov_b32 m0, s3
	s_add_u32 s10, s80, 0x20000
	s_addc_u32 s11, s81, 0
	s_add_i32 s97, s35, 0x4000
	s_mov_b32 s3, m0
	s_mov_b32 m0, s97
	s_nop 0
	global_load_lds_dwordx4 v162, s[10:11]
	s_mov_b32 m0, s3
	s_add_i32 s3, s35, 0x6000
	s_mov_b32 s12, m0
	s_mov_b32 m0, s3
	s_nop 0
	global_load_lds_dwordx4 v164, s[10:11]
	s_mov_b32 m0, s12
	s_cmp_eq_u32 s2, 1
	s_mov_b32 s5, 0
	s_cselect_b64 s[8:9], -1, 0
	s_cmp_lg_u32 s2, 1
	s_cbranch_scc1 .LBB0_205
	s_barrier
.LBB0_205:
	v_bfe_u32 v167, v0, 4, 2
	v_and_b32_e32 v166, 15, v0
	v_lshlrev_b32_e32 v2, 4, v167
	v_lshlrev_b32_e32 v4, 2, v0
	s_lshl_b32 s24, s2, 6
	v_lshl_or_b32 v3, v166, 6, v2
	s_lshl_b32 s2, s2, 13
	v_and_b32_e32 v4, 32, v4
	v_bitop3_b32 v3, v3, s2, v4 bitop3:0xde
	s_lshl_b32 s2, s7, 5
	s_and_b32 s25, s2, 0x60
	v_lshlrev_b32_e32 v5, 6, v0
	s_movk_i32 s2, 0x3c0
	v_and_or_b32 v2, v5, s2, v2
	s_lshl_b32 s2, s25, 7
	s_add_u32 s10, s78, 0x80
	v_bitop3_b32 v2, s2, v2, v4 bitop3:0xf6
	s_waitcnt vmcnt(2)
	s_barrier
	s_addc_u32 s11, s79, 0
	s_add_i32 s90, s35, 0x18000
	s_mov_b32 s2, m0
	s_mov_b32 m0, s90
	s_nop 0
	global_load_lds_dwordx4 v163, s[10:11]
	s_mov_b32 m0, s2
	s_add_i32 s28, s35, 0x1a000
	s_mov_b32 s2, m0
	s_mov_b32 m0, s28
	s_nop 0
	global_load_lds_dwordx4 v165, s[10:11]
	s_mov_b32 m0, s2
	s_add_u32 s10, s80, 0x80
	s_addc_u32 s11, s81, 0
	s_add_i32 s93, s35, 0x8000
	s_mov_b32 s2, m0
	s_mov_b32 m0, s93
	s_nop 0
	global_load_lds_dwordx4 v162, s[10:11]
	s_mov_b32 m0, s2
	s_add_i32 s2, s35, 0xa000
	s_mov_b32 s7, m0
	s_mov_b32 m0, s2
	s_nop 0
	global_load_lds_dwordx4 v164, s[10:11]
	s_mov_b32 m0, s7
	s_add_u32 s10, s78, 0x20080
	s_addc_u32 s11, s79, 0
	s_add_i32 s94, s35, 0x1c000
	s_mov_b32 s7, m0
	s_mov_b32 m0, s94
	s_nop 0
	global_load_lds_dwordx4 v163, s[10:11]
	s_mov_b32 m0, s7
	s_add_i32 s95, s35, 0x1e000
	s_mov_b32 s7, m0
	s_mov_b32 m0, s95
	s_nop 0
	global_load_lds_dwordx4 v165, s[10:11]
	s_mov_b32 m0, s7
	s_waitcnt vmcnt(6)
	s_add_i32 s91, s35, 0xc000
	s_cmpk_lt_u32 s6, 0x100
	v_readlane_b32 s6, v253, 46
	v_add_u32_e32 v2, 0, v2
	s_mov_b32 s96, 0xc000
	s_cselect_b64 s[10:11], -1, 0
	s_add_i32 s92, s35, 0xe000
	s_add_i32 s6, s6, 24
	v_add_u32_e32 v168, 0x10000, v2
	v_add_u32_e32 v169, 0x14000, v2
	v_add_u32_e32 v170, 0, v3
	v_add_u32_e32 v172, 0x18000, v2
	v_add_u32_e32 v174, 0x1c000, v2
	s_mov_b32 s12, 0x3b800000
	s_mov_b32 s52, 0xc3e00000
	s_mov_b64 s[14:15], 0x4000
	s_mov_b64 s[16:17], 0x8000
	s_mov_b64 s[18:19], 0xc000
	s_mov_b32 s53, 0x20000
	s_mov_b64 s[20:21], 0x24000
	s_mov_b32 s64, 0x24000
	s_mov_b64 s[22:23], 0x28000
	s_mov_b32 s65, 0x28000
	s_mov_b64 s[40:41], 0x2c000
	s_mov_b32 s30, 0x2c000
	s_mov_b32 s54, 0x3a000000
	v_mov_b32_e32 v175, 0x43e00000
	s_mov_b32 s33, 0
	s_barrier
	v_writelane_b32 v253, s6, 47
	s_branch .LBB0_208

.LBB0_217:
	s_cmp_lt_i32 s33, 0
	s_cbranch_scc1 .Lpeel1
	ds_read_b128 v[18:21], v168
	ds_read_b128 v[22:25], v168 offset:1024
	ds_read_b128 v[26:29], v168 offset:2048
	ds_read_b128 v[30:33], v168 offset:3072
	ds_read_b128 v[2:5], v169
	ds_read_b128 v[6:9], v169 offset:1024
	ds_read_b128 v[10:13], v169 offset:2048
	ds_read_b128 v[14:17], v169 offset:3072
	s_add_u32 s78, s80, 0x100
	s_addc_u32 s79, s81, 0
	s_cmp_eq_u32 s33, 4
	s_cselect_b32 s86, s57, s78
	s_cselect_b32 s87, s7, s79
	s_cselect_b32 s84, vcc_lo, vcc_hi
	s_cselect_b32 s85, s59, s89
	s_add_u32 s82, s86, 0x80
	s_addc_u32 s83, s87, 0
	ds_read_b128 v[176:179], v170
	ds_read_b128 v[180:183], v170 offset:1024
	ds_read_b128 v[184:187], v170 offset:2048
	ds_read_b128 v[188:191], v170 offset:3072
	ds_read_b128 v[192:195], v170 offset:4096
	ds_read_b128 v[196:199], v170 offset:5120
	ds_read_b128 v[200:203], v170 offset:6144
	ds_read_b128 v[204:207], v170 offset:7168
	s_add_u32 s80, s80, 0x20080
	s_addc_u32 s81, s81, 0
	s_mov_b32 s29, m0
	s_mov_b32 m0, s91
	s_nop 0
	global_load_lds_dwordx4 v162, s[80:81]
	s_mov_b32 m0, s29
	s_nop 0
	s_mov_b32 s29, m0
	s_mov_b32 m0, s92
	s_nop 0
	global_load_lds_dwordx4 v164, s[80:81]
	s_mov_b32 m0, s29
	s_waitcnt vmcnt(8)
	s_waitcnt lgkmcnt(0)
	s_barrier
	s_setprio 1
	s_waitcnt lgkmcnt(6)
	v_mfma_f32_16x16x128_f8f6f4 v[158:161], v[18:25], v[176:183], v[158:161]
	v_mfma_f32_16x16x128_f8f6f4 v[154:157], v[26:33], v[176:183], v[154:157]
	s_waitcnt lgkmcnt(4)
	v_mfma_f32_16x16x128_f8f6f4 v[146:149], v[18:25], v[184:191], v[146:149]
	v_mfma_f32_16x16x128_f8f6f4 v[138:141], v[26:33], v[184:191], v[138:141]
	s_waitcnt lgkmcnt(2)
	v_mfma_f32_16x16x128_f8f6f4 v[130:133], v[18:25], v[192:199], v[130:133]
	v_mfma_f32_16x16x128_f8f6f4 v[122:125], v[26:33], v[192:199], v[122:125]
	s_waitcnt lgkmcnt(0)
	v_mfma_f32_16x16x128_f8f6f4 v[114:117], v[18:25], v[200:207], v[114:117]
	v_mfma_f32_16x16x128_f8f6f4 v[106:109], v[26:33], v[200:207], v[106:109]
	s_setprio 0
	s_setprio 1
	v_mfma_f32_16x16x128_f8f6f4 v[150:153], v[2:9], v[176:183], v[150:153]
	v_mfma_f32_16x16x128_f8f6f4 v[142:145], v[10:17], v[176:183], v[142:145]
	v_mfma_f32_16x16x128_f8f6f4 v[134:137], v[2:9], v[184:191], v[134:137]
	v_mfma_f32_16x16x128_f8f6f4 v[126:129], v[10:17], v[184:191], v[126:129]
	v_mfma_f32_16x16x128_f8f6f4 v[118:121], v[2:9], v[192:199], v[118:121]
	v_mfma_f32_16x16x128_f8f6f4 v[110:113], v[10:17], v[192:199], v[110:113]
	v_mfma_f32_16x16x128_f8f6f4 v[102:105], v[2:9], v[200:207], v[102:105]
	v_mfma_f32_16x16x128_f8f6f4 v[98:101], v[10:17], v[200:207], v[98:101]
	s_setprio 0
	s_barrier
	ds_read_b128 v[176:179], v170 offset:16384
	ds_read_b128 v[180:183], v170 offset:17408
	ds_read_b128 v[184:187], v170 offset:18432
	ds_read_b128 v[188:191], v170 offset:19456
	ds_read_b128 v[192:195], v170 offset:20480
	ds_read_b128 v[196:199], v170 offset:21504
	ds_read_b128 v[200:203], v170 offset:22528
	ds_read_b128 v[204:207], v170 offset:23552
	s_mov_b32 s29, m0
	s_mov_b32 m0, s36
	s_nop 0
	global_load_lds_dwordx4 v163, s[84:85]
	s_mov_b32 m0, s29
	s_add_u32 s80, s84, 0x20000
	s_mov_b32 s29, m0
	s_mov_b32 m0, s37
	s_nop 0
	global_load_lds_dwordx4 v165, s[84:85]
	s_mov_b32 m0, s29
	s_addc_u32 s81, s85, 0
	s_mov_b32 s29, m0
	s_mov_b32 m0, s55
	s_nop 0
	global_load_lds_dwordx4 v163, s[80:81]
	s_mov_b32 m0, s29
	s_nop 0
	s_mov_b32 s29, m0
	s_mov_b32 m0, s77
	s_nop 0
	global_load_lds_dwordx4 v165, s[80:81]
	s_mov_b32 m0, s29
	s_nop 0
	s_mov_b32 s29, m0
	s_mov_b32 m0, s35
	s_nop 0
	global_load_lds_dwordx4 v162, s[86:87]
	s_mov_b32 m0, s29
	s_nop 0
	s_mov_b32 s29, m0
	s_mov_b32 m0, s88
	s_nop 0
	global_load_lds_dwordx4 v164, s[86:87]
	s_mov_b32 m0, s29
	s_waitcnt vmcnt(8)
	s_waitcnt lgkmcnt(0)
	s_barrier
	s_setprio 1
	s_waitcnt lgkmcnt(6)
	v_mfma_f32_16x16x128_f8f6f4 v[94:97], v[18:25], v[176:183], v[94:97]
	v_mfma_f32_16x16x128_f8f6f4 v[90:93], v[26:33], v[176:183], v[90:93]
	s_waitcnt lgkmcnt(4)
	v_mfma_f32_16x16x128_f8f6f4 v[82:85], v[18:25], v[184:191], v[82:85]
	v_mfma_f32_16x16x128_f8f6f4 v[74:77], v[26:33], v[184:191], v[74:77]
	s_waitcnt lgkmcnt(2)
	v_mfma_f32_16x16x128_f8f6f4 v[66:69], v[18:25], v[192:199], v[66:69]
	v_mfma_f32_16x16x128_f8f6f4 v[58:61], v[26:33], v[192:199], v[58:61]
	s_waitcnt lgkmcnt(0)
	v_mfma_f32_16x16x128_f8f6f4 v[50:53], v[18:25], v[200:207], v[50:53]
	v_mfma_f32_16x16x128_f8f6f4 v[42:45], v[26:33], v[200:207], v[42:45]
	s_setprio 0
	s_setprio 1
	v_mfma_f32_16x16x128_f8f6f4 v[86:89], v[2:9], v[176:183], v[86:89]
	v_mfma_f32_16x16x128_f8f6f4 v[78:81], v[10:17], v[176:183], v[78:81]
	v_mfma_f32_16x16x128_f8f6f4 v[70:73], v[2:9], v[184:191], v[70:73]
	v_mfma_f32_16x16x128_f8f6f4 v[62:65], v[10:17], v[184:191], v[62:65]
	v_mfma_f32_16x16x128_f8f6f4 v[54:57], v[2:9], v[192:199], v[54:57]
	v_mfma_f32_16x16x128_f8f6f4 v[46:49], v[10:17], v[192:199], v[46:49]
	v_mfma_f32_16x16x128_f8f6f4 v[38:41], v[2:9], v[200:207], v[38:41]
	v_mfma_f32_16x16x128_f8f6f4 v[34:37], v[10:17], v[200:207], v[34:37]
	s_setprio 0
	s_barrier
.Lmid1:
	ds_read_b128 v[2:5], v172
	ds_read_b128 v[6:9], v172 offset:1024
	ds_read_b128 v[10:13], v172 offset:2048
	ds_read_b128 v[14:17], v172 offset:3072
	ds_read_b128 v[18:21], v174
	ds_read_b128 v[22:25], v174 offset:1024
	ds_read_b128 v[26:29], v174 offset:2048
	ds_read_b128 v[30:33], v174 offset:3072
	ds_read_b128 v[176:179], v170 offset:32768
	ds_read_b128 v[180:183], v170 offset:33792
	ds_read_b128 v[184:187], v170 offset:34816
	ds_read_b128 v[188:191], v170 offset:35840
	ds_read_b128 v[192:195], v170 offset:36864
	ds_read_b128 v[196:199], v170 offset:37888
	ds_read_b128 v[200:203], v170 offset:38912
	ds_read_b128 v[204:207], v170 offset:39936
	s_add_u32 s80, s86, 0x20000
	s_addc_u32 s81, s87, 0
	s_mov_b32 s29, m0
	s_mov_b32 m0, s97
	s_nop 0
	global_load_lds_dwordx4 v162, s[80:81]
	s_mov_b32 m0, s29
	s_nop 0
	s_mov_b32 s29, m0
	s_mov_b32 m0, s3
	s_nop 0
	global_load_lds_dwordx4 v164, s[80:81]
	s_mov_b32 m0, s29
	s_waitcnt vmcnt(8)
	s_waitcnt lgkmcnt(0)
	s_barrier
	s_setprio 1
	s_waitcnt lgkmcnt(6)
	v_mfma_f32_16x16x128_f8f6f4 v[158:161], v[2:9], v[176:183], v[158:161]
	v_mfma_f32_16x16x128_f8f6f4 v[154:157], v[10:17], v[176:183], v[154:157]
	s_waitcnt lgkmcnt(4)
	v_mfma_f32_16x16x128_f8f6f4 v[146:149], v[2:9], v[184:191], v[146:149]
	v_mfma_f32_16x16x128_f8f6f4 v[138:141], v[10:17], v[184:191], v[138:141]
	s_waitcnt lgkmcnt(2)
	v_mfma_f32_16x16x128_f8f6f4 v[130:133], v[2:9], v[192:199], v[130:133]
	v_mfma_f32_16x16x128_f8f6f4 v[122:125], v[10:17], v[192:199], v[122:125]
	s_waitcnt lgkmcnt(0)
	v_mfma_f32_16x16x128_f8f6f4 v[114:117], v[2:9], v[200:207], v[114:117]
	v_mfma_f32_16x16x128_f8f6f4 v[106:109], v[10:17], v[200:207], v[106:109]
	s_setprio 0
	s_setprio 1
	v_mfma_f32_16x16x128_f8f6f4 v[150:153], v[18:25], v[176:183], v[150:153]
	v_mfma_f32_16x16x128_f8f6f4 v[142:145], v[26:33], v[176:183], v[142:145]
	v_mfma_f32_16x16x128_f8f6f4 v[134:137], v[18:25], v[184:191], v[134:137]
	v_mfma_f32_16x16x128_f8f6f4 v[126:129], v[26:33], v[184:191], v[126:129]
	v_mfma_f32_16x16x128_f8f6f4 v[118:121], v[18:25], v[192:199], v[118:121]
	v_mfma_f32_16x16x128_f8f6f4 v[110:113], v[26:33], v[192:199], v[110:113]
	v_mfma_f32_16x16x128_f8f6f4 v[102:105], v[18:25], v[200:207], v[102:105]
	v_mfma_f32_16x16x128_f8f6f4 v[98:101], v[26:33], v[200:207], v[98:101]
	s_setprio 0
	s_barrier
	ds_read_b128 v[176:179], v170 offset:49152
	ds_read_b128 v[180:183], v170 offset:50176
	ds_read_b128 v[184:187], v170 offset:51200
	ds_read_b128 v[188:191], v170 offset:52224
	ds_read_b128 v[192:195], v170 offset:53248
	ds_read_b128 v[196:199], v170 offset:54272
	ds_read_b128 v[200:203], v170 offset:55296
	ds_read_b128 v[204:207], v170 offset:56320
	s_add_u32 s80, s84, 0x80
	s_addc_u32 s81, s85, 0
	s_mov_b32 s29, m0
	s_mov_b32 m0, s90
	s_nop 0
	global_load_lds_dwordx4 v163, s[80:81]
	s_mov_b32 m0, s29
	s_nop 0
	s_mov_b32 s29, m0
	s_mov_b32 m0, s28
	s_nop 0
	global_load_lds_dwordx4 v165, s[80:81]
	s_mov_b32 m0, s29
	s_add_u32 s80, s84, 0x20080
	s_addc_u32 s81, s85, 0
	s_mov_b32 s29, m0
	s_mov_b32 m0, s94
	s_nop 0
	global_load_lds_dwordx4 v163, s[80:81]
	s_mov_b32 m0, s29
	s_nop 0
	s_mov_b32 s29, m0
	s_mov_b32 m0, s95
	s_nop 0
	global_load_lds_dwordx4 v165, s[80:81]
	s_mov_b32 m0, s29
	s_nop 0
	s_mov_b32 s29, m0
	s_mov_b32 m0, s93
	s_nop 0
	global_load_lds_dwordx4 v162, s[82:83]
	s_mov_b32 m0, s29
	s_nop 0
	s_mov_b32 s29, m0
	s_mov_b32 m0, s2
	s_nop 0
	global_load_lds_dwordx4 v164, s[82:83]
	s_mov_b32 m0, s29
	s_waitcnt vmcnt(8)
	s_waitcnt lgkmcnt(0)
	s_barrier
	s_setprio 1
	s_waitcnt lgkmcnt(6)
	v_mfma_f32_16x16x128_f8f6f4 v[94:97], v[2:9], v[176:183], v[94:97]
	v_mfma_f32_16x16x128_f8f6f4 v[90:93], v[10:17], v[176:183], v[90:93]
	s_waitcnt lgkmcnt(4)
	v_mfma_f32_16x16x128_f8f6f4 v[82:85], v[2:9], v[184:191], v[82:85]
	v_mfma_f32_16x16x128_f8f6f4 v[74:77], v[10:17], v[184:191], v[74:77]
	s_waitcnt lgkmcnt(2)
	v_mfma_f32_16x16x128_f8f6f4 v[66:69], v[2:9], v[192:199], v[66:69]
	v_mfma_f32_16x16x128_f8f6f4 v[58:61], v[10:17], v[192:199], v[58:61]
	s_waitcnt lgkmcnt(0)
	v_mfma_f32_16x16x128_f8f6f4 v[50:53], v[2:9], v[200:207], v[50:53]
	v_mfma_f32_16x16x128_f8f6f4 v[42:45], v[10:17], v[200:207], v[42:45]
	s_setprio 0
	s_setprio 1
	v_mfma_f32_16x16x128_f8f6f4 v[86:89], v[18:25], v[176:183], v[86:89]
	v_mfma_f32_16x16x128_f8f6f4 v[78:81], v[26:33], v[176:183], v[78:81]
	v_mfma_f32_16x16x128_f8f6f4 v[70:73], v[18:25], v[184:191], v[70:73]
	v_mfma_f32_16x16x128_f8f6f4 v[62:65], v[26:33], v[184:191], v[62:65]
	v_mfma_f32_16x16x128_f8f6f4 v[54:57], v[18:25], v[192:199], v[54:57]
	v_mfma_f32_16x16x128_f8f6f4 v[46:49], v[26:33], v[192:199], v[46:49]
	v_mfma_f32_16x16x128_f8f6f4 v[38:41], v[18:25], v[200:207], v[38:41]
	v_mfma_f32_16x16x128_f8f6f4 v[34:37], v[26:33], v[200:207], v[34:37]
	s_setprio 0
	s_cmp_lt_i32 s33, 4
	s_cbranch_scc1 .Lkb1_do
	s_cmp_lg_u64 s[10:11], 0
	s_cbranch_scc0 .Lkb1_skip

.Lpeel1:
	ds_read_b128 v[18:21], v168
	ds_read_b128 v[22:25], v168 offset:1024
	ds_read_b128 v[26:29], v168 offset:2048
	ds_read_b128 v[30:33], v168 offset:3072
	ds_read_b128 v[2:5], v169
	ds_read_b128 v[6:9], v169 offset:1024
	ds_read_b128 v[10:13], v169 offset:2048
	ds_read_b128 v[14:17], v169 offset:3072
	s_add_u32 s78, s80, 0x100
	s_addc_u32 s79, s81, 0
	s_cmp_eq_u32 s33, 4
	s_cselect_b32 s86, s57, s78
	s_cselect_b32 s87, s7, s79
	s_cselect_b32 s84, vcc_lo, vcc_hi
	s_cselect_b32 s85, s59, s89
	s_add_u32 s82, s86, 0x80
	s_addc_u32 s83, s87, 0
	ds_read_b128 v[176:179], v170
	ds_read_b128 v[180:183], v170 offset:1024
	ds_read_b128 v[184:187], v170 offset:2048
	ds_read_b128 v[188:191], v170 offset:3072
	ds_read_b128 v[192:195], v170 offset:4096
	ds_read_b128 v[196:199], v170 offset:5120
	ds_read_b128 v[200:203], v170 offset:6144
	ds_read_b128 v[204:207], v170 offset:7168
	s_add_u32 s80, s80, 0x20080
	s_addc_u32 s81, s81, 0
	s_mov_b32 s29, m0
	s_mov_b32 m0, s91
	s_nop 0
	global_load_lds_dwordx4 v162, s[80:81]
	s_mov_b32 m0, s29
	s_nop 0
	s_mov_b32 s29, m0
	s_mov_b32 m0, s92
	s_nop 0
	global_load_lds_dwordx4 v164, s[80:81]
	s_mov_b32 m0, s29
	s_waitcnt vmcnt(8)
	s_waitcnt lgkmcnt(0)
	s_barrier
	s_setprio 1
	s_waitcnt lgkmcnt(6)
	v_mfma_f32_16x16x128_f8f6f4 v[158:161], v[18:25], v[176:183], 0
	v_mfma_f32_16x16x128_f8f6f4 v[154:157], v[26:33], v[176:183], 0
	s_waitcnt lgkmcnt(4)
	v_mfma_f32_16x16x128_f8f6f4 v[146:149], v[18:25], v[184:191], 0
	v_mfma_f32_16x16x128_f8f6f4 v[138:141], v[26:33], v[184:191], 0
	s_waitcnt lgkmcnt(2)
	v_mfma_f32_16x16x128_f8f6f4 v[130:133], v[18:25], v[192:199], 0
	v_mfma_f32_16x16x128_f8f6f4 v[122:125], v[26:33], v[192:199], 0
	s_waitcnt lgkmcnt(0)
	v_mfma_f32_16x16x128_f8f6f4 v[114:117], v[18:25], v[200:207], 0
	v_mfma_f32_16x16x128_f8f6f4 v[106:109], v[26:33], v[200:207], 0
	s_setprio 0
	s_setprio 1
	v_mfma_f32_16x16x128_f8f6f4 v[150:153], v[2:9], v[176:183], 0
	v_mfma_f32_16x16x128_f8f6f4 v[142:145], v[10:17], v[176:183], 0
	v_mfma_f32_16x16x128_f8f6f4 v[134:137], v[2:9], v[184:191], 0
	v_mfma_f32_16x16x128_f8f6f4 v[126:129], v[10:17], v[184:191], 0
	v_mfma_f32_16x16x128_f8f6f4 v[118:121], v[2:9], v[192:199], 0
	v_mfma_f32_16x16x128_f8f6f4 v[110:113], v[10:17], v[192:199], 0
	v_mfma_f32_16x16x128_f8f6f4 v[102:105], v[2:9], v[200:207], 0
	v_mfma_f32_16x16x128_f8f6f4 v[98:101], v[10:17], v[200:207], 0
	s_setprio 0
	s_barrier
	ds_read_b128 v[176:179], v170 offset:16384
	ds_read_b128 v[180:183], v170 offset:17408
	ds_read_b128 v[184:187], v170 offset:18432
	ds_read_b128 v[188:191], v170 offset:19456
	ds_read_b128 v[192:195], v170 offset:20480
	ds_read_b128 v[196:199], v170 offset:21504
	ds_read_b128 v[200:203], v170 offset:22528
	ds_read_b128 v[204:207], v170 offset:23552
	s_mov_b32 s29, m0
	s_mov_b32 m0, s36
	s_nop 0
	global_load_lds_dwordx4 v163, s[84:85]
	s_mov_b32 m0, s29
	s_add_u32 s80, s84, 0x20000
	s_mov_b32 s29, m0
	s_mov_b32 m0, s37
	s_nop 0
	global_load_lds_dwordx4 v165, s[84:85]
	s_mov_b32 m0, s29
	s_addc_u32 s81, s85, 0
	s_mov_b32 s29, m0
	s_mov_b32 m0, s55
	s_nop 0
	global_load_lds_dwordx4 v163, s[80:81]
	s_mov_b32 m0, s29
	s_nop 0
	s_mov_b32 s29, m0
	s_mov_b32 m0, s77
	s_nop 0
	global_load_lds_dwordx4 v165, s[80:81]
	s_mov_b32 m0, s29
	s_nop 0
	s_mov_b32 s29, m0
	s_mov_b32 m0, s35
	s_nop 0
	global_load_lds_dwordx4 v162, s[86:87]
	s_mov_b32 m0, s29
	s_nop 0
	s_mov_b32 s29, m0
	s_mov_b32 m0, s88
	s_nop 0
	global_load_lds_dwordx4 v164, s[86:87]
	s_mov_b32 m0, s29
	s_waitcnt vmcnt(8)
	s_waitcnt lgkmcnt(0)
	s_barrier
	s_setprio 1
	s_waitcnt lgkmcnt(6)
	v_mfma_f32_16x16x128_f8f6f4 v[94:97], v[18:25], v[176:183], 0
	v_mfma_f32_16x16x128_f8f6f4 v[90:93], v[26:33], v[176:183], 0
	s_waitcnt lgkmcnt(4)
	v_mfma_f32_16x16x128_f8f6f4 v[82:85], v[18:25], v[184:191], 0
	v_mfma_f32_16x16x128_f8f6f4 v[74:77], v[26:33], v[184:191], 0
	s_waitcnt lgkmcnt(2)
	v_mfma_f32_16x16x128_f8f6f4 v[66:69], v[18:25], v[192:199], 0
	v_mfma_f32_16x16x128_f8f6f4 v[58:61], v[26:33], v[192:199], 0
	s_waitcnt lgkmcnt(0)
	v_mfma_f32_16x16x128_f8f6f4 v[50:53], v[18:25], v[200:207], 0
	v_mfma_f32_16x16x128_f8f6f4 v[42:45], v[26:33], v[200:207], 0
	s_setprio 0
	s_setprio 1
	v_mfma_f32_16x16x128_f8f6f4 v[86:89], v[2:9], v[176:183], 0
	v_mfma_f32_16x16x128_f8f6f4 v[78:81], v[10:17], v[176:183], 0
	v_mfma_f32_16x16x128_f8f6f4 v[70:73], v[2:9], v[184:191], 0
	v_mfma_f32_16x16x128_f8f6f4 v[62:65], v[10:17], v[184:191], 0
	v_mfma_f32_16x16x128_f8f6f4 v[54:57], v[2:9], v[192:199], 0
	v_mfma_f32_16x16x128_f8f6f4 v[46:49], v[10:17], v[192:199], 0
	v_mfma_f32_16x16x128_f8f6f4 v[38:41], v[2:9], v[200:207], 0
	v_mfma_f32_16x16x128_f8f6f4 v[34:37], v[10:17], v[200:207], 0
	s_setprio 0
	s_barrier
	s_branch .Lmid1

.LBB0_1034:
	s_ashr_i32 s4, s12, 3
	s_waitcnt vmcnt(15)
	v_lshrrev_b32_e32 v4, 1, v0
	v_bfe_u32 v5, v0, 2, 2
	s_add_u32 s69, s74, 0x15800000
	v_and_b32_e32 v2, 32, v0
	v_bfe_u32 v3, v0, 2, 4
	v_and_or_b32 v4, v4, 24, v5
	v_lshrrev_b32_e32 v5, 3, v0
	s_waitcnt vmcnt(14)
	v_lshrrev_b32_e32 v8, 5, v0
	s_addc_u32 s76, s75, 0
	v_bitop3_b32 v2, v164, v2, 48 bitop3:0x6c
	v_and_or_b32 v6, v5, 48, v3
	v_and_or_b32 v5, v5, 32, v8
	s_add_u32 s77, s74, 0xa00000
	v_and_or_b32 v7, v0, 64, v2
	v_and_or_b32 v5, v5, 36, v4
	s_addc_u32 s78, s75, 0
	v_lshl_or_b32 v166, v5, 11, v7
	v_or_b32_e32 v5, 0x2000, v164
	s_add_i32 s2, s2, s4
	v_lshl_or_b32 v165, v6, 11, v7
	v_lshrrev_b32_e32 v5, 7, v5
	s_movk_i32 s12, 0x70
	v_lshrrev_b32_e32 v6, 4, v164
	s_ashr_i32 s4, s2, 31
	v_and_or_b32 v3, v5, s12, v3
	v_and_or_b32 v2, v6, 64, v2
	v_lshrrev_b32_e32 v6, 9, v164
	s_movk_i32 s12, 0x60
	s_lshr_b32 s4, s4, 27
	v_and_or_b32 v5, v5, s12, v6
	s_movk_i32 s12, 0x64
	s_add_i32 s4, s2, s4
	v_and_or_b32 v4, v5, s12, v4
	s_ashr_i32 s12, s4, 5
	s_and_b32 s4, s4, 0xffe0
	s_sub_i32 s2, s2, s4
	s_bfe_i32 s4, s2, 0x80000
	s_bfe_u32 s4, s4, 0x3000c
	s_add_i32 s13, s2, s4
	s_bfe_i32 s4, s13, 0x80000
	s_and_b32 s13, s13, 0xf8
	s_sub_i32 s2, s2, s13
	s_lshl_b32 s12, s12, 3
	s_sext_i32_i16 s4, s4
	s_sext_i32_i8 s2, s2
	s_lshr_b32 s5, s3, 8
	s_lshr_b32 s4, s4, 3
	s_add_i32 s60, s12, s2
	s_lshr_b32 s20, s3, 6
	s_ashr_i32 s61, s60, 31
	s_bfe_i64 s[14:15], s[4:5], 0x100000
	s_lshl_b32 s16, s20, 10
	s_lshl_b64 s[12:13], s[60:61], 19
	s_lshl_b64 s[14:15], s[14:15], 19
	s_add_u32 s62, s77, s14
	s_addc_u32 s63, s78, s15
	s_add_i32 s79, s16, 0
	s_add_i32 s80, s79, 0x10000
	s_mov_b32 s2, m0
	s_mov_b32 m0, s80
	s_nop 0
	global_load_lds_dwordx4 v166, s[62:63]
	s_mov_b32 m0, s2
	s_add_i32 s81, s79, 0x12000
	v_lshl_or_b32 v168, v4, 11, v2
	s_mov_b32 s2, m0
	s_mov_b32 m0, s81
	s_nop 0
	global_load_lds_dwordx4 v168, s[62:63]
	s_mov_b32 m0, s2
	s_add_u32 s14, s62, 0x40000
	s_addc_u32 s15, s63, 0
	s_add_i32 s82, s79, 0x14000
	s_mov_b32 s2, m0
	s_mov_b32 m0, s82
	s_nop 0
	global_load_lds_dwordx4 v166, s[14:15]
	s_mov_b32 m0, s2
	s_add_i32 s83, s79, 0x16000
	s_mov_b32 s2, m0
	s_mov_b32 m0, s83
	s_nop 0
	global_load_lds_dwordx4 v168, s[14:15]
	s_mov_b32 m0, s2
	s_add_u32 s64, s69, s12
	s_addc_u32 s65, s76, s13
	s_mov_b32 s2, m0
	s_mov_b32 m0, s79
	s_nop 0
	global_load_lds_dwordx4 v165, s[64:65]
	s_mov_b32 m0, s2
	s_add_i32 s84, s79, 0x2000
	v_lshl_or_b32 v167, v3, 11, v2
	s_mov_b32 s2, m0
	s_mov_b32 m0, s84
	s_nop 0
	global_load_lds_dwordx4 v167, s[64:65]
	s_mov_b32 m0, s2
	s_add_u32 s14, s64, 0x40000
	s_addc_u32 s15, s65, 0
	s_add_i32 s85, s79, 0x4000
	s_mov_b32 s2, m0
	s_mov_b32 m0, s85
	s_nop 0
	global_load_lds_dwordx4 v165, s[14:15]
	s_mov_b32 m0, s2
	s_add_i32 s86, s79, 0x6000
	s_mov_b32 s2, m0
	s_mov_b32 m0, s86
	s_nop 0
	global_load_lds_dwordx4 v167, s[14:15]
	s_mov_b32 m0, s2
	s_cmp_eq_u32 s5, 1
	s_mov_b32 s89, s93
	s_mov_b32 s88, s92
	s_mov_b32 s53, s97
	s_mov_b32 s61, 0
	s_cselect_b64 s[12:13], -1, 0
	s_cmp_lg_u32 s5, 1
	s_cbranch_scc1 .LBB0_1036
	s_barrier
.LBB0_1036:
	s_add_u32 s14, s74, 0x11800000
	s_addc_u32 s15, s75, 0
	s_add_u32 s16, s74, 0x13800000
	s_addc_u32 s17, s75, 0
	v_and_b32_e32 v170, 3, v1
	s_add_u32 s18, s74, 0x17800000
	v_and_b32_e32 v169, 15, v0
	v_lshlrev_b32_e32 v4, 4, v170
	v_lshlrev_b32_e32 v6, 2, v0
	s_sext_i32_i8 s2, s4
	s_addc_u32 s19, s75, 0
	v_lshl_or_b32 v5, v169, 6, v4
	s_lshl_b32 s4, s5, 13
	v_and_b32_e32 v6, 32, v6
	v_bitop3_b32 v5, v5, s4, v6 bitop3:0xde
	s_lshl_b32 s4, s20, 5
	s_and_b32 s91, s4, 0x60
	v_lshlrev_b32_e32 v7, 6, v0
	s_movk_i32 s4, 0x3c0
	s_lshl_b32 s87, s5, 6
	v_and_or_b32 v4, v7, s4, v4
	s_lshl_b32 s4, s91, 7
	v_bitop3_b32 v4, s4, v4, v6 bitop3:0xf6
	s_add_u32 s4, s62, 0x80
	s_waitcnt vmcnt(2)
	s_barrier
	s_addc_u32 s5, s63, 0
	s_add_i32 s92, s79, 0x18000
	s_mov_b32 s20, m0
	s_mov_b32 m0, s92
	s_nop 0
	global_load_lds_dwordx4 v166, s[4:5]
	s_mov_b32 m0, s20
	s_add_i32 s93, s79, 0x1a000
	s_mov_b32 s20, m0
	s_mov_b32 m0, s93
	s_nop 0
	global_load_lds_dwordx4 v168, s[4:5]
	s_mov_b32 m0, s20
	s_add_u32 s4, s64, 0x80
	s_addc_u32 s5, s65, 0
	s_add_i32 s94, s79, 0x8000
	s_mov_b32 s20, m0
	s_mov_b32 m0, s94
	s_nop 0
	global_load_lds_dwordx4 v165, s[4:5]
	s_mov_b32 m0, s20
	s_add_i32 s95, s79, 0xa000
	s_mov_b32 s20, m0
	s_mov_b32 m0, s95
	s_nop 0
	global_load_lds_dwordx4 v167, s[4:5]
	s_mov_b32 m0, s20
	s_add_u32 s4, s62, 0x40080
	s_addc_u32 s5, s63, 0
	s_add_i32 s96, s79, 0x1c000
	s_mov_b32 s20, m0
	s_mov_b32 m0, s96
	s_nop 0
	global_load_lds_dwordx4 v166, s[4:5]
	s_mov_b32 m0, s20
	v_or_b32_e32 v2, s87, v169
	s_add_i32 s97, s79, 0x1e000
	s_mov_b32 s20, m0
	s_mov_b32 m0, s97
	s_nop 0
	global_load_lds_dwordx4 v168, s[4:5]
	s_mov_b32 m0, s20
	v_lshlrev_b32_e32 v3, 3, v170
	s_waitcnt vmcnt(6)
	s_add_i32 s26, s79, 0xc000
	v_lshlrev_b32_e32 v2, 10, v2
	s_cmpk_lt_u32 s3, 0x100
	v_or3_b32 v171, v3, v2, s91
	v_add_u32_e32 v2, 0, v4
	s_cselect_b64 s[20:21], -1, 0
	s_add_i32 s27, s79, 0xe000
	s_ashr_i32 s34, s90, 31
	v_mov_b64_e32 v[130:131], 0x100
	v_mov_b64_e32 v[132:133], 0xff
	v_add_u32_e32 v172, 0x10000, v2
	v_add_u32_e32 v173, 0x14000, v2
	v_add_u32_e32 v174, 0, v5
	v_add_u32_e32 v175, 0x18000, v2
	v_add_u32_e32 v176, 0x1c000, v2
	s_mov_b32 s35, 0xc2a00000
	v_mov_b32_e32 v135, 0
	v_mov_b32_e32 v177, 0x42a00000
	s_lshl_b32 s32, s2, 16
	s_lshl_b32 s37, s60, 18
	s_add_i32 s32, s32, s37
	v_lshrrev_b32_e32 v214, 6, v0
	v_lshlrev_b32_e32 v214, 13, v214
	v_and_b32_e32 v215, 63, v0
	v_lshl_add_u32 v214, v215, 3, v214
	v_add_u32_e32 v252, s32, v214
	global_load_dwordx2 v[220:221], v252, s[14:15]
	global_load_dwordx2 v[222:223], v252, s[16:17]
	global_load_dwordx2 v[224:225], v252, s[14:15] offset:512
	global_load_dwordx2 v[226:227], v252, s[16:17] offset:512
	global_load_dwordx2 v[228:229], v252, s[14:15] offset:1024
	global_load_dwordx2 v[230:231], v252, s[16:17] offset:1024
	global_load_dwordx2 v[232:233], v252, s[14:15] offset:1536
	global_load_dwordx2 v[234:235], v252, s[16:17] offset:1536
	global_load_dwordx2 v[236:237], v252, s[14:15] offset:2048
	global_load_dwordx2 v[238:239], v252, s[16:17] offset:2048
	global_load_dwordx2 v[240:241], v252, s[14:15] offset:2560
	global_load_dwordx2 v[242:243], v252, s[16:17] offset:2560
	global_load_dwordx2 v[244:245], v252, s[14:15] offset:3072
	global_load_dwordx2 v[246:247], v252, s[16:17] offset:3072
	global_load_dwordx2 v[248:249], v252, s[14:15] offset:3584
	global_load_dwordx2 v[250:251], v252, s[16:17] offset:3584
	s_mov_b32 s37, 1
	s_barrier
	s_branch .LBB0_1039

.Lpeel1046:
	ds_read_b128 v[136:139], v172
	ds_read_b128 v[140:143], v172 offset:1024
	ds_read_b128 v[144:147], v172 offset:2048
	ds_read_b128 v[148:151], v172 offset:3072
	ds_read_b128 v[152:155], v173
	ds_read_b128 v[156:159], v173 offset:1024
	ds_read_b128 v[160:163], v173 offset:2048
	ds_read_b128 v[178:181], v173 offset:3072
	s_add_u32 s25, s64, s56
	s_addc_u32 s33, s65, s57
	s_add_u32 s66, s25, 0x100
	s_addc_u32 s67, s33, 0
	s_add_u32 s23, s62, s56
	s_addc_u32 s24, s63, s57
	s_add_u32 s28, s23, 0x100
	s_addc_u32 s29, s24, 0
	s_add_u32 s58, s25, 0x180
	s_addc_u32 s59, s33, 0
	ds_read_b128 v[182:185], v174
	ds_read_b128 v[186:189], v174 offset:1024
	ds_read_b128 v[190:193], v174 offset:2048
	ds_read_b128 v[194:197], v174 offset:3072
	ds_read_b128 v[198:201], v174 offset:4096
	ds_read_b128 v[202:205], v174 offset:5120
	ds_read_b128 v[206:209], v174 offset:6144
	ds_read_b128 v[210:213], v174 offset:7168
	s_add_u32 s30, s25, 0x40080
	s_addc_u32 s31, s33, 0
	s_mov_b32 s36, m0
	s_mov_b32 m0, s26
	s_nop 0
	global_load_lds_dwordx4 v165, s[30:31]
	s_mov_b32 m0, s36
	s_nop 0
	s_mov_b32 s36, m0
	s_mov_b32 m0, s27
	s_nop 0
	global_load_lds_dwordx4 v167, s[30:31]
	s_mov_b32 m0, s36
	s_waitcnt vmcnt(8)
	s_waitcnt lgkmcnt(0)
	s_barrier
	s_setprio 1
	s_waitcnt lgkmcnt(7)
	v_mfma_f32_16x16x32_bf16 v[26:29], v[136:139], v[182:185], 0
	v_mfma_f32_16x16x32_bf16 v[30:33], v[144:147], v[182:185], 0
	s_waitcnt lgkmcnt(5)
	v_mfma_f32_16x16x32_bf16 v[50:53], v[136:139], v[190:193], 0
	v_mfma_f32_16x16x32_bf16 v[54:57], v[144:147], v[190:193], 0
	s_waitcnt lgkmcnt(3)
	v_mfma_f32_16x16x32_bf16 v[74:77], v[136:139], v[198:201], 0
	v_mfma_f32_16x16x32_bf16 v[78:81], v[144:147], v[198:201], 0
	s_waitcnt lgkmcnt(1)
	v_mfma_f32_16x16x32_bf16 v[94:97], v[136:139], v[206:209], 0
	v_mfma_f32_16x16x32_bf16 v[102:105], v[144:147], v[206:209], 0
	v_mfma_f32_16x16x32_bf16 v[26:29], v[140:143], v[186:189], v[26:29]
	v_mfma_f32_16x16x32_bf16 v[30:33], v[148:151], v[186:189], v[30:33]
	v_mfma_f32_16x16x32_bf16 v[50:53], v[140:143], v[194:197], v[50:53]
	v_mfma_f32_16x16x32_bf16 v[54:57], v[148:151], v[194:197], v[54:57]
	v_mfma_f32_16x16x32_bf16 v[74:77], v[140:143], v[202:205], v[74:77]
	v_mfma_f32_16x16x32_bf16 v[78:81], v[148:151], v[202:205], v[78:81]
	s_waitcnt lgkmcnt(0)
	v_mfma_f32_16x16x32_bf16 v[94:97], v[140:143], v[210:213], v[94:97]
	v_mfma_f32_16x16x32_bf16 v[102:105], v[148:151], v[210:213], v[102:105]
	s_setprio 0
	s_setprio 1
	v_mfma_f32_16x16x32_bf16 v[38:41], v[152:155], v[182:185], 0
	v_mfma_f32_16x16x32_bf16 v[42:45], v[160:163], v[182:185], 0
	v_mfma_f32_16x16x32_bf16 v[62:65], v[152:155], v[190:193], 0
	v_mfma_f32_16x16x32_bf16 v[66:69], v[160:163], v[190:193], 0
	v_mfma_f32_16x16x32_bf16 v[82:85], v[152:155], v[198:201], 0
	v_mfma_f32_16x16x32_bf16 v[90:93], v[160:163], v[198:201], 0
	v_mfma_f32_16x16x32_bf16 v[106:109], v[152:155], v[206:209], 0
	v_mfma_f32_16x16x32_bf16 v[114:117], v[160:163], v[206:209], 0
	v_mfma_f32_16x16x32_bf16 v[38:41], v[156:159], v[186:189], v[38:41]
	v_mfma_f32_16x16x32_bf16 v[42:45], v[178:181], v[186:189], v[42:45]
	v_mfma_f32_16x16x32_bf16 v[62:65], v[156:159], v[194:197], v[62:65]
	v_mfma_f32_16x16x32_bf16 v[66:69], v[178:181], v[194:197], v[66:69]
	v_mfma_f32_16x16x32_bf16 v[82:85], v[156:159], v[202:205], v[82:85]
	v_mfma_f32_16x16x32_bf16 v[90:93], v[178:181], v[202:205], v[90:93]
	v_mfma_f32_16x16x32_bf16 v[106:109], v[156:159], v[210:213], v[106:109]
	v_mfma_f32_16x16x32_bf16 v[114:117], v[178:181], v[210:213], v[114:117]
	s_setprio 0
	s_barrier
	ds_read_b128 v[182:185], v174 offset:16384
	ds_read_b128 v[186:189], v174 offset:17408
	ds_read_b128 v[190:193], v174 offset:18432
	ds_read_b128 v[194:197], v174 offset:19456
	ds_read_b128 v[198:201], v174 offset:20480
	ds_read_b128 v[202:205], v174 offset:21504
	ds_read_b128 v[206:209], v174 offset:22528
	ds_read_b128 v[210:213], v174 offset:23552
	s_mov_b32 s30, m0
	s_mov_b32 m0, s80
	s_nop 0
	global_load_lds_dwordx4 v166, s[28:29]
	s_mov_b32 m0, s30
	s_nop 0
	s_mov_b32 s30, m0
	s_mov_b32 m0, s81
	s_nop 0
	global_load_lds_dwordx4 v168, s[28:29]
	s_mov_b32 m0, s30
	s_add_u32 s28, s23, 0x40100
	s_addc_u32 s29, s24, 0
	s_mov_b32 s30, m0
	s_mov_b32 m0, s82
	s_nop 0
	global_load_lds_dwordx4 v166, s[28:29]
	s_mov_b32 m0, s30
	s_nop 0
	s_mov_b32 s30, m0
	s_mov_b32 m0, s83
	s_nop 0
	global_load_lds_dwordx4 v168, s[28:29]
	s_mov_b32 m0, s30
	s_mov_b32 s28, m0
	s_mov_b32 m0, s79
	s_nop 0
	global_load_lds_dwordx4 v165, s[66:67]
	s_mov_b32 m0, s28
	s_nop 0
	s_mov_b32 s28, m0
	s_mov_b32 m0, s84
	s_nop 0
	global_load_lds_dwordx4 v167, s[66:67]
	s_mov_b32 m0, s28
	s_waitcnt vmcnt(8)
	s_waitcnt lgkmcnt(0)
	s_barrier
	s_setprio 1
	s_waitcnt lgkmcnt(7)
	v_mfma_f32_16x16x32_bf16 v[118:121], v[136:139], v[182:185], 0
	v_mfma_f32_16x16x32_bf16 v[126:129], v[144:147], v[182:185], 0
	s_waitcnt lgkmcnt(5)
	v_mfma_f32_16x16x32_bf16 v[98:101], v[136:139], v[190:193], 0
	v_mfma_f32_16x16x32_bf16 v[86:89], v[144:147], v[190:193], 0
	s_waitcnt lgkmcnt(3)
	v_mfma_f32_16x16x32_bf16 v[46:49], v[136:139], v[198:201], 0
	v_mfma_f32_16x16x32_bf16 v[34:37], v[144:147], v[198:201], 0
	s_waitcnt lgkmcnt(1)
	v_mfma_f32_16x16x32_bf16 v[14:17], v[136:139], v[206:209], 0
	v_mfma_f32_16x16x32_bf16 v[10:13], v[144:147], v[206:209], 0
	v_mfma_f32_16x16x32_bf16 v[118:121], v[140:143], v[186:189], v[118:121]
	v_mfma_f32_16x16x32_bf16 v[126:129], v[148:151], v[186:189], v[126:129]
	v_mfma_f32_16x16x32_bf16 v[98:101], v[140:143], v[194:197], v[98:101]
	v_mfma_f32_16x16x32_bf16 v[86:89], v[148:151], v[194:197], v[86:89]
	v_mfma_f32_16x16x32_bf16 v[46:49], v[140:143], v[202:205], v[46:49]
	v_mfma_f32_16x16x32_bf16 v[34:37], v[148:151], v[202:205], v[34:37]
	s_waitcnt lgkmcnt(0)
	v_mfma_f32_16x16x32_bf16 v[14:17], v[140:143], v[210:213], v[14:17]
	v_mfma_f32_16x16x32_bf16 v[10:13], v[148:151], v[210:213], v[10:13]
	s_setprio 0
	s_setprio 1
	v_mfma_f32_16x16x32_bf16 v[122:125], v[152:155], v[182:185], 0
	v_mfma_f32_16x16x32_bf16 v[110:113], v[160:163], v[182:185], 0
	v_mfma_f32_16x16x32_bf16 v[70:73], v[152:155], v[190:193], 0
	v_mfma_f32_16x16x32_bf16 v[58:61], v[160:163], v[190:193], 0
	v_mfma_f32_16x16x32_bf16 v[22:25], v[152:155], v[198:201], 0
	v_mfma_f32_16x16x32_bf16 v[18:21], v[160:163], v[198:201], 0
	v_mfma_f32_16x16x32_bf16 v[6:9], v[152:155], v[206:209], 0
	v_mfma_f32_16x16x32_bf16 v[2:5], v[160:163], v[206:209], 0
	v_mfma_f32_16x16x32_bf16 v[122:125], v[156:159], v[186:189], v[122:125]
	v_mfma_f32_16x16x32_bf16 v[110:113], v[178:181], v[186:189], v[110:113]
	v_mfma_f32_16x16x32_bf16 v[70:73], v[156:159], v[194:197], v[70:73]
	v_mfma_f32_16x16x32_bf16 v[58:61], v[178:181], v[194:197], v[58:61]
	v_mfma_f32_16x16x32_bf16 v[22:25], v[156:159], v[202:205], v[22:25]
	v_mfma_f32_16x16x32_bf16 v[18:21], v[178:181], v[202:205], v[18:21]
	v_mfma_f32_16x16x32_bf16 v[6:9], v[156:159], v[210:213], v[6:9]
	v_mfma_f32_16x16x32_bf16 v[2:5], v[178:181], v[210:213], v[2:5]
	s_setprio 0
	s_barrier
	s_branch .Lmid1046
.LBB0_1046:
	ds_read_b128 v[136:139], v172
	ds_read_b128 v[140:143], v172 offset:1024
	ds_read_b128 v[144:147], v172 offset:2048
	ds_read_b128 v[148:151], v172 offset:3072
	ds_read_b128 v[152:155], v173
	ds_read_b128 v[156:159], v173 offset:1024
	ds_read_b128 v[160:163], v173 offset:2048
	ds_read_b128 v[178:181], v173 offset:3072
	s_add_u32 s25, s64, s56
	s_addc_u32 s33, s65, s57
	s_add_u32 s66, s25, 0x100
	s_addc_u32 s67, s33, 0
	s_add_u32 s23, s62, s56
	s_addc_u32 s24, s63, s57
	s_add_u32 s28, s23, 0x100
	s_addc_u32 s29, s24, 0
	s_add_u32 s58, s25, 0x180
	s_addc_u32 s59, s33, 0
	ds_read_b128 v[182:185], v174
	ds_read_b128 v[186:189], v174 offset:1024
	ds_read_b128 v[190:193], v174 offset:2048
	ds_read_b128 v[194:197], v174 offset:3072
	ds_read_b128 v[198:201], v174 offset:4096
	ds_read_b128 v[202:205], v174 offset:5120
	ds_read_b128 v[206:209], v174 offset:6144
	ds_read_b128 v[210:213], v174 offset:7168
	s_add_u32 s30, s25, 0x40080
	s_addc_u32 s31, s33, 0
	s_mov_b32 s36, m0
	s_mov_b32 m0, s26
	s_nop 0
	global_load_lds_dwordx4 v165, s[30:31]
	s_mov_b32 m0, s36
	s_nop 0
	s_mov_b32 s36, m0
	s_mov_b32 m0, s27
	s_nop 0
	global_load_lds_dwordx4 v167, s[30:31]
	s_mov_b32 m0, s36
	s_waitcnt vmcnt(8)
	s_waitcnt lgkmcnt(0)
	s_barrier
	s_setprio 1
	s_waitcnt lgkmcnt(7)
	v_mfma_f32_16x16x32_bf16 v[26:29], v[136:139], v[182:185], v[26:29]
	v_mfma_f32_16x16x32_bf16 v[30:33], v[144:147], v[182:185], v[30:33]
	s_waitcnt lgkmcnt(5)
	v_mfma_f32_16x16x32_bf16 v[50:53], v[136:139], v[190:193], v[50:53]
	v_mfma_f32_16x16x32_bf16 v[54:57], v[144:147], v[190:193], v[54:57]
	s_waitcnt lgkmcnt(3)
	v_mfma_f32_16x16x32_bf16 v[74:77], v[136:139], v[198:201], v[74:77]
	v_mfma_f32_16x16x32_bf16 v[78:81], v[144:147], v[198:201], v[78:81]
	s_waitcnt lgkmcnt(1)
	v_mfma_f32_16x16x32_bf16 v[94:97], v[136:139], v[206:209], v[94:97]
	v_mfma_f32_16x16x32_bf16 v[102:105], v[144:147], v[206:209], v[102:105]
	v_mfma_f32_16x16x32_bf16 v[26:29], v[140:143], v[186:189], v[26:29]
	v_mfma_f32_16x16x32_bf16 v[30:33], v[148:151], v[186:189], v[30:33]
	v_mfma_f32_16x16x32_bf16 v[50:53], v[140:143], v[194:197], v[50:53]
	v_mfma_f32_16x16x32_bf16 v[54:57], v[148:151], v[194:197], v[54:57]
	v_mfma_f32_16x16x32_bf16 v[74:77], v[140:143], v[202:205], v[74:77]
	v_mfma_f32_16x16x32_bf16 v[78:81], v[148:151], v[202:205], v[78:81]
	s_waitcnt lgkmcnt(0)
	v_mfma_f32_16x16x32_bf16 v[94:97], v[140:143], v[210:213], v[94:97]
	v_mfma_f32_16x16x32_bf16 v[102:105], v[148:151], v[210:213], v[102:105]
	s_setprio 0
	s_setprio 1
	v_mfma_f32_16x16x32_bf16 v[38:41], v[152:155], v[182:185], v[38:41]
	v_mfma_f32_16x16x32_bf16 v[42:45], v[160:163], v[182:185], v[42:45]
	v_mfma_f32_16x16x32_bf16 v[62:65], v[152:155], v[190:193], v[62:65]
	v_mfma_f32_16x16x32_bf16 v[66:69], v[160:163], v[190:193], v[66:69]
	v_mfma_f32_16x16x32_bf16 v[82:85], v[152:155], v[198:201], v[82:85]
	v_mfma_f32_16x16x32_bf16 v[90:93], v[160:163], v[198:201], v[90:93]
	v_mfma_f32_16x16x32_bf16 v[106:109], v[152:155], v[206:209], v[106:109]
	v_mfma_f32_16x16x32_bf16 v[114:117], v[160:163], v[206:209], v[114:117]
	v_mfma_f32_16x16x32_bf16 v[38:41], v[156:159], v[186:189], v[38:41]
	v_mfma_f32_16x16x32_bf16 v[42:45], v[178:181], v[186:189], v[42:45]
	v_mfma_f32_16x16x32_bf16 v[62:65], v[156:159], v[194:197], v[62:65]
	v_mfma_f32_16x16x32_bf16 v[66:69], v[178:181], v[194:197], v[66:69]
	v_mfma_f32_16x16x32_bf16 v[82:85], v[156:159], v[202:205], v[82:85]
	v_mfma_f32_16x16x32_bf16 v[90:93], v[178:181], v[202:205], v[90:93]
	v_mfma_f32_16x16x32_bf16 v[106:109], v[156:159], v[210:213], v[106:109]
	v_mfma_f32_16x16x32_bf16 v[114:117], v[178:181], v[210:213], v[114:117]
	s_setprio 0
	s_barrier
	ds_read_b128 v[182:185], v174 offset:16384
	ds_read_b128 v[186:189], v174 offset:17408
	ds_read_b128 v[190:193], v174 offset:18432
	ds_read_b128 v[194:197], v174 offset:19456
	ds_read_b128 v[198:201], v174 offset:20480
	ds_read_b128 v[202:205], v174 offset:21504
	ds_read_b128 v[206:209], v174 offset:22528
	ds_read_b128 v[210:213], v174 offset:23552
	s_mov_b32 s30, m0
	s_mov_b32 m0, s80
	s_nop 0
	global_load_lds_dwordx4 v166, s[28:29]
	s_mov_b32 m0, s30
	s_nop 0
	s_mov_b32 s30, m0
	s_mov_b32 m0, s81
	s_nop 0
	global_load_lds_dwordx4 v168, s[28:29]
	s_mov_b32 m0, s30
	s_add_u32 s28, s23, 0x40100
	s_addc_u32 s29, s24, 0
	s_mov_b32 s30, m0
	s_mov_b32 m0, s82
	s_nop 0
	global_load_lds_dwordx4 v166, s[28:29]
	s_mov_b32 m0, s30
	s_nop 0
	s_mov_b32 s30, m0
	s_mov_b32 m0, s83
	s_nop 0
	global_load_lds_dwordx4 v168, s[28:29]
	s_mov_b32 m0, s30
	s_mov_b32 s28, m0
	s_mov_b32 m0, s79
	s_nop 0
	global_load_lds_dwordx4 v165, s[66:67]
	s_mov_b32 m0, s28
	s_nop 0
	s_mov_b32 s28, m0
	s_mov_b32 m0, s84
	s_nop 0
	global_load_lds_dwordx4 v167, s[66:67]
	s_mov_b32 m0, s28
	s_waitcnt vmcnt(8)
	s_waitcnt lgkmcnt(0)
	s_barrier
	s_setprio 1
	s_waitcnt lgkmcnt(7)
	v_mfma_f32_16x16x32_bf16 v[118:121], v[136:139], v[182:185], v[118:121]
	v_mfma_f32_16x16x32_bf16 v[126:129], v[144:147], v[182:185], v[126:129]
	s_waitcnt lgkmcnt(5)
	v_mfma_f32_16x16x32_bf16 v[98:101], v[136:139], v[190:193], v[98:101]
	v_mfma_f32_16x16x32_bf16 v[86:89], v[144:147], v[190:193], v[86:89]
	s_waitcnt lgkmcnt(3)
	v_mfma_f32_16x16x32_bf16 v[46:49], v[136:139], v[198:201], v[46:49]
	v_mfma_f32_16x16x32_bf16 v[34:37], v[144:147], v[198:201], v[34:37]
	s_waitcnt lgkmcnt(1)
	v_mfma_f32_16x16x32_bf16 v[14:17], v[136:139], v[206:209], v[14:17]
	v_mfma_f32_16x16x32_bf16 v[10:13], v[144:147], v[206:209], v[10:13]
	v_mfma_f32_16x16x32_bf16 v[118:121], v[140:143], v[186:189], v[118:121]
	v_mfma_f32_16x16x32_bf16 v[126:129], v[148:151], v[186:189], v[126:129]
	v_mfma_f32_16x16x32_bf16 v[98:101], v[140:143], v[194:197], v[98:101]
	v_mfma_f32_16x16x32_bf16 v[86:89], v[148:151], v[194:197], v[86:89]
	v_mfma_f32_16x16x32_bf16 v[46:49], v[140:143], v[202:205], v[46:49]
	v_mfma_f32_16x16x32_bf16 v[34:37], v[148:151], v[202:205], v[34:37]
	s_waitcnt lgkmcnt(0)
	v_mfma_f32_16x16x32_bf16 v[14:17], v[140:143], v[210:213], v[14:17]
	v_mfma_f32_16x16x32_bf16 v[10:13], v[148:151], v[210:213], v[10:13]
	s_setprio 0
	s_setprio 1
	v_mfma_f32_16x16x32_bf16 v[122:125], v[152:155], v[182:185], v[122:125]
	v_mfma_f32_16x16x32_bf16 v[110:113], v[160:163], v[182:185], v[110:113]
	v_mfma_f32_16x16x32_bf16 v[70:73], v[152:155], v[190:193], v[70:73]
	v_mfma_f32_16x16x32_bf16 v[58:61], v[160:163], v[190:193], v[58:61]
	v_mfma_f32_16x16x32_bf16 v[22:25], v[152:155], v[198:201], v[22:25]
	v_mfma_f32_16x16x32_bf16 v[18:21], v[160:163], v[198:201], v[18:21]
	v_mfma_f32_16x16x32_bf16 v[6:9], v[152:155], v[206:209], v[6:9]
	v_mfma_f32_16x16x32_bf16 v[2:5], v[160:163], v[206:209], v[2:5]
	v_mfma_f32_16x16x32_bf16 v[122:125], v[156:159], v[186:189], v[122:125]
	v_mfma_f32_16x16x32_bf16 v[110:113], v[178:181], v[186:189], v[110:113]
	v_mfma_f32_16x16x32_bf16 v[70:73], v[156:159], v[194:197], v[70:73]
	v_mfma_f32_16x16x32_bf16 v[58:61], v[178:181], v[194:197], v[58:61]
	v_mfma_f32_16x16x32_bf16 v[22:25], v[156:159], v[202:205], v[22:25]
	v_mfma_f32_16x16x32_bf16 v[18:21], v[178:181], v[202:205], v[18:21]
	v_mfma_f32_16x16x32_bf16 v[6:9], v[156:159], v[210:213], v[6:9]
	v_mfma_f32_16x16x32_bf16 v[2:5], v[178:181], v[210:213], v[2:5]
	s_setprio 0
	s_barrier
.Lmid1046:
	ds_read_b128 v[136:139], v175
	ds_read_b128 v[140:143], v175 offset:1024
	ds_read_b128 v[144:147], v175 offset:2048
	ds_read_b128 v[148:151], v175 offset:3072
	ds_read_b128 v[152:155], v176
	ds_read_b128 v[156:159], v176 offset:1024
	ds_read_b128 v[160:163], v176 offset:2048
	ds_read_b128 v[178:181], v176 offset:3072
	ds_read_b128 v[182:185], v174 offset:32768
	ds_read_b128 v[186:189], v174 offset:33792
	ds_read_b128 v[190:193], v174 offset:34816
	ds_read_b128 v[194:197], v174 offset:35840
	ds_read_b128 v[198:201], v174 offset:36864
	ds_read_b128 v[202:205], v174 offset:37888
	ds_read_b128 v[206:209], v174 offset:38912
	ds_read_b128 v[210:213], v174 offset:39936
	s_add_u32 s28, s25, 0x40100
	s_addc_u32 s29, s33, 0
	s_mov_b32 s25, m0
	s_mov_b32 m0, s85
	s_nop 0
	global_load_lds_dwordx4 v165, s[28:29]
	s_mov_b32 m0, s25
	s_nop 0
	s_mov_b32 s25, m0
	s_mov_b32 m0, s86
	s_nop 0
	global_load_lds_dwordx4 v167, s[28:29]
	s_mov_b32 m0, s25
	s_waitcnt vmcnt(8)
	s_waitcnt lgkmcnt(0)
	s_barrier
	s_setprio 1
	s_waitcnt lgkmcnt(7)
	v_mfma_f32_16x16x32_bf16 v[26:29], v[136:139], v[182:185], v[26:29]
	v_mfma_f32_16x16x32_bf16 v[30:33], v[144:147], v[182:185], v[30:33]
	s_waitcnt lgkmcnt(5)
	v_mfma_f32_16x16x32_bf16 v[50:53], v[136:139], v[190:193], v[50:53]
	v_mfma_f32_16x16x32_bf16 v[54:57], v[144:147], v[190:193], v[54:57]
	s_waitcnt lgkmcnt(3)
	v_mfma_f32_16x16x32_bf16 v[74:77], v[136:139], v[198:201], v[74:77]
	v_mfma_f32_16x16x32_bf16 v[78:81], v[144:147], v[198:201], v[78:81]
	s_waitcnt lgkmcnt(1)
	v_mfma_f32_16x16x32_bf16 v[94:97], v[136:139], v[206:209], v[94:97]
	v_mfma_f32_16x16x32_bf16 v[102:105], v[144:147], v[206:209], v[102:105]
	v_mfma_f32_16x16x32_bf16 v[26:29], v[140:143], v[186:189], v[26:29]
	v_mfma_f32_16x16x32_bf16 v[30:33], v[148:151], v[186:189], v[30:33]
	v_mfma_f32_16x16x32_bf16 v[50:53], v[140:143], v[194:197], v[50:53]
	v_mfma_f32_16x16x32_bf16 v[54:57], v[148:151], v[194:197], v[54:57]
	v_mfma_f32_16x16x32_bf16 v[74:77], v[140:143], v[202:205], v[74:77]
	v_mfma_f32_16x16x32_bf16 v[78:81], v[148:151], v[202:205], v[78:81]
	s_waitcnt lgkmcnt(0)
	v_mfma_f32_16x16x32_bf16 v[94:97], v[140:143], v[210:213], v[94:97]
	v_mfma_f32_16x16x32_bf16 v[102:105], v[148:151], v[210:213], v[102:105]
	s_setprio 0
	s_setprio 1
	v_mfma_f32_16x16x32_bf16 v[38:41], v[152:155], v[182:185], v[38:41]
	v_mfma_f32_16x16x32_bf16 v[42:45], v[160:163], v[182:185], v[42:45]
	v_mfma_f32_16x16x32_bf16 v[62:65], v[152:155], v[190:193], v[62:65]
	v_mfma_f32_16x16x32_bf16 v[66:69], v[160:163], v[190:193], v[66:69]
	v_mfma_f32_16x16x32_bf16 v[82:85], v[152:155], v[198:201], v[82:85]
	v_mfma_f32_16x16x32_bf16 v[90:93], v[160:163], v[198:201], v[90:93]
	v_mfma_f32_16x16x32_bf16 v[106:109], v[152:155], v[206:209], v[106:109]
	v_mfma_f32_16x16x32_bf16 v[114:117], v[160:163], v[206:209], v[114:117]
	v_mfma_f32_16x16x32_bf16 v[38:41], v[156:159], v[186:189], v[38:41]
	v_mfma_f32_16x16x32_bf16 v[42:45], v[178:181], v[186:189], v[42:45]
	v_mfma_f32_16x16x32_bf16 v[62:65], v[156:159], v[194:197], v[62:65]
	v_mfma_f32_16x16x32_bf16 v[66:69], v[178:181], v[194:197], v[66:69]
	v_mfma_f32_16x16x32_bf16 v[82:85], v[156:159], v[202:205], v[82:85]
	v_mfma_f32_16x16x32_bf16 v[90:93], v[178:181], v[202:205], v[90:93]
	v_mfma_f32_16x16x32_bf16 v[106:109], v[156:159], v[210:213], v[106:109]
	v_mfma_f32_16x16x32_bf16 v[114:117], v[178:181], v[210:213], v[114:117]
	s_setprio 0
	s_barrier
	ds_read_b128 v[182:185], v174 offset:49152
	ds_read_b128 v[186:189], v174 offset:50176
	ds_read_b128 v[190:193], v174 offset:51200
	ds_read_b128 v[194:197], v174 offset:52224
	ds_read_b128 v[198:201], v174 offset:53248
	ds_read_b128 v[202:205], v174 offset:54272
	ds_read_b128 v[206:209], v174 offset:55296
	ds_read_b128 v[210:213], v174 offset:56320
	s_add_u32 s28, s23, 0x180
	s_addc_u32 s29, s24, 0
	s_mov_b32 s25, m0
	s_mov_b32 m0, s92
	s_nop 0
	global_load_lds_dwordx4 v166, s[28:29]
	s_mov_b32 m0, s25
	s_nop 0
	s_mov_b32 s25, m0
	s_mov_b32 m0, s93
	s_nop 0
	global_load_lds_dwordx4 v168, s[28:29]
	s_mov_b32 m0, s25
	s_add_u32 s28, s23, 0x40180
	s_addc_u32 s29, s24, 0
	s_mov_b32 s23, m0
	s_mov_b32 m0, s96
	s_nop 0
	global_load_lds_dwordx4 v166, s[28:29]
	s_mov_b32 m0, s23
	s_nop 0
	s_mov_b32 s23, m0
	s_mov_b32 m0, s97
	s_nop 0
	global_load_lds_dwordx4 v168, s[28:29]
	s_mov_b32 m0, s23
	s_nop 0
	s_mov_b32 s23, m0
	s_mov_b32 m0, s94
	s_nop 0
	global_load_lds_dwordx4 v165, s[58:59]
	s_mov_b32 m0, s23
	s_nop 0
	s_mov_b32 s23, m0
	s_mov_b32 m0, s95
	s_nop 0
	global_load_lds_dwordx4 v167, s[58:59]
	s_mov_b32 m0, s23
	s_waitcnt vmcnt(8)
	s_waitcnt lgkmcnt(0)
	s_barrier
	s_setprio 1
	s_waitcnt lgkmcnt(7)
	v_mfma_f32_16x16x32_bf16 v[118:121], v[136:139], v[182:185], v[118:121]
	v_mfma_f32_16x16x32_bf16 v[126:129], v[144:147], v[182:185], v[126:129]
	s_waitcnt lgkmcnt(5)
	v_mfma_f32_16x16x32_bf16 v[98:101], v[136:139], v[190:193], v[98:101]
	v_mfma_f32_16x16x32_bf16 v[86:89], v[144:147], v[190:193], v[86:89]
	s_waitcnt lgkmcnt(3)
	v_mfma_f32_16x16x32_bf16 v[46:49], v[136:139], v[198:201], v[46:49]
	v_mfma_f32_16x16x32_bf16 v[34:37], v[144:147], v[198:201], v[34:37]
	s_waitcnt lgkmcnt(1)
	v_mfma_f32_16x16x32_bf16 v[14:17], v[136:139], v[206:209], v[14:17]
	v_mfma_f32_16x16x32_bf16 v[10:13], v[144:147], v[206:209], v[10:13]
	v_mfma_f32_16x16x32_bf16 v[118:121], v[140:143], v[186:189], v[118:121]
	v_mfma_f32_16x16x32_bf16 v[126:129], v[148:151], v[186:189], v[126:129]
	v_mfma_f32_16x16x32_bf16 v[98:101], v[140:143], v[194:197], v[98:101]
	v_mfma_f32_16x16x32_bf16 v[86:89], v[148:151], v[194:197], v[86:89]
	v_mfma_f32_16x16x32_bf16 v[46:49], v[140:143], v[202:205], v[46:49]
	v_mfma_f32_16x16x32_bf16 v[34:37], v[148:151], v[202:205], v[34:37]
	s_waitcnt lgkmcnt(0)
	v_mfma_f32_16x16x32_bf16 v[14:17], v[140:143], v[210:213], v[14:17]
	v_mfma_f32_16x16x32_bf16 v[10:13], v[148:151], v[210:213], v[10:13]
	s_setprio 0
	s_setprio 1
	v_mfma_f32_16x16x32_bf16 v[122:125], v[152:155], v[182:185], v[122:125]
	v_mfma_f32_16x16x32_bf16 v[110:113], v[160:163], v[182:185], v[110:113]
	v_mfma_f32_16x16x32_bf16 v[70:73], v[152:155], v[190:193], v[70:73]
	v_mfma_f32_16x16x32_bf16 v[58:61], v[160:163], v[190:193], v[58:61]
	v_mfma_f32_16x16x32_bf16 v[22:25], v[152:155], v[198:201], v[22:25]
	v_mfma_f32_16x16x32_bf16 v[18:21], v[160:163], v[198:201], v[18:21]
	v_mfma_f32_16x16x32_bf16 v[6:9], v[152:155], v[206:209], v[6:9]
	v_mfma_f32_16x16x32_bf16 v[2:5], v[160:163], v[206:209], v[2:5]
	v_mfma_f32_16x16x32_bf16 v[122:125], v[156:159], v[186:189], v[122:125]
	v_mfma_f32_16x16x32_bf16 v[110:113], v[178:181], v[186:189], v[110:113]
	v_mfma_f32_16x16x32_bf16 v[70:73], v[156:159], v[194:197], v[70:73]
	v_mfma_f32_16x16x32_bf16 v[58:61], v[178:181], v[194:197], v[58:61]
	v_mfma_f32_16x16x32_bf16 v[22:25], v[156:159], v[202:205], v[22:25]
	v_mfma_f32_16x16x32_bf16 v[18:21], v[178:181], v[202:205], v[18:21]
	v_mfma_f32_16x16x32_bf16 v[6:9], v[156:159], v[210:213], v[6:9]
	v_mfma_f32_16x16x32_bf16 v[2:5], v[178:181], v[210:213], v[2:5]
	s_setprio 0
	s_barrier
	s_add_i32 s3, s3, 2
	s_add_u32 s56, s56, 0x100
	s_addc_u32 s57, s57, 0
	s_cmp_gt_u32 s3, 5
	s_cbranch_scc0 .LBB0_1046
	s_ashr_i32 s55, s54, 31
	s_lshl_b64 s[24:25], s[54:55], 19
	s_add_u32 s56, s69, s24
	s_addc_u32 s57, s76, s25
	s_ashr_i32 s23, s22, 31
	s_lshl_b64 s[24:25], s[22:23], 19
	s_add_u32 s58, s77, s24
	s_addc_u32 s59, s78, s25
	s_lshl_b32 s3, s60, 18
	s_lshl_b32 s23, s2, 8
	s_lshl_b32 s32, s2, 16
	s_add_i32 s2, s32, s3
	v_lshrrev_b32_e32 v214, 6, v0
	v_lshlrev_b32_e32 v214, 13, v214
	v_and_b32_e32 v215, 63, v0
	v_lshl_add_u32 v214, v215, 3, v214
	v_add_u32_e32 v134, s2, v214
	s_cmp_lg_u32 s37, 0
	s_cbranch_scc1 .Lmpf_have
	global_load_dwordx2 v[162:163], v134, s[14:15]
	global_load_dwordx2 v[178:179], v134, s[16:17]
	v_or_b32_e32 v136, 0x200, v134
	v_add_u32_e32 v137, 0x400, v134
	v_add_u32_e32 v138, 0x600, v134
	v_add_u32_e32 v139, 0x800, v134
	v_add_u32_e32 v140, 0xa00, v134
	v_add_u32_e32 v141, 0xc00, v134
	v_add_u32_e32 v161, 0xe00, v134
	global_load_dwordx2 v[180:181], v136, s[14:15]
	global_load_dwordx2 v[182:183], v136, s[16:17]
	global_load_dwordx2 v[158:159], v137, s[14:15]
	global_load_dwordx2 v[156:157], v137, s[16:17]
	global_load_dwordx2 v[154:155], v138, s[14:15]
	global_load_dwordx2 v[152:153], v138, s[16:17]
	global_load_dwordx2 v[150:151], v139, s[14:15]
	global_load_dwordx2 v[148:149], v139, s[16:17]
	global_load_dwordx2 v[146:147], v140, s[14:15]
	global_load_dwordx2 v[144:145], v140, s[16:17]
	global_load_dwordx2 v[142:143], v141, s[14:15]
	s_nop 0
	global_load_dwordx2 v[140:141], v141, s[16:17]
	s_nop 0
	global_load_dwordx2 v[138:139], v161, s[14:15]
	global_load_dwordx2 v[136:137], v161, s[16:17]
	s_branch .Lmpf_join

.LBB0_1048:
	ds_read_b128 v[136:139], v172
	ds_read_b128 v[140:143], v172 offset:1024
	ds_read_b128 v[144:147], v172 offset:2048
	ds_read_b128 v[148:151], v172 offset:3072
	ds_read_b128 v[152:155], v173
	ds_read_b128 v[156:159], v173 offset:1024
	ds_read_b128 v[160:163], v173 offset:2048
	ds_read_b128 v[178:181], v173 offset:3072
	s_cmp_eq_u32 s33, 12
	s_cselect_b32 s66, s3, s28
	s_cselect_b32 s67, s2, s29
	s_cselect_b32 s64, s25, s30
	s_cselect_b32 s65, s24, s31
	s_add_u32 s62, s66, 0x80
	s_addc_u32 s63, s67, 0
	ds_read_b128 v[182:185], v174
	ds_read_b128 v[186:189], v174 offset:1024
	ds_read_b128 v[190:193], v174 offset:2048
	ds_read_b128 v[194:197], v174 offset:3072
	ds_read_b128 v[198:201], v174 offset:4096
	ds_read_b128 v[202:205], v174 offset:5120
	ds_read_b128 v[206:209], v174 offset:6144
	ds_read_b128 v[210:213], v174 offset:7168
	s_add_u32 s36, s28, 0x3ff80
	s_addc_u32 s37, s29, 0
	s_mov_b32 s52, m0
	s_mov_b32 m0, s26
	s_nop 0
	global_load_lds_dwordx4 v165, s[36:37]
	s_mov_b32 m0, s52
	s_nop 0
	s_mov_b32 s52, m0
	s_mov_b32 m0, s27
	s_nop 0
	global_load_lds_dwordx4 v167, s[36:37]
	s_mov_b32 m0, s52
	s_waitcnt vmcnt(8)
	s_waitcnt lgkmcnt(0)
	s_barrier
	s_setprio 1
	s_waitcnt lgkmcnt(7)
	v_mfma_f32_16x16x32_bf16 v[26:29], v[136:139], v[182:185], v[26:29]
	v_mfma_f32_16x16x32_bf16 v[30:33], v[144:147], v[182:185], v[30:33]
	s_waitcnt lgkmcnt(5)
	v_mfma_f32_16x16x32_bf16 v[50:53], v[136:139], v[190:193], v[50:53]
	v_mfma_f32_16x16x32_bf16 v[54:57], v[144:147], v[190:193], v[54:57]
	s_waitcnt lgkmcnt(3)
	v_mfma_f32_16x16x32_bf16 v[74:77], v[136:139], v[198:201], v[74:77]
	v_mfma_f32_16x16x32_bf16 v[78:81], v[144:147], v[198:201], v[78:81]
	s_waitcnt lgkmcnt(1)
	v_mfma_f32_16x16x32_bf16 v[94:97], v[136:139], v[206:209], v[94:97]
	v_mfma_f32_16x16x32_bf16 v[102:105], v[144:147], v[206:209], v[102:105]
	v_mfma_f32_16x16x32_bf16 v[26:29], v[140:143], v[186:189], v[26:29]
	v_mfma_f32_16x16x32_bf16 v[30:33], v[148:151], v[186:189], v[30:33]
	v_mfma_f32_16x16x32_bf16 v[50:53], v[140:143], v[194:197], v[50:53]
	v_mfma_f32_16x16x32_bf16 v[54:57], v[148:151], v[194:197], v[54:57]
	v_mfma_f32_16x16x32_bf16 v[74:77], v[140:143], v[202:205], v[74:77]
	v_mfma_f32_16x16x32_bf16 v[78:81], v[148:151], v[202:205], v[78:81]
	s_waitcnt lgkmcnt(0)
	v_mfma_f32_16x16x32_bf16 v[94:97], v[140:143], v[210:213], v[94:97]
	v_mfma_f32_16x16x32_bf16 v[102:105], v[148:151], v[210:213], v[102:105]
	s_setprio 0
	s_setprio 1
	v_mfma_f32_16x16x32_bf16 v[38:41], v[152:155], v[182:185], v[38:41]
	v_mfma_f32_16x16x32_bf16 v[42:45], v[160:163], v[182:185], v[42:45]
	v_mfma_f32_16x16x32_bf16 v[62:65], v[152:155], v[190:193], v[62:65]
	v_mfma_f32_16x16x32_bf16 v[66:69], v[160:163], v[190:193], v[66:69]
	v_mfma_f32_16x16x32_bf16 v[82:85], v[152:155], v[198:201], v[82:85]
	v_mfma_f32_16x16x32_bf16 v[90:93], v[160:163], v[198:201], v[90:93]
	v_mfma_f32_16x16x32_bf16 v[106:109], v[152:155], v[206:209], v[106:109]
	v_mfma_f32_16x16x32_bf16 v[114:117], v[160:163], v[206:209], v[114:117]
	v_mfma_f32_16x16x32_bf16 v[38:41], v[156:159], v[186:189], v[38:41]
	v_mfma_f32_16x16x32_bf16 v[42:45], v[178:181], v[186:189], v[42:45]
	v_mfma_f32_16x16x32_bf16 v[62:65], v[156:159], v[194:197], v[62:65]
	v_mfma_f32_16x16x32_bf16 v[66:69], v[178:181], v[194:197], v[66:69]
	v_mfma_f32_16x16x32_bf16 v[82:85], v[156:159], v[202:205], v[82:85]
	v_mfma_f32_16x16x32_bf16 v[90:93], v[178:181], v[202:205], v[90:93]
	v_mfma_f32_16x16x32_bf16 v[106:109], v[156:159], v[210:213], v[106:109]
	v_mfma_f32_16x16x32_bf16 v[114:117], v[178:181], v[210:213], v[114:117]
	s_setprio 0
	s_barrier
	ds_read_b128 v[182:185], v174 offset:16384
	ds_read_b128 v[186:189], v174 offset:17408
	ds_read_b128 v[190:193], v174 offset:18432
	ds_read_b128 v[194:197], v174 offset:19456
	ds_read_b128 v[198:201], v174 offset:20480
	ds_read_b128 v[202:205], v174 offset:21504
	ds_read_b128 v[206:209], v174 offset:22528
	ds_read_b128 v[210:213], v174 offset:23552
	s_mov_b32 s36, m0
	s_mov_b32 m0, s80
	s_nop 0
	global_load_lds_dwordx4 v166, s[64:65]
	s_mov_b32 m0, s36
	s_nop 0
	s_mov_b32 s36, m0
	s_mov_b32 m0, s81
	s_nop 0
	global_load_lds_dwordx4 v168, s[64:65]
	s_mov_b32 m0, s36
	s_add_u32 s36, s64, 0x40000
	s_addc_u32 s37, s65, 0
	s_mov_b32 s52, m0
	s_mov_b32 m0, s82
	s_nop 0
	global_load_lds_dwordx4 v166, s[36:37]
	s_mov_b32 m0, s52
	s_nop 0
	s_mov_b32 s52, m0
	s_mov_b32 m0, s83
	s_nop 0
	global_load_lds_dwordx4 v168, s[36:37]
	s_mov_b32 m0, s52
	s_mov_b32 s36, m0
	s_mov_b32 m0, s79
	s_nop 0
	global_load_lds_dwordx4 v165, s[66:67]
	s_mov_b32 m0, s36
	s_nop 0
	s_mov_b32 s36, m0
	s_mov_b32 m0, s84
	s_nop 0
	global_load_lds_dwordx4 v167, s[66:67]
	s_mov_b32 m0, s36
	s_waitcnt vmcnt(8)
	s_waitcnt lgkmcnt(0)
	s_barrier
	s_setprio 1
	s_waitcnt lgkmcnt(7)
	v_mfma_f32_16x16x32_bf16 v[118:121], v[136:139], v[182:185], v[118:121]
	v_mfma_f32_16x16x32_bf16 v[126:129], v[144:147], v[182:185], v[126:129]
	s_waitcnt lgkmcnt(5)
	v_mfma_f32_16x16x32_bf16 v[98:101], v[136:139], v[190:193], v[98:101]
	v_mfma_f32_16x16x32_bf16 v[86:89], v[144:147], v[190:193], v[86:89]
	s_waitcnt lgkmcnt(3)
	v_mfma_f32_16x16x32_bf16 v[46:49], v[136:139], v[198:201], v[46:49]
	v_mfma_f32_16x16x32_bf16 v[34:37], v[144:147], v[198:201], v[34:37]
	s_waitcnt lgkmcnt(1)
	v_mfma_f32_16x16x32_bf16 v[14:17], v[136:139], v[206:209], v[14:17]
	v_mfma_f32_16x16x32_bf16 v[10:13], v[144:147], v[206:209], v[10:13]
	v_mfma_f32_16x16x32_bf16 v[118:121], v[140:143], v[186:189], v[118:121]
	v_mfma_f32_16x16x32_bf16 v[126:129], v[148:151], v[186:189], v[126:129]
	v_mfma_f32_16x16x32_bf16 v[98:101], v[140:143], v[194:197], v[98:101]
	v_mfma_f32_16x16x32_bf16 v[86:89], v[148:151], v[194:197], v[86:89]
	v_mfma_f32_16x16x32_bf16 v[46:49], v[140:143], v[202:205], v[46:49]
	v_mfma_f32_16x16x32_bf16 v[34:37], v[148:151], v[202:205], v[34:37]
	s_waitcnt lgkmcnt(0)
	v_mfma_f32_16x16x32_bf16 v[14:17], v[140:143], v[210:213], v[14:17]
	v_mfma_f32_16x16x32_bf16 v[10:13], v[148:151], v[210:213], v[10:13]
	s_setprio 0
	s_setprio 1
	v_mfma_f32_16x16x32_bf16 v[122:125], v[152:155], v[182:185], v[122:125]
	v_mfma_f32_16x16x32_bf16 v[110:113], v[160:163], v[182:185], v[110:113]
	v_mfma_f32_16x16x32_bf16 v[70:73], v[152:155], v[190:193], v[70:73]
	v_mfma_f32_16x16x32_bf16 v[58:61], v[160:163], v[190:193], v[58:61]
	v_mfma_f32_16x16x32_bf16 v[22:25], v[152:155], v[198:201], v[22:25]
	v_mfma_f32_16x16x32_bf16 v[18:21], v[160:163], v[198:201], v[18:21]
	v_mfma_f32_16x16x32_bf16 v[6:9], v[152:155], v[206:209], v[6:9]
	v_mfma_f32_16x16x32_bf16 v[2:5], v[160:163], v[206:209], v[2:5]
	v_mfma_f32_16x16x32_bf16 v[122:125], v[156:159], v[186:189], v[122:125]
	v_mfma_f32_16x16x32_bf16 v[110:113], v[178:181], v[186:189], v[110:113]
	v_mfma_f32_16x16x32_bf16 v[70:73], v[156:159], v[194:197], v[70:73]
	v_mfma_f32_16x16x32_bf16 v[58:61], v[178:181], v[194:197], v[58:61]
	v_mfma_f32_16x16x32_bf16 v[22:25], v[156:159], v[202:205], v[22:25]
	v_mfma_f32_16x16x32_bf16 v[18:21], v[178:181], v[202:205], v[18:21]
	v_mfma_f32_16x16x32_bf16 v[6:9], v[156:159], v[210:213], v[6:9]
	v_mfma_f32_16x16x32_bf16 v[2:5], v[178:181], v[210:213], v[2:5]
	s_setprio 0
	s_barrier
	ds_read_b128 v[136:139], v175
	ds_read_b128 v[140:143], v175 offset:1024
	ds_read_b128 v[144:147], v175 offset:2048
	ds_read_b128 v[148:151], v175 offset:3072
	ds_read_b128 v[152:155], v176
	ds_read_b128 v[156:159], v176 offset:1024
	ds_read_b128 v[160:163], v176 offset:2048
	ds_read_b128 v[178:181], v176 offset:3072
	ds_read_b128 v[182:185], v174 offset:32768
	ds_read_b128 v[186:189], v174 offset:33792
	ds_read_b128 v[190:193], v174 offset:34816
	ds_read_b128 v[194:197], v174 offset:35840
	ds_read_b128 v[198:201], v174 offset:36864
	ds_read_b128 v[202:205], v174 offset:37888
	ds_read_b128 v[206:209], v174 offset:38912
	ds_read_b128 v[210:213], v174 offset:39936
	s_add_u32 s36, s66, 0x40000
	s_addc_u32 s37, s67, 0
	s_mov_b32 s52, m0
	s_mov_b32 m0, s85
	s_nop 0
	global_load_lds_dwordx4 v165, s[36:37]
	s_mov_b32 m0, s52
	s_nop 0
	s_mov_b32 s52, m0
	s_mov_b32 m0, s86
	s_nop 0
	global_load_lds_dwordx4 v167, s[36:37]
	s_mov_b32 m0, s52
	s_waitcnt vmcnt(8)
	s_waitcnt lgkmcnt(0)
	s_barrier
	s_setprio 1
	s_waitcnt lgkmcnt(7)
	v_mfma_f32_16x16x32_bf16 v[26:29], v[136:139], v[182:185], v[26:29]
	v_mfma_f32_16x16x32_bf16 v[30:33], v[144:147], v[182:185], v[30:33]
	s_waitcnt lgkmcnt(5)
	v_mfma_f32_16x16x32_bf16 v[50:53], v[136:139], v[190:193], v[50:53]
	v_mfma_f32_16x16x32_bf16 v[54:57], v[144:147], v[190:193], v[54:57]
	s_waitcnt lgkmcnt(3)
	v_mfma_f32_16x16x32_bf16 v[74:77], v[136:139], v[198:201], v[74:77]
	v_mfma_f32_16x16x32_bf16 v[78:81], v[144:147], v[198:201], v[78:81]
	s_waitcnt lgkmcnt(1)
	v_mfma_f32_16x16x32_bf16 v[94:97], v[136:139], v[206:209], v[94:97]
	v_mfma_f32_16x16x32_bf16 v[102:105], v[144:147], v[206:209], v[102:105]
	v_mfma_f32_16x16x32_bf16 v[26:29], v[140:143], v[186:189], v[26:29]
	v_mfma_f32_16x16x32_bf16 v[30:33], v[148:151], v[186:189], v[30:33]
	v_mfma_f32_16x16x32_bf16 v[50:53], v[140:143], v[194:197], v[50:53]
	v_mfma_f32_16x16x32_bf16 v[54:57], v[148:151], v[194:197], v[54:57]
	v_mfma_f32_16x16x32_bf16 v[74:77], v[140:143], v[202:205], v[74:77]
	v_mfma_f32_16x16x32_bf16 v[78:81], v[148:151], v[202:205], v[78:81]
	s_waitcnt lgkmcnt(0)
	v_mfma_f32_16x16x32_bf16 v[94:97], v[140:143], v[210:213], v[94:97]
	v_mfma_f32_16x16x32_bf16 v[102:105], v[148:151], v[210:213], v[102:105]
	s_setprio 0
	s_setprio 1
	v_mfma_f32_16x16x32_bf16 v[38:41], v[152:155], v[182:185], v[38:41]
	v_mfma_f32_16x16x32_bf16 v[42:45], v[160:163], v[182:185], v[42:45]
	v_mfma_f32_16x16x32_bf16 v[62:65], v[152:155], v[190:193], v[62:65]
	v_mfma_f32_16x16x32_bf16 v[66:69], v[160:163], v[190:193], v[66:69]
	v_mfma_f32_16x16x32_bf16 v[82:85], v[152:155], v[198:201], v[82:85]
	v_mfma_f32_16x16x32_bf16 v[90:93], v[160:163], v[198:201], v[90:93]
	v_mfma_f32_16x16x32_bf16 v[106:109], v[152:155], v[206:209], v[106:109]
	v_mfma_f32_16x16x32_bf16 v[114:117], v[160:163], v[206:209], v[114:117]
	v_mfma_f32_16x16x32_bf16 v[38:41], v[156:159], v[186:189], v[38:41]
	v_mfma_f32_16x16x32_bf16 v[42:45], v[178:181], v[186:189], v[42:45]
	v_mfma_f32_16x16x32_bf16 v[62:65], v[156:159], v[194:197], v[62:65]
	v_mfma_f32_16x16x32_bf16 v[66:69], v[178:181], v[194:197], v[66:69]
	v_mfma_f32_16x16x32_bf16 v[82:85], v[156:159], v[202:205], v[82:85]
	v_mfma_f32_16x16x32_bf16 v[90:93], v[178:181], v[202:205], v[90:93]
	v_mfma_f32_16x16x32_bf16 v[106:109], v[156:159], v[210:213], v[106:109]
	v_mfma_f32_16x16x32_bf16 v[114:117], v[178:181], v[210:213], v[114:117]
	s_setprio 0
	s_barrier
	ds_read_b128 v[182:185], v174 offset:49152
	ds_read_b128 v[186:189], v174 offset:50176
	ds_read_b128 v[190:193], v174 offset:51200
	ds_read_b128 v[194:197], v174 offset:52224
	ds_read_b128 v[198:201], v174 offset:53248
	ds_read_b128 v[202:205], v174 offset:54272
	ds_read_b128 v[206:209], v174 offset:55296
	ds_read_b128 v[210:213], v174 offset:56320
	s_add_u32 s36, s64, 0x80
	s_addc_u32 s37, s65, 0
	s_mov_b32 s52, m0
	s_mov_b32 m0, s92
	s_nop 0
	global_load_lds_dwordx4 v166, s[36:37]
	s_mov_b32 m0, s52
	s_nop 0
	s_mov_b32 s52, m0
	s_mov_b32 m0, s93
	s_nop 0
	global_load_lds_dwordx4 v168, s[36:37]
	s_mov_b32 m0, s52
	s_add_u32 s36, s64, 0x40080
	s_addc_u32 s37, s65, 0
	s_mov_b32 s52, m0
	s_mov_b32 m0, s96
	s_nop 0
	global_load_lds_dwordx4 v166, s[36:37]
	s_mov_b32 m0, s52
	s_nop 0
	s_mov_b32 s52, m0
	s_mov_b32 m0, s97
	s_nop 0
	global_load_lds_dwordx4 v168, s[36:37]
	s_mov_b32 m0, s52
	s_mov_b32 s36, m0
	s_mov_b32 m0, s94
	s_nop 0
	global_load_lds_dwordx4 v165, s[62:63]
	s_mov_b32 m0, s36
	s_nop 0
	s_mov_b32 s36, m0
	s_mov_b32 m0, s95
	s_nop 0
	global_load_lds_dwordx4 v167, s[62:63]
	s_mov_b32 m0, s36
	s_waitcnt vmcnt(8)
	s_waitcnt lgkmcnt(0)
	s_barrier
	s_setprio 1
	s_waitcnt lgkmcnt(7)
	v_mfma_f32_16x16x32_bf16 v[118:121], v[136:139], v[182:185], v[118:121]
	v_mfma_f32_16x16x32_bf16 v[126:129], v[144:147], v[182:185], v[126:129]
	s_waitcnt lgkmcnt(5)
	v_mfma_f32_16x16x32_bf16 v[98:101], v[136:139], v[190:193], v[98:101]
	v_mfma_f32_16x16x32_bf16 v[86:89], v[144:147], v[190:193], v[86:89]
	s_waitcnt lgkmcnt(3)
	v_mfma_f32_16x16x32_bf16 v[46:49], v[136:139], v[198:201], v[46:49]
	v_mfma_f32_16x16x32_bf16 v[34:37], v[144:147], v[198:201], v[34:37]
	s_waitcnt lgkmcnt(1)
	v_mfma_f32_16x16x32_bf16 v[14:17], v[136:139], v[206:209], v[14:17]
	v_mfma_f32_16x16x32_bf16 v[10:13], v[144:147], v[206:209], v[10:13]
	v_mfma_f32_16x16x32_bf16 v[118:121], v[140:143], v[186:189], v[118:121]
	v_mfma_f32_16x16x32_bf16 v[126:129], v[148:151], v[186:189], v[126:129]
	v_mfma_f32_16x16x32_bf16 v[98:101], v[140:143], v[194:197], v[98:101]
	v_mfma_f32_16x16x32_bf16 v[86:89], v[148:151], v[194:197], v[86:89]
	v_mfma_f32_16x16x32_bf16 v[46:49], v[140:143], v[202:205], v[46:49]
	v_mfma_f32_16x16x32_bf16 v[34:37], v[148:151], v[202:205], v[34:37]
	s_waitcnt lgkmcnt(0)
	v_mfma_f32_16x16x32_bf16 v[14:17], v[140:143], v[210:213], v[14:17]
	v_mfma_f32_16x16x32_bf16 v[10:13], v[148:151], v[210:213], v[10:13]
	s_setprio 0
	s_setprio 1
	v_mfma_f32_16x16x32_bf16 v[122:125], v[152:155], v[182:185], v[122:125]
	v_mfma_f32_16x16x32_bf16 v[110:113], v[160:163], v[182:185], v[110:113]
	v_mfma_f32_16x16x32_bf16 v[70:73], v[152:155], v[190:193], v[70:73]
	v_mfma_f32_16x16x32_bf16 v[58:61], v[160:163], v[190:193], v[58:61]
	v_mfma_f32_16x16x32_bf16 v[22:25], v[152:155], v[198:201], v[22:25]
	v_mfma_f32_16x16x32_bf16 v[18:21], v[160:163], v[198:201], v[18:21]
	v_mfma_f32_16x16x32_bf16 v[6:9], v[152:155], v[206:209], v[6:9]
	v_mfma_f32_16x16x32_bf16 v[2:5], v[160:163], v[206:209], v[2:5]
	v_mfma_f32_16x16x32_bf16 v[122:125], v[156:159], v[186:189], v[122:125]
	v_mfma_f32_16x16x32_bf16 v[110:113], v[178:181], v[186:189], v[110:113]
	v_mfma_f32_16x16x32_bf16 v[70:73], v[156:159], v[194:197], v[70:73]
	v_mfma_f32_16x16x32_bf16 v[58:61], v[178:181], v[194:197], v[58:61]
	v_mfma_f32_16x16x32_bf16 v[22:25], v[156:159], v[202:205], v[22:25]
	v_mfma_f32_16x16x32_bf16 v[18:21], v[178:181], v[202:205], v[18:21]
	v_mfma_f32_16x16x32_bf16 v[6:9], v[156:159], v[210:213], v[6:9]
	v_mfma_f32_16x16x32_bf16 v[2:5], v[178:181], v[210:213], v[2:5]
	s_setprio 0
	s_barrier
	s_add_i32 s33, s33, 2
	s_add_u32 s28, s28, 0x100
	s_addc_u32 s29, s29, 0
	s_add_u32 s30, s30, 0x100
	s_addc_u32 s31, s31, 0
	s_cmp_lt_u32 s33, 14
	s_cbranch_scc1 .LBB0_1048
	s_and_b64 vcc, exec, s[20:21]
	s_cbranch_vccz .LBB0_1051
	s_barrier

.LBB0_1428:
	s_ashr_i32 s4, s3, 3
	s_waitcnt vmcnt(15)
	v_lshrrev_b32_e32 v4, 1, v0
	v_bfe_u32 v5, v0, 2, 2
	s_add_u32 s89, s74, 0x17800000
	v_and_b32_e32 v2, 32, v0
	v_bfe_u32 v3, v0, 2, 4
	v_and_or_b32 v4, v4, 24, v5
	v_lshrrev_b32_e32 v5, 3, v0
	s_waitcnt vmcnt(14)
	v_lshrrev_b32_e32 v8, 5, v0
	s_addc_u32 s24, s75, 0
	v_bitop3_b32 v2, v1, v2, 48 bitop3:0x6c
	v_and_or_b32 v6, v5, 48, v3
	v_and_or_b32 v5, v5, 32, v8
	s_add_u32 s25, s74, 0xc00000
	v_and_or_b32 v7, v0, 64, v2
	v_and_or_b32 v5, v5, 36, v4
	s_addc_u32 s26, s75, 0
	v_lshl_or_b32 v229, v5, 11, v7
	v_or_b32_e32 v5, 0x2000, v1
	s_add_i32 s4, s12, s4
	v_lshl_or_b32 v228, v6, 11, v7
	v_lshrrev_b32_e32 v5, 7, v5
	s_movk_i32 s13, 0x70
	v_lshrrev_b32_e32 v6, 4, v1
	s_ashr_i32 s12, s4, 31
	v_and_or_b32 v3, v5, s13, v3
	v_and_or_b32 v2, v6, 64, v2
	v_lshrrev_b32_e32 v6, 9, v1
	s_movk_i32 s13, 0x60
	s_lshr_b32 s12, s12, 27
	v_and_or_b32 v5, v5, s13, v6
	s_movk_i32 s13, 0x64
	s_add_i32 s12, s4, s12
	v_and_or_b32 v4, v5, s13, v4
	s_ashr_i32 s13, s12, 5
	s_and_b32 s12, s12, 0xffe0
	s_sub_i32 s12, s4, s12
	s_bfe_i32 s4, s12, 0x80000
	s_bfe_u32 s4, s4, 0x3000c
	s_add_i32 s14, s12, s4
	s_bfe_i32 s4, s14, 0x80000
	s_and_b32 s14, s14, 0xf8
	s_sub_i32 s12, s12, s14
	s_lshl_b32 s13, s13, 3
	s_sext_i32_i16 s4, s4
	s_sext_i32_i8 s12, s12
	s_lshr_b32 s5, s16, 8
	s_lshr_b32 s4, s4, 3
	s_add_i32 s56, s13, s12
	s_lshr_b32 s17, s16, 6
	s_ashr_i32 s57, s56, 31
	s_bfe_i64 s[14:15], s[4:5], 0x100000
	s_lshl_b32 s18, s17, 10
	s_lshl_b64 s[12:13], s[56:57], 19
	s_lshl_b64 s[14:15], s[14:15], 19
	s_add_u32 s60, s25, s14
	s_addc_u32 s61, s26, s15
	s_add_i32 s28, s18, 0
	s_add_i32 s30, s28, 0x10000
	s_mov_b32 s14, m0
	s_mov_b32 m0, s30
	s_nop 0
	global_load_lds_dwordx4 v229, s[60:61]
	s_mov_b32 m0, s14
	v_lshl_or_b32 v231, v4, 11, v2
	s_add_i32 s31, s28, 0x12000
	s_mov_b32 s14, m0
	s_mov_b32 m0, s31
	s_nop 0
	global_load_lds_dwordx4 v231, s[60:61]
	s_mov_b32 m0, s14
	s_add_u32 s14, s60, 0x40000
	s_addc_u32 s15, s61, 0
	s_add_i32 s34, s28, 0x14000
	s_mov_b32 s18, m0
	s_mov_b32 m0, s34
	s_nop 0
	global_load_lds_dwordx4 v229, s[14:15]
	s_mov_b32 m0, s18
	s_add_i32 s35, s28, 0x16000
	s_mov_b32 s18, m0
	s_mov_b32 m0, s35
	s_nop 0
	global_load_lds_dwordx4 v231, s[14:15]
	s_mov_b32 m0, s18
	s_add_u32 s58, s89, s12
	v_writelane_b32 v253, s10, 39
	s_addc_u32 s59, s24, s13
	s_mov_b32 s12, m0
	s_mov_b32 m0, s28
	s_nop 0
	global_load_lds_dwordx4 v228, s[58:59]
	s_mov_b32 m0, s12
	s_add_i32 s36, s28, 0x2000
	v_writelane_b32 v253, s11, 40
	v_lshl_or_b32 v230, v3, 11, v2
	s_mov_b32 s12, m0
	s_mov_b32 m0, s36
	s_nop 0
	global_load_lds_dwordx4 v230, s[58:59]
	s_mov_b32 m0, s12
	s_add_u32 s14, s58, 0x40000
	v_writelane_b32 v253, s8, 35
	s_addc_u32 s15, s59, 0
	s_add_i32 s37, s28, 0x4000
	s_mov_b32 s12, m0
	s_mov_b32 m0, s37
	s_nop 0
	global_load_lds_dwordx4 v228, s[14:15]
	s_mov_b32 m0, s12
	v_writelane_b32 v253, s9, 36
	s_add_i32 s52, s28, 0x6000
	s_mov_b32 s18, m0
	s_mov_b32 m0, s52
	s_nop 0
	global_load_lds_dwordx4 v230, s[14:15]
	s_mov_b32 m0, s18
	v_writelane_b32 v253, s6, 31
	s_cmp_eq_u32 s5, 1
	s_mov_b32 s96, s93
	v_writelane_b32 v253, s7, 32
	s_mov_b32 s27, 0
	s_mov_b32 s29, 0x10000
	s_cselect_b64 s[94:95], -1, 0
	s_cmp_lg_u32 s5, 1
	v_writelane_b32 v253, s92, 43
	s_cbranch_scc1 .LBB0_1430
	s_barrier
.LBB0_1430:
	v_and_b32_e32 v233, 3, v219
	s_add_u32 s92, s74, 0x19800000
	v_and_b32_e32 v232, 15, v0
	v_lshlrev_b32_e32 v2, 4, v233
	v_lshlrev_b32_e32 v4, 2, v0
	s_sext_i32_i8 s83, s4
	s_addc_u32 s93, s75, 0
	v_lshl_or_b32 v3, v232, 6, v2
	s_lshl_b32 s4, s5, 13
	v_and_b32_e32 v4, 32, v4
	v_bitop3_b32 v3, v3, s4, v4 bitop3:0xde
	s_lshl_b32 s4, s17, 5
	s_and_b32 s57, s4, 0x60
	v_lshlrev_b32_e32 v5, 6, v0
	s_movk_i32 s4, 0x3c0
	s_lshl_b32 s53, s5, 6
	v_and_or_b32 v2, v5, s4, v2
	s_lshl_b32 s4, s57, 7
	v_bitop3_b32 v2, s4, v2, v4 bitop3:0xf6
	s_add_u32 s4, s60, 0x80
	s_waitcnt vmcnt(2)
	s_barrier
	s_addc_u32 s5, s61, 0
	s_add_i32 s68, s28, 0x18000
	s_mov_b32 s17, m0
	s_mov_b32 m0, s68
	s_nop 0
	global_load_lds_dwordx4 v229, s[4:5]
	s_mov_b32 m0, s17
	s_add_i32 s69, s28, 0x1a000
	s_mov_b32 s17, m0
	s_mov_b32 m0, s69
	s_nop 0
	global_load_lds_dwordx4 v231, s[4:5]
	s_mov_b32 m0, s17
	s_add_u32 s4, s58, 0x80
	s_addc_u32 s5, s59, 0
	s_add_i32 s76, s28, 0x8000
	s_mov_b32 s17, m0
	s_mov_b32 m0, s76
	s_nop 0
	global_load_lds_dwordx4 v228, s[4:5]
	s_mov_b32 m0, s17
	s_add_i32 s77, s28, 0xa000
	s_mov_b32 s17, m0
	s_mov_b32 m0, s77
	s_nop 0
	global_load_lds_dwordx4 v230, s[4:5]
	s_mov_b32 m0, s17
	s_add_u32 s4, s60, 0x40080
	s_addc_u32 s5, s61, 0
	s_add_i32 s78, s28, 0x1c000
	s_mov_b32 s17, m0
	s_mov_b32 m0, s78
	s_nop 0
	global_load_lds_dwordx4 v229, s[4:5]
	s_mov_b32 m0, s17
	s_add_i32 s79, s28, 0x1e000
	s_mov_b32 s17, m0
	s_mov_b32 m0, s79
	s_nop 0
	global_load_lds_dwordx4 v231, s[4:5]
	s_mov_b32 m0, s17
	s_waitcnt vmcnt(6)
	s_add_i32 s80, s28, 0xc000
	s_cmpk_lt_u32 s16, 0x100
	v_add_u32_e32 v2, 0, v2
	s_cselect_b64 s[16:17], -1, 0
	s_add_i32 s81, s28, 0xe000
	s_ashr_i32 s82, s90, 31
	v_mov_b64_e32 v[220:221], 0x100
	v_mov_b64_e32 v[222:223], 0xff
	v_add_u32_e32 v234, 0x10000, v2
	v_add_u32_e32 v235, 0x14000, v2
	v_add_u32_e32 v236, 0, v3
	v_add_u32_e32 v237, 0x18000, v2
	v_add_u32_e32 v238, 0x1c000, v2
	v_mov_b32_e32 v225, 0
	s_lshl_b32 s2, s56, 8
	s_add_i32 s2, s2, s53
	v_add_lshl_u32 v224, s2, v232, 10
	s_lshl_b32 s2, s83, 8
	s_or_b32 s2, s2, s57
	v_lshlrev_b32_e32 v226, 3, v233
	v_readlane_b32 s0, v253, 8
	v_add3_u32 v224, s2, v226, v224
	v_readlane_b32 s1, v253, 9
	s_mov_b64 s[2:3], 0x10000
	s_nop 1
	v_lshl_add_u64 v[226:227], v[224:225], 2, s[0:1]
	global_load_dwordx4 v[240:243], v[226:227], off
	global_load_dwordx4 v[244:247], v[226:227], off offset:16
	global_load_dwordx4 v[210:213], v[226:227], off offset:528
	global_load_dwordx4 v[214:217], v[226:227], off offset:512
	v_lshl_add_u64 v[248:249], v[226:227], 0, s[2:3]
	global_load_dwordx4 v[206:209], v[248:249], off
	global_load_dwordx4 v[202:205], v[248:249], off offset:16
	global_load_dwordx4 v[198:201], v[248:249], off offset:512
	global_load_dwordx4 v[194:197], v[248:249], off offset:528
	s_mov_b32 s32, 1
	s_barrier
	s_branch .LBB0_1433

.Lpeel1440:
	ds_read_b128 v[130:133], v234
	ds_read_b128 v[134:137], v234 offset:1024
	ds_read_b128 v[138:141], v234 offset:2048
	ds_read_b128 v[142:145], v234 offset:3072
	ds_read_b128 v[146:149], v235
	ds_read_b128 v[150:153], v235 offset:1024
	ds_read_b128 v[154:157], v235 offset:2048
	ds_read_b128 v[158:161], v235 offset:3072
	s_add_u32 s60, s58, 0x100
	s_addc_u32 s61, s59, 0
	s_cmp_eq_u32 s87, 12
	s_cselect_b32 s66, s33, s60
	s_cselect_b32 s67, s21, s61
	s_cselect_b32 s64, s84, s85
	s_cselect_b32 s65, s19, s86
	s_add_u32 s62, s66, 0x80
	s_addc_u32 s63, s67, 0
	ds_read_b128 v[162:165], v236
	ds_read_b128 v[166:169], v236 offset:1024
	ds_read_b128 v[170:173], v236 offset:2048
	ds_read_b128 v[174:177], v236 offset:3072
	ds_read_b128 v[178:181], v236 offset:4096
	ds_read_b128 v[182:185], v236 offset:5120
	ds_read_b128 v[186:189], v236 offset:6144
	ds_read_b128 v[190:193], v236 offset:7168
	s_add_u32 s58, s58, 0x40080
	s_addc_u32 s59, s59, 0
	s_mov_b32 s88, m0
	s_mov_b32 m0, s80
	s_nop 0
	global_load_lds_dwordx4 v228, s[58:59]
	s_mov_b32 m0, s88
	s_nop 0
	s_mov_b32 s88, m0
	s_mov_b32 m0, s81
	s_nop 0
	global_load_lds_dwordx4 v230, s[58:59]
	s_mov_b32 m0, s88
	s_waitcnt vmcnt(8)
	s_waitcnt lgkmcnt(0)
	s_barrier
	s_setprio 1
	s_waitcnt lgkmcnt(7)
	v_mfma_f32_16x16x32_bf16 v[126:129], v[130:133], v[162:165], 0
	v_mfma_f32_16x16x32_bf16 v[122:125], v[138:141], v[162:165], 0
	s_waitcnt lgkmcnt(5)
	v_mfma_f32_16x16x32_bf16 v[114:117], v[130:133], v[170:173], 0
	v_mfma_f32_16x16x32_bf16 v[106:109], v[138:141], v[170:173], 0
	s_waitcnt lgkmcnt(3)
	v_mfma_f32_16x16x32_bf16 v[94:97], v[130:133], v[178:181], 0
	v_mfma_f32_16x16x32_bf16 v[90:93], v[138:141], v[178:181], 0
	s_waitcnt lgkmcnt(1)
	v_mfma_f32_16x16x32_bf16 v[86:89], v[130:133], v[186:189], 0
	v_mfma_f32_16x16x32_bf16 v[78:81], v[138:141], v[186:189], 0
	v_mfma_f32_16x16x32_bf16 v[126:129], v[134:137], v[166:169], v[126:129]
	v_mfma_f32_16x16x32_bf16 v[122:125], v[142:145], v[166:169], v[122:125]
	v_mfma_f32_16x16x32_bf16 v[114:117], v[134:137], v[174:177], v[114:117]
	v_mfma_f32_16x16x32_bf16 v[106:109], v[142:145], v[174:177], v[106:109]
	v_mfma_f32_16x16x32_bf16 v[94:97], v[134:137], v[182:185], v[94:97]
	v_mfma_f32_16x16x32_bf16 v[90:93], v[142:145], v[182:185], v[90:93]
	s_waitcnt lgkmcnt(0)
	v_mfma_f32_16x16x32_bf16 v[86:89], v[134:137], v[190:193], v[86:89]
	v_mfma_f32_16x16x32_bf16 v[78:81], v[142:145], v[190:193], v[78:81]
	s_setprio 0
	s_setprio 1
	v_mfma_f32_16x16x32_bf16 v[118:121], v[146:149], v[162:165], 0
	v_mfma_f32_16x16x32_bf16 v[110:113], v[154:157], v[162:165], 0
	v_mfma_f32_16x16x32_bf16 v[102:105], v[146:149], v[170:173], 0
	v_mfma_f32_16x16x32_bf16 v[98:101], v[154:157], v[170:173], 0
	v_mfma_f32_16x16x32_bf16 v[82:85], v[146:149], v[178:181], 0
	v_mfma_f32_16x16x32_bf16 v[74:77], v[154:157], v[178:181], 0
	v_mfma_f32_16x16x32_bf16 v[70:73], v[146:149], v[186:189], 0
	v_mfma_f32_16x16x32_bf16 v[66:69], v[154:157], v[186:189], 0
	v_mfma_f32_16x16x32_bf16 v[118:121], v[150:153], v[166:169], v[118:121]
	v_mfma_f32_16x16x32_bf16 v[110:113], v[158:161], v[166:169], v[110:113]
	v_mfma_f32_16x16x32_bf16 v[102:105], v[150:153], v[174:177], v[102:105]
	v_mfma_f32_16x16x32_bf16 v[98:101], v[158:161], v[174:177], v[98:101]
	v_mfma_f32_16x16x32_bf16 v[82:85], v[150:153], v[182:185], v[82:85]
	v_mfma_f32_16x16x32_bf16 v[74:77], v[158:161], v[182:185], v[74:77]
	v_mfma_f32_16x16x32_bf16 v[70:73], v[150:153], v[190:193], v[70:73]
	v_mfma_f32_16x16x32_bf16 v[66:69], v[158:161], v[190:193], v[66:69]
	s_setprio 0
	s_barrier
	ds_read_b128 v[162:165], v236 offset:16384
	ds_read_b128 v[166:169], v236 offset:17408
	ds_read_b128 v[170:173], v236 offset:18432
	ds_read_b128 v[174:177], v236 offset:19456
	ds_read_b128 v[178:181], v236 offset:20480
	ds_read_b128 v[182:185], v236 offset:21504
	ds_read_b128 v[186:189], v236 offset:22528
	ds_read_b128 v[190:193], v236 offset:23552
	s_mov_b32 s58, m0
	s_mov_b32 m0, s30
	s_nop 0
	global_load_lds_dwordx4 v229, s[64:65]
	s_mov_b32 m0, s58
	s_nop 0
	s_mov_b32 s58, m0
	s_mov_b32 m0, s31
	s_nop 0
	global_load_lds_dwordx4 v231, s[64:65]
	s_mov_b32 m0, s58
	s_add_u32 s58, s64, 0x40000
	s_addc_u32 s59, s65, 0
	s_mov_b32 s88, m0
	s_mov_b32 m0, s34
	s_nop 0
	global_load_lds_dwordx4 v229, s[58:59]
	s_mov_b32 m0, s88
	s_nop 0
	s_mov_b32 s88, m0
	s_mov_b32 m0, s35
	s_nop 0
	global_load_lds_dwordx4 v231, s[58:59]
	s_mov_b32 m0, s88
	s_mov_b32 s58, m0
	s_mov_b32 m0, s28
	s_nop 0
	global_load_lds_dwordx4 v228, s[66:67]
	s_mov_b32 m0, s58
	s_nop 0
	s_mov_b32 s58, m0
	s_mov_b32 m0, s36
	s_nop 0
	global_load_lds_dwordx4 v230, s[66:67]
	s_mov_b32 m0, s58
	s_waitcnt vmcnt(8)
	s_waitcnt lgkmcnt(0)
	s_barrier
	s_setprio 1
	s_waitcnt lgkmcnt(7)
	v_mfma_f32_16x16x32_bf16 v[62:65], v[130:133], v[162:165], 0
	v_mfma_f32_16x16x32_bf16 v[58:61], v[138:141], v[162:165], 0
	s_waitcnt lgkmcnt(5)
	v_mfma_f32_16x16x32_bf16 v[54:57], v[130:133], v[170:173], 0
	v_mfma_f32_16x16x32_bf16 v[46:49], v[138:141], v[170:173], 0
	s_waitcnt lgkmcnt(3)
	v_mfma_f32_16x16x32_bf16 v[38:41], v[130:133], v[178:181], 0
	v_mfma_f32_16x16x32_bf16 v[30:33], v[138:141], v[178:181], 0
	s_waitcnt lgkmcnt(1)
	v_mfma_f32_16x16x32_bf16 v[22:25], v[130:133], v[186:189], 0
	v_mfma_f32_16x16x32_bf16 v[14:17], v[138:141], v[186:189], 0
	v_mfma_f32_16x16x32_bf16 v[62:65], v[134:137], v[166:169], v[62:65]
	v_mfma_f32_16x16x32_bf16 v[58:61], v[142:145], v[166:169], v[58:61]
	v_mfma_f32_16x16x32_bf16 v[54:57], v[134:137], v[174:177], v[54:57]
	v_mfma_f32_16x16x32_bf16 v[46:49], v[142:145], v[174:177], v[46:49]
	v_mfma_f32_16x16x32_bf16 v[38:41], v[134:137], v[182:185], v[38:41]
	v_mfma_f32_16x16x32_bf16 v[30:33], v[142:145], v[182:185], v[30:33]
	s_waitcnt lgkmcnt(0)
	v_mfma_f32_16x16x32_bf16 v[22:25], v[134:137], v[190:193], v[22:25]
	v_mfma_f32_16x16x32_bf16 v[14:17], v[142:145], v[190:193], v[14:17]
	s_setprio 0
	s_setprio 1
	v_mfma_f32_16x16x32_bf16 v[50:53], v[146:149], v[162:165], 0
	v_mfma_f32_16x16x32_bf16 v[42:45], v[154:157], v[162:165], 0
	v_mfma_f32_16x16x32_bf16 v[34:37], v[146:149], v[170:173], 0
	v_mfma_f32_16x16x32_bf16 v[26:29], v[154:157], v[170:173], 0
	v_mfma_f32_16x16x32_bf16 v[18:21], v[146:149], v[178:181], 0
	v_mfma_f32_16x16x32_bf16 v[10:13], v[154:157], v[178:181], 0
	v_mfma_f32_16x16x32_bf16 v[6:9], v[146:149], v[186:189], 0
	v_mfma_f32_16x16x32_bf16 v[2:5], v[154:157], v[186:189], 0
	v_mfma_f32_16x16x32_bf16 v[50:53], v[150:153], v[166:169], v[50:53]
	v_mfma_f32_16x16x32_bf16 v[42:45], v[158:161], v[166:169], v[42:45]
	v_mfma_f32_16x16x32_bf16 v[34:37], v[150:153], v[174:177], v[34:37]
	v_mfma_f32_16x16x32_bf16 v[26:29], v[158:161], v[174:177], v[26:29]
	v_mfma_f32_16x16x32_bf16 v[18:21], v[150:153], v[182:185], v[18:21]
	v_mfma_f32_16x16x32_bf16 v[10:13], v[158:161], v[182:185], v[10:13]
	v_mfma_f32_16x16x32_bf16 v[6:9], v[150:153], v[190:193], v[6:9]
	v_mfma_f32_16x16x32_bf16 v[2:5], v[158:161], v[190:193], v[2:5]
	s_setprio 0
	s_barrier
	s_branch .Lmid1440
.LBB0_1440:
	ds_read_b128 v[130:133], v234
	ds_read_b128 v[134:137], v234 offset:1024
	ds_read_b128 v[138:141], v234 offset:2048
	ds_read_b128 v[142:145], v234 offset:3072
	ds_read_b128 v[146:149], v235
	ds_read_b128 v[150:153], v235 offset:1024
	ds_read_b128 v[154:157], v235 offset:2048
	ds_read_b128 v[158:161], v235 offset:3072
	s_add_u32 s60, s58, 0x100
	s_addc_u32 s61, s59, 0
	s_cmp_eq_u32 s87, 12
	s_cselect_b32 s66, s33, s60
	s_cselect_b32 s67, s21, s61
	s_cselect_b32 s64, s84, s85
	s_cselect_b32 s65, s19, s86
	s_add_u32 s62, s66, 0x80
	s_addc_u32 s63, s67, 0
	ds_read_b128 v[162:165], v236
	ds_read_b128 v[166:169], v236 offset:1024
	ds_read_b128 v[170:173], v236 offset:2048
	ds_read_b128 v[174:177], v236 offset:3072
	ds_read_b128 v[178:181], v236 offset:4096
	ds_read_b128 v[182:185], v236 offset:5120
	ds_read_b128 v[186:189], v236 offset:6144
	ds_read_b128 v[190:193], v236 offset:7168
	s_add_u32 s58, s58, 0x40080
	s_addc_u32 s59, s59, 0
	s_mov_b32 s88, m0
	s_mov_b32 m0, s80
	s_nop 0
	global_load_lds_dwordx4 v228, s[58:59]
	s_mov_b32 m0, s88
	s_nop 0
	s_mov_b32 s88, m0
	s_mov_b32 m0, s81
	s_nop 0
	global_load_lds_dwordx4 v230, s[58:59]
	s_mov_b32 m0, s88
	s_waitcnt vmcnt(8)
	s_waitcnt lgkmcnt(0)
	s_barrier
	s_setprio 1
	s_waitcnt lgkmcnt(7)
	v_mfma_f32_16x16x32_bf16 v[126:129], v[130:133], v[162:165], v[126:129]
	v_mfma_f32_16x16x32_bf16 v[122:125], v[138:141], v[162:165], v[122:125]
	s_waitcnt lgkmcnt(5)
	v_mfma_f32_16x16x32_bf16 v[114:117], v[130:133], v[170:173], v[114:117]
	v_mfma_f32_16x16x32_bf16 v[106:109], v[138:141], v[170:173], v[106:109]
	s_waitcnt lgkmcnt(3)
	v_mfma_f32_16x16x32_bf16 v[94:97], v[130:133], v[178:181], v[94:97]
	v_mfma_f32_16x16x32_bf16 v[90:93], v[138:141], v[178:181], v[90:93]
	s_waitcnt lgkmcnt(1)
	v_mfma_f32_16x16x32_bf16 v[86:89], v[130:133], v[186:189], v[86:89]
	v_mfma_f32_16x16x32_bf16 v[78:81], v[138:141], v[186:189], v[78:81]
	v_mfma_f32_16x16x32_bf16 v[126:129], v[134:137], v[166:169], v[126:129]
	v_mfma_f32_16x16x32_bf16 v[122:125], v[142:145], v[166:169], v[122:125]
	v_mfma_f32_16x16x32_bf16 v[114:117], v[134:137], v[174:177], v[114:117]
	v_mfma_f32_16x16x32_bf16 v[106:109], v[142:145], v[174:177], v[106:109]
	v_mfma_f32_16x16x32_bf16 v[94:97], v[134:137], v[182:185], v[94:97]
	v_mfma_f32_16x16x32_bf16 v[90:93], v[142:145], v[182:185], v[90:93]
	s_waitcnt lgkmcnt(0)
	v_mfma_f32_16x16x32_bf16 v[86:89], v[134:137], v[190:193], v[86:89]
	v_mfma_f32_16x16x32_bf16 v[78:81], v[142:145], v[190:193], v[78:81]
	s_setprio 0
	s_setprio 1
	v_mfma_f32_16x16x32_bf16 v[118:121], v[146:149], v[162:165], v[118:121]
	v_mfma_f32_16x16x32_bf16 v[110:113], v[154:157], v[162:165], v[110:113]
	v_mfma_f32_16x16x32_bf16 v[102:105], v[146:149], v[170:173], v[102:105]
	v_mfma_f32_16x16x32_bf16 v[98:101], v[154:157], v[170:173], v[98:101]
	v_mfma_f32_16x16x32_bf16 v[82:85], v[146:149], v[178:181], v[82:85]
	v_mfma_f32_16x16x32_bf16 v[74:77], v[154:157], v[178:181], v[74:77]
	v_mfma_f32_16x16x32_bf16 v[70:73], v[146:149], v[186:189], v[70:73]
	v_mfma_f32_16x16x32_bf16 v[66:69], v[154:157], v[186:189], v[66:69]
	v_mfma_f32_16x16x32_bf16 v[118:121], v[150:153], v[166:169], v[118:121]
	v_mfma_f32_16x16x32_bf16 v[110:113], v[158:161], v[166:169], v[110:113]
	v_mfma_f32_16x16x32_bf16 v[102:105], v[150:153], v[174:177], v[102:105]
	v_mfma_f32_16x16x32_bf16 v[98:101], v[158:161], v[174:177], v[98:101]
	v_mfma_f32_16x16x32_bf16 v[82:85], v[150:153], v[182:185], v[82:85]
	v_mfma_f32_16x16x32_bf16 v[74:77], v[158:161], v[182:185], v[74:77]
	v_mfma_f32_16x16x32_bf16 v[70:73], v[150:153], v[190:193], v[70:73]
	v_mfma_f32_16x16x32_bf16 v[66:69], v[158:161], v[190:193], v[66:69]
	s_setprio 0
	s_barrier
	ds_read_b128 v[162:165], v236 offset:16384
	ds_read_b128 v[166:169], v236 offset:17408
	ds_read_b128 v[170:173], v236 offset:18432
	ds_read_b128 v[174:177], v236 offset:19456
	ds_read_b128 v[178:181], v236 offset:20480
	ds_read_b128 v[182:185], v236 offset:21504
	ds_read_b128 v[186:189], v236 offset:22528
	ds_read_b128 v[190:193], v236 offset:23552
	s_mov_b32 s58, m0
	s_mov_b32 m0, s30
	s_nop 0
	global_load_lds_dwordx4 v229, s[64:65]
	s_mov_b32 m0, s58
	s_nop 0
	s_mov_b32 s58, m0
	s_mov_b32 m0, s31
	s_nop 0
	global_load_lds_dwordx4 v231, s[64:65]
	s_mov_b32 m0, s58
	s_add_u32 s58, s64, 0x40000
	s_addc_u32 s59, s65, 0
	s_mov_b32 s88, m0
	s_mov_b32 m0, s34
	s_nop 0
	global_load_lds_dwordx4 v229, s[58:59]
	s_mov_b32 m0, s88
	s_nop 0
	s_mov_b32 s88, m0
	s_mov_b32 m0, s35
	s_nop 0
	global_load_lds_dwordx4 v231, s[58:59]
	s_mov_b32 m0, s88
	s_mov_b32 s58, m0
	s_mov_b32 m0, s28
	s_nop 0
	global_load_lds_dwordx4 v228, s[66:67]
	s_mov_b32 m0, s58
	s_nop 0
	s_mov_b32 s58, m0
	s_mov_b32 m0, s36
	s_nop 0
	global_load_lds_dwordx4 v230, s[66:67]
	s_mov_b32 m0, s58
	s_waitcnt vmcnt(8)
	s_waitcnt lgkmcnt(0)
	s_barrier
	s_setprio 1
	s_waitcnt lgkmcnt(7)
	v_mfma_f32_16x16x32_bf16 v[62:65], v[130:133], v[162:165], v[62:65]
	v_mfma_f32_16x16x32_bf16 v[58:61], v[138:141], v[162:165], v[58:61]
	s_waitcnt lgkmcnt(5)
	v_mfma_f32_16x16x32_bf16 v[54:57], v[130:133], v[170:173], v[54:57]
	v_mfma_f32_16x16x32_bf16 v[46:49], v[138:141], v[170:173], v[46:49]
	s_waitcnt lgkmcnt(3)
	v_mfma_f32_16x16x32_bf16 v[38:41], v[130:133], v[178:181], v[38:41]
	v_mfma_f32_16x16x32_bf16 v[30:33], v[138:141], v[178:181], v[30:33]
	s_waitcnt lgkmcnt(1)
	v_mfma_f32_16x16x32_bf16 v[22:25], v[130:133], v[186:189], v[22:25]
	v_mfma_f32_16x16x32_bf16 v[14:17], v[138:141], v[186:189], v[14:17]
	v_mfma_f32_16x16x32_bf16 v[62:65], v[134:137], v[166:169], v[62:65]
	v_mfma_f32_16x16x32_bf16 v[58:61], v[142:145], v[166:169], v[58:61]
	v_mfma_f32_16x16x32_bf16 v[54:57], v[134:137], v[174:177], v[54:57]
	v_mfma_f32_16x16x32_bf16 v[46:49], v[142:145], v[174:177], v[46:49]
	v_mfma_f32_16x16x32_bf16 v[38:41], v[134:137], v[182:185], v[38:41]
	v_mfma_f32_16x16x32_bf16 v[30:33], v[142:145], v[182:185], v[30:33]
	s_waitcnt lgkmcnt(0)
	v_mfma_f32_16x16x32_bf16 v[22:25], v[134:137], v[190:193], v[22:25]
	v_mfma_f32_16x16x32_bf16 v[14:17], v[142:145], v[190:193], v[14:17]
	s_setprio 0
	s_setprio 1
	v_mfma_f32_16x16x32_bf16 v[50:53], v[146:149], v[162:165], v[50:53]
	v_mfma_f32_16x16x32_bf16 v[42:45], v[154:157], v[162:165], v[42:45]
	v_mfma_f32_16x16x32_bf16 v[34:37], v[146:149], v[170:173], v[34:37]
	v_mfma_f32_16x16x32_bf16 v[26:29], v[154:157], v[170:173], v[26:29]
	v_mfma_f32_16x16x32_bf16 v[18:21], v[146:149], v[178:181], v[18:21]
	v_mfma_f32_16x16x32_bf16 v[10:13], v[154:157], v[178:181], v[10:13]
	v_mfma_f32_16x16x32_bf16 v[6:9], v[146:149], v[186:189], v[6:9]
	v_mfma_f32_16x16x32_bf16 v[2:5], v[154:157], v[186:189], v[2:5]
	v_mfma_f32_16x16x32_bf16 v[50:53], v[150:153], v[166:169], v[50:53]
	v_mfma_f32_16x16x32_bf16 v[42:45], v[158:161], v[166:169], v[42:45]
	v_mfma_f32_16x16x32_bf16 v[34:37], v[150:153], v[174:177], v[34:37]
	v_mfma_f32_16x16x32_bf16 v[26:29], v[158:161], v[174:177], v[26:29]
	v_mfma_f32_16x16x32_bf16 v[18:21], v[150:153], v[182:185], v[18:21]
	v_mfma_f32_16x16x32_bf16 v[10:13], v[158:161], v[182:185], v[10:13]
	v_mfma_f32_16x16x32_bf16 v[6:9], v[150:153], v[190:193], v[6:9]
	v_mfma_f32_16x16x32_bf16 v[2:5], v[158:161], v[190:193], v[2:5]
	s_setprio 0
	s_barrier
.Lmid1440:
	ds_read_b128 v[130:133], v237
	ds_read_b128 v[134:137], v237 offset:1024
	ds_read_b128 v[138:141], v237 offset:2048
	ds_read_b128 v[142:145], v237 offset:3072
	ds_read_b128 v[146:149], v238
	ds_read_b128 v[150:153], v238 offset:1024
	ds_read_b128 v[154:157], v238 offset:2048
	ds_read_b128 v[158:161], v238 offset:3072
	ds_read_b128 v[162:165], v236 offset:32768
	ds_read_b128 v[166:169], v236 offset:33792
	ds_read_b128 v[170:173], v236 offset:34816
	ds_read_b128 v[174:177], v236 offset:35840
	ds_read_b128 v[178:181], v236 offset:36864
	ds_read_b128 v[182:185], v236 offset:37888
	ds_read_b128 v[186:189], v236 offset:38912
	ds_read_b128 v[190:193], v236 offset:39936
	s_add_u32 s58, s66, 0x40000
	s_addc_u32 s59, s67, 0
	s_mov_b32 s66, m0
	s_mov_b32 m0, s37
	s_nop 0
	global_load_lds_dwordx4 v228, s[58:59]
	s_mov_b32 m0, s66
	s_nop 0
	s_mov_b32 s66, m0
	s_mov_b32 m0, s52
	s_nop 0
	global_load_lds_dwordx4 v230, s[58:59]
	s_mov_b32 m0, s66
	s_waitcnt vmcnt(8)
	s_waitcnt lgkmcnt(0)
	s_barrier
	s_setprio 1
	s_waitcnt lgkmcnt(7)
	v_mfma_f32_16x16x32_bf16 v[126:129], v[130:133], v[162:165], v[126:129]
	v_mfma_f32_16x16x32_bf16 v[122:125], v[138:141], v[162:165], v[122:125]
	s_waitcnt lgkmcnt(5)
	v_mfma_f32_16x16x32_bf16 v[114:117], v[130:133], v[170:173], v[114:117]
	v_mfma_f32_16x16x32_bf16 v[106:109], v[138:141], v[170:173], v[106:109]
	s_waitcnt lgkmcnt(3)
	v_mfma_f32_16x16x32_bf16 v[94:97], v[130:133], v[178:181], v[94:97]
	v_mfma_f32_16x16x32_bf16 v[90:93], v[138:141], v[178:181], v[90:93]
	s_waitcnt lgkmcnt(1)
	v_mfma_f32_16x16x32_bf16 v[86:89], v[130:133], v[186:189], v[86:89]
	v_mfma_f32_16x16x32_bf16 v[78:81], v[138:141], v[186:189], v[78:81]
	v_mfma_f32_16x16x32_bf16 v[126:129], v[134:137], v[166:169], v[126:129]
	v_mfma_f32_16x16x32_bf16 v[122:125], v[142:145], v[166:169], v[122:125]
	v_mfma_f32_16x16x32_bf16 v[114:117], v[134:137], v[174:177], v[114:117]
	v_mfma_f32_16x16x32_bf16 v[106:109], v[142:145], v[174:177], v[106:109]
	v_mfma_f32_16x16x32_bf16 v[94:97], v[134:137], v[182:185], v[94:97]
	v_mfma_f32_16x16x32_bf16 v[90:93], v[142:145], v[182:185], v[90:93]
	s_waitcnt lgkmcnt(0)
	v_mfma_f32_16x16x32_bf16 v[86:89], v[134:137], v[190:193], v[86:89]
	v_mfma_f32_16x16x32_bf16 v[78:81], v[142:145], v[190:193], v[78:81]
	s_setprio 0
	s_setprio 1
	v_mfma_f32_16x16x32_bf16 v[118:121], v[146:149], v[162:165], v[118:121]
	v_mfma_f32_16x16x32_bf16 v[110:113], v[154:157], v[162:165], v[110:113]
	v_mfma_f32_16x16x32_bf16 v[102:105], v[146:149], v[170:173], v[102:105]
	v_mfma_f32_16x16x32_bf16 v[98:101], v[154:157], v[170:173], v[98:101]
	v_mfma_f32_16x16x32_bf16 v[82:85], v[146:149], v[178:181], v[82:85]
	v_mfma_f32_16x16x32_bf16 v[74:77], v[154:157], v[178:181], v[74:77]
	v_mfma_f32_16x16x32_bf16 v[70:73], v[146:149], v[186:189], v[70:73]
	v_mfma_f32_16x16x32_bf16 v[66:69], v[154:157], v[186:189], v[66:69]
	v_mfma_f32_16x16x32_bf16 v[118:121], v[150:153], v[166:169], v[118:121]
	v_mfma_f32_16x16x32_bf16 v[110:113], v[158:161], v[166:169], v[110:113]
	v_mfma_f32_16x16x32_bf16 v[102:105], v[150:153], v[174:177], v[102:105]
	v_mfma_f32_16x16x32_bf16 v[98:101], v[158:161], v[174:177], v[98:101]
	v_mfma_f32_16x16x32_bf16 v[82:85], v[150:153], v[182:185], v[82:85]
	v_mfma_f32_16x16x32_bf16 v[74:77], v[158:161], v[182:185], v[74:77]
	v_mfma_f32_16x16x32_bf16 v[70:73], v[150:153], v[190:193], v[70:73]
	v_mfma_f32_16x16x32_bf16 v[66:69], v[158:161], v[190:193], v[66:69]
	s_setprio 0
	s_barrier
	ds_read_b128 v[162:165], v236 offset:49152
	ds_read_b128 v[166:169], v236 offset:50176
	ds_read_b128 v[170:173], v236 offset:51200
	ds_read_b128 v[174:177], v236 offset:52224
	ds_read_b128 v[178:181], v236 offset:53248
	ds_read_b128 v[182:185], v236 offset:54272
	ds_read_b128 v[186:189], v236 offset:55296
	ds_read_b128 v[190:193], v236 offset:56320
	s_add_u32 s58, s64, 0x80
	s_addc_u32 s59, s65, 0
	s_mov_b32 s66, m0
	s_mov_b32 m0, s68
	s_nop 0
	global_load_lds_dwordx4 v229, s[58:59]
	s_mov_b32 m0, s66
	s_nop 0
	s_mov_b32 s66, m0
	s_mov_b32 m0, s69
	s_nop 0
	global_load_lds_dwordx4 v231, s[58:59]
	s_mov_b32 m0, s66
	s_add_u32 s58, s64, 0x40080
	s_addc_u32 s59, s65, 0
	s_mov_b32 s64, m0
	s_mov_b32 m0, s78
	s_nop 0
	global_load_lds_dwordx4 v229, s[58:59]
	s_mov_b32 m0, s64
	s_nop 0
	s_mov_b32 s64, m0
	s_mov_b32 m0, s79
	s_nop 0
	global_load_lds_dwordx4 v231, s[58:59]
	s_mov_b32 m0, s64
	s_mov_b32 s58, m0
	s_mov_b32 m0, s76
	s_nop 0
	global_load_lds_dwordx4 v228, s[62:63]
	s_mov_b32 m0, s58
	s_nop 0
	s_mov_b32 s58, m0
	s_mov_b32 m0, s77
	s_nop 0
	global_load_lds_dwordx4 v230, s[62:63]
	s_mov_b32 m0, s58
	s_waitcnt vmcnt(8)
	s_waitcnt lgkmcnt(0)
	s_barrier
	s_setprio 1
	s_waitcnt lgkmcnt(7)
	v_mfma_f32_16x16x32_bf16 v[62:65], v[130:133], v[162:165], v[62:65]
	v_mfma_f32_16x16x32_bf16 v[58:61], v[138:141], v[162:165], v[58:61]
	s_waitcnt lgkmcnt(5)
	v_mfma_f32_16x16x32_bf16 v[54:57], v[130:133], v[170:173], v[54:57]
	v_mfma_f32_16x16x32_bf16 v[46:49], v[138:141], v[170:173], v[46:49]
	s_waitcnt lgkmcnt(3)
	v_mfma_f32_16x16x32_bf16 v[38:41], v[130:133], v[178:181], v[38:41]
	v_mfma_f32_16x16x32_bf16 v[30:33], v[138:141], v[178:181], v[30:33]
	s_waitcnt lgkmcnt(1)
	v_mfma_f32_16x16x32_bf16 v[22:25], v[130:133], v[186:189], v[22:25]
	v_mfma_f32_16x16x32_bf16 v[14:17], v[138:141], v[186:189], v[14:17]
	v_mfma_f32_16x16x32_bf16 v[62:65], v[134:137], v[166:169], v[62:65]
	v_mfma_f32_16x16x32_bf16 v[58:61], v[142:145], v[166:169], v[58:61]
	v_mfma_f32_16x16x32_bf16 v[54:57], v[134:137], v[174:177], v[54:57]
	v_mfma_f32_16x16x32_bf16 v[46:49], v[142:145], v[174:177], v[46:49]
	v_mfma_f32_16x16x32_bf16 v[38:41], v[134:137], v[182:185], v[38:41]
	v_mfma_f32_16x16x32_bf16 v[30:33], v[142:145], v[182:185], v[30:33]
	s_waitcnt lgkmcnt(0)
	v_mfma_f32_16x16x32_bf16 v[22:25], v[134:137], v[190:193], v[22:25]
	v_mfma_f32_16x16x32_bf16 v[14:17], v[142:145], v[190:193], v[14:17]
	s_setprio 0
	s_setprio 1
	v_mfma_f32_16x16x32_bf16 v[50:53], v[146:149], v[162:165], v[50:53]
	v_mfma_f32_16x16x32_bf16 v[42:45], v[154:157], v[162:165], v[42:45]
	v_mfma_f32_16x16x32_bf16 v[34:37], v[146:149], v[170:173], v[34:37]
	v_mfma_f32_16x16x32_bf16 v[26:29], v[154:157], v[170:173], v[26:29]
	v_mfma_f32_16x16x32_bf16 v[18:21], v[146:149], v[178:181], v[18:21]
	v_mfma_f32_16x16x32_bf16 v[10:13], v[154:157], v[178:181], v[10:13]
	v_mfma_f32_16x16x32_bf16 v[6:9], v[146:149], v[186:189], v[6:9]
	v_mfma_f32_16x16x32_bf16 v[2:5], v[154:157], v[186:189], v[2:5]
	v_mfma_f32_16x16x32_bf16 v[50:53], v[150:153], v[166:169], v[50:53]
	v_mfma_f32_16x16x32_bf16 v[42:45], v[158:161], v[166:169], v[42:45]
	v_mfma_f32_16x16x32_bf16 v[34:37], v[150:153], v[174:177], v[34:37]
	v_mfma_f32_16x16x32_bf16 v[26:29], v[158:161], v[174:177], v[26:29]
	v_mfma_f32_16x16x32_bf16 v[18:21], v[150:153], v[182:185], v[18:21]
	v_mfma_f32_16x16x32_bf16 v[10:13], v[158:161], v[182:185], v[10:13]
	v_mfma_f32_16x16x32_bf16 v[6:9], v[150:153], v[190:193], v[6:9]
	v_mfma_f32_16x16x32_bf16 v[2:5], v[158:161], v[190:193], v[2:5]
	s_setprio 0
	s_barrier
	s_add_i32 s87, s87, 2
	s_add_u32 s85, s85, 0x100
	s_addc_u32 s86, s86, 0
	s_cmp_gt_u32 s87, 13
	s_mov_b64 s[58:59], s[60:61]
	s_cbranch_scc0 .LBB0_1440
	s_and_b64 vcc, exec, s[16:17]
	s_cbranch_vccz .LBB0_1443
	s_barrier

.LBB0_1717:
	s_mov_b32 s0, m0
	s_mov_b32 m0, s3
	s_nop 0
	global_load_lds_dwordx4 v178, s[12:13]
	s_mov_b32 m0, s0
	s_and_b64 vcc, exec, s[8:9]
	s_mov_b32 s0, m0
	s_mov_b32 m0, s26
	s_nop 0
	global_load_lds_dwordx4 v179, s[12:13]
	s_mov_b32 m0, s0
	s_nop 0
	s_mov_b32 s0, m0
	s_mov_b32 m0, s27
	s_nop 0
	global_load_lds_dwordx4 v180, s[12:13]
	s_mov_b32 m0, s0
	s_nop 0
	s_mov_b32 s0, m0
	s_mov_b32 m0, s34
	s_nop 0
	global_load_lds_dwordx4 v181, s[12:13]
	s_mov_b32 m0, s0
	s_nop 0
	s_mov_b32 s0, m0
	s_mov_b32 m0, s35
	s_nop 0
	global_load_lds_dwordx4 v182, s[12:13]
	s_mov_b32 m0, s0
	s_nop 0
	s_mov_b32 s0, m0
	s_mov_b32 m0, s56
	s_nop 0
	global_load_lds_dwordx4 v183, s[12:13]
	s_mov_b32 m0, s0
	s_nop 0
	s_mov_b32 s0, m0
	s_mov_b32 m0, s57
	s_nop 0
	global_load_lds_dwordx4 v184, s[12:13]
	s_mov_b32 m0, s0
	s_nop 0
	s_mov_b32 s0, m0
	s_mov_b32 m0, s58
	s_nop 0
	global_load_lds_dwordx4 v185, s[12:13]
	s_mov_b32 m0, s0
	s_nop 0
	s_mov_b32 s0, m0
	s_mov_b32 m0, s59
	s_nop 0
	global_load_lds_dwordx4 v186, s[12:13]
	s_mov_b32 m0, s0
	s_nop 0
	s_mov_b32 s0, m0
	s_mov_b32 m0, s60
	s_nop 0
	global_load_lds_dwordx4 v187, s[12:13]
	s_mov_b32 m0, s0
	s_nop 0
	s_mov_b32 s0, m0
	s_mov_b32 m0, s61
	s_nop 0
	global_load_lds_dwordx4 v188, s[12:13]
	s_mov_b32 m0, s0
	s_nop 0
	s_mov_b32 s0, m0
	s_mov_b32 m0, s62
	s_nop 0
	global_load_lds_dwordx4 v189, s[12:13]
	s_mov_b32 m0, s0
	s_nop 0
	s_mov_b32 s0, m0
	s_mov_b32 m0, s63
	s_nop 0
	global_load_lds_dwordx4 v190, s[12:13]
	s_mov_b32 m0, s0
	s_nop 0
	s_mov_b32 s0, m0
	s_mov_b32 m0, s64
	s_nop 0
	global_load_lds_dwordx4 v191, s[12:13]
	s_mov_b32 m0, s0
	s_nop 0
	s_mov_b32 s0, m0
	s_mov_b32 m0, s65
	s_nop 0
	global_load_lds_dwordx4 v192, s[12:13]
	s_mov_b32 m0, s0
	s_nop 0
	s_mov_b32 s0, m0
	s_mov_b32 m0, s66
	s_nop 0
	global_load_lds_dwordx4 v193, s[12:13]
	s_mov_b32 m0, s0
	s_waitcnt vmcnt(0)
	s_waitcnt lgkmcnt(0)
	s_barrier
	s_cbranch_vccnz .LBB0_1721
	v_add_u32_e32 v136, v175, v194
	ds_read_b128 v[132:135], v136
	ds_read_b128 v[136:139], v136 offset:32768
	v_add_u32_e32 v140, v176, v194
	ds_read_b128 v[140:143], v140
	v_add_u32_e32 v144, v177, v194
	s_waitcnt vmcnt(31) lgkmcnt(2)
	v_mfma_f32_16x16x32_bf16 v[132:135], v[126:129], v[132:135], 0
	ds_read_b128 v[144:147], v144
	v_and_b32_e32 v149, 0xffff0000, v127
	v_med3_f32 v150, v149, s78, v240
	s_waitcnt lgkmcnt(2)
	v_mfma_f32_16x16x32_bf16 v[136:139], v[126:129], v[136:139], 0
	v_lshlrev_b32_e32 v151, 16, v128
	v_and_b32_e32 v153, 0xffff0000, v128
	v_med3_f32 v152, v151, s78, v240
	s_waitcnt lgkmcnt(1)
	v_mfma_f32_16x16x32_bf16 v[132:135], v[126:129], v[140:143], v[132:135]
	v_lshlrev_b32_e32 v141, 16, v126
	v_and_b32_e32 v143, 0xffff0000, v126
	v_med3_f32 v154, v153, s78, v240
	s_waitcnt lgkmcnt(0)
	v_mfma_f32_16x16x32_bf16 v[136:139], v[126:129], v[144:147], v[136:139]
	v_med3_f32 v145, v141, s78, v240
	v_med3_f32 v146, v143, s78, v240
	v_mov_b32_e32 v144, 0
	v_cvt_pk_fp8_f32 v144, v145, v146
	v_lshlrev_b32_e32 v147, 16, v127
	v_med3_f32 v145, v147, s78, v240
	v_lshlrev_b32_e32 v155, 16, v129
	v_cvt_pk_fp8_f32 v144, v145, v150 op_sel:[0,0,1]
	v_mov_b32_e32 v145, 0
	v_cvt_pk_fp8_f32 v145, v152, v154
	v_and_b32_e32 v157, 0xffff0000, v129
	v_med3_f32 v152, v155, s78, v240
	v_med3_f32 v154, v157, s78, v240
	v_cvt_pk_fp8_f32 v145, v152, v154 op_sel:[0,0,1]
	v_lshlrev_b64 v[130:131], 10, v[130:131]
	v_lshl_add_u64 v[130:131], v[164:165], 0, v[130:131]
	s_waitcnt vmcnt(30)
	v_and_b32_e32 v142, 0xffff0000, v122
	v_lshlrev_b32_e32 v140, 16, v122
	v_and_b32_e32 v148, 0xffff0000, v123
	global_store_dwordx2 v[130:131], v[144:145], off
	v_pk_mul_f32 v[144:145], v[142:143], v[142:143]
	v_lshlrev_b32_e32 v146, 16, v123
	v_pk_fma_f32 v[144:145], v[140:141], v[140:141], v[144:145]
	v_pk_mul_f32 v[158:159], v[148:149], v[148:149]
	v_med3_f32 v140, v140, s78, v240
	v_med3_f32 v141, v142, s78, v240
	v_mov_b32_e32 v160, 0
	v_and_b32_e32 v152, 0xffff0000, v124
	v_pk_fma_f32 v[158:159], v[146:147], v[146:147], v[158:159]
	v_cvt_pk_fp8_f32 v160, v140, v141
	v_lshlrev_b32_e32 v150, 16, v124
	v_pk_add_f32 v[144:145], v[144:145], v[158:159]
	v_pk_mul_f32 v[158:159], v[152:153], v[152:153]
	v_and_b32_e32 v156, 0xffff0000, v125
	v_pk_fma_f32 v[158:159], v[150:151], v[150:151], v[158:159]
	v_lshlrev_b32_e32 v154, 16, v125
	v_pk_add_f32 v[158:159], v[158:159], v[144:145]
	v_pk_mul_f32 v[144:145], v[156:157], v[156:157]
	v_med3_f32 v140, v146, s78, v240
	v_med3_f32 v141, v148, s78, v240
	v_add_u32_e32 v146, v175, v195
	v_pk_fma_f32 v[244:245], v[154:155], v[154:155], v[144:145]
	v_cvt_pk_fp8_f32 v160, v140, v141 op_sel:[0,0,1]
	v_med3_f32 v144, v150, s78, v240
	v_med3_f32 v145, v152, s78, v240
	ds_read_b128 v[140:143], v146
	v_mov_b32_e32 v161, 0
	v_cvt_pk_fp8_f32 v161, v144, v145
	ds_read_b128 v[144:147], v146 offset:32768
	s_waitcnt lgkmcnt(1)
	v_mfma_f32_16x16x32_bf16 v[132:135], v[122:125], v[140:143], v[132:135]
	v_add_u32_e32 v140, v176, v195
	ds_read_b128 v[140:143], v140
	v_med3_f32 v148, v154, s78, v240
	s_waitcnt lgkmcnt(1)
	v_mfma_f32_16x16x32_bf16 v[136:139], v[122:125], v[144:147], v[136:139]
	v_add_u32_e32 v144, v177, v195
	ds_read_b128 v[144:147], v144
	v_med3_f32 v149, v156, s78, v240
	s_waitcnt lgkmcnt(1)
	v_mfma_f32_16x16x32_bf16 v[132:135], v[122:125], v[140:143], v[132:135]
	v_add_f32_e64 v140, v244, v158
	v_add_f32_e64 v141, v245, v159
	s_waitcnt vmcnt(30)
	v_and_b32_e32 v143, 0xffff0000, v119
	v_and_b32_e32 v142, 0xffff0000, v118
	v_cvt_pk_fp8_f32 v161, v148, v149 op_sel:[0,0,1]
	v_pk_add_f32 v[148:149], v[140:141], v[140:141] op_sel_hi:[0,1]
	s_waitcnt lgkmcnt(0)
	v_mfma_f32_16x16x32_bf16 v[136:139], v[122:125], v[144:147], v[136:139]
	v_lshlrev_b32_e32 v141, 16, v119
	v_lshlrev_b32_e32 v140, 16, v118
	v_pk_mul_f32 v[144:145], v[142:143], v[142:143]
	v_med3_f32 v142, v142, s78, v240
	v_pk_fma_f32 v[144:145], v[140:141], v[140:141], v[144:145]
	v_med3_f32 v140, v140, s78, v240
	v_mov_b32_e32 v154, 0
	v_cvt_pk_fp8_f32 v154, v140, v142
	v_and_b32_e32 v151, 0xffff0000, v121
	v_and_b32_e32 v150, 0xffff0000, v120
	v_lshlrev_b32_e32 v147, 16, v121
	v_lshlrev_b32_e32 v146, 16, v120
	v_pk_mul_f32 v[152:153], v[150:151], v[150:151]
	v_add_f32_e32 v148, v144, v145
	v_pk_fma_f32 v[152:153], v[146:147], v[146:147], v[152:153]
	v_med3_f32 v140, v141, s78, v240
	v_med3_f32 v141, v143, s78, v240
	v_med3_f32 v144, v146, s78, v240
	v_med3_f32 v145, v150, s78, v240
	v_add_u32_e32 v146, v175, v196
	v_mov_b32_e32 v155, 0
	v_cvt_pk_fp8_f32 v154, v140, v141 op_sel:[0,0,1]
	ds_read_b128 v[140:143], v146
	v_cvt_pk_fp8_f32 v155, v144, v145
	v_med3_f32 v150, v147, s78, v240
	ds_read_b128 v[144:147], v146 offset:32768
	s_waitcnt lgkmcnt(1)
	v_mfma_f32_16x16x32_bf16 v[132:135], v[118:121], v[140:143], v[132:135]
	v_add_u32_e32 v140, v176, v196
	ds_read_b128 v[140:143], v140
	v_med3_f32 v151, v151, s78, v240
	s_waitcnt lgkmcnt(1)
	v_mfma_f32_16x16x32_bf16 v[136:139], v[118:121], v[144:147], v[136:139]
	v_add_u32_e32 v144, v177, v196
	ds_read_b128 v[144:147], v144
	v_cvt_pk_fp8_f32 v155, v150, v151 op_sel:[0,0,1]
	s_waitcnt lgkmcnt(1)
	v_mfma_f32_16x16x32_bf16 v[132:135], v[118:121], v[140:143], v[132:135]
	v_add_f32_e32 v140, v152, v148
	v_pk_add_f32 v[150:151], v[152:153], v[140:141] op_sel_hi:[1,0]
	global_store_dwordx2 v[130:131], v[154:155], off offset:64
	s_waitcnt lgkmcnt(0)
	v_mfma_f32_16x16x32_bf16 v[136:139], v[118:121], v[144:147], v[136:139]
	s_waitcnt vmcnt(30)
	v_lshlrev_b32_e32 v144, 16, v114
	v_and_b32_e32 v145, 0xffff0000, v114
	v_mul_f32_e32 v140, v144, v144
	v_add_u32_e32 v147, v175, v197
	v_pk_fma_f32 v[152:153], v[144:145], v[144:145], v[140:141] op_sel_hi:[1,1,0]
	v_lshlrev_b32_e32 v154, 16, v115
	ds_read_b128 v[140:143], v147
	v_and_b32_e32 v155, 0xffff0000, v115
	v_mul_f32_e32 v146, v154, v154
	v_pk_fma_f32 v[156:157], v[154:155], v[154:155], v[146:147] op_sel_hi:[1,1,0]
	v_med3_f32 v148, v144, s78, v240
	v_med3_f32 v150, v145, s78, v240
	ds_read_b128 v[144:147], v147 offset:32768
	s_waitcnt lgkmcnt(1)
	v_mfma_f32_16x16x32_bf16 v[132:135], v[114:117], v[140:143], v[132:135]
	v_add_u32_e32 v140, v176, v197
	ds_read_b128 v[140:143], v140
	v_mov_b32_e32 v158, 0
	s_waitcnt lgkmcnt(1)
	v_mfma_f32_16x16x32_bf16 v[136:139], v[114:117], v[144:147], v[136:139]
	v_add_u32_e32 v144, v177, v197
	v_cvt_pk_fp8_f32 v158, v148, v150
	ds_read_b128 v[144:147], v144
	s_waitcnt lgkmcnt(1)
	v_mfma_f32_16x16x32_bf16 v[132:135], v[114:117], v[140:143], v[132:135]
	v_med3_f32 v140, v154, s78, v240
	v_med3_f32 v141, v155, s78, v240
	v_cvt_pk_fp8_f32 v158, v140, v141 op_sel:[0,0,1]
	v_lshlrev_b32_e32 v141, 16, v116
	v_and_b32_e32 v143, 0xffff0000, v116
	s_waitcnt lgkmcnt(0)
	v_mfma_f32_16x16x32_bf16 v[136:139], v[114:117], v[144:147], v[136:139]
	v_med3_f32 v142, v141, s78, v240
	v_med3_f32 v144, v143, s78, v240
	v_mov_b32_e32 v159, 0
	v_cvt_pk_fp8_f32 v159, v142, v144
	v_lshlrev_b32_e32 v145, 16, v117
	v_and_b32_e32 v147, 0xffff0000, v117
	v_med3_f32 v142, v145, s78, v240
	v_med3_f32 v144, v147, s78, v240
	global_store_dwordx2 v[130:131], v[160:161], off offset:32
	s_waitcnt vmcnt(30)
	v_lshlrev_b32_e32 v160, 16, v111
	v_and_b32_e32 v161, 0xffff0000, v111
	v_cvt_pk_fp8_f32 v159, v142, v144 op_sel:[0,0,1]
	v_and_b32_e32 v142, 0xffff0000, v110
	v_mul_f32_e32 v152, v160, v160
	v_mul_f32_e32 v156, v161, v161
	v_lshlrev_b32_e32 v140, 16, v110
	v_pk_mul_f32 v[154:155], v[142:143], v[142:143]
	v_and_b32_e32 v146, 0xffff0000, v112
	v_pk_fma_f32 v[154:155], v[140:141], v[140:141], v[154:155]
	v_pk_add_f32 v[152:153], v[152:153], v[156:157]
	v_lshlrev_b32_e32 v144, 16, v112
	v_pk_add_f32 v[152:153], v[154:155], v[152:153]
	v_pk_mul_f32 v[154:155], v[146:147], v[146:147]
	v_med3_f32 v140, v140, s78, v240
	v_pk_fma_f32 v[154:155], v[144:145], v[144:145], v[154:155]
	v_med3_f32 v141, v142, s78, v240
	v_pk_add_f32 v[152:153], v[154:155], v[152:153]
	v_mov_b32_e32 v154, 0
	v_cvt_pk_fp8_f32 v154, v140, v141
	v_med3_f32 v140, v160, s78, v240
	v_med3_f32 v141, v161, s78, v240
	v_med3_f32 v145, v146, s78, v240
	v_add_u32_e32 v146, v175, v198
	v_cvt_pk_fp8_f32 v154, v140, v141 op_sel:[0,0,1]
	v_med3_f32 v144, v144, s78, v240
	ds_read_b128 v[140:143], v146
	v_mov_b32_e32 v155, 0
	v_cvt_pk_fp8_f32 v155, v144, v145
	ds_read_b128 v[144:147], v146 offset:32768
	s_waitcnt lgkmcnt(1)
	v_mfma_f32_16x16x32_bf16 v[132:135], v[110:113], v[140:143], v[132:135]
	v_add_u32_e32 v140, v176, v198
	v_lshlrev_b32_e32 v173, 16, v113
	v_and_b32_e32 v243, 0xffff0000, v113
	ds_read_b128 v[140:143], v140
	s_waitcnt lgkmcnt(1)
	v_mfma_f32_16x16x32_bf16 v[136:139], v[110:113], v[144:147], v[136:139]
	v_add_u32_e32 v144, v177, v198
	v_mul_f32_e32 v150, v173, v173
	v_mul_f32_e32 v148, v243, v243
	ds_read_b128 v[144:147], v144
	v_pk_add_f32 v[148:149], v[150:151], v[148:149]
	v_med3_f32 v150, v173, s78, v240
	v_med3_f32 v151, v243, s78, v240
	v_cvt_pk_fp8_f32 v155, v150, v151 op_sel:[0,0,1]
	s_waitcnt lgkmcnt(1)
	v_mfma_f32_16x16x32_bf16 v[132:135], v[110:113], v[140:143], v[132:135]
	v_add_f32_e64 v140, v152, v148
	v_add_f32_e64 v141, v153, v149
	s_waitcnt vmcnt(29)
	v_and_b32_e32 v143, 0xffff0000, v107
	v_and_b32_e32 v142, 0xffff0000, v106
	v_pk_add_f32 v[148:149], v[140:141], v[140:141] op_sel_hi:[0,1]
	s_waitcnt lgkmcnt(0)
	v_mfma_f32_16x16x32_bf16 v[136:139], v[110:113], v[144:147], v[136:139]
	v_lshlrev_b32_e32 v141, 16, v107
	v_lshlrev_b32_e32 v140, 16, v106
	v_pk_mul_f32 v[144:145], v[142:143], v[142:143]
	global_store_dwordx2 v[130:131], v[154:155], off offset:128
	v_pk_fma_f32 v[144:145], v[140:141], v[140:141], v[144:145]
	v_med3_f32 v140, v140, s78, v240
	v_med3_f32 v142, v142, s78, v240
	v_mov_b32_e32 v154, 0
	v_cvt_pk_fp8_f32 v154, v140, v142
	v_and_b32_e32 v151, 0xffff0000, v109
	v_and_b32_e32 v150, 0xffff0000, v108
	v_lshlrev_b32_e32 v147, 16, v109
	v_lshlrev_b32_e32 v146, 16, v108
	v_pk_mul_f32 v[152:153], v[150:151], v[150:151]
	v_add_f32_e32 v148, v144, v145
	v_pk_fma_f32 v[152:153], v[146:147], v[146:147], v[152:153]
	v_med3_f32 v140, v141, s78, v240
	v_med3_f32 v141, v143, s78, v240
	v_med3_f32 v144, v146, s78, v240
	v_med3_f32 v145, v150, s78, v240
	v_add_u32_e32 v146, v175, v199
	v_mov_b32_e32 v155, 0
	v_cvt_pk_fp8_f32 v154, v140, v141 op_sel:[0,0,1]
	ds_read_b128 v[140:143], v146
	v_cvt_pk_fp8_f32 v155, v144, v145
	v_med3_f32 v150, v147, s78, v240
	ds_read_b128 v[144:147], v146 offset:32768
	s_waitcnt lgkmcnt(1)
	v_mfma_f32_16x16x32_bf16 v[132:135], v[106:109], v[140:143], v[132:135]
	v_add_u32_e32 v140, v176, v199
	ds_read_b128 v[140:143], v140
	v_med3_f32 v151, v151, s78, v240
	s_waitcnt lgkmcnt(1)
	v_mfma_f32_16x16x32_bf16 v[136:139], v[106:109], v[144:147], v[136:139]
	v_add_u32_e32 v144, v177, v199
	ds_read_b128 v[144:147], v144
	v_cvt_pk_fp8_f32 v155, v150, v151 op_sel:[0,0,1]
	s_waitcnt lgkmcnt(1)
	v_mfma_f32_16x16x32_bf16 v[132:135], v[106:109], v[140:143], v[132:135]
	v_add_f32_e32 v140, v152, v148
	v_pk_add_f32 v[150:151], v[152:153], v[140:141] op_sel_hi:[1,0]
	global_store_dwordx2 v[130:131], v[154:155], off offset:160
	s_waitcnt lgkmcnt(0)
	v_mfma_f32_16x16x32_bf16 v[136:139], v[106:109], v[144:147], v[136:139]
	s_waitcnt vmcnt(30)
	v_lshlrev_b32_e32 v144, 16, v102
	v_and_b32_e32 v145, 0xffff0000, v102
	v_mul_f32_e32 v140, v144, v144
	v_add_u32_e32 v147, v175, v200
	v_pk_fma_f32 v[152:153], v[144:145], v[144:145], v[140:141] op_sel_hi:[1,1,0]
	v_lshlrev_b32_e32 v154, 16, v103
	ds_read_b128 v[140:143], v147
	v_and_b32_e32 v155, 0xffff0000, v103
	v_mul_f32_e32 v146, v154, v154
	v_pk_fma_f32 v[156:157], v[154:155], v[154:155], v[146:147] op_sel_hi:[1,1,0]
	v_med3_f32 v148, v144, s78, v240
	v_med3_f32 v150, v145, s78, v240
	ds_read_b128 v[144:147], v147 offset:32768
	s_waitcnt lgkmcnt(1)
	v_mfma_f32_16x16x32_bf16 v[132:135], v[102:105], v[140:143], v[132:135]
	v_add_u32_e32 v140, v176, v200
	ds_read_b128 v[140:143], v140
	global_store_dwordx2 v[130:131], v[158:159], off offset:96
	v_mov_b32_e32 v158, 0
	s_waitcnt lgkmcnt(1)
	v_mfma_f32_16x16x32_bf16 v[136:139], v[102:105], v[144:147], v[136:139]
	v_add_u32_e32 v144, v177, v200
	v_cvt_pk_fp8_f32 v158, v148, v150
	ds_read_b128 v[144:147], v144
	s_waitcnt lgkmcnt(1)
	v_mfma_f32_16x16x32_bf16 v[132:135], v[102:105], v[140:143], v[132:135]
	v_med3_f32 v140, v154, s78, v240
	v_med3_f32 v141, v155, s78, v240
	v_cvt_pk_fp8_f32 v158, v140, v141 op_sel:[0,0,1]
	v_lshlrev_b32_e32 v141, 16, v104
	v_and_b32_e32 v143, 0xffff0000, v104
	s_waitcnt lgkmcnt(0)
	v_mfma_f32_16x16x32_bf16 v[136:139], v[102:105], v[144:147], v[136:139]
	v_med3_f32 v142, v141, s78, v240
	v_med3_f32 v144, v143, s78, v240
	v_mov_b32_e32 v159, 0
	v_cvt_pk_fp8_f32 v159, v142, v144
	v_lshlrev_b32_e32 v145, 16, v105
	v_and_b32_e32 v147, 0xffff0000, v105
	v_med3_f32 v142, v145, s78, v240
	v_med3_f32 v144, v147, s78, v240
	s_waitcnt vmcnt(30)
	v_lshlrev_b32_e32 v160, 16, v99
	v_and_b32_e32 v161, 0xffff0000, v99
	v_cvt_pk_fp8_f32 v159, v142, v144 op_sel:[0,0,1]
	v_and_b32_e32 v142, 0xffff0000, v98
	v_mul_f32_e32 v152, v160, v160
	v_mul_f32_e32 v156, v161, v161
	v_lshlrev_b32_e32 v140, 16, v98
	v_pk_mul_f32 v[154:155], v[142:143], v[142:143]
	v_and_b32_e32 v146, 0xffff0000, v100
	v_pk_fma_f32 v[154:155], v[140:141], v[140:141], v[154:155]
	v_pk_add_f32 v[152:153], v[152:153], v[156:157]
	v_lshlrev_b32_e32 v144, 16, v100
	v_pk_add_f32 v[152:153], v[154:155], v[152:153]
	v_pk_mul_f32 v[154:155], v[146:147], v[146:147]
	v_med3_f32 v140, v140, s78, v240
	v_pk_fma_f32 v[154:155], v[144:145], v[144:145], v[154:155]
	v_med3_f32 v141, v142, s78, v240
	v_pk_add_f32 v[152:153], v[154:155], v[152:153]
	v_mov_b32_e32 v154, 0
	v_cvt_pk_fp8_f32 v154, v140, v141
	v_med3_f32 v140, v160, s78, v240
	v_med3_f32 v141, v161, s78, v240
	v_med3_f32 v145, v146, s78, v240
	v_add_u32_e32 v146, v175, v201
	v_cvt_pk_fp8_f32 v154, v140, v141 op_sel:[0,0,1]
	v_med3_f32 v144, v144, s78, v240
	ds_read_b128 v[140:143], v146
	v_mov_b32_e32 v155, 0
	v_cvt_pk_fp8_f32 v155, v144, v145
	ds_read_b128 v[144:147], v146 offset:32768
	s_waitcnt lgkmcnt(1)
	v_mfma_f32_16x16x32_bf16 v[132:135], v[98:101], v[140:143], v[132:135]
	v_add_u32_e32 v140, v176, v201
	v_lshlrev_b32_e32 v173, 16, v101
	v_and_b32_e32 v243, 0xffff0000, v101
	ds_read_b128 v[140:143], v140
	s_waitcnt lgkmcnt(1)
	v_mfma_f32_16x16x32_bf16 v[136:139], v[98:101], v[144:147], v[136:139]
	v_add_u32_e32 v144, v177, v201
	v_mul_f32_e32 v150, v173, v173
	v_mul_f32_e32 v148, v243, v243
	ds_read_b128 v[144:147], v144
	v_pk_add_f32 v[148:149], v[150:151], v[148:149]
	v_med3_f32 v150, v173, s78, v240
	v_med3_f32 v151, v243, s78, v240
	v_cvt_pk_fp8_f32 v155, v150, v151 op_sel:[0,0,1]
	s_waitcnt lgkmcnt(1)
	v_mfma_f32_16x16x32_bf16 v[132:135], v[98:101], v[140:143], v[132:135]
	v_add_f32_e64 v140, v152, v148
	v_add_f32_e64 v141, v153, v149
	s_waitcnt vmcnt(29)
	v_and_b32_e32 v143, 0xffff0000, v95
	v_and_b32_e32 v142, 0xffff0000, v94
	v_pk_add_f32 v[148:149], v[140:141], v[140:141] op_sel_hi:[0,1]
	s_waitcnt lgkmcnt(0)
	v_mfma_f32_16x16x32_bf16 v[136:139], v[98:101], v[144:147], v[136:139]
	v_lshlrev_b32_e32 v141, 16, v95
	v_lshlrev_b32_e32 v140, 16, v94
	v_pk_mul_f32 v[144:145], v[142:143], v[142:143]
	global_store_dwordx2 v[130:131], v[154:155], off offset:224
	v_pk_fma_f32 v[144:145], v[140:141], v[140:141], v[144:145]
	v_med3_f32 v140, v140, s78, v240
	v_med3_f32 v142, v142, s78, v240
	v_mov_b32_e32 v154, 0
	v_cvt_pk_fp8_f32 v154, v140, v142
	v_and_b32_e32 v151, 0xffff0000, v97
	v_and_b32_e32 v150, 0xffff0000, v96
	v_lshlrev_b32_e32 v147, 16, v97
	v_lshlrev_b32_e32 v146, 16, v96
	v_pk_mul_f32 v[152:153], v[150:151], v[150:151]
	v_add_f32_e32 v148, v144, v145
	v_pk_fma_f32 v[152:153], v[146:147], v[146:147], v[152:153]
	v_med3_f32 v140, v141, s78, v240
	v_med3_f32 v141, v143, s78, v240
	v_med3_f32 v144, v146, s78, v240
	v_med3_f32 v145, v150, s78, v240
	v_add_u32_e32 v146, v175, v202
	v_mov_b32_e32 v155, 0
	v_cvt_pk_fp8_f32 v154, v140, v141 op_sel:[0,0,1]
	ds_read_b128 v[140:143], v146
	v_cvt_pk_fp8_f32 v155, v144, v145
	v_med3_f32 v150, v147, s78, v240
	ds_read_b128 v[144:147], v146 offset:32768
	s_waitcnt lgkmcnt(1)
	v_mfma_f32_16x16x32_bf16 v[132:135], v[94:97], v[140:143], v[132:135]
	v_add_u32_e32 v140, v176, v202
	ds_read_b128 v[140:143], v140
	v_med3_f32 v151, v151, s78, v240
	s_waitcnt lgkmcnt(1)
	v_mfma_f32_16x16x32_bf16 v[136:139], v[94:97], v[144:147], v[136:139]
	v_add_u32_e32 v144, v177, v202
	ds_read_b128 v[144:147], v144
	v_cvt_pk_fp8_f32 v155, v150, v151 op_sel:[0,0,1]
	s_waitcnt lgkmcnt(1)
	v_mfma_f32_16x16x32_bf16 v[132:135], v[94:97], v[140:143], v[132:135]
	v_add_f32_e32 v140, v152, v148
	v_pk_add_f32 v[150:151], v[152:153], v[140:141] op_sel_hi:[1,0]
	global_store_dwordx2 v[130:131], v[154:155], off offset:256
	s_waitcnt lgkmcnt(0)
	v_mfma_f32_16x16x32_bf16 v[136:139], v[94:97], v[144:147], v[136:139]
	s_waitcnt vmcnt(30)
	v_lshlrev_b32_e32 v144, 16, v90
	v_and_b32_e32 v145, 0xffff0000, v90
	v_mul_f32_e32 v140, v144, v144
	v_add_u32_e32 v147, v175, v203
	v_pk_fma_f32 v[152:153], v[144:145], v[144:145], v[140:141] op_sel_hi:[1,1,0]
	v_lshlrev_b32_e32 v154, 16, v91
	ds_read_b128 v[140:143], v147
	v_and_b32_e32 v155, 0xffff0000, v91
	v_mul_f32_e32 v146, v154, v154
	v_pk_fma_f32 v[156:157], v[154:155], v[154:155], v[146:147] op_sel_hi:[1,1,0]
	v_med3_f32 v148, v144, s78, v240
	v_med3_f32 v150, v145, s78, v240
	ds_read_b128 v[144:147], v147 offset:32768
	s_waitcnt lgkmcnt(1)
	v_mfma_f32_16x16x32_bf16 v[132:135], v[90:93], v[140:143], v[132:135]
	v_add_u32_e32 v140, v176, v203
	ds_read_b128 v[140:143], v140
	global_store_dwordx2 v[130:131], v[158:159], off offset:192
	v_mov_b32_e32 v158, 0
	s_waitcnt lgkmcnt(1)
	v_mfma_f32_16x16x32_bf16 v[136:139], v[90:93], v[144:147], v[136:139]
	v_add_u32_e32 v144, v177, v203
	v_cvt_pk_fp8_f32 v158, v148, v150
	ds_read_b128 v[144:147], v144
	s_waitcnt lgkmcnt(1)
	v_mfma_f32_16x16x32_bf16 v[132:135], v[90:93], v[140:143], v[132:135]
	v_med3_f32 v140, v154, s78, v240
	v_med3_f32 v141, v155, s78, v240
	v_cvt_pk_fp8_f32 v158, v140, v141 op_sel:[0,0,1]
	v_lshlrev_b32_e32 v141, 16, v92
	v_and_b32_e32 v143, 0xffff0000, v92
	s_waitcnt lgkmcnt(0)
	v_mfma_f32_16x16x32_bf16 v[136:139], v[90:93], v[144:147], v[136:139]
	v_med3_f32 v142, v141, s78, v240
	v_med3_f32 v144, v143, s78, v240
	v_mov_b32_e32 v159, 0
	v_cvt_pk_fp8_f32 v159, v142, v144
	v_lshlrev_b32_e32 v145, 16, v93
	v_and_b32_e32 v147, 0xffff0000, v93
	v_med3_f32 v142, v145, s78, v240
	v_med3_f32 v144, v147, s78, v240
	s_waitcnt vmcnt(30)
	v_lshlrev_b32_e32 v160, 16, v87
	v_and_b32_e32 v161, 0xffff0000, v87
	v_cvt_pk_fp8_f32 v159, v142, v144 op_sel:[0,0,1]
	v_and_b32_e32 v142, 0xffff0000, v86
	v_mul_f32_e32 v152, v160, v160
	v_mul_f32_e32 v156, v161, v161
	v_lshlrev_b32_e32 v140, 16, v86
	v_pk_mul_f32 v[154:155], v[142:143], v[142:143]
	v_and_b32_e32 v146, 0xffff0000, v88
	v_pk_fma_f32 v[154:155], v[140:141], v[140:141], v[154:155]
	v_pk_add_f32 v[152:153], v[152:153], v[156:157]
	v_lshlrev_b32_e32 v144, 16, v88
	v_pk_add_f32 v[152:153], v[154:155], v[152:153]
	v_pk_mul_f32 v[154:155], v[146:147], v[146:147]
	v_med3_f32 v140, v140, s78, v240
	v_pk_fma_f32 v[154:155], v[144:145], v[144:145], v[154:155]
	v_med3_f32 v141, v142, s78, v240
	v_pk_add_f32 v[152:153], v[154:155], v[152:153]
	v_mov_b32_e32 v154, 0
	v_cvt_pk_fp8_f32 v154, v140, v141
	v_med3_f32 v140, v160, s78, v240
	v_med3_f32 v141, v161, s78, v240
	v_med3_f32 v145, v146, s78, v240
	v_add_u32_e32 v146, v175, v204
	v_cvt_pk_fp8_f32 v154, v140, v141 op_sel:[0,0,1]
	v_med3_f32 v144, v144, s78, v240
	ds_read_b128 v[140:143], v146
	v_mov_b32_e32 v155, 0
	v_cvt_pk_fp8_f32 v155, v144, v145
	ds_read_b128 v[144:147], v146 offset:32768
	s_waitcnt lgkmcnt(1)
	v_mfma_f32_16x16x32_bf16 v[132:135], v[86:89], v[140:143], v[132:135]
	v_add_u32_e32 v140, v176, v204
	v_lshlrev_b32_e32 v173, 16, v89
	v_and_b32_e32 v243, 0xffff0000, v89
	ds_read_b128 v[140:143], v140
	s_waitcnt lgkmcnt(1)
	v_mfma_f32_16x16x32_bf16 v[136:139], v[86:89], v[144:147], v[136:139]
	v_add_u32_e32 v144, v177, v204
	v_mul_f32_e32 v150, v173, v173
	v_mul_f32_e32 v148, v243, v243
	ds_read_b128 v[144:147], v144
	v_pk_add_f32 v[148:149], v[150:151], v[148:149]
	v_med3_f32 v150, v173, s78, v240
	v_med3_f32 v151, v243, s78, v240
	v_cvt_pk_fp8_f32 v155, v150, v151 op_sel:[0,0,1]
	s_waitcnt lgkmcnt(1)
	v_mfma_f32_16x16x32_bf16 v[132:135], v[86:89], v[140:143], v[132:135]
	v_add_f32_e64 v140, v152, v148
	v_add_f32_e64 v141, v153, v149
	s_waitcnt vmcnt(29)
	v_and_b32_e32 v143, 0xffff0000, v83
	v_and_b32_e32 v142, 0xffff0000, v82
	v_pk_add_f32 v[148:149], v[140:141], v[140:141] op_sel_hi:[0,1]
	s_waitcnt lgkmcnt(0)
	v_mfma_f32_16x16x32_bf16 v[136:139], v[86:89], v[144:147], v[136:139]
	v_lshlrev_b32_e32 v141, 16, v83
	v_lshlrev_b32_e32 v140, 16, v82
	v_pk_mul_f32 v[144:145], v[142:143], v[142:143]
	global_store_dwordx2 v[130:131], v[154:155], off offset:320
	v_pk_fma_f32 v[144:145], v[140:141], v[140:141], v[144:145]
	v_med3_f32 v140, v140, s78, v240
	v_med3_f32 v142, v142, s78, v240
	v_mov_b32_e32 v154, 0
	v_cvt_pk_fp8_f32 v154, v140, v142
	v_and_b32_e32 v151, 0xffff0000, v85
	v_and_b32_e32 v150, 0xffff0000, v84
	v_lshlrev_b32_e32 v147, 16, v85
	v_lshlrev_b32_e32 v146, 16, v84
	v_pk_mul_f32 v[152:153], v[150:151], v[150:151]
	v_add_f32_e32 v148, v144, v145
	v_pk_fma_f32 v[152:153], v[146:147], v[146:147], v[152:153]
	v_med3_f32 v140, v141, s78, v240
	v_med3_f32 v141, v143, s78, v240
	v_med3_f32 v144, v146, s78, v240
	v_med3_f32 v145, v150, s78, v240
	v_add_u32_e32 v146, v175, v205
	v_mov_b32_e32 v155, 0
	v_cvt_pk_fp8_f32 v154, v140, v141 op_sel:[0,0,1]
	ds_read_b128 v[140:143], v146
	v_cvt_pk_fp8_f32 v155, v144, v145
	v_med3_f32 v150, v147, s78, v240
	ds_read_b128 v[144:147], v146 offset:32768
	s_waitcnt lgkmcnt(1)
	v_mfma_f32_16x16x32_bf16 v[132:135], v[82:85], v[140:143], v[132:135]
	v_add_u32_e32 v140, v176, v205
	ds_read_b128 v[140:143], v140
	v_med3_f32 v151, v151, s78, v240
	s_waitcnt lgkmcnt(1)
	v_mfma_f32_16x16x32_bf16 v[136:139], v[82:85], v[144:147], v[136:139]
	v_add_u32_e32 v144, v177, v205
	ds_read_b128 v[144:147], v144
	v_cvt_pk_fp8_f32 v155, v150, v151 op_sel:[0,0,1]
	s_waitcnt lgkmcnt(1)
	v_mfma_f32_16x16x32_bf16 v[132:135], v[82:85], v[140:143], v[132:135]
	v_add_f32_e32 v140, v152, v148
	v_pk_add_f32 v[150:151], v[152:153], v[140:141] op_sel_hi:[1,0]
	global_store_dwordx2 v[130:131], v[154:155], off offset:352
	s_waitcnt lgkmcnt(0)
	v_mfma_f32_16x16x32_bf16 v[136:139], v[82:85], v[144:147], v[136:139]
	s_waitcnt vmcnt(30)
	v_lshlrev_b32_e32 v144, 16, v78
	v_and_b32_e32 v145, 0xffff0000, v78
	v_mul_f32_e32 v140, v144, v144
	v_add_u32_e32 v147, v175, v206
	v_pk_fma_f32 v[152:153], v[144:145], v[144:145], v[140:141] op_sel_hi:[1,1,0]
	v_lshlrev_b32_e32 v154, 16, v79
	ds_read_b128 v[140:143], v147
	v_and_b32_e32 v155, 0xffff0000, v79
	v_mul_f32_e32 v146, v154, v154
	v_pk_fma_f32 v[156:157], v[154:155], v[154:155], v[146:147] op_sel_hi:[1,1,0]
	v_med3_f32 v148, v144, s78, v240
	v_med3_f32 v150, v145, s78, v240
	ds_read_b128 v[144:147], v147 offset:32768
	s_waitcnt lgkmcnt(1)
	v_mfma_f32_16x16x32_bf16 v[132:135], v[78:81], v[140:143], v[132:135]
	v_add_u32_e32 v140, v176, v206
	ds_read_b128 v[140:143], v140
	global_store_dwordx2 v[130:131], v[158:159], off offset:288
	v_mov_b32_e32 v158, 0
	s_waitcnt lgkmcnt(1)
	v_mfma_f32_16x16x32_bf16 v[136:139], v[78:81], v[144:147], v[136:139]
	v_add_u32_e32 v144, v177, v206
	v_cvt_pk_fp8_f32 v158, v148, v150
	ds_read_b128 v[144:147], v144
	s_waitcnt lgkmcnt(1)
	v_mfma_f32_16x16x32_bf16 v[132:135], v[78:81], v[140:143], v[132:135]
	v_med3_f32 v140, v154, s78, v240
	v_med3_f32 v141, v155, s78, v240
	v_cvt_pk_fp8_f32 v158, v140, v141 op_sel:[0,0,1]
	v_lshlrev_b32_e32 v141, 16, v80
	v_and_b32_e32 v143, 0xffff0000, v80
	s_waitcnt lgkmcnt(0)
	v_mfma_f32_16x16x32_bf16 v[136:139], v[78:81], v[144:147], v[136:139]
	v_med3_f32 v142, v141, s78, v240
	v_med3_f32 v144, v143, s78, v240
	v_mov_b32_e32 v159, 0
	v_cvt_pk_fp8_f32 v159, v142, v144
	v_lshlrev_b32_e32 v145, 16, v81
	v_and_b32_e32 v147, 0xffff0000, v81
	v_med3_f32 v142, v145, s78, v240
	v_med3_f32 v144, v147, s78, v240
	s_waitcnt vmcnt(30)
	v_lshlrev_b32_e32 v160, 16, v75
	v_and_b32_e32 v161, 0xffff0000, v75
	v_cvt_pk_fp8_f32 v159, v142, v144 op_sel:[0,0,1]
	v_and_b32_e32 v142, 0xffff0000, v74
	v_mul_f32_e32 v152, v160, v160
	v_mul_f32_e32 v156, v161, v161
	v_lshlrev_b32_e32 v140, 16, v74
	v_pk_mul_f32 v[154:155], v[142:143], v[142:143]
	v_and_b32_e32 v146, 0xffff0000, v76
	v_pk_fma_f32 v[154:155], v[140:141], v[140:141], v[154:155]
	v_pk_add_f32 v[152:153], v[152:153], v[156:157]
	v_lshlrev_b32_e32 v144, 16, v76
	v_pk_add_f32 v[152:153], v[154:155], v[152:153]
	v_pk_mul_f32 v[154:155], v[146:147], v[146:147]
	v_med3_f32 v140, v140, s78, v240
	v_pk_fma_f32 v[154:155], v[144:145], v[144:145], v[154:155]
	v_med3_f32 v141, v142, s78, v240
	v_pk_add_f32 v[152:153], v[154:155], v[152:153]
	v_mov_b32_e32 v154, 0
	v_cvt_pk_fp8_f32 v154, v140, v141
	v_med3_f32 v140, v160, s78, v240
	v_med3_f32 v141, v161, s78, v240
	v_med3_f32 v145, v146, s78, v240
	v_add_u32_e32 v146, v175, v207
	v_cvt_pk_fp8_f32 v154, v140, v141 op_sel:[0,0,1]
	v_med3_f32 v144, v144, s78, v240
	ds_read_b128 v[140:143], v146
	v_mov_b32_e32 v155, 0
	v_cvt_pk_fp8_f32 v155, v144, v145
	ds_read_b128 v[144:147], v146 offset:32768
	s_waitcnt lgkmcnt(1)
	v_mfma_f32_16x16x32_bf16 v[132:135], v[74:77], v[140:143], v[132:135]
	v_add_u32_e32 v140, v176, v207
	v_lshlrev_b32_e32 v173, 16, v77
	v_and_b32_e32 v243, 0xffff0000, v77
	ds_read_b128 v[140:143], v140
	s_waitcnt lgkmcnt(1)
	v_mfma_f32_16x16x32_bf16 v[136:139], v[74:77], v[144:147], v[136:139]
	v_add_u32_e32 v144, v177, v207
	v_mul_f32_e32 v150, v173, v173
	v_mul_f32_e32 v148, v243, v243
	ds_read_b128 v[144:147], v144
	v_pk_add_f32 v[148:149], v[150:151], v[148:149]
	v_med3_f32 v150, v173, s78, v240
	v_med3_f32 v151, v243, s78, v240
	v_cvt_pk_fp8_f32 v155, v150, v151 op_sel:[0,0,1]
	s_waitcnt lgkmcnt(1)
	v_mfma_f32_16x16x32_bf16 v[132:135], v[74:77], v[140:143], v[132:135]
	v_add_f32_e64 v140, v152, v148
	v_add_f32_e64 v141, v153, v149
	s_waitcnt vmcnt(29)
	v_and_b32_e32 v143, 0xffff0000, v71
	v_and_b32_e32 v142, 0xffff0000, v70
	v_pk_add_f32 v[148:149], v[140:141], v[140:141] op_sel_hi:[0,1]
	s_waitcnt lgkmcnt(0)
	v_mfma_f32_16x16x32_bf16 v[136:139], v[74:77], v[144:147], v[136:139]
	v_lshlrev_b32_e32 v141, 16, v71
	v_lshlrev_b32_e32 v140, 16, v70
	v_pk_mul_f32 v[144:145], v[142:143], v[142:143]
	global_store_dwordx2 v[130:131], v[154:155], off offset:416
	v_pk_fma_f32 v[144:145], v[140:141], v[140:141], v[144:145]
	v_med3_f32 v140, v140, s78, v240
	v_med3_f32 v142, v142, s78, v240
	v_mov_b32_e32 v154, 0
	v_cvt_pk_fp8_f32 v154, v140, v142
	v_and_b32_e32 v151, 0xffff0000, v73
	v_and_b32_e32 v150, 0xffff0000, v72
	v_lshlrev_b32_e32 v147, 16, v73
	v_lshlrev_b32_e32 v146, 16, v72
	v_pk_mul_f32 v[152:153], v[150:151], v[150:151]
	v_add_f32_e32 v148, v144, v145
	v_pk_fma_f32 v[152:153], v[146:147], v[146:147], v[152:153]
	v_med3_f32 v140, v141, s78, v240
	v_med3_f32 v141, v143, s78, v240
	v_med3_f32 v144, v146, s78, v240
	v_med3_f32 v145, v150, s78, v240
	v_add_u32_e32 v146, v175, v208
	v_mov_b32_e32 v155, 0
	v_cvt_pk_fp8_f32 v154, v140, v141 op_sel:[0,0,1]
	ds_read_b128 v[140:143], v146
	v_cvt_pk_fp8_f32 v155, v144, v145
	v_med3_f32 v150, v147, s78, v240
	ds_read_b128 v[144:147], v146 offset:32768
	s_waitcnt lgkmcnt(1)
	v_mfma_f32_16x16x32_bf16 v[132:135], v[70:73], v[140:143], v[132:135]
	v_add_u32_e32 v140, v176, v208
	ds_read_b128 v[140:143], v140
	v_med3_f32 v151, v151, s78, v240
	s_waitcnt lgkmcnt(1)
	v_mfma_f32_16x16x32_bf16 v[136:139], v[70:73], v[144:147], v[136:139]
	v_add_u32_e32 v144, v177, v208
	ds_read_b128 v[144:147], v144
	v_cvt_pk_fp8_f32 v155, v150, v151 op_sel:[0,0,1]
	s_waitcnt lgkmcnt(1)
	v_mfma_f32_16x16x32_bf16 v[132:135], v[70:73], v[140:143], v[132:135]
	v_add_f32_e32 v140, v152, v148
	v_pk_add_f32 v[150:151], v[152:153], v[140:141] op_sel_hi:[1,0]
	global_store_dwordx2 v[130:131], v[154:155], off offset:448
	s_waitcnt lgkmcnt(0)
	v_mfma_f32_16x16x32_bf16 v[136:139], v[70:73], v[144:147], v[136:139]
	s_waitcnt vmcnt(30)
	v_lshlrev_b32_e32 v144, 16, v66
	v_and_b32_e32 v145, 0xffff0000, v66
	v_mul_f32_e32 v140, v144, v144
	v_add_u32_e32 v147, v175, v209
	v_pk_fma_f32 v[152:153], v[144:145], v[144:145], v[140:141] op_sel_hi:[1,1,0]
	v_lshlrev_b32_e32 v154, 16, v67
	ds_read_b128 v[140:143], v147
	v_and_b32_e32 v155, 0xffff0000, v67
	v_mul_f32_e32 v146, v154, v154
	v_pk_fma_f32 v[156:157], v[154:155], v[154:155], v[146:147] op_sel_hi:[1,1,0]
	v_med3_f32 v148, v144, s78, v240
	v_med3_f32 v150, v145, s78, v240
	ds_read_b128 v[144:147], v147 offset:32768
	s_waitcnt lgkmcnt(1)
	v_mfma_f32_16x16x32_bf16 v[132:135], v[66:69], v[140:143], v[132:135]
	v_add_u32_e32 v140, v176, v209
	ds_read_b128 v[140:143], v140
	global_store_dwordx2 v[130:131], v[158:159], off offset:384
	v_mov_b32_e32 v158, 0
	s_waitcnt lgkmcnt(1)
	v_mfma_f32_16x16x32_bf16 v[136:139], v[66:69], v[144:147], v[136:139]
	v_add_u32_e32 v144, v177, v209
	v_cvt_pk_fp8_f32 v158, v148, v150
	ds_read_b128 v[144:147], v144
	s_waitcnt lgkmcnt(1)
	v_mfma_f32_16x16x32_bf16 v[132:135], v[66:69], v[140:143], v[132:135]
	v_med3_f32 v140, v154, s78, v240
	v_med3_f32 v141, v155, s78, v240
	v_cvt_pk_fp8_f32 v158, v140, v141 op_sel:[0,0,1]
	v_lshlrev_b32_e32 v141, 16, v68
	v_and_b32_e32 v143, 0xffff0000, v68
	s_waitcnt lgkmcnt(0)
	v_mfma_f32_16x16x32_bf16 v[136:139], v[66:69], v[144:147], v[136:139]
	v_med3_f32 v142, v141, s78, v240
	v_med3_f32 v144, v143, s78, v240
	v_mov_b32_e32 v159, 0
	v_cvt_pk_fp8_f32 v159, v142, v144
	v_lshlrev_b32_e32 v145, 16, v69
	v_and_b32_e32 v147, 0xffff0000, v69
	v_med3_f32 v142, v145, s78, v240
	v_med3_f32 v144, v147, s78, v240
	s_waitcnt vmcnt(16)
	v_lshlrev_b32_e32 v160, 16, v63
	v_and_b32_e32 v161, 0xffff0000, v63
	v_cvt_pk_fp8_f32 v159, v142, v144 op_sel:[0,0,1]
	v_and_b32_e32 v142, 0xffff0000, v62
	v_mul_f32_e32 v152, v160, v160
	v_mul_f32_e32 v156, v161, v161
	v_lshlrev_b32_e32 v140, 16, v62
	v_pk_mul_f32 v[154:155], v[142:143], v[142:143]
	v_and_b32_e32 v146, 0xffff0000, v64
	v_pk_fma_f32 v[154:155], v[140:141], v[140:141], v[154:155]
	v_pk_add_f32 v[152:153], v[152:153], v[156:157]
	v_lshlrev_b32_e32 v144, 16, v64
	v_pk_add_f32 v[152:153], v[154:155], v[152:153]
	v_pk_mul_f32 v[154:155], v[146:147], v[146:147]
	v_med3_f32 v140, v140, s78, v240
	v_pk_fma_f32 v[154:155], v[144:145], v[144:145], v[154:155]
	v_med3_f32 v141, v142, s78, v240
	v_pk_add_f32 v[152:153], v[154:155], v[152:153]
	v_mov_b32_e32 v154, 0
	v_cvt_pk_fp8_f32 v154, v140, v141
	v_med3_f32 v140, v160, s78, v240
	v_med3_f32 v141, v161, s78, v240
	v_med3_f32 v145, v146, s78, v240
	v_add_u32_e32 v146, v175, v210
	v_cvt_pk_fp8_f32 v154, v140, v141 op_sel:[0,0,1]
	v_med3_f32 v144, v144, s78, v240
	ds_read_b128 v[140:143], v146
	v_mov_b32_e32 v155, 0
	v_cvt_pk_fp8_f32 v155, v144, v145
	ds_read_b128 v[144:147], v146 offset:32768
	s_waitcnt lgkmcnt(1)
	v_mfma_f32_16x16x32_bf16 v[132:135], v[62:65], v[140:143], v[132:135]
	v_add_u32_e32 v140, v176, v210
	v_lshlrev_b32_e32 v173, 16, v65
	v_and_b32_e32 v243, 0xffff0000, v65
	ds_read_b128 v[140:143], v140
	s_waitcnt lgkmcnt(1)
	v_mfma_f32_16x16x32_bf16 v[136:139], v[62:65], v[144:147], v[136:139]
	v_add_u32_e32 v144, v177, v210
	v_mul_f32_e32 v150, v173, v173
	v_mul_f32_e32 v148, v243, v243
	ds_read_b128 v[144:147], v144
	v_pk_add_f32 v[148:149], v[150:151], v[148:149]
	v_med3_f32 v150, v173, s78, v240
	v_med3_f32 v151, v243, s78, v240
	v_cvt_pk_fp8_f32 v155, v150, v151 op_sel:[0,0,1]
	s_waitcnt lgkmcnt(1)
	v_mfma_f32_16x16x32_bf16 v[132:135], v[62:65], v[140:143], v[132:135]
	v_add_f32_e64 v140, v152, v148
	v_add_f32_e64 v141, v153, v149
	s_waitcnt vmcnt(15)
	v_and_b32_e32 v143, 0xffff0000, v59
	v_and_b32_e32 v142, 0xffff0000, v58
	v_pk_add_f32 v[148:149], v[140:141], v[140:141] op_sel_hi:[0,1]
	s_waitcnt lgkmcnt(0)
	v_mfma_f32_16x16x32_bf16 v[136:139], v[62:65], v[144:147], v[136:139]
	v_lshlrev_b32_e32 v141, 16, v59
	v_lshlrev_b32_e32 v140, 16, v58
	v_pk_mul_f32 v[144:145], v[142:143], v[142:143]
	global_store_dwordx2 v[130:131], v[154:155], off offset:512
	v_pk_fma_f32 v[144:145], v[140:141], v[140:141], v[144:145]
	v_med3_f32 v140, v140, s78, v240
	v_med3_f32 v142, v142, s78, v240
	v_mov_b32_e32 v154, 0
	v_cvt_pk_fp8_f32 v154, v140, v142
	v_and_b32_e32 v151, 0xffff0000, v61
	v_and_b32_e32 v150, 0xffff0000, v60
	v_lshlrev_b32_e32 v147, 16, v61
	v_lshlrev_b32_e32 v146, 16, v60
	v_pk_mul_f32 v[152:153], v[150:151], v[150:151]
	v_add_f32_e32 v148, v144, v145
	v_pk_fma_f32 v[152:153], v[146:147], v[146:147], v[152:153]
	v_med3_f32 v140, v141, s78, v240
	v_med3_f32 v141, v143, s78, v240
	v_med3_f32 v144, v146, s78, v240
	v_med3_f32 v145, v150, s78, v240
	v_add_u32_e32 v146, v175, v211
	v_mov_b32_e32 v155, 0
	v_cvt_pk_fp8_f32 v154, v140, v141 op_sel:[0,0,1]
	ds_read_b128 v[140:143], v146
	v_cvt_pk_fp8_f32 v155, v144, v145
	v_med3_f32 v150, v147, s78, v240
	ds_read_b128 v[144:147], v146 offset:32768
	s_waitcnt lgkmcnt(1)
	v_mfma_f32_16x16x32_bf16 v[132:135], v[58:61], v[140:143], v[132:135]
	v_add_u32_e32 v140, v176, v211
	ds_read_b128 v[140:143], v140
	v_med3_f32 v151, v151, s78, v240
	s_waitcnt lgkmcnt(1)
	v_mfma_f32_16x16x32_bf16 v[136:139], v[58:61], v[144:147], v[136:139]
	v_add_u32_e32 v144, v177, v211
	ds_read_b128 v[144:147], v144
	v_cvt_pk_fp8_f32 v155, v150, v151 op_sel:[0,0,1]
	s_waitcnt lgkmcnt(1)
	v_mfma_f32_16x16x32_bf16 v[132:135], v[58:61], v[140:143], v[132:135]
	v_add_f32_e32 v140, v152, v148
	v_pk_add_f32 v[150:151], v[152:153], v[140:141] op_sel_hi:[1,0]
	global_store_dwordx2 v[130:131], v[154:155], off offset:544
	s_waitcnt lgkmcnt(0)
	v_mfma_f32_16x16x32_bf16 v[136:139], v[58:61], v[144:147], v[136:139]
	v_lshlrev_b32_e32 v144, 16, v54
	v_and_b32_e32 v145, 0xffff0000, v54
	v_mul_f32_e32 v140, v144, v144
	v_add_u32_e32 v147, v175, v212
	v_pk_fma_f32 v[152:153], v[144:145], v[144:145], v[140:141] op_sel_hi:[1,1,0]
	v_lshlrev_b32_e32 v154, 16, v55
	ds_read_b128 v[140:143], v147
	v_and_b32_e32 v155, 0xffff0000, v55
	v_mul_f32_e32 v146, v154, v154
	v_pk_fma_f32 v[156:157], v[154:155], v[154:155], v[146:147] op_sel_hi:[1,1,0]
	v_med3_f32 v148, v144, s78, v240
	v_med3_f32 v150, v145, s78, v240
	ds_read_b128 v[144:147], v147 offset:32768
	s_waitcnt lgkmcnt(1)
	v_mfma_f32_16x16x32_bf16 v[132:135], v[54:57], v[140:143], v[132:135]
	v_add_u32_e32 v140, v176, v212
	ds_read_b128 v[140:143], v140
	global_store_dwordx2 v[130:131], v[158:159], off offset:480
	v_mov_b32_e32 v158, 0
	s_waitcnt lgkmcnt(1)
	v_mfma_f32_16x16x32_bf16 v[136:139], v[54:57], v[144:147], v[136:139]
	v_add_u32_e32 v144, v177, v212
	v_cvt_pk_fp8_f32 v158, v148, v150
	ds_read_b128 v[144:147], v144
	s_waitcnt lgkmcnt(1)
	v_mfma_f32_16x16x32_bf16 v[132:135], v[54:57], v[140:143], v[132:135]
	v_med3_f32 v140, v154, s78, v240
	v_med3_f32 v141, v155, s78, v240
	v_cvt_pk_fp8_f32 v158, v140, v141 op_sel:[0,0,1]
	v_lshlrev_b32_e32 v141, 16, v56
	v_and_b32_e32 v143, 0xffff0000, v56
	s_waitcnt lgkmcnt(0)
	v_mfma_f32_16x16x32_bf16 v[136:139], v[54:57], v[144:147], v[136:139]
	v_med3_f32 v142, v141, s78, v240
	v_med3_f32 v144, v143, s78, v240
	v_mov_b32_e32 v159, 0
	v_cvt_pk_fp8_f32 v159, v142, v144
	v_lshlrev_b32_e32 v145, 16, v57
	v_and_b32_e32 v147, 0xffff0000, v57
	v_med3_f32 v142, v145, s78, v240
	v_med3_f32 v144, v147, s78, v240
	v_lshlrev_b32_e32 v160, 16, v51
	v_and_b32_e32 v161, 0xffff0000, v51
	v_cvt_pk_fp8_f32 v159, v142, v144 op_sel:[0,0,1]
	v_and_b32_e32 v142, 0xffff0000, v50
	v_mul_f32_e32 v152, v160, v160
	v_mul_f32_e32 v156, v161, v161
	v_lshlrev_b32_e32 v140, 16, v50
	v_pk_mul_f32 v[154:155], v[142:143], v[142:143]
	v_and_b32_e32 v146, 0xffff0000, v52
	v_pk_fma_f32 v[154:155], v[140:141], v[140:141], v[154:155]
	v_pk_add_f32 v[152:153], v[152:153], v[156:157]
	v_lshlrev_b32_e32 v144, 16, v52
	v_pk_add_f32 v[152:153], v[154:155], v[152:153]
	v_pk_mul_f32 v[154:155], v[146:147], v[146:147]
	v_med3_f32 v140, v140, s78, v240
	v_pk_fma_f32 v[154:155], v[144:145], v[144:145], v[154:155]
	v_med3_f32 v141, v142, s78, v240
	v_pk_add_f32 v[152:153], v[154:155], v[152:153]
	v_mov_b32_e32 v154, 0
	v_cvt_pk_fp8_f32 v154, v140, v141
	v_med3_f32 v140, v160, s78, v240
	v_med3_f32 v141, v161, s78, v240
	v_med3_f32 v145, v146, s78, v240
	v_add_u32_e32 v146, v175, v213
	v_cvt_pk_fp8_f32 v154, v140, v141 op_sel:[0,0,1]
	v_med3_f32 v144, v144, s78, v240
	ds_read_b128 v[140:143], v146
	v_mov_b32_e32 v155, 0
	v_cvt_pk_fp8_f32 v155, v144, v145
	ds_read_b128 v[144:147], v146 offset:32768
	s_waitcnt lgkmcnt(1)
	v_mfma_f32_16x16x32_bf16 v[132:135], v[50:53], v[140:143], v[132:135]
	v_add_u32_e32 v140, v176, v213
	v_lshlrev_b32_e32 v173, 16, v53
	v_and_b32_e32 v243, 0xffff0000, v53
	ds_read_b128 v[140:143], v140
	s_waitcnt lgkmcnt(1)
	v_mfma_f32_16x16x32_bf16 v[136:139], v[50:53], v[144:147], v[136:139]
	v_add_u32_e32 v144, v177, v213
	v_mul_f32_e32 v150, v173, v173
	v_mul_f32_e32 v148, v243, v243
	ds_read_b128 v[144:147], v144
	v_pk_add_f32 v[148:149], v[150:151], v[148:149]
	v_med3_f32 v150, v173, s78, v240
	v_med3_f32 v151, v243, s78, v240
	v_cvt_pk_fp8_f32 v155, v150, v151 op_sel:[0,0,1]
	s_waitcnt lgkmcnt(1)
	v_mfma_f32_16x16x32_bf16 v[132:135], v[50:53], v[140:143], v[132:135]
	v_add_f32_e64 v140, v152, v148
	v_add_f32_e64 v141, v153, v149
	v_and_b32_e32 v143, 0xffff0000, v47
	v_and_b32_e32 v142, 0xffff0000, v46
	v_pk_add_f32 v[148:149], v[140:141], v[140:141] op_sel_hi:[0,1]
	s_waitcnt lgkmcnt(0)
	v_mfma_f32_16x16x32_bf16 v[136:139], v[50:53], v[144:147], v[136:139]
	v_lshlrev_b32_e32 v141, 16, v47
	v_lshlrev_b32_e32 v140, 16, v46
	v_pk_mul_f32 v[144:145], v[142:143], v[142:143]
	global_store_dwordx2 v[130:131], v[154:155], off offset:608
	v_pk_fma_f32 v[144:145], v[140:141], v[140:141], v[144:145]
	v_med3_f32 v140, v140, s78, v240
	v_med3_f32 v142, v142, s78, v240
	v_mov_b32_e32 v154, 0
	v_cvt_pk_fp8_f32 v154, v140, v142
	v_and_b32_e32 v151, 0xffff0000, v49
	v_and_b32_e32 v150, 0xffff0000, v48
	v_lshlrev_b32_e32 v147, 16, v49
	v_lshlrev_b32_e32 v146, 16, v48
	v_pk_mul_f32 v[152:153], v[150:151], v[150:151]
	v_add_f32_e32 v148, v144, v145
	v_pk_fma_f32 v[152:153], v[146:147], v[146:147], v[152:153]
	v_med3_f32 v140, v141, s78, v240
	v_med3_f32 v141, v143, s78, v240
	v_med3_f32 v144, v146, s78, v240
	v_med3_f32 v145, v150, s78, v240
	v_add_u32_e32 v146, v175, v214
	v_mov_b32_e32 v155, 0
	v_cvt_pk_fp8_f32 v154, v140, v141 op_sel:[0,0,1]
	ds_read_b128 v[140:143], v146
	v_cvt_pk_fp8_f32 v155, v144, v145
	v_med3_f32 v150, v147, s78, v240
	ds_read_b128 v[144:147], v146 offset:32768
	s_waitcnt lgkmcnt(1)
	v_mfma_f32_16x16x32_bf16 v[132:135], v[46:49], v[140:143], v[132:135]
	v_add_u32_e32 v140, v176, v214
	ds_read_b128 v[140:143], v140
	v_med3_f32 v151, v151, s78, v240
	s_waitcnt lgkmcnt(1)
	v_mfma_f32_16x16x32_bf16 v[136:139], v[46:49], v[144:147], v[136:139]
	v_add_u32_e32 v144, v177, v214
	ds_read_b128 v[144:147], v144
	v_cvt_pk_fp8_f32 v155, v150, v151 op_sel:[0,0,1]
	s_waitcnt lgkmcnt(1)
	v_mfma_f32_16x16x32_bf16 v[132:135], v[46:49], v[140:143], v[132:135]
	v_add_f32_e32 v140, v152, v148
	v_pk_add_f32 v[150:151], v[152:153], v[140:141] op_sel_hi:[1,0]
	global_store_dwordx2 v[130:131], v[154:155], off offset:640
	s_waitcnt lgkmcnt(0)
	v_mfma_f32_16x16x32_bf16 v[136:139], v[46:49], v[144:147], v[136:139]
	v_lshlrev_b32_e32 v144, 16, v42
	v_and_b32_e32 v145, 0xffff0000, v42
	v_mul_f32_e32 v140, v144, v144
	v_add_u32_e32 v147, v175, v215
	v_pk_fma_f32 v[152:153], v[144:145], v[144:145], v[140:141] op_sel_hi:[1,1,0]
	v_lshlrev_b32_e32 v154, 16, v43
	ds_read_b128 v[140:143], v147
	v_and_b32_e32 v155, 0xffff0000, v43
	v_mul_f32_e32 v146, v154, v154
	v_pk_fma_f32 v[156:157], v[154:155], v[154:155], v[146:147] op_sel_hi:[1,1,0]
	v_med3_f32 v148, v144, s78, v240
	v_med3_f32 v150, v145, s78, v240
	ds_read_b128 v[144:147], v147 offset:32768
	s_waitcnt lgkmcnt(1)
	v_mfma_f32_16x16x32_bf16 v[132:135], v[42:45], v[140:143], v[132:135]
	v_add_u32_e32 v140, v176, v215
	ds_read_b128 v[140:143], v140
	global_store_dwordx2 v[130:131], v[158:159], off offset:576
	v_mov_b32_e32 v158, 0
	s_waitcnt lgkmcnt(1)
	v_mfma_f32_16x16x32_bf16 v[136:139], v[42:45], v[144:147], v[136:139]
	v_add_u32_e32 v144, v177, v215
	v_cvt_pk_fp8_f32 v158, v148, v150
	ds_read_b128 v[144:147], v144
	s_waitcnt lgkmcnt(1)
	v_mfma_f32_16x16x32_bf16 v[132:135], v[42:45], v[140:143], v[132:135]
	v_med3_f32 v140, v154, s78, v240
	v_med3_f32 v141, v155, s78, v240
	v_cvt_pk_fp8_f32 v158, v140, v141 op_sel:[0,0,1]
	v_lshlrev_b32_e32 v141, 16, v44
	v_and_b32_e32 v143, 0xffff0000, v44
	s_waitcnt lgkmcnt(0)
	v_mfma_f32_16x16x32_bf16 v[136:139], v[42:45], v[144:147], v[136:139]
	v_med3_f32 v142, v141, s78, v240
	v_med3_f32 v144, v143, s78, v240
	v_mov_b32_e32 v159, 0
	v_cvt_pk_fp8_f32 v159, v142, v144
	v_lshlrev_b32_e32 v145, 16, v45
	v_and_b32_e32 v147, 0xffff0000, v45
	v_med3_f32 v142, v145, s78, v240
	v_med3_f32 v144, v147, s78, v240
	v_lshlrev_b32_e32 v160, 16, v39
	v_and_b32_e32 v161, 0xffff0000, v39
	v_cvt_pk_fp8_f32 v159, v142, v144 op_sel:[0,0,1]
	v_and_b32_e32 v142, 0xffff0000, v38
	v_mul_f32_e32 v152, v160, v160
	v_mul_f32_e32 v156, v161, v161
	v_lshlrev_b32_e32 v140, 16, v38
	v_pk_mul_f32 v[154:155], v[142:143], v[142:143]
	v_and_b32_e32 v146, 0xffff0000, v40
	v_pk_fma_f32 v[154:155], v[140:141], v[140:141], v[154:155]
	v_pk_add_f32 v[152:153], v[152:153], v[156:157]
	v_lshlrev_b32_e32 v144, 16, v40
	v_pk_add_f32 v[152:153], v[154:155], v[152:153]
	v_pk_mul_f32 v[154:155], v[146:147], v[146:147]
	v_med3_f32 v140, v140, s78, v240
	v_pk_fma_f32 v[154:155], v[144:145], v[144:145], v[154:155]
	v_med3_f32 v141, v142, s78, v240
	v_pk_add_f32 v[152:153], v[154:155], v[152:153]
	v_mov_b32_e32 v154, 0
	v_cvt_pk_fp8_f32 v154, v140, v141
	v_med3_f32 v140, v160, s78, v240
	v_med3_f32 v141, v161, s78, v240
	v_med3_f32 v145, v146, s78, v240
	v_add_u32_e32 v146, v175, v216
	v_cvt_pk_fp8_f32 v154, v140, v141 op_sel:[0,0,1]
	v_med3_f32 v144, v144, s78, v240
	ds_read_b128 v[140:143], v146
	v_mov_b32_e32 v155, 0
	v_cvt_pk_fp8_f32 v155, v144, v145
	ds_read_b128 v[144:147], v146 offset:32768
	s_waitcnt lgkmcnt(1)
	v_mfma_f32_16x16x32_bf16 v[132:135], v[38:41], v[140:143], v[132:135]
	v_add_u32_e32 v140, v176, v216
	v_lshlrev_b32_e32 v173, 16, v41
	v_and_b32_e32 v243, 0xffff0000, v41
	ds_read_b128 v[140:143], v140
	s_waitcnt lgkmcnt(1)
	v_mfma_f32_16x16x32_bf16 v[136:139], v[38:41], v[144:147], v[136:139]
	v_add_u32_e32 v144, v177, v216
	v_mul_f32_e32 v150, v173, v173
	v_mul_f32_e32 v148, v243, v243
	ds_read_b128 v[144:147], v144
	v_pk_add_f32 v[148:149], v[150:151], v[148:149]
	v_med3_f32 v150, v173, s78, v240
	v_med3_f32 v151, v243, s78, v240
	v_cvt_pk_fp8_f32 v155, v150, v151 op_sel:[0,0,1]
	s_waitcnt lgkmcnt(1)
	v_mfma_f32_16x16x32_bf16 v[132:135], v[38:41], v[140:143], v[132:135]
	v_add_f32_e64 v140, v152, v148
	v_add_f32_e64 v141, v153, v149
	v_and_b32_e32 v143, 0xffff0000, v35
	v_and_b32_e32 v142, 0xffff0000, v34
	v_pk_add_f32 v[148:149], v[140:141], v[140:141] op_sel_hi:[0,1]
	s_waitcnt lgkmcnt(0)
	v_mfma_f32_16x16x32_bf16 v[136:139], v[38:41], v[144:147], v[136:139]
	v_lshlrev_b32_e32 v141, 16, v35
	v_lshlrev_b32_e32 v140, 16, v34
	v_pk_mul_f32 v[144:145], v[142:143], v[142:143]
	global_store_dwordx2 v[130:131], v[154:155], off offset:704
	v_pk_fma_f32 v[144:145], v[140:141], v[140:141], v[144:145]
	v_med3_f32 v140, v140, s78, v240
	v_med3_f32 v142, v142, s78, v240
	v_mov_b32_e32 v154, 0
	v_cvt_pk_fp8_f32 v154, v140, v142
	v_and_b32_e32 v151, 0xffff0000, v37
	v_and_b32_e32 v150, 0xffff0000, v36
	v_lshlrev_b32_e32 v147, 16, v37
	v_lshlrev_b32_e32 v146, 16, v36
	v_pk_mul_f32 v[152:153], v[150:151], v[150:151]
	v_add_f32_e32 v148, v144, v145
	v_pk_fma_f32 v[152:153], v[146:147], v[146:147], v[152:153]
	v_med3_f32 v140, v141, s78, v240
	v_med3_f32 v141, v143, s78, v240
	v_med3_f32 v144, v146, s78, v240
	v_med3_f32 v145, v150, s78, v240
	v_add_u32_e32 v146, v175, v217
	v_mov_b32_e32 v155, 0
	v_cvt_pk_fp8_f32 v154, v140, v141 op_sel:[0,0,1]
	ds_read_b128 v[140:143], v146
	v_cvt_pk_fp8_f32 v155, v144, v145
	v_med3_f32 v150, v147, s78, v240
	ds_read_b128 v[144:147], v146 offset:32768
	s_waitcnt lgkmcnt(1)
	v_mfma_f32_16x16x32_bf16 v[132:135], v[34:37], v[140:143], v[132:135]
	v_add_u32_e32 v140, v176, v217
	ds_read_b128 v[140:143], v140
	v_med3_f32 v151, v151, s78, v240
	s_waitcnt lgkmcnt(1)
	v_mfma_f32_16x16x32_bf16 v[136:139], v[34:37], v[144:147], v[136:139]
	v_add_u32_e32 v144, v177, v217
	ds_read_b128 v[144:147], v144
	v_cvt_pk_fp8_f32 v155, v150, v151 op_sel:[0,0,1]
	s_waitcnt lgkmcnt(1)
	v_mfma_f32_16x16x32_bf16 v[132:135], v[34:37], v[140:143], v[132:135]
	v_add_f32_e32 v140, v152, v148
	v_pk_add_f32 v[150:151], v[152:153], v[140:141] op_sel_hi:[1,0]
	global_store_dwordx2 v[130:131], v[154:155], off offset:736
	s_waitcnt lgkmcnt(0)
	v_mfma_f32_16x16x32_bf16 v[136:139], v[34:37], v[144:147], v[136:139]
	v_lshlrev_b32_e32 v144, 16, v30
	v_and_b32_e32 v145, 0xffff0000, v30
	v_mul_f32_e32 v140, v144, v144
	v_add_u32_e32 v147, v175, v219
	v_pk_fma_f32 v[152:153], v[144:145], v[144:145], v[140:141] op_sel_hi:[1,1,0]
	v_lshlrev_b32_e32 v154, 16, v31
	ds_read_b128 v[140:143], v147
	v_and_b32_e32 v155, 0xffff0000, v31
	v_mul_f32_e32 v146, v154, v154
	v_pk_fma_f32 v[156:157], v[154:155], v[154:155], v[146:147] op_sel_hi:[1,1,0]
	v_med3_f32 v148, v144, s78, v240
	v_med3_f32 v150, v145, s78, v240
	ds_read_b128 v[144:147], v147 offset:32768
	s_waitcnt lgkmcnt(1)
	v_mfma_f32_16x16x32_bf16 v[132:135], v[30:33], v[140:143], v[132:135]
	v_add_u32_e32 v140, v176, v219
	ds_read_b128 v[140:143], v140
	global_store_dwordx2 v[130:131], v[158:159], off offset:672
	v_mov_b32_e32 v158, 0
	s_waitcnt lgkmcnt(1)
	v_mfma_f32_16x16x32_bf16 v[136:139], v[30:33], v[144:147], v[136:139]
	v_add_u32_e32 v144, v177, v219
	v_cvt_pk_fp8_f32 v158, v148, v150
	ds_read_b128 v[144:147], v144
	s_waitcnt lgkmcnt(1)
	v_mfma_f32_16x16x32_bf16 v[132:135], v[30:33], v[140:143], v[132:135]
	v_med3_f32 v140, v154, s78, v240
	v_med3_f32 v141, v155, s78, v240
	v_cvt_pk_fp8_f32 v158, v140, v141 op_sel:[0,0,1]
	v_lshlrev_b32_e32 v141, 16, v32
	v_and_b32_e32 v143, 0xffff0000, v32
	s_waitcnt lgkmcnt(0)
	v_mfma_f32_16x16x32_bf16 v[136:139], v[30:33], v[144:147], v[136:139]
	v_med3_f32 v142, v141, s78, v240
	v_med3_f32 v144, v143, s78, v240
	v_mov_b32_e32 v159, 0
	v_cvt_pk_fp8_f32 v159, v142, v144
	v_lshlrev_b32_e32 v145, 16, v33
	v_and_b32_e32 v147, 0xffff0000, v33
	v_med3_f32 v142, v145, s78, v240
	v_med3_f32 v144, v147, s78, v240
	v_lshlrev_b32_e32 v160, 16, v27
	v_and_b32_e32 v161, 0xffff0000, v27
	v_cvt_pk_fp8_f32 v159, v142, v144 op_sel:[0,0,1]
	v_and_b32_e32 v142, 0xffff0000, v26
	v_mul_f32_e32 v152, v160, v160
	v_mul_f32_e32 v156, v161, v161
	v_lshlrev_b32_e32 v140, 16, v26
	v_pk_mul_f32 v[154:155], v[142:143], v[142:143]
	v_and_b32_e32 v146, 0xffff0000, v28
	v_pk_fma_f32 v[154:155], v[140:141], v[140:141], v[154:155]
	v_pk_add_f32 v[152:153], v[152:153], v[156:157]
	v_lshlrev_b32_e32 v144, 16, v28
	v_pk_add_f32 v[152:153], v[154:155], v[152:153]
	v_pk_mul_f32 v[154:155], v[146:147], v[146:147]
	v_med3_f32 v140, v140, s78, v240
	v_pk_fma_f32 v[154:155], v[144:145], v[144:145], v[154:155]
	v_med3_f32 v141, v142, s78, v240
	v_pk_add_f32 v[152:153], v[154:155], v[152:153]
	v_mov_b32_e32 v154, 0
	v_cvt_pk_fp8_f32 v154, v140, v141
	v_med3_f32 v140, v160, s78, v240
	v_med3_f32 v141, v161, s78, v240
	v_med3_f32 v145, v146, s78, v240
	v_add_u32_e32 v146, v175, v220
	v_cvt_pk_fp8_f32 v154, v140, v141 op_sel:[0,0,1]
	v_med3_f32 v144, v144, s78, v240
	ds_read_b128 v[140:143], v146
	v_mov_b32_e32 v155, 0
	v_cvt_pk_fp8_f32 v155, v144, v145
	ds_read_b128 v[144:147], v146 offset:32768
	s_waitcnt lgkmcnt(1)
	v_mfma_f32_16x16x32_bf16 v[132:135], v[26:29], v[140:143], v[132:135]
	v_add_u32_e32 v140, v176, v220
	v_lshlrev_b32_e32 v173, 16, v29
	v_and_b32_e32 v243, 0xffff0000, v29
	ds_read_b128 v[140:143], v140
	s_waitcnt lgkmcnt(1)
	v_mfma_f32_16x16x32_bf16 v[136:139], v[26:29], v[144:147], v[136:139]
	v_add_u32_e32 v144, v177, v220
	v_mul_f32_e32 v150, v173, v173
	v_mul_f32_e32 v148, v243, v243
	ds_read_b128 v[144:147], v144
	v_pk_add_f32 v[148:149], v[150:151], v[148:149]
	v_med3_f32 v150, v173, s78, v240
	v_med3_f32 v151, v243, s78, v240
	v_cvt_pk_fp8_f32 v155, v150, v151 op_sel:[0,0,1]
	s_waitcnt lgkmcnt(1)
	v_mfma_f32_16x16x32_bf16 v[132:135], v[26:29], v[140:143], v[132:135]
	v_add_f32_e64 v140, v152, v148
	v_add_f32_e64 v141, v153, v149
	v_and_b32_e32 v143, 0xffff0000, v23
	v_and_b32_e32 v142, 0xffff0000, v22
	v_pk_add_f32 v[148:149], v[140:141], v[140:141] op_sel_hi:[0,1]
	s_waitcnt lgkmcnt(0)
	v_mfma_f32_16x16x32_bf16 v[136:139], v[26:29], v[144:147], v[136:139]
	v_lshlrev_b32_e32 v141, 16, v23
	v_lshlrev_b32_e32 v140, 16, v22
	v_pk_mul_f32 v[144:145], v[142:143], v[142:143]
	global_store_dwordx2 v[130:131], v[154:155], off offset:800
	v_pk_fma_f32 v[144:145], v[140:141], v[140:141], v[144:145]
	v_med3_f32 v140, v140, s78, v240
	v_med3_f32 v142, v142, s78, v240
	v_mov_b32_e32 v154, 0
	v_cvt_pk_fp8_f32 v154, v140, v142
	v_and_b32_e32 v151, 0xffff0000, v25
	v_and_b32_e32 v150, 0xffff0000, v24
	v_lshlrev_b32_e32 v147, 16, v25
	v_lshlrev_b32_e32 v146, 16, v24
	v_pk_mul_f32 v[152:153], v[150:151], v[150:151]
	v_add_f32_e32 v148, v144, v145
	v_pk_fma_f32 v[152:153], v[146:147], v[146:147], v[152:153]
	v_med3_f32 v140, v141, s78, v240
	v_med3_f32 v141, v143, s78, v240
	v_med3_f32 v144, v146, s78, v240
	v_med3_f32 v145, v150, s78, v240
	v_add_u32_e32 v146, v175, v221
	v_mov_b32_e32 v155, 0
	v_cvt_pk_fp8_f32 v154, v140, v141 op_sel:[0,0,1]
	ds_read_b128 v[140:143], v146
	v_cvt_pk_fp8_f32 v155, v144, v145
	v_med3_f32 v150, v147, s78, v240
	ds_read_b128 v[144:147], v146 offset:32768
	s_waitcnt lgkmcnt(1)
	v_mfma_f32_16x16x32_bf16 v[132:135], v[22:25], v[140:143], v[132:135]
	v_add_u32_e32 v140, v176, v221
	ds_read_b128 v[140:143], v140
	v_med3_f32 v151, v151, s78, v240
	s_waitcnt lgkmcnt(1)
	v_mfma_f32_16x16x32_bf16 v[136:139], v[22:25], v[144:147], v[136:139]
	v_add_u32_e32 v144, v177, v221
	ds_read_b128 v[144:147], v144
	v_cvt_pk_fp8_f32 v155, v150, v151 op_sel:[0,0,1]
	s_waitcnt lgkmcnt(1)
	v_mfma_f32_16x16x32_bf16 v[132:135], v[22:25], v[140:143], v[132:135]
	v_add_f32_e32 v140, v152, v148
	v_pk_add_f32 v[150:151], v[152:153], v[140:141] op_sel_hi:[1,0]
	global_store_dwordx2 v[130:131], v[154:155], off offset:832
	s_waitcnt lgkmcnt(0)
	v_mfma_f32_16x16x32_bf16 v[136:139], v[22:25], v[144:147], v[136:139]
	v_lshlrev_b32_e32 v144, 16, v18
	v_and_b32_e32 v145, 0xffff0000, v18
	v_mul_f32_e32 v140, v144, v144
	v_add_u32_e32 v147, v175, v222
	v_pk_fma_f32 v[152:153], v[144:145], v[144:145], v[140:141] op_sel_hi:[1,1,0]
	v_lshlrev_b32_e32 v154, 16, v19
	ds_read_b128 v[140:143], v147
	v_and_b32_e32 v155, 0xffff0000, v19
	v_mul_f32_e32 v146, v154, v154
	v_pk_fma_f32 v[156:157], v[154:155], v[154:155], v[146:147] op_sel_hi:[1,1,0]
	v_med3_f32 v148, v144, s78, v240
	v_med3_f32 v150, v145, s78, v240
	ds_read_b128 v[144:147], v147 offset:32768
	s_waitcnt lgkmcnt(1)
	v_mfma_f32_16x16x32_bf16 v[132:135], v[18:21], v[140:143], v[132:135]
	v_add_u32_e32 v140, v176, v222
	ds_read_b128 v[140:143], v140
	global_store_dwordx2 v[130:131], v[158:159], off offset:768
	v_mov_b32_e32 v158, 0
	s_waitcnt lgkmcnt(1)
	v_mfma_f32_16x16x32_bf16 v[136:139], v[18:21], v[144:147], v[136:139]
	v_add_u32_e32 v144, v177, v222
	v_cvt_pk_fp8_f32 v158, v148, v150
	ds_read_b128 v[144:147], v144
	s_waitcnt lgkmcnt(1)
	v_mfma_f32_16x16x32_bf16 v[132:135], v[18:21], v[140:143], v[132:135]
	v_med3_f32 v140, v154, s78, v240
	v_med3_f32 v141, v155, s78, v240
	v_cvt_pk_fp8_f32 v158, v140, v141 op_sel:[0,0,1]
	v_lshlrev_b32_e32 v141, 16, v20
	v_and_b32_e32 v143, 0xffff0000, v20
	s_waitcnt lgkmcnt(0)
	v_mfma_f32_16x16x32_bf16 v[136:139], v[18:21], v[144:147], v[136:139]
	v_med3_f32 v142, v141, s78, v240
	v_med3_f32 v144, v143, s78, v240
	v_mov_b32_e32 v159, 0
	v_cvt_pk_fp8_f32 v159, v142, v144
	v_lshlrev_b32_e32 v145, 16, v21
	v_and_b32_e32 v147, 0xffff0000, v21
	v_med3_f32 v142, v145, s78, v240
	v_med3_f32 v144, v147, s78, v240
	v_lshlrev_b32_e32 v160, 16, v15
	v_and_b32_e32 v161, 0xffff0000, v15
	v_cvt_pk_fp8_f32 v159, v142, v144 op_sel:[0,0,1]
	v_and_b32_e32 v142, 0xffff0000, v14
	v_mul_f32_e32 v152, v160, v160
	v_mul_f32_e32 v156, v161, v161
	v_lshlrev_b32_e32 v140, 16, v14
	v_pk_mul_f32 v[154:155], v[142:143], v[142:143]
	v_and_b32_e32 v146, 0xffff0000, v16
	v_pk_fma_f32 v[154:155], v[140:141], v[140:141], v[154:155]
	v_pk_add_f32 v[152:153], v[152:153], v[156:157]
	v_lshlrev_b32_e32 v144, 16, v16
	v_pk_add_f32 v[152:153], v[154:155], v[152:153]
	v_pk_mul_f32 v[154:155], v[146:147], v[146:147]
	v_med3_f32 v140, v140, s78, v240
	v_pk_fma_f32 v[154:155], v[144:145], v[144:145], v[154:155]
	v_med3_f32 v141, v142, s78, v240
	v_pk_add_f32 v[152:153], v[154:155], v[152:153]
	v_mov_b32_e32 v154, 0
	v_cvt_pk_fp8_f32 v154, v140, v141
	v_med3_f32 v140, v160, s78, v240
	v_med3_f32 v141, v161, s78, v240
	v_med3_f32 v145, v146, s78, v240
	v_add_u32_e32 v146, v175, v223
	v_cvt_pk_fp8_f32 v154, v140, v141 op_sel:[0,0,1]
	v_med3_f32 v144, v144, s78, v240
	ds_read_b128 v[140:143], v146
	v_mov_b32_e32 v155, 0
	v_cvt_pk_fp8_f32 v155, v144, v145
	ds_read_b128 v[144:147], v146 offset:32768
	s_waitcnt lgkmcnt(1)
	v_mfma_f32_16x16x32_bf16 v[132:135], v[14:17], v[140:143], v[132:135]
	v_add_u32_e32 v140, v176, v223
	v_lshlrev_b32_e32 v173, 16, v17
	v_and_b32_e32 v243, 0xffff0000, v17
	ds_read_b128 v[140:143], v140
	s_waitcnt lgkmcnt(1)
	v_mfma_f32_16x16x32_bf16 v[136:139], v[14:17], v[144:147], v[136:139]
	v_add_u32_e32 v144, v177, v223
	v_mul_f32_e32 v150, v173, v173
	v_mul_f32_e32 v148, v243, v243
	ds_read_b128 v[144:147], v144
	v_pk_add_f32 v[148:149], v[150:151], v[148:149]
	v_med3_f32 v150, v173, s78, v240
	v_med3_f32 v151, v243, s78, v240
	v_cvt_pk_fp8_f32 v155, v150, v151 op_sel:[0,0,1]
	s_waitcnt lgkmcnt(1)
	v_mfma_f32_16x16x32_bf16 v[132:135], v[14:17], v[140:143], v[132:135]
	v_add_f32_e64 v140, v152, v148
	v_add_f32_e64 v141, v153, v149
	v_and_b32_e32 v143, 0xffff0000, v11
	v_and_b32_e32 v142, 0xffff0000, v10
	v_pk_add_f32 v[148:149], v[140:141], v[140:141] op_sel_hi:[0,1]
	s_waitcnt lgkmcnt(0)
	v_mfma_f32_16x16x32_bf16 v[136:139], v[14:17], v[144:147], v[136:139]
	v_lshlrev_b32_e32 v141, 16, v11
	v_lshlrev_b32_e32 v140, 16, v10
	v_pk_mul_f32 v[144:145], v[142:143], v[142:143]
	global_store_dwordx2 v[130:131], v[154:155], off offset:896
	v_pk_fma_f32 v[144:145], v[140:141], v[140:141], v[144:145]
	v_med3_f32 v140, v140, s78, v240
	v_med3_f32 v142, v142, s78, v240
	v_mov_b32_e32 v154, 0
	v_cvt_pk_fp8_f32 v154, v140, v142
	v_and_b32_e32 v151, 0xffff0000, v13
	v_and_b32_e32 v150, 0xffff0000, v12
	v_lshlrev_b32_e32 v147, 16, v13
	v_lshlrev_b32_e32 v146, 16, v12
	v_pk_mul_f32 v[152:153], v[150:151], v[150:151]
	v_add_f32_e32 v148, v144, v145
	v_pk_fma_f32 v[152:153], v[146:147], v[146:147], v[152:153]
	v_med3_f32 v140, v141, s78, v240
	v_med3_f32 v141, v143, s78, v240
	v_med3_f32 v144, v146, s78, v240
	v_add_u32_e32 v146, v175, v224
	v_cvt_pk_fp8_f32 v154, v140, v141 op_sel:[0,0,1]
	ds_read_b128 v[140:143], v146
	v_med3_f32 v145, v150, s78, v240
	v_mov_b32_e32 v155, 0
	v_cvt_pk_fp8_f32 v155, v144, v145
	v_med3_f32 v150, v147, s78, v240
	ds_read_b128 v[144:147], v146 offset:32768
	s_waitcnt lgkmcnt(1)
	v_mfma_f32_16x16x32_bf16 v[132:135], v[10:13], v[140:143], v[132:135]
	v_add_u32_e32 v140, v176, v224
	ds_read_b128 v[140:143], v140
	v_med3_f32 v151, v151, s78, v240
	s_waitcnt lgkmcnt(1)
	v_mfma_f32_16x16x32_bf16 v[136:139], v[10:13], v[144:147], v[136:139]
	v_add_u32_e32 v144, v177, v224
	v_cvt_pk_fp8_f32 v155, v150, v151 op_sel:[0,0,1]
	ds_read_b128 v[144:147], v144
	s_waitcnt lgkmcnt(1)
	v_mfma_f32_16x16x32_bf16 v[132:135], v[10:13], v[140:143], v[132:135]
	v_add_f32_e32 v140, v152, v148
	v_pk_add_f32 v[150:151], v[152:153], v[140:141] op_sel_hi:[1,0]
	v_lshlrev_b32_e32 v140, 16, v6
	global_store_dwordx2 v[130:131], v[154:155], off offset:928
	v_and_b32_e32 v141, 0xffff0000, v6
	v_mul_f32_e32 v142, v140, v140
	v_lshlrev_b32_e32 v154, 16, v7
	s_waitcnt lgkmcnt(0)
	v_mfma_f32_16x16x32_bf16 v[136:139], v[10:13], v[144:147], v[136:139]
	v_fma_f32 v152, v140, v140, v142
	v_fma_f32 v153, v141, v141, v142
	v_and_b32_e32 v155, 0xffff0000, v7
	v_mul_f32_e32 v142, v154, v154
	v_add_u32_e32 v146, v175, v225
	v_pk_fma_f32 v[156:157], v[154:155], v[154:155], v[142:143] op_sel_hi:[1,1,0]
	v_med3_f32 v144, v140, s78, v240
	v_med3_f32 v145, v141, s78, v240
	ds_read_b128 v[140:143], v146
	global_store_dwordx2 v[130:131], v[158:159], off offset:864
	v_mov_b32_e32 v158, 0
	v_cvt_pk_fp8_f32 v158, v144, v145
	ds_read_b128 v[144:147], v146 offset:32768
	s_waitcnt lgkmcnt(1)
	v_mfma_f32_16x16x32_bf16 v[132:135], v[6:9], v[140:143], v[132:135]
	v_add_u32_e32 v140, v176, v225
	ds_read_b128 v[140:143], v140
	v_med3_f32 v148, v154, s78, v240
	s_waitcnt lgkmcnt(1)
	v_mfma_f32_16x16x32_bf16 v[136:139], v[6:9], v[144:147], v[136:139]
	v_add_u32_e32 v144, v177, v225
	ds_read_b128 v[144:147], v144
	v_med3_f32 v150, v155, s78, v240
	s_waitcnt lgkmcnt(1)
	v_mfma_f32_16x16x32_bf16 v[132:135], v[6:9], v[140:143], v[132:135]
	v_lshlrev_b32_e32 v141, 16, v8
	v_and_b32_e32 v143, 0xffff0000, v8
	v_med3_f32 v154, v141, s78, v240
	v_med3_f32 v155, v143, s78, v240
	v_mov_b32_e32 v159, 0
	v_cvt_pk_fp8_f32 v159, v154, v155
	v_lshlrev_b32_e32 v155, 16, v9
	v_and_b32_e32 v161, 0xffff0000, v9
	v_lshlrev_b32_e32 v140, 16, v2
	v_and_b32_e32 v142, 0xffff0000, v2
	v_med3_f32 v244, v155, s78, v240
	v_med3_f32 v245, v161, s78, v240
	v_lshlrev_b32_e32 v154, 16, v4
	v_and_b32_e32 v160, 0xffff0000, v4
	v_cvt_pk_fp8_f32 v159, v244, v245 op_sel:[0,0,1]
	v_med3_f32 v245, v140, s78, v240
	v_med3_f32 v246, v142, s78, v240
	v_mov_b32_e32 v244, 0
	v_cvt_pk_fp8_f32 v244, v245, v246
	v_med3_f32 v246, v154, s78, v240
	v_med3_f32 v247, v160, s78, v240
	v_mov_b32_e32 v245, 0
	v_cvt_pk_fp8_f32 v245, v246, v247
	v_cvt_pk_fp8_f32 v158, v148, v150 op_sel:[0,0,1]
	v_lshlrev_b32_e32 v148, 16, v3
	v_and_b32_e32 v150, 0xffff0000, v3
	v_lshlrev_b32_e32 v173, 16, v5
	v_and_b32_e32 v243, 0xffff0000, v5
	v_mul_f32_e32 v152, v148, v148
	v_mul_f32_e32 v156, v150, v150
	v_med3_f32 v148, v148, s78, v240
	v_med3_f32 v150, v150, s78, v240
	v_cvt_pk_fp8_f32 v244, v148, v150 op_sel:[0,0,1]
	v_med3_f32 v148, v173, s78, v240
	v_med3_f32 v150, v243, s78, v240
	v_cvt_pk_fp8_f32 v245, v148, v150 op_sel:[0,0,1]
	global_store_dwordx2 v[130:131], v[158:159], off offset:960
	global_store_dwordx2 v[130:131], v[244:245], off offset:992
	global_load_dword v158, v[168:169], off
	s_nop 0
	global_load_dword v159, v[168:169], off offset:64
	v_pk_mul_f32 v[130:131], v[142:143], v[142:143]
	v_mul_f32_e32 v150, v173, v173
	v_pk_fma_f32 v[130:131], v[140:141], v[140:141], v[130:131]
	v_pk_add_f32 v[140:141], v[152:153], v[156:157]
	v_mul_f32_e32 v148, v243, v243
	v_pk_add_f32 v[130:131], v[130:131], v[140:141]
	v_pk_mul_f32 v[140:141], v[160:161], v[160:161]
	s_waitcnt lgkmcnt(0)
	v_mfma_f32_16x16x32_bf16 v[136:139], v[6:9], v[144:147], v[136:139]
	v_fma_f32 v140, v154, v154, v140
	v_fma_f32 v141, v155, v155, v141
	v_add_u32_e32 v144, v175, v226
	v_pk_add_f32 v[130:131], v[140:141], v[130:131]
	v_pk_add_f32 v[140:141], v[150:151], v[148:149]
	v_and_b32_e32 v148, 64, v241
	v_pk_add_f32 v[130:131], v[130:131], v[140:141]
	v_add_u32_e32 v149, 64, v148
	v_add_f32_e32 v130, v130, v131
	v_xor_b32_e32 v131, 16, v241
	v_cmp_lt_i32_e32 vcc, v131, v149
	ds_read_b128 v[140:143], v144
	s_mov_b32 s0, 0xf800000
	v_cndmask_b32_e32 v131, v241, v131, vcc
	v_lshlrev_b32_e32 v131, 2, v131
	ds_bpermute_b32 v131, v131, v130
	s_waitcnt lgkmcnt(1)
	v_mfma_f32_16x16x32_bf16 v[132:135], v[2:5], v[140:143], v[132:135]
	ds_read_b128 v[144:147], v144 offset:32768
	v_mov_b32_e32 v243, 0
	v_mov_b32_e32 v244, 0
	s_waitcnt lgkmcnt(1)
	v_add_f32_e32 v130, v130, v131
	v_xor_b32_e32 v131, 32, v241
	v_cmp_lt_i32_e32 vcc, v131, v149
	v_mov_b32_e32 v245, 0
	s_nop 0
	v_cndmask_b32_e32 v131, v241, v131, vcc
	v_lshlrev_b32_e32 v131, 2, v131
	ds_bpermute_b32 v149, v131, v130
	v_mov_b32_e32 v131, 0
	s_waitcnt lgkmcnt(0)
	v_add_f32_e32 v130, v130, v149
	v_fmamk_f32 v130, v130, 0x3a800000, v166
	v_mul_f32_e32 v140, 0x4f800000, v130
	v_cmp_gt_f32_e32 vcc, s0, v130
	s_nop 1
	v_cndmask_b32_e32 v130, v130, v140, vcc
	v_sqrt_f32_e32 v149, v130
	v_add_u32_e32 v140, v176, v226
	ds_read_b128 v[140:143], v140
	v_mfma_f32_16x16x32_bf16 v[136:139], v[2:5], v[144:147], v[136:139]
	v_add_u32_e32 v144, -1, v149
	v_fma_f32 v145, -v144, v149, v130
	v_cmp_ge_f32_e64 s[0:1], 0, v145
	v_add_u32_e32 v145, 1, v149
	v_fma_f32 v146, -v145, v149, v130
	v_cndmask_b32_e64 v144, v149, v144, s[0:1]
	v_cmp_lt_f32_e64 s[0:1], 0, v146
	s_waitcnt lgkmcnt(0)
	v_mfma_f32_16x16x32_bf16 v[132:135], v[2:5], v[140:143], v[132:135]
	v_cndmask_b32_e64 v144, v144, v145, s[0:1]
	v_mul_f32_e32 v145, 0x37800000, v144
	v_cndmask_b32_e32 v144, v144, v145, vcc
	v_cmp_class_f32_e32 vcc, v130, v237
	s_nop 1
	v_cndmask_b32_e32 v130, v144, v130, vcc
	v_div_scale_f32 v149, s[0:1], v130, v130, 1.0
	v_rcp_f32_e32 v150, v149
	v_add_u32_e32 v144, v177, v226
	ds_read_b128 v[144:147], v144
	v_fma_f32 v140, -v149, v150, 1.0
	v_fmac_f32_e32 v150, v140, v150
	v_div_scale_f32 v140, vcc, 1.0, v130, 1.0
	v_mul_f32_e32 v141, v140, v150
	v_fma_f32 v142, -v149, v141, v140
	v_fmac_f32_e32 v141, v142, v150
	v_fma_f32 v140, -v149, v141, v140
	v_div_fmas_f32 v140, v140, v150, v141
	v_div_fixup_f32 v173, v140, v130, 1.0
	v_or_b32_e32 v130, v148, v227
	v_lshlrev_b32_e32 v130, 2, v130
	v_or_b32_e32 v140, v148, v229
	ds_bpermute_b32 v130, v130, v173
	v_lshlrev_b32_e32 v140, 2, v140
	ds_bpermute_b32 v140, v140, v173
	s_waitcnt lgkmcnt(2)
	v_mfma_f32_16x16x32_bf16 v[136:139], v[2:5], v[144:147], v[136:139]
	s_waitcnt vmcnt(1) lgkmcnt(1)
	v_fma_f32 v132, v132, v130, v158
	s_waitcnt vmcnt(0)
	s_nop 4
	v_fma_f32 v130, v136, v130, v159
	ds_write2_b32 v228, v132, v130 offset1:16
	s_waitcnt lgkmcnt(1)
	v_fma_f32 v130, v133, v140, v158
	v_or_b32_e32 v133, v148, v231
	v_or_b32_e32 v136, v148, v233
	v_lshlrev_b32_e32 v133, 2, v133
	v_lshlrev_b32_e32 v136, 2, v136
	ds_bpermute_b32 v133, v133, v173
	ds_bpermute_b32 v136, v136, v173
	v_fma_f32 v132, v137, v140, v159
	ds_write2_b32 v230, v130, v132 offset1:16
	v_mov_b32_e32 v137, 0
	s_waitcnt lgkmcnt(2)
	v_fma_f32 v130, v134, v133, v158
	v_fma_f32 v132, v138, v133, v159
	s_waitcnt lgkmcnt(1)
	v_fmac_f32_e32 v158, v135, v136
	v_fmac_f32_e32 v159, v139, v136
	ds_write2_b32 v232, v130, v132 offset1:16
	ds_write2_b32 v234, v158, v159 offset1:16
	s_waitcnt lgkmcnt(0)
	v_mov_b32_e32 v130, 0
	v_mov_b32_e32 v134, 0
	v_mov_b32_e32 v133, 0
	v_mov_b32_e32 v132, 0
	v_mov_b32_e32 v135, 0
	v_mov_b32_e32 v136, 0
	v_mov_b32_e32 v138, 0
	s_and_saveexec_b64 s[54:55], s[4:5]
	s_cbranch_execz .LBB0_1720
	ds_read_b128 v[158:161], v238
	ds_read_b128 v[154:157], v238 offset:16
	ds_read_b128 v[150:153], v238 offset:32
	ds_read_b128 v[146:149], v238 offset:48
	ds_read_b128 v[142:145], v238 offset:64
	ds_read_b128 v[138:141], v238 offset:80
	ds_read_b128 v[134:137], v238 offset:96
	ds_read_b128 v[130:133], v238 offset:112
	s_waitcnt lgkmcnt(7)
	v_max_f32_e32 v243, v158, v158
	s_mov_b32 s0, 0xff61b1e6
	v_max_f32_e32 v243, 0xff61b1e6, v243
	v_cmp_lt_f32_e32 vcc, s0, v158
	v_cmp_gt_f32_e64 s[0:1], v159, v243
	s_nop 1
	v_cndmask_b32_e64 v243, v243, v159, s[0:1]
	v_cndmask_b32_e64 v244, 0, 1, s[0:1]
	v_cmp_gt_f32_e64 s[0:1], v160, v243
	s_nop 1
	v_cndmask_b32_e64 v243, v243, v160, s[0:1]
	v_cndmask_b32_e64 v244, v244, 2, s[0:1]
	v_cmp_gt_f32_e64 s[0:1], v161, v243
	s_nop 1
	v_cndmask_b32_e64 v243, v243, v161, s[0:1]
	v_cndmask_b32_e64 v244, v244, 3, s[0:1]
	s_waitcnt lgkmcnt(6)
	v_cmp_gt_f32_e64 s[0:1], v154, v243
	s_nop 1
	v_cndmask_b32_e64 v243, v243, v154, s[0:1]
	v_cndmask_b32_e64 v244, v244, 4, s[0:1]
	v_cmp_gt_f32_e64 s[0:1], v155, v243
	s_nop 1
	v_cndmask_b32_e64 v243, v243, v155, s[0:1]
	v_cndmask_b32_e64 v244, v244, 5, s[0:1]
	v_cmp_gt_f32_e64 s[0:1], v156, v243
	s_nop 1
	v_cndmask_b32_e64 v243, v243, v156, s[0:1]
	v_cndmask_b32_e64 v244, v244, 6, s[0:1]
	v_cmp_gt_f32_e64 s[0:1], v157, v243
	s_nop 1
	v_cndmask_b32_e64 v243, v243, v157, s[0:1]
	v_cndmask_b32_e64 v244, v244, 7, s[0:1]
	s_waitcnt lgkmcnt(5)
	v_cmp_gt_f32_e64 s[0:1], v150, v243
	s_nop 1
	v_cndmask_b32_e64 v243, v243, v150, s[0:1]
	v_cndmask_b32_e64 v244, v244, 8, s[0:1]
	v_cmp_gt_f32_e64 s[0:1], v151, v243
	s_nop 1
	v_cndmask_b32_e64 v243, v243, v151, s[0:1]
	v_cndmask_b32_e64 v244, v244, 9, s[0:1]
	v_cmp_gt_f32_e64 s[0:1], v152, v243
	s_nop 1
	v_cndmask_b32_e64 v243, v243, v152, s[0:1]
	v_cndmask_b32_e64 v244, v244, 10, s[0:1]
	v_cmp_gt_f32_e64 s[0:1], v153, v243
	s_nop 1
	v_cndmask_b32_e64 v243, v243, v153, s[0:1]
	v_cndmask_b32_e64 v244, v244, 11, s[0:1]
	s_waitcnt lgkmcnt(4)
	v_cmp_gt_f32_e64 s[0:1], v146, v243
	s_nop 1
	v_cndmask_b32_e64 v243, v243, v146, s[0:1]
	v_cndmask_b32_e64 v244, v244, 12, s[0:1]
	v_cmp_gt_f32_e64 s[0:1], v147, v243
	s_nop 1
	v_cndmask_b32_e64 v243, v243, v147, s[0:1]
	v_cndmask_b32_e64 v244, v244, 13, s[0:1]
	v_cmp_gt_f32_e64 s[0:1], v148, v243
	s_nop 1
	v_cndmask_b32_e64 v243, v243, v148, s[0:1]
	v_cndmask_b32_e64 v244, v244, 14, s[0:1]
	v_cmp_gt_f32_e64 s[0:1], v149, v243
	s_nop 1
	v_cndmask_b32_e64 v243, v243, v149, s[0:1]
	v_cndmask_b32_e64 v244, v244, 15, s[0:1]
	s_waitcnt lgkmcnt(3)
	v_cmp_gt_f32_e64 s[0:1], v142, v243
	s_nop 1
	v_cndmask_b32_e64 v243, v243, v142, s[0:1]
	v_cndmask_b32_e64 v244, v244, 16, s[0:1]
	v_cmp_gt_f32_e64 s[0:1], v143, v243
	s_nop 1
	v_cndmask_b32_e64 v243, v243, v143, s[0:1]
	v_cndmask_b32_e64 v244, v244, 17, s[0:1]
	v_cmp_gt_f32_e64 s[0:1], v144, v243
	s_nop 1
	v_cndmask_b32_e64 v243, v243, v144, s[0:1]
	v_cndmask_b32_e64 v244, v244, 18, s[0:1]
	v_cmp_gt_f32_e64 s[0:1], v145, v243
	s_nop 1
	v_cndmask_b32_e64 v243, v243, v145, s[0:1]
	v_cndmask_b32_e64 v244, v244, 19, s[0:1]
	s_waitcnt lgkmcnt(2)
	v_cmp_gt_f32_e64 s[0:1], v138, v243
	s_nop 1
	v_cndmask_b32_e64 v243, v243, v138, s[0:1]
	v_cndmask_b32_e64 v244, v244, 20, s[0:1]
	v_cmp_gt_f32_e64 s[0:1], v139, v243
	s_nop 1
	v_cndmask_b32_e64 v243, v243, v139, s[0:1]
	v_cndmask_b32_e64 v244, v244, 21, s[0:1]
	v_cmp_gt_f32_e64 s[0:1], v140, v243
	s_nop 1
	v_cndmask_b32_e64 v243, v243, v140, s[0:1]
	v_cndmask_b32_e64 v244, v244, 22, s[0:1]
	v_cmp_gt_f32_e64 s[0:1], v141, v243
	s_nop 1
	v_cndmask_b32_e64 v243, v243, v141, s[0:1]
	v_cndmask_b32_e64 v244, v244, 23, s[0:1]
	s_waitcnt lgkmcnt(1)
	v_cmp_gt_f32_e64 s[0:1], v134, v243
	s_nop 1
	v_cndmask_b32_e64 v243, v243, v134, s[0:1]
	v_cndmask_b32_e64 v244, v244, 24, s[0:1]
	v_cmp_gt_f32_e64 s[0:1], v135, v243
	s_nop 1
	v_cndmask_b32_e64 v243, v243, v135, s[0:1]
	v_cndmask_b32_e64 v244, v244, 25, s[0:1]
	v_cmp_gt_f32_e64 s[0:1], v136, v243
	s_nop 1
	v_cndmask_b32_e64 v243, v243, v136, s[0:1]
	v_cndmask_b32_e64 v244, v244, 26, s[0:1]
	v_cmp_gt_f32_e64 s[0:1], v137, v243
	s_nop 1
	v_cndmask_b32_e64 v243, v243, v137, s[0:1]
	v_cndmask_b32_e64 v244, v244, 27, s[0:1]
	s_waitcnt lgkmcnt(0)
	v_cmp_gt_f32_e64 s[0:1], v130, v243
	s_nop 1
	v_cndmask_b32_e64 v243, v243, v130, s[0:1]
	v_cndmask_b32_e64 v244, v244, 28, s[0:1]
	v_cmp_gt_f32_e64 s[0:1], v131, v243
	s_nop 1
	v_cndmask_b32_e64 v243, v243, v131, s[0:1]
	v_cndmask_b32_e64 v244, v244, 29, s[0:1]
	v_cmp_gt_f32_e64 s[0:1], v132, v243
	s_nop 1
	v_cndmask_b32_e64 v245, v243, v132, s[0:1]
	v_cndmask_b32_e64 v244, v244, 30, s[0:1]
	v_cmp_gt_f32_e64 s[0:1], v133, v245
	s_nop 1
	v_cndmask_b32_e64 v243, v244, 31, s[0:1]
	v_cndmask_b32_e64 v246, v245, v133, s[0:1]
	v_cmp_ne_u32_e64 s[0:1], 0, v243
	v_lshlrev_b32_e64 v245, v243, 1
	s_and_b64 s[0:1], s[0:1], vcc
	v_cndmask_b32_e64 v244, v242, v158, s[0:1]
	v_and_b32_e32 v247, 2, v245
	v_cmp_eq_u32_e64 s[0:1], 0, v247
	v_cmp_gt_f32_e64 s[8:9], v159, v244
	s_and_b64 s[0:1], s[0:1], s[8:9]
	v_cndmask_b32_e64 v244, v244, v159, s[0:1]
	v_and_b32_e32 v248, 4, v245
	v_cndmask_b32_e64 v247, 0, 1, s[0:1]
	v_cmp_eq_u32_e64 s[0:1], 0, v248
	v_cmp_gt_f32_e64 s[8:9], v160, v244
	s_and_b64 s[0:1], s[0:1], s[8:9]
	v_cndmask_b32_e64 v244, v244, v160, s[0:1]
	v_and_b32_e32 v248, 8, v245
	v_cndmask_b32_e64 v247, v247, 2, s[0:1]
	v_cmp_eq_u32_e64 s[0:1], 0, v248
	v_cmp_gt_f32_e64 s[8:9], v161, v244
	s_and_b64 s[0:1], s[0:1], s[8:9]
	v_cndmask_b32_e64 v244, v244, v161, s[0:1]
	v_and_b32_e32 v248, 16, v245
	v_cndmask_b32_e64 v247, v247, 3, s[0:1]
	v_cmp_eq_u32_e64 s[0:1], 0, v248
	v_cmp_gt_f32_e64 s[8:9], v154, v244
	s_and_b64 s[0:1], s[0:1], s[8:9]
	v_cndmask_b32_e64 v244, v244, v154, s[0:1]
	v_and_b32_e32 v248, 32, v245
	v_cndmask_b32_e64 v247, v247, 4, s[0:1]
	v_cmp_eq_u32_e64 s[0:1], 0, v248
	v_cmp_gt_f32_e64 s[8:9], v155, v244
	s_and_b64 s[0:1], s[0:1], s[8:9]
	v_cndmask_b32_e64 v244, v244, v155, s[0:1]
	v_and_b32_e32 v248, 64, v245
	v_cndmask_b32_e64 v247, v247, 5, s[0:1]
	v_cmp_eq_u32_e64 s[0:1], 0, v248
	v_cmp_gt_f32_e64 s[8:9], v156, v244
	s_and_b64 s[0:1], s[0:1], s[8:9]
	v_cndmask_b32_e64 v244, v244, v156, s[0:1]
	v_and_b32_e32 v248, 0x80, v245
	v_cndmask_b32_e64 v247, v247, 6, s[0:1]
	v_cmp_eq_u32_e64 s[0:1], 0, v248
	v_cmp_gt_f32_e64 s[8:9], v157, v244
	s_and_b64 s[0:1], s[0:1], s[8:9]
	v_cndmask_b32_e64 v244, v244, v157, s[0:1]
	v_and_b32_e32 v248, 0x100, v245
	v_cndmask_b32_e64 v247, v247, 7, s[0:1]
	v_cmp_eq_u32_e64 s[0:1], 0, v248
	v_cmp_gt_f32_e64 s[8:9], v150, v244
	s_and_b64 s[0:1], s[0:1], s[8:9]
	v_cndmask_b32_e64 v244, v244, v150, s[0:1]
	v_and_b32_e32 v248, 0x200, v245
	v_cndmask_b32_e64 v247, v247, 8, s[0:1]
	v_cmp_eq_u32_e64 s[0:1], 0, v248
	v_cmp_gt_f32_e64 s[8:9], v151, v244
	s_and_b64 s[0:1], s[0:1], s[8:9]
	v_cndmask_b32_e64 v244, v244, v151, s[0:1]
	v_and_b32_e32 v248, 0x400, v245
	v_cndmask_b32_e64 v247, v247, 9, s[0:1]
	v_cmp_eq_u32_e64 s[0:1], 0, v248
	v_cmp_gt_f32_e64 s[8:9], v152, v244
	s_and_b64 s[0:1], s[0:1], s[8:9]
	v_cndmask_b32_e64 v244, v244, v152, s[0:1]
	v_and_b32_e32 v248, 0x800, v245
	v_cndmask_b32_e64 v247, v247, 10, s[0:1]
	v_cmp_eq_u32_e64 s[0:1], 0, v248
	v_cmp_gt_f32_e64 s[8:9], v153, v244
	s_and_b64 s[0:1], s[0:1], s[8:9]
	v_cndmask_b32_e64 v244, v244, v153, s[0:1]
	v_and_b32_e32 v248, 0x1000, v245
	v_cndmask_b32_e64 v247, v247, 11, s[0:1]
	v_cmp_eq_u32_e64 s[0:1], 0, v248
	v_cmp_gt_f32_e64 s[8:9], v146, v244
	s_and_b64 s[0:1], s[0:1], s[8:9]
	v_cndmask_b32_e64 v244, v244, v146, s[0:1]
	v_and_b32_e32 v248, 0x2000, v245
	v_cndmask_b32_e64 v247, v247, 12, s[0:1]
	v_cmp_eq_u32_e64 s[0:1], 0, v248
	v_cmp_gt_f32_e64 s[8:9], v147, v244
	s_and_b64 s[0:1], s[0:1], s[8:9]
	v_cndmask_b32_e64 v244, v244, v147, s[0:1]
	v_and_b32_e32 v248, 0x4000, v245
	v_cndmask_b32_e64 v247, v247, 13, s[0:1]
	v_cmp_eq_u32_e64 s[0:1], 0, v248
	v_cmp_gt_f32_e64 s[8:9], v148, v244
	s_and_b64 s[0:1], s[0:1], s[8:9]
	v_cndmask_b32_e64 v244, v244, v148, s[0:1]
	v_and_b32_e32 v248, 0x8000, v245
	v_cndmask_b32_e64 v247, v247, 14, s[0:1]
	v_cmp_eq_u32_e64 s[0:1], 0, v248
	v_cmp_gt_f32_e64 s[8:9], v149, v244
	s_and_b64 s[0:1], s[0:1], s[8:9]
	v_cndmask_b32_e64 v244, v244, v149, s[0:1]
	v_and_b32_e32 v248, 0x10000, v245
	v_cndmask_b32_e64 v247, v247, 15, s[0:1]
	v_cmp_eq_u32_e64 s[0:1], 0, v248
	v_cmp_gt_f32_e64 s[8:9], v142, v244
	s_and_b64 s[0:1], s[0:1], s[8:9]
	v_cndmask_b32_e64 v244, v244, v142, s[0:1]
	v_and_b32_e32 v248, 0x20000, v245
	v_cndmask_b32_e64 v247, v247, 16, s[0:1]
	v_cmp_eq_u32_e64 s[0:1], 0, v248
	v_cmp_gt_f32_e64 s[8:9], v143, v244
	s_and_b64 s[0:1], s[0:1], s[8:9]
	v_cndmask_b32_e64 v244, v244, v143, s[0:1]
	v_and_b32_e32 v248, 0x40000, v245
	v_cndmask_b32_e64 v247, v247, 17, s[0:1]
	v_cmp_eq_u32_e64 s[0:1], 0, v248
	v_cmp_gt_f32_e64 s[8:9], v144, v244
	s_and_b64 s[0:1], s[0:1], s[8:9]
	v_cndmask_b32_e64 v244, v244, v144, s[0:1]
	v_and_b32_e32 v248, 0x80000, v245
	v_cndmask_b32_e64 v247, v247, 18, s[0:1]
	v_cmp_eq_u32_e64 s[0:1], 0, v248
	v_cmp_gt_f32_e64 s[8:9], v145, v244
	s_and_b64 s[0:1], s[0:1], s[8:9]
	v_cndmask_b32_e64 v244, v244, v145, s[0:1]
	v_and_b32_e32 v248, 0x100000, v245
	v_cndmask_b32_e64 v247, v247, 19, s[0:1]
	v_cmp_eq_u32_e64 s[0:1], 0, v248
	v_cmp_gt_f32_e64 s[8:9], v138, v244
	s_and_b64 s[0:1], s[0:1], s[8:9]
	v_cndmask_b32_e64 v244, v244, v138, s[0:1]
	v_and_b32_e32 v248, 0x200000, v245
	v_cndmask_b32_e64 v247, v247, 20, s[0:1]
	v_cmp_eq_u32_e64 s[0:1], 0, v248
	v_cmp_gt_f32_e64 s[8:9], v139, v244
	s_and_b64 s[0:1], s[0:1], s[8:9]
	v_cndmask_b32_e64 v244, v244, v139, s[0:1]
	v_and_b32_e32 v248, 0x400000, v245
	v_cndmask_b32_e64 v247, v247, 21, s[0:1]
	v_cmp_eq_u32_e64 s[0:1], 0, v248
	v_cmp_gt_f32_e64 s[8:9], v140, v244
	s_and_b64 s[0:1], s[0:1], s[8:9]
	v_cndmask_b32_e64 v244, v244, v140, s[0:1]
	v_and_b32_e32 v248, 0x800000, v245
	v_cndmask_b32_e64 v247, v247, 22, s[0:1]
	v_cmp_eq_u32_e64 s[0:1], 0, v248
	v_cmp_gt_f32_e64 s[8:9], v141, v244
	s_and_b64 s[0:1], s[0:1], s[8:9]
	v_cndmask_b32_e64 v244, v244, v141, s[0:1]
	v_and_b32_e32 v248, 0x1000000, v245
	v_cndmask_b32_e64 v247, v247, 23, s[0:1]
	v_cmp_eq_u32_e64 s[0:1], 0, v248
	v_cmp_gt_f32_e64 s[8:9], v134, v244
	s_and_b64 s[0:1], s[0:1], s[8:9]
	v_cndmask_b32_e64 v244, v244, v134, s[0:1]
	v_and_b32_e32 v248, 0x2000000, v245
	v_cndmask_b32_e64 v247, v247, 24, s[0:1]
	v_cmp_eq_u32_e64 s[0:1], 0, v248
	v_cmp_gt_f32_e64 s[8:9], v135, v244
	s_and_b64 s[0:1], s[0:1], s[8:9]
	v_cndmask_b32_e64 v244, v244, v135, s[0:1]
	v_and_b32_e32 v248, 0x4000000, v245
	v_cndmask_b32_e64 v247, v247, 25, s[0:1]
	v_cmp_eq_u32_e64 s[0:1], 0, v248
	v_cmp_gt_f32_e64 s[8:9], v136, v244
	s_and_b64 s[0:1], s[0:1], s[8:9]
	v_cndmask_b32_e64 v244, v244, v136, s[0:1]
	v_and_b32_e32 v248, 0x8000000, v245
	v_cndmask_b32_e64 v247, v247, 26, s[0:1]
	v_cmp_eq_u32_e64 s[0:1], 0, v248
	v_cmp_gt_f32_e64 s[8:9], v137, v244
	s_and_b64 s[0:1], s[0:1], s[8:9]
	v_cndmask_b32_e64 v244, v244, v137, s[0:1]
	v_and_b32_e32 v248, 0x10000000, v245
	v_cndmask_b32_e64 v247, v247, 27, s[0:1]
	v_cmp_eq_u32_e64 s[0:1], 0, v248
	v_cmp_gt_f32_e64 s[8:9], v130, v244
	s_and_b64 s[0:1], s[0:1], s[8:9]
	v_cndmask_b32_e64 v244, v244, v130, s[0:1]
	v_and_b32_e32 v248, 0x20000000, v245
	v_cndmask_b32_e64 v247, v247, 28, s[0:1]
	v_cmp_eq_u32_e64 s[0:1], 0, v248
	v_cmp_gt_f32_e64 s[8:9], v131, v244
	s_and_b64 s[0:1], s[0:1], s[8:9]
	v_cndmask_b32_e64 v244, v244, v131, s[0:1]
	v_and_b32_e32 v248, 2.0, v245
	v_cndmask_b32_e64 v247, v247, 29, s[0:1]
	v_cmp_eq_u32_e64 s[0:1], 0, v248
	v_cmp_gt_f32_e64 s[8:9], v132, v244
	s_and_b64 s[0:1], s[0:1], s[8:9]
	v_cndmask_b32_e64 v248, v244, v132, s[0:1]
	v_cndmask_b32_e64 v247, v247, 30, s[0:1]
	v_cmp_ne_u32_e64 s[0:1], 31, v243
	v_cmp_gt_f32_e64 s[8:9], v133, v248
	s_and_b64 s[0:1], s[0:1], s[8:9]
	v_cndmask_b32_e64 v244, v247, 31, s[0:1]
	v_cndmask_b32_e64 v247, v248, v133, s[0:1]
	v_lshl_or_b32 v248, 1, v244, v245
	v_and_b32_e32 v245, 1, v248
	v_cmp_eq_u32_e64 s[0:1], 0, v245
	s_and_b64 s[0:1], s[0:1], vcc
	v_and_b32_e32 v249, 2, v248
	v_cndmask_b32_e64 v245, v242, v158, s[0:1]
	v_cmp_eq_u32_e64 s[0:1], 0, v249
	v_cmp_gt_f32_e64 s[8:9], v159, v245
	s_and_b64 s[0:1], s[0:1], s[8:9]
	v_cndmask_b32_e64 v245, v245, v159, s[0:1]
	v_and_b32_e32 v250, 4, v248
	v_cndmask_b32_e64 v249, 0, 1, s[0:1]
	v_cmp_eq_u32_e64 s[0:1], 0, v250
	v_cmp_gt_f32_e64 s[8:9], v160, v245
	s_and_b64 s[0:1], s[0:1], s[8:9]
	v_cndmask_b32_e64 v245, v245, v160, s[0:1]
	v_and_b32_e32 v250, 8, v248
	v_cndmask_b32_e64 v249, v249, 2, s[0:1]
	v_cmp_eq_u32_e64 s[0:1], 0, v250
	v_cmp_gt_f32_e64 s[8:9], v161, v245
	s_and_b64 s[0:1], s[0:1], s[8:9]
	v_cndmask_b32_e64 v245, v245, v161, s[0:1]
	v_and_b32_e32 v250, 16, v248
	v_cndmask_b32_e64 v249, v249, 3, s[0:1]
	v_cmp_eq_u32_e64 s[0:1], 0, v250
	v_cmp_gt_f32_e64 s[8:9], v154, v245
	s_and_b64 s[0:1], s[0:1], s[8:9]
	v_cndmask_b32_e64 v245, v245, v154, s[0:1]
	v_and_b32_e32 v250, 32, v248
	v_cndmask_b32_e64 v249, v249, 4, s[0:1]
	v_cmp_eq_u32_e64 s[0:1], 0, v250
	v_cmp_gt_f32_e64 s[8:9], v155, v245
	s_and_b64 s[0:1], s[0:1], s[8:9]
	v_cndmask_b32_e64 v245, v245, v155, s[0:1]
	v_and_b32_e32 v250, 64, v248
	v_cndmask_b32_e64 v249, v249, 5, s[0:1]
	v_cmp_eq_u32_e64 s[0:1], 0, v250
	v_cmp_gt_f32_e64 s[8:9], v156, v245
	s_and_b64 s[0:1], s[0:1], s[8:9]
	v_cndmask_b32_e64 v245, v245, v156, s[0:1]
	v_and_b32_e32 v250, 0x80, v248
	v_cndmask_b32_e64 v249, v249, 6, s[0:1]
	v_cmp_eq_u32_e64 s[0:1], 0, v250
	v_cmp_gt_f32_e64 s[8:9], v157, v245
	s_and_b64 s[0:1], s[0:1], s[8:9]
	v_cndmask_b32_e64 v245, v245, v157, s[0:1]
	v_and_b32_e32 v250, 0x100, v248
	v_cndmask_b32_e64 v249, v249, 7, s[0:1]
	v_cmp_eq_u32_e64 s[0:1], 0, v250
	v_cmp_gt_f32_e64 s[8:9], v150, v245
	s_and_b64 s[0:1], s[0:1], s[8:9]
	v_cndmask_b32_e64 v245, v245, v150, s[0:1]
	v_and_b32_e32 v250, 0x200, v248
	v_cndmask_b32_e64 v249, v249, 8, s[0:1]
	v_cmp_eq_u32_e64 s[0:1], 0, v250
	v_cmp_gt_f32_e64 s[8:9], v151, v245
	s_and_b64 s[0:1], s[0:1], s[8:9]
	v_cndmask_b32_e64 v245, v245, v151, s[0:1]
	v_and_b32_e32 v250, 0x400, v248
	v_cndmask_b32_e64 v249, v249, 9, s[0:1]
	v_cmp_eq_u32_e64 s[0:1], 0, v250
	v_cmp_gt_f32_e64 s[8:9], v152, v245
	s_and_b64 s[0:1], s[0:1], s[8:9]
	v_cndmask_b32_e64 v245, v245, v152, s[0:1]
	v_and_b32_e32 v250, 0x800, v248
	v_cndmask_b32_e64 v249, v249, 10, s[0:1]
	v_cmp_eq_u32_e64 s[0:1], 0, v250
	v_cmp_gt_f32_e64 s[8:9], v153, v245
	s_and_b64 s[0:1], s[0:1], s[8:9]
	v_cndmask_b32_e64 v245, v245, v153, s[0:1]
	v_and_b32_e32 v250, 0x1000, v248
	v_cndmask_b32_e64 v249, v249, 11, s[0:1]
	v_cmp_eq_u32_e64 s[0:1], 0, v250
	v_cmp_gt_f32_e64 s[8:9], v146, v245
	s_and_b64 s[0:1], s[0:1], s[8:9]
	v_cndmask_b32_e64 v245, v245, v146, s[0:1]
	v_and_b32_e32 v250, 0x2000, v248
	v_cndmask_b32_e64 v249, v249, 12, s[0:1]
	v_cmp_eq_u32_e64 s[0:1], 0, v250
	v_cmp_gt_f32_e64 s[8:9], v147, v245
	s_and_b64 s[0:1], s[0:1], s[8:9]
	v_cndmask_b32_e64 v245, v245, v147, s[0:1]
	v_and_b32_e32 v250, 0x4000, v248
	v_cndmask_b32_e64 v249, v249, 13, s[0:1]
	v_cmp_eq_u32_e64 s[0:1], 0, v250
	v_cmp_gt_f32_e64 s[8:9], v148, v245
	s_and_b64 s[0:1], s[0:1], s[8:9]
	v_cndmask_b32_e64 v245, v245, v148, s[0:1]
	v_and_b32_e32 v250, 0x8000, v248
	v_cndmask_b32_e64 v249, v249, 14, s[0:1]
	v_cmp_eq_u32_e64 s[0:1], 0, v250
	v_cmp_gt_f32_e64 s[8:9], v149, v245
	s_and_b64 s[0:1], s[0:1], s[8:9]
	v_cndmask_b32_e64 v245, v245, v149, s[0:1]
	v_and_b32_e32 v250, 0x10000, v248
	v_cndmask_b32_e64 v249, v249, 15, s[0:1]
	v_cmp_eq_u32_e64 s[0:1], 0, v250
	v_cmp_gt_f32_e64 s[8:9], v142, v245
	s_and_b64 s[0:1], s[0:1], s[8:9]
	v_cndmask_b32_e64 v245, v245, v142, s[0:1]
	v_and_b32_e32 v250, 0x20000, v248
	v_cndmask_b32_e64 v249, v249, 16, s[0:1]
	v_cmp_eq_u32_e64 s[0:1], 0, v250
	v_cmp_gt_f32_e64 s[8:9], v143, v245
	s_and_b64 s[0:1], s[0:1], s[8:9]
	v_cndmask_b32_e64 v245, v245, v143, s[0:1]
	v_and_b32_e32 v250, 0x40000, v248
	v_cndmask_b32_e64 v249, v249, 17, s[0:1]
	v_cmp_eq_u32_e64 s[0:1], 0, v250
	v_cmp_gt_f32_e64 s[8:9], v144, v245
	s_and_b64 s[0:1], s[0:1], s[8:9]
	v_cndmask_b32_e64 v245, v245, v144, s[0:1]
	v_and_b32_e32 v250, 0x80000, v248
	v_cndmask_b32_e64 v249, v249, 18, s[0:1]
	v_cmp_eq_u32_e64 s[0:1], 0, v250
	v_cmp_gt_f32_e64 s[8:9], v145, v245
	s_and_b64 s[0:1], s[0:1], s[8:9]
	v_cndmask_b32_e64 v245, v245, v145, s[0:1]
	v_and_b32_e32 v250, 0x100000, v248
	v_cndmask_b32_e64 v249, v249, 19, s[0:1]
	v_cmp_eq_u32_e64 s[0:1], 0, v250
	v_cmp_gt_f32_e64 s[8:9], v138, v245
	s_and_b64 s[0:1], s[0:1], s[8:9]
	v_cndmask_b32_e64 v245, v245, v138, s[0:1]
	v_and_b32_e32 v250, 0x200000, v248
	v_cndmask_b32_e64 v249, v249, 20, s[0:1]
	v_cmp_eq_u32_e64 s[0:1], 0, v250
	v_cmp_gt_f32_e64 s[8:9], v139, v245
	s_and_b64 s[0:1], s[0:1], s[8:9]
	v_cndmask_b32_e64 v245, v245, v139, s[0:1]
	v_and_b32_e32 v250, 0x400000, v248
	v_cndmask_b32_e64 v249, v249, 21, s[0:1]
	v_cmp_eq_u32_e64 s[0:1], 0, v250
	v_cmp_gt_f32_e64 s[8:9], v140, v245
	s_and_b64 s[0:1], s[0:1], s[8:9]
	v_cndmask_b32_e64 v245, v245, v140, s[0:1]
	v_and_b32_e32 v250, 0x800000, v248
	v_cndmask_b32_e64 v249, v249, 22, s[0:1]
	v_cmp_eq_u32_e64 s[0:1], 0, v250
	v_cmp_gt_f32_e64 s[8:9], v141, v245
	s_and_b64 s[0:1], s[0:1], s[8:9]
	v_cndmask_b32_e64 v245, v245, v141, s[0:1]
	v_and_b32_e32 v250, 0x1000000, v248
	v_cndmask_b32_e64 v249, v249, 23, s[0:1]
	v_cmp_eq_u32_e64 s[0:1], 0, v250
	v_cmp_gt_f32_e64 s[8:9], v134, v245
	s_and_b64 s[0:1], s[0:1], s[8:9]
	v_cndmask_b32_e64 v245, v245, v134, s[0:1]
	v_and_b32_e32 v250, 0x2000000, v248
	v_cndmask_b32_e64 v249, v249, 24, s[0:1]
	v_cmp_eq_u32_e64 s[0:1], 0, v250
	v_cmp_gt_f32_e64 s[8:9], v135, v245
	s_and_b64 s[0:1], s[0:1], s[8:9]
	v_cndmask_b32_e64 v245, v245, v135, s[0:1]
	v_and_b32_e32 v250, 0x4000000, v248
	v_cndmask_b32_e64 v249, v249, 25, s[0:1]
	v_cmp_eq_u32_e64 s[0:1], 0, v250
	v_cmp_gt_f32_e64 s[8:9], v136, v245
	s_and_b64 s[0:1], s[0:1], s[8:9]
	v_cndmask_b32_e64 v245, v245, v136, s[0:1]
	v_and_b32_e32 v250, 0x8000000, v248
	v_cndmask_b32_e64 v249, v249, 26, s[0:1]
	v_cmp_eq_u32_e64 s[0:1], 0, v250
	v_cmp_gt_f32_e64 s[8:9], v137, v245
	s_and_b64 s[0:1], s[0:1], s[8:9]
	v_cndmask_b32_e64 v245, v245, v137, s[0:1]
	v_and_b32_e32 v250, 0x10000000, v248
	v_cndmask_b32_e64 v249, v249, 27, s[0:1]
	v_cmp_eq_u32_e64 s[0:1], 0, v250
	v_cmp_gt_f32_e64 s[8:9], v130, v245
	s_and_b64 s[0:1], s[0:1], s[8:9]
	v_cndmask_b32_e64 v245, v245, v130, s[0:1]
	v_and_b32_e32 v250, 0x20000000, v248
	v_cndmask_b32_e64 v249, v249, 28, s[0:1]
	v_cmp_eq_u32_e64 s[0:1], 0, v250
	v_cmp_gt_f32_e64 s[8:9], v131, v245
	s_and_b64 s[0:1], s[0:1], s[8:9]
	v_cndmask_b32_e64 v245, v245, v131, s[0:1]
	v_and_b32_e32 v250, 2.0, v248
	v_cndmask_b32_e64 v249, v249, 29, s[0:1]
	v_cmp_eq_u32_e64 s[0:1], 0, v250
	v_cmp_gt_f32_e64 s[8:9], v132, v245
	s_and_b64 s[0:1], s[0:1], s[8:9]
	v_cndmask_b32_e64 v250, v245, v132, s[0:1]
	v_cndmask_b32_e64 v249, v249, 30, s[0:1]
	v_cmp_lt_i32_e64 s[0:1], -1, v248
	v_cmp_gt_f32_e64 s[8:9], v133, v250
	s_and_b64 s[0:1], s[0:1], s[8:9]
	v_cndmask_b32_e64 v245, v249, 31, s[0:1]
	v_cndmask_b32_e64 v249, v250, v133, s[0:1]
	v_lshlrev_b32_e64 v250, v245, 1
	v_bitop3_b32 v252, v250, 1, v248 bitop3:0xc8
	v_cmp_eq_u32_e64 s[0:1], 0, v252
	s_and_b64 vcc, s[0:1], vcc
	v_cndmask_b32_e32 v158, v242, v158, vcc
	v_bitop3_b32 v252, v250, 2, v248 bitop3:0xc8
	v_cmp_eq_u32_e32 vcc, 0, v252
	v_cmp_gt_f32_e64 s[0:1], v159, v158
	s_and_b64 vcc, vcc, s[0:1]
	v_cndmask_b32_e32 v158, v158, v159, vcc
	v_bitop3_b32 v159, v250, 4, v248 bitop3:0xc8
	v_cndmask_b32_e64 v252, 0, 1, vcc
	v_cmp_eq_u32_e32 vcc, 0, v159
	v_cmp_gt_f32_e64 s[0:1], v160, v158
	s_and_b64 vcc, vcc, s[0:1]
	v_cndmask_b32_e32 v158, v158, v160, vcc
	v_bitop3_b32 v160, v250, 8, v248 bitop3:0xc8
	v_cndmask_b32_e64 v159, v252, 2, vcc
	v_cmp_eq_u32_e32 vcc, 0, v160
	v_cmp_gt_f32_e64 s[0:1], v161, v158
	s_and_b64 vcc, vcc, s[0:1]
	v_cndmask_b32_e32 v158, v158, v161, vcc
	v_bitop3_b32 v160, v250, 16, v248 bitop3:0xc8
	v_cndmask_b32_e64 v159, v159, 3, vcc
	v_cmp_eq_u32_e32 vcc, 0, v160
	v_cmp_gt_f32_e64 s[0:1], v154, v158
	s_and_b64 vcc, vcc, s[0:1]
	v_cndmask_b32_e32 v154, v158, v154, vcc
	v_bitop3_b32 v158, v250, 32, v248 bitop3:0xc8
	v_cndmask_b32_e64 v159, v159, 4, vcc
	v_cmp_eq_u32_e32 vcc, 0, v158
	v_cmp_gt_f32_e64 s[0:1], v155, v154
	s_and_b64 vcc, vcc, s[0:1]
	v_cndmask_b32_e32 v154, v154, v155, vcc
	v_bitop3_b32 v155, v250, 64, v248 bitop3:0xc8
	v_cndmask_b32_e64 v158, v159, 5, vcc
	v_cmp_eq_u32_e32 vcc, 0, v155
	v_cmp_gt_f32_e64 s[0:1], v156, v154
	s_and_b64 vcc, vcc, s[0:1]
	s_movk_i32 s0, 0x80
	v_cndmask_b32_e32 v154, v154, v156, vcc
	v_bitop3_b32 v156, v250, s0, v248 bitop3:0xc8
	v_cndmask_b32_e64 v155, v158, 6, vcc
	v_cmp_eq_u32_e32 vcc, 0, v156
	v_cmp_gt_f32_e64 s[0:1], v157, v154
	s_and_b64 vcc, vcc, s[0:1]
	s_movk_i32 s0, 0x100
	v_cndmask_b32_e32 v154, v154, v157, vcc
	v_bitop3_b32 v156, v250, s0, v248 bitop3:0xc8
	v_cndmask_b32_e64 v155, v155, 7, vcc
	v_cmp_eq_u32_e32 vcc, 0, v156
	v_cmp_gt_f32_e64 s[0:1], v150, v154
	s_and_b64 vcc, vcc, s[0:1]
	s_movk_i32 s0, 0x200
	v_cndmask_b32_e32 v150, v154, v150, vcc
	v_bitop3_b32 v154, v250, s0, v248 bitop3:0xc8
	v_cndmask_b32_e64 v155, v155, 8, vcc
	v_cmp_eq_u32_e32 vcc, 0, v154
	v_cmp_gt_f32_e64 s[0:1], v151, v150
	s_and_b64 vcc, vcc, s[0:1]
	s_movk_i32 s0, 0x400
	v_cndmask_b32_e32 v150, v150, v151, vcc
	v_bitop3_b32 v151, v250, s0, v248 bitop3:0xc8
	v_cndmask_b32_e64 v154, v155, 9, vcc
	v_cmp_eq_u32_e32 vcc, 0, v151
	v_cmp_gt_f32_e64 s[0:1], v152, v150
	s_and_b64 vcc, vcc, s[0:1]
	s_movk_i32 s0, 0x800
	v_cndmask_b32_e32 v150, v150, v152, vcc
	v_bitop3_b32 v152, v250, s0, v248 bitop3:0xc8
	v_cndmask_b32_e64 v151, v154, 10, vcc
	v_cmp_eq_u32_e32 vcc, 0, v152
	v_cmp_gt_f32_e64 s[0:1], v153, v150
	s_and_b64 vcc, vcc, s[0:1]
	s_movk_i32 s0, 0x1000
	v_cndmask_b32_e32 v150, v150, v153, vcc
	v_bitop3_b32 v152, v250, s0, v248 bitop3:0xc8
	v_cndmask_b32_e64 v151, v151, 11, vcc
	v_cmp_eq_u32_e32 vcc, 0, v152
	v_cmp_gt_f32_e64 s[0:1], v146, v150
	s_and_b64 vcc, vcc, s[0:1]
	s_movk_i32 s0, 0x2000
	v_cndmask_b32_e32 v146, v150, v146, vcc
	v_bitop3_b32 v150, v250, s0, v248 bitop3:0xc8
	v_cndmask_b32_e64 v151, v151, 12, vcc
	v_cmp_eq_u32_e32 vcc, 0, v150
	v_cmp_gt_f32_e64 s[0:1], v147, v146
	s_and_b64 vcc, vcc, s[0:1]
	s_movk_i32 s0, 0x4000
	v_cndmask_b32_e32 v146, v146, v147, vcc
	v_bitop3_b32 v147, v250, s0, v248 bitop3:0xc8
	v_cndmask_b32_e64 v150, v151, 13, vcc
	v_cmp_eq_u32_e32 vcc, 0, v147
	v_cmp_gt_f32_e64 s[0:1], v148, v146
	s_and_b64 vcc, vcc, s[0:1]
	s_mov_b32 s0, 0x8000
	v_cndmask_b32_e32 v146, v146, v148, vcc
	v_bitop3_b32 v148, v250, s0, v248 bitop3:0xc8
	v_cndmask_b32_e64 v147, v150, 14, vcc
	v_cmp_eq_u32_e32 vcc, 0, v148
	v_cmp_gt_f32_e64 s[0:1], v149, v146
	s_and_b64 vcc, vcc, s[0:1]
	s_mov_b32 s0, 0x10000
	v_cndmask_b32_e32 v146, v146, v149, vcc
	v_bitop3_b32 v148, v250, s0, v248 bitop3:0xc8
	v_cndmask_b32_e64 v147, v147, 15, vcc
	v_cmp_eq_u32_e32 vcc, 0, v148
	v_cmp_gt_f32_e64 s[0:1], v142, v146
	s_and_b64 vcc, vcc, s[0:1]
	s_mov_b32 s0, 0x20000
	v_cndmask_b32_e32 v142, v146, v142, vcc
	v_bitop3_b32 v146, v250, s0, v248 bitop3:0xc8
	v_cndmask_b32_e64 v147, v147, 16, vcc
	v_cmp_eq_u32_e32 vcc, 0, v146
	v_cmp_gt_f32_e64 s[0:1], v143, v142
	s_and_b64 vcc, vcc, s[0:1]
	v_cndmask_b32_e32 v142, v142, v143, vcc
	v_bitop3_b32 v143, v250, s79, v248 bitop3:0xc8
	v_cndmask_b32_e64 v146, v147, 17, vcc
	v_cmp_eq_u32_e32 vcc, 0, v143
	v_cmp_gt_f32_e64 s[0:1], v144, v142
	s_and_b64 vcc, vcc, s[0:1]
	v_cndmask_b32_e32 v142, v142, v144, vcc
	v_bitop3_b32 v144, v250, s80, v248 bitop3:0xc8
	v_cndmask_b32_e64 v143, v146, 18, vcc
	v_cmp_eq_u32_e32 vcc, 0, v144
	v_cmp_gt_f32_e64 s[0:1], v145, v142
	s_and_b64 vcc, vcc, s[0:1]
	v_cndmask_b32_e32 v142, v142, v145, vcc
	v_bitop3_b32 v144, v250, s81, v248 bitop3:0xc8
	v_cndmask_b32_e64 v143, v143, 19, vcc
	v_cmp_eq_u32_e32 vcc, 0, v144
	v_cmp_gt_f32_e64 s[0:1], v138, v142
	s_and_b64 vcc, vcc, s[0:1]
	v_cndmask_b32_e32 v138, v142, v138, vcc
	v_bitop3_b32 v142, v250, s82, v248 bitop3:0xc8
	v_cndmask_b32_e64 v143, v143, 20, vcc
	v_cmp_eq_u32_e32 vcc, 0, v142
	v_cmp_gt_f32_e64 s[0:1], v139, v138
	s_and_b64 vcc, vcc, s[0:1]
	v_cndmask_b32_e32 v138, v138, v139, vcc
	v_bitop3_b32 v139, v250, s83, v248 bitop3:0xc8
	v_cndmask_b32_e64 v142, v143, 21, vcc
	v_cmp_eq_u32_e32 vcc, 0, v139
	v_cmp_gt_f32_e64 s[0:1], v140, v138
	s_and_b64 vcc, vcc, s[0:1]
	v_cndmask_b32_e32 v138, v138, v140, vcc
	v_bitop3_b32 v140, v250, s84, v248 bitop3:0xc8
	v_cndmask_b32_e64 v139, v142, 22, vcc
	v_cmp_eq_u32_e32 vcc, 0, v140
	v_cmp_gt_f32_e64 s[0:1], v141, v138
	s_and_b64 vcc, vcc, s[0:1]
	v_cndmask_b32_e32 v138, v138, v141, vcc
	v_bitop3_b32 v140, v250, s85, v248 bitop3:0xc8
	v_cndmask_b32_e64 v139, v139, 23, vcc
	v_cmp_eq_u32_e32 vcc, 0, v140
	v_cmp_gt_f32_e64 s[0:1], v134, v138
	s_and_b64 vcc, vcc, s[0:1]
	v_cndmask_b32_e32 v134, v138, v134, vcc
	v_bitop3_b32 v138, v250, s86, v248 bitop3:0xc8
	v_cndmask_b32_e64 v139, v139, 24, vcc
	v_cmp_eq_u32_e32 vcc, 0, v138
	v_cmp_gt_f32_e64 s[0:1], v135, v134
	s_and_b64 vcc, vcc, s[0:1]
	v_cndmask_b32_e32 v134, v134, v135, vcc
	v_bitop3_b32 v135, v250, s87, v248 bitop3:0xc8
	v_cndmask_b32_e64 v138, v139, 25, vcc
	v_cmp_eq_u32_e32 vcc, 0, v135
	v_cmp_gt_f32_e64 s[0:1], v136, v134
	s_and_b64 vcc, vcc, s[0:1]
	v_cndmask_b32_e32 v134, v134, v136, vcc
	v_bitop3_b32 v136, v250, s91, v248 bitop3:0xc8
	v_cndmask_b32_e64 v135, v138, 26, vcc
	v_cmp_eq_u32_e32 vcc, 0, v136
	v_cmp_gt_f32_e64 s[0:1], v137, v134
	s_and_b64 vcc, vcc, s[0:1]
	v_cndmask_b32_e32 v134, v134, v137, vcc
	v_bitop3_b32 v136, v250, s92, v248 bitop3:0xc8
	v_cndmask_b32_e64 v135, v135, 27, vcc
	v_cmp_eq_u32_e32 vcc, 0, v136
	v_cmp_gt_f32_e64 s[0:1], v130, v134
	s_and_b64 vcc, vcc, s[0:1]
	v_cndmask_b32_e32 v130, v134, v130, vcc
	v_bitop3_b32 v134, v250, s93, v248 bitop3:0xc8
	v_cndmask_b32_e64 v135, v135, 28, vcc
	v_cmp_eq_u32_e32 vcc, 0, v134
	v_cmp_gt_f32_e64 s[0:1], v131, v130
	s_and_b64 vcc, vcc, s[0:1]
	v_cndmask_b32_e32 v130, v130, v131, vcc
	v_bitop3_b32 v131, v250, 2.0, v248 bitop3:0xc8
	v_cndmask_b32_e64 v134, v135, 29, vcc
	v_cmp_eq_u32_e32 vcc, 0, v131
	v_cmp_gt_f32_e64 s[0:1], v132, v130
	s_and_b64 vcc, vcc, s[0:1]
	v_or_b32_e32 v251, v250, v248
	v_cndmask_b32_e32 v130, v130, v132, vcc
	v_cndmask_b32_e64 v131, v134, 30, vcc
	v_cmp_lt_i32_e32 vcc, -1, v251
	v_cmp_gt_f32_e64 s[0:1], v133, v130
	s_and_b64 vcc, vcc, s[0:1]
	v_cndmask_b32_e32 v132, v130, v133, vcc
	v_sub_f32_e32 v130, v247, v246
	v_cndmask_b32_e64 v134, v131, 31, vcc
	v_mul_f32_e32 v130, 0x3fb8aa3b, v130
	v_sub_f32_e32 v131, v249, v246
	v_exp_f32_e32 v130, v130
	v_mul_f32_e32 v131, 0x3fb8aa3b, v131
	v_sub_f32_e32 v132, v132, v246
	v_exp_f32_e32 v131, v131
	v_mul_f32_e32 v132, 0x3fb8aa3b, v132
	v_exp_f32_e32 v133, v132
	v_add_f32_e32 v132, 1.0, v130
	v_add_f32_e32 v132, v132, v131
	v_add_f32_e32 v132, v132, v133
	v_div_scale_f32 v135, s[0:1], v132, v132, 1.0
	v_rcp_f32_e32 v139, v135
	s_nop 0
	v_fma_f32 v136, -v135, v139, 1.0
	v_fmac_f32_e32 v139, v136, v139
	v_div_scale_f32 v136, vcc, 1.0, v132, 1.0
	v_mul_f32_e32 v140, v136, v139
	v_fma_f32 v137, -v135, v140, v136
	v_fmac_f32_e32 v140, v137, v139
	v_fma_f32 v141, -v135, v140, v136
	v_lshl_add_u32 v135, v243, 2, s67
	ds_add_rtn_u32 v138, v135, v239
	v_lshl_add_u32 v135, v244, 2, s67
	ds_add_rtn_u32 v137, v135, v239
	v_lshl_add_u32 v135, v245, 2, s67
	ds_add_rtn_u32 v136, v135, v239
	v_lshl_add_u32 v135, v134, 2, s67
	ds_add_rtn_u32 v135, v135, v239
	v_div_fmas_f32 v139, v141, v139, v140
	v_div_fixup_f32 v132, v139, v132, 1.0
	v_pk_mul_f32 v[130:131], v[130:131], v[132:133] op_sel_hi:[1,0]
	v_mul_f32_e32 v133, v133, v132

.LBB0_1884:
	s_and_b64 vcc, exec, s[0:1]
	s_cbranch_vccnz .LBB0_1926
	v_lshlrev_b32_e32 v1, 4, v0
	s_waitcnt vmcnt(0)
	v_and_b32_e32 v2, 32, v0
	v_bitop3_b32 v2, v1, v2, 48 bitop3:0x6c
	v_lshrrev_b32_e32 v1, 1, v0
	v_bfe_u32 v3, v0, 2, 2
	v_lshrrev_b32_e32 v4, 3, v0
	s_movk_i32 s0, 0x60
	v_and_or_b32 v3, v1, 24, v3
	v_and_b32_e32 v1, 32, v4
	v_bitop3_b32 v4, v4, s0, 64 bitop3:0xc8
	s_lshl_b32 s0, s30, 2
	v_lshrrev_b32_e32 v6, 5, v0
	s_add_i32 s0, s0, 0
	v_and_b32_e32 v6, 4, v6
	s_add_i32 s0, s0, 0x201c0
	v_or3_b32 v1, v6, v1, v3
	v_or3_b32 v3, v6, v4, v3
	v_mov_b32_e32 v4, s0
	ds_read_b32 v4, v4 offset:288
	s_lshr_b32 s66, s4, 6
	s_ashr_i32 s15, s14, 31
	s_lshl_b32 s1, s66, 10
	s_lshl_b64 s[16:17], s[14:15], 18
	s_waitcnt lgkmcnt(0)
	v_readfirstlane_b32 s8, v4
	s_ashr_i32 s9, s8, 31
	s_lshl_b64 s[8:9], s[8:9], 21
	s_add_u32 s5, s3, s8
	s_addc_u32 s8, s21, s9
	s_add_u32 s40, s5, s16
	v_and_b32_e32 v5, 64, v0
	v_lshlrev_b32_e32 v1, 10, v1
	s_addc_u32 s41, s8, s17
	s_add_i32 s15, s1, 0
	v_or3_b32 v1, v1, v5, v2
	v_lshlrev_b32_e32 v3, 10, v3
	s_add_i32 s67, s15, 0x10000
	s_mov_b32 s1, m0
	s_mov_b32 m0, s67
	s_nop 0
	global_load_lds_dwordx4 v1, s[40:41]
	s_mov_b32 m0, s1
	s_add_i32 s68, s15, 0x12000
	v_or3_b32 v163, v3, v5, v2
	s_mov_b32 s1, m0
	s_mov_b32 m0, s68
	s_nop 0
	global_load_lds_dwordx4 v163, s[40:41]
	s_mov_b32 m0, s1
	s_add_u32 s8, s40, 0x20000
	s_addc_u32 s9, s41, 0
	s_add_i32 s69, s15, 0x14000
	s_mov_b32 s1, m0
	s_mov_b32 m0, s69
	s_nop 0
	global_load_lds_dwordx4 v1, s[8:9]
	s_mov_b32 m0, s1
	s_add_i32 s76, s15, 0x16000
	s_mov_b32 s1, m0
	s_mov_b32 m0, s76
	s_nop 0
	global_load_lds_dwordx4 v163, s[8:9]
	s_mov_b32 m0, s1
	s_cmp_lt_u32 s4, 64
	v_writelane_b32 v253, s24, 33
	s_cselect_b64 s[18:19], -1, 0
	s_cmp_gt_u32 s4, 63
	v_writelane_b32 v253, s25, 34
	s_cbranch_scc1 .LBB0_1887
	v_mov_b32_e32 v2, s0
	ds_read_b32 v2, v2 offset:288
	v_lshlrev_b32_e32 v3, 4, v218
	s_waitcnt lgkmcnt(0)
	v_readfirstlane_b32 s0, v2
	s_lshl_b32 s1, s0, 2
	s_add_i32 s1, s1, 0
	s_add_i32 s1, s1, 0x20240
	v_mov_b32_e32 v2, s1
	ds_read_b32 v2, v2
	s_lshl_b32 s0, s0, 14
	s_ashr_i32 s1, s0, 31
	s_lshl_b64 s[0:1], s[0:1], 2
	s_waitcnt lgkmcnt(0)
	v_readfirstlane_b32 s5, v2
	s_sub_i32 s5, s30, s5
	s_lshl_b32 s8, s5, 8
	s_add_u32 s5, s58, s0
	s_addc_u32 s16, s59, s1
	s_ashr_i32 s9, s8, 31
	s_lshl_b64 s[0:1], s[8:9], 2
	s_add_u32 s0, s5, s0
	s_addc_u32 s1, s16, s1
	s_add_i32 s5, 0, 0x20800
	s_mov_b32 s8, m0
	s_mov_b32 m0, s5
	s_nop 0
	global_load_lds_dwordx4 v3, s[0:1]
	s_mov_b32 m0, s8
.LBB0_1887:
	v_mov_b32_e32 v2, v0
	s_waitcnt vmcnt(0)
	s_barrier
	s_add_i32 s0, 0, 0x20800
	v_ashrrev_i32_e32 v3, 31, v2
	v_lshrrev_b32_e32 v3, 26, v3
	v_lshlrev_b32_e32 v4, 4, v2
	v_add_u32_e32 v3, v2, v3
	v_bfe_i32 v2, v2, 27, 1
	v_lshrrev_b32_e32 v2, 22, v2
	v_add_u32_e32 v2, v4, v2
	v_and_b32_e32 v2, 0xfffffc00, v2
	v_sub_u32_e32 v2, v4, v2
	v_lshrrev_b32_e32 v5, 4, v2
	v_ashrrev_i32_e32 v6, 31, v2
	v_and_b32_e32 v5, 32, v5
	v_lshrrev_b32_e32 v6, 26, v6
	v_add_u32_e32 v4, 0x2000, v4
	v_xad_u32 v2, v5, v2, v6
	v_ashrrev_i32_e32 v5, 31, v4
	v_lshrrev_b32_e32 v5, 22, v5
	v_add_u32_e32 v5, v4, v5
	v_ashrrev_i32_e32 v5, 10, v5
	v_mul_i32_i24_e32 v6, 0x400, v5
	v_sub_u32_e32 v4, v4, v6
	v_lshrrev_b32_e32 v6, 4, v4
	v_ashrrev_i32_e32 v7, 31, v4
	v_ashrrev_i32_e32 v3, 6, v3
	v_and_b32_e32 v6, 32, v6
	v_lshrrev_b32_e32 v7, 26, v7
	v_lshlrev_b32_e32 v3, 3, v3
	v_lshlrev_b32_e32 v5, 3, v5
	v_xad_u32 v4, v6, v4, v7
	v_and_b32_e32 v3, 0x3ffffff0, v3
	v_ashrrev_i32_e32 v2, 6, v2
	v_and_b32_e32 v5, 0x3ffffff0, v5
	v_ashrrev_i32_e32 v4, 6, v4
	v_add_u32_e32 v2, v2, v3
	v_add_u32_e32 v4, v4, v5
	v_lshl_add_u32 v2, v2, 2, s0
	v_lshl_add_u32 v4, v4, 2, s0
	v_mov_b32_e32 v6, v0
	ds_read2st64_b32 v[2:3], v2 offset1:2
	ds_read2st64_b32 v[4:5], v4 offset1:2
	v_mov_b32_e32 v165, 1
	v_ashrrev_i32_e32 v8, 31, v6
	v_lshrrev_b32_e32 v8, 26, v8
	v_lshlrev_b32_e32 v7, 4, v6
	v_add_u32_e32 v8, v6, v8
	v_bfe_i32 v6, v6, 27, 1
	v_lshrrev_b32_e32 v6, 22, v6
	v_add_u32_e32 v6, v7, v6
	v_and_b32_e32 v6, 0xfffffc00, v6
	v_sub_u32_e32 v6, v7, v6
	v_lshrrev_b32_e32 v9, 4, v6
	v_bitop3_b32 v9, v9, v6, 32 bitop3:0x6c
	v_ashrrev_i32_e32 v6, 31, v6
	v_lshrrev_b32_e32 v6, 26, v6
	v_add_u32_e32 v6, v9, v6
	v_and_b32_e32 v6, 0xc0, v6
	v_sub_u32_e32 v6, v9, v6
	v_lshrrev_b32_e32 v8, 1, v8
	v_ashrrev_i16_sdwa v6, v165, sext(v6) dst_sel:DWORD dst_unused:UNUSED_PAD src0_sel:DWORD src1_sel:BYTE_0
	v_and_b32_e32 v8, 32, v8
	v_bfe_i32 v6, v6, 0, 16
	s_waitcnt lgkmcnt(1)
	v_min_u32_e32 v2, 0x3fff, v2
	v_add_lshl_u32 v6, v8, v6, 1
	v_min_u32_e32 v3, 0x3fff, v3
	v_lshl_add_u32 v168, v2, 10, v6
	v_add_u32_e32 v2, 0x2000, v7
	v_lshl_add_u32 v169, v3, 10, v6
	v_ashrrev_i32_e32 v3, 31, v2
	v_lshrrev_b32_e32 v3, 22, v3
	v_add_u32_e32 v3, v2, v3
	v_ashrrev_i32_e32 v3, 10, v3
	v_mul_i32_i24_e32 v6, 0x400, v3
	v_sub_u32_e32 v2, v2, v6
	v_lshrrev_b32_e32 v6, 4, v2
	v_bitop3_b32 v6, v6, v2, 32 bitop3:0x6c
	v_ashrrev_i32_e32 v2, 31, v2
	v_lshrrev_b32_e32 v2, 26, v2
	v_add_u32_e32 v2, v6, v2
	v_and_b32_e32 v2, 0xc0, v2
	v_sub_u32_e32 v2, v6, v2
	v_lshlrev_b32_e32 v3, 5, v3
	v_ashrrev_i16_sdwa v2, v165, sext(v2) dst_sel:DWORD dst_unused:UNUSED_PAD src0_sel:DWORD src1_sel:BYTE_0
	v_and_b32_e32 v3, 32, v3
	v_bfe_i32 v2, v2, 0, 16
	s_waitcnt lgkmcnt(0)
	v_min_u32_e32 v4, 0x3fff, v4
	v_add_lshl_u32 v2, v3, v2, 1
	s_mov_b32 s0, m0
	s_mov_b32 m0, s15
	s_nop 0
	global_load_lds_dwordx4 v168, s[10:11]
	s_mov_b32 m0, s0
	v_lshl_add_u32 v172, v4, 10, v2
	s_add_i32 s79, s15, 0x2000
	s_mov_b32 s0, m0
	s_mov_b32 m0, s79
	s_nop 0
	global_load_lds_dwordx4 v172, s[10:11]
	s_mov_b32 m0, s0
	v_min_u32_e32 v5, 0x3fff, v5
	s_add_i32 s80, s15, 0x4000
	s_mov_b32 s0, m0
	s_mov_b32 m0, s80
	s_nop 0
	global_load_lds_dwordx4 v169, s[10:11]
	s_mov_b32 m0, s0
	s_lshr_b32 s5, s4, 8
	v_lshl_add_u32 v175, v5, 10, v2
	s_add_i32 s81, s15, 0x6000
	s_mov_b32 s8, m0
	s_mov_b32 m0, s81
	s_nop 0
	global_load_lds_dwordx4 v175, s[10:11]
	s_mov_b32 m0, s8
	s_cmp_eq_u32 s5, 1
	s_mov_b32 s20, s93
	v_writelane_b32 v253, s92, 43
	s_cselect_b64 s[0:1], -1, 0
	s_cmp_lg_u32 s5, 1
	v_writelane_b32 v253, s97, 44
	s_cbranch_scc1 .LBB0_1889
	s_barrier
.LBB0_1889:
	s_add_u32 s8, s74, 0x20000
	v_and_b32_e32 v166, 15, v0
	v_and_b32_e32 v2, 48, v0
	v_lshlrev_b32_e32 v4, 2, v0
	v_writelane_b32 v253, s8, 8
	s_addc_u32 s8, s75, 0
	s_lshl_b32 s82, s5, 6
	v_lshl_or_b32 v3, v166, 6, v2
	s_lshl_b32 s5, s5, 13
	v_and_b32_e32 v4, 32, v4
	v_bitop3_b32 v3, v3, s5, v4 bitop3:0xde
	s_lshl_b32 s5, s66, 5
	s_and_b32 s83, s5, 0x60
	v_lshlrev_b32_e32 v5, 6, v0
	s_movk_i32 s5, 0x3c0
	v_and_or_b32 v2, v5, s5, v2
	s_lshl_b32 s5, s83, 7
	v_writelane_b32 v253, s8, 31
	s_add_u32 s8, s40, 0x80
	v_bitop3_b32 v2, s5, v2, v4 bitop3:0xf6
	s_waitcnt vmcnt(2)
	s_barrier
	s_addc_u32 s9, s41, 0
	s_add_i32 s84, s15, 0x18000
	s_mov_b32 s5, m0
	s_mov_b32 m0, s84
	s_nop 0
	global_load_lds_dwordx4 v1, s[8:9]
	s_mov_b32 m0, s5
	s_add_i32 s85, s15, 0x1a000
	s_mov_b32 s5, m0
	s_mov_b32 m0, s85
	s_nop 0
	global_load_lds_dwordx4 v163, s[8:9]
	s_mov_b32 m0, s5
	s_add_u32 s8, s74, 0x1d800080
	s_addc_u32 s9, s75, 0
	s_add_i32 s86, s15, 0x8000
	s_mov_b32 s5, m0
	s_mov_b32 m0, s86
	s_nop 0
	global_load_lds_dwordx4 v168, s[8:9]
	s_mov_b32 m0, s5
	s_add_i32 s87, s15, 0xa000
	s_mov_b32 s5, m0
	s_mov_b32 m0, s87
	s_nop 0
	global_load_lds_dwordx4 v172, s[8:9]
	s_mov_b32 m0, s5
	s_add_u32 s8, s40, 0x20080
	s_addc_u32 s9, s41, 0
	s_add_i32 s91, s15, 0x1c000
	s_mov_b32 s5, m0
	s_mov_b32 m0, s91
	s_nop 0
	global_load_lds_dwordx4 v1, s[8:9]
	s_mov_b32 m0, s5
	s_add_i32 s92, s15, 0x1e000
	s_add_i32 s93, s15, 0xc000
	s_mov_b32 s5, m0
	s_mov_b32 m0, s92
	s_nop 0
	global_load_lds_dwordx4 v163, s[8:9]
	s_mov_b32 m0, s5
	s_cmpk_lt_u32 s4, 0x100
	s_waitcnt vmcnt(6)
	s_cselect_b64 s[16:17], -1, 0
	s_add_i32 s94, s15, 0xe000
	s_lshr_b32 s2, s2, 5
	s_and_b64 s[6:7], s[6:7], exec
	v_mov_b32_e32 v171, 0
	v_lshrrev_b32_e32 v167, 4, v218
	s_mov_b32 s88, 0
	v_lshlrev_b32_e32 v170, 4, v218
	v_cmp_eq_u32_e64 s[4:5], 0, v218
	s_cselect_b32 s95, s2, 0
	v_writelane_b32 v253, s20, 45
	s_bfe_u32 s96, s20, 0x50003
	s_add_i32 s97, 0, 0x201c0
	s_xor_b64 s[18:19], s[18:19], -1
	v_add_u32_e32 v173, 0, v2
	v_add_u32_e32 v174, 0, v3
	s_mov_b32 s37, 0xc0e00000
	s_mov_b32 s20, 0xc01d265f
	v_mov_b32_e32 v176, 0x40e00000
	v_mov_b32_e32 v177, v175
	v_mov_b32_e32 v178, v169
	s_mov_b32 s36, s30
	v_mov_b32_e32 v34, 0
	v_mov_b32_e32 v35, v171
	v_mov_b32_e32 v36, v171
	v_mov_b32_e32 v37, v171
	v_mov_b32_e32 v38, 0
	v_mov_b32_e32 v39, v171
	v_mov_b32_e32 v40, v171
	v_mov_b32_e32 v41, v171
	v_mov_b32_e32 v42, 0
	v_mov_b32_e32 v43, v171
	v_mov_b32_e32 v44, v171
	v_mov_b32_e32 v45, v171
	v_mov_b32_e32 v46, 0
	v_mov_b32_e32 v47, v171
	v_mov_b32_e32 v48, v171
	v_mov_b32_e32 v49, v171
	v_mov_b32_e32 v50, 0
	v_mov_b32_e32 v51, v171
	v_mov_b32_e32 v52, v171
	v_mov_b32_e32 v53, v171
	v_mov_b32_e32 v54, 0
	v_mov_b32_e32 v55, v171
	v_mov_b32_e32 v56, v171
	v_mov_b32_e32 v57, v171
	v_mov_b32_e32 v58, 0
	v_mov_b32_e32 v59, v171
	v_mov_b32_e32 v60, v171
	v_mov_b32_e32 v61, v171
	v_mov_b32_e32 v62, 0
	v_mov_b32_e32 v63, v171
	v_mov_b32_e32 v64, v171
	v_mov_b32_e32 v65, v171
	v_mov_b32_e32 v66, 0
	v_mov_b32_e32 v67, v171
	v_mov_b32_e32 v68, v171
	v_mov_b32_e32 v69, v171
	v_mov_b32_e32 v70, 0
	v_mov_b32_e32 v71, v171
	v_mov_b32_e32 v72, v171
	v_mov_b32_e32 v73, v171
	v_mov_b32_e32 v74, 0
	v_mov_b32_e32 v75, v171
	v_mov_b32_e32 v76, v171
	v_mov_b32_e32 v77, v171
	v_mov_b32_e32 v78, 0
	v_mov_b32_e32 v79, v171
	v_mov_b32_e32 v80, v171
	v_mov_b32_e32 v81, v171
	v_mov_b32_e32 v82, 0
	v_mov_b32_e32 v83, v171
	v_mov_b32_e32 v84, v171
	v_mov_b32_e32 v85, v171
	v_mov_b32_e32 v86, 0
	v_mov_b32_e32 v87, v171
	v_mov_b32_e32 v88, v171
	v_mov_b32_e32 v89, v171
	v_mov_b32_e32 v90, 0
	v_mov_b32_e32 v91, v171
	v_mov_b32_e32 v92, v171
	v_mov_b32_e32 v93, v171
	v_mov_b32_e32 v94, 0
	v_mov_b32_e32 v95, v171
	v_mov_b32_e32 v96, v171
	v_mov_b32_e32 v97, v171
	v_mov_b32_e32 v98, 0
	v_mov_b32_e32 v99, v171
	v_mov_b32_e32 v100, v171
	v_mov_b32_e32 v101, v171
	v_mov_b32_e32 v102, 0
	v_mov_b32_e32 v103, v171
	v_mov_b32_e32 v104, v171
	v_mov_b32_e32 v105, v171
	v_mov_b32_e32 v106, 0
	v_mov_b32_e32 v107, v171
	v_mov_b32_e32 v108, v171
	v_mov_b32_e32 v109, v171
	v_mov_b32_e32 v110, 0
	v_mov_b32_e32 v111, v171
	v_mov_b32_e32 v112, v171
	v_mov_b32_e32 v113, v171
	v_mov_b32_e32 v114, 0
	v_mov_b32_e32 v115, v171
	v_mov_b32_e32 v116, v171
	v_mov_b32_e32 v117, v171
	v_mov_b32_e32 v118, 0
	v_mov_b32_e32 v119, v171
	v_mov_b32_e32 v120, v171
	v_mov_b32_e32 v121, v171
	v_mov_b32_e32 v122, 0
	v_mov_b32_e32 v123, v171
	v_mov_b32_e32 v124, v171
	v_mov_b32_e32 v125, v171
	v_mov_b32_e32 v126, 0
	v_mov_b32_e32 v127, v171
	v_mov_b32_e32 v128, v171
	v_mov_b32_e32 v129, v171
	v_mov_b32_e32 v130, 0
	v_mov_b32_e32 v131, v171
	v_mov_b32_e32 v132, v171
	v_mov_b32_e32 v133, v171
	v_mov_b32_e32 v134, 0
	v_mov_b32_e32 v135, v171
	v_mov_b32_e32 v136, v171
	v_mov_b32_e32 v137, v171
	v_mov_b32_e32 v138, 0
	v_mov_b32_e32 v139, v171
	v_mov_b32_e32 v140, v171
	v_mov_b32_e32 v141, v171
	v_mov_b32_e32 v142, 0
	v_mov_b32_e32 v143, v171
	v_mov_b32_e32 v144, v171
	v_mov_b32_e32 v145, v171
	v_mov_b32_e32 v146, 0
	v_mov_b32_e32 v147, v171
	v_mov_b32_e32 v148, v171
	v_mov_b32_e32 v149, v171
	v_mov_b32_e32 v150, 0
	v_mov_b32_e32 v151, v171
	v_mov_b32_e32 v152, v171
	v_mov_b32_e32 v153, v171
	v_mov_b32_e32 v154, 0
	v_mov_b32_e32 v155, v171
	v_mov_b32_e32 v156, v171
	v_mov_b32_e32 v157, v171
	v_mov_b32_e32 v158, 0
	v_mov_b32_e32 v159, v171
	v_mov_b32_e32 v160, v171
	v_mov_b32_e32 v161, v171
	s_barrier
	v_lshrrev_b32_e32 v212, 6, v0
	v_and_b32_e32 v213, 63, v0
	v_lshlrev_b32_e32 v213, 4, v213
	v_lshrrev_b32_e32 v214, 4, v213
	v_and_b32_e32 v214, 32, v214
	v_xor_b32_e32 v213, v214, v213
	v_lshrrev_b32_e32 v214, 6, v213
	v_lshrrev_b32_e32 v215, 1, v212
	v_lshl_add_u32 v214, v215, 4, v214
	v_and_b32_e32 v212, 1, v212
	v_and_b32_e32 v213, 62, v213
	v_lshl_add_u32 v213, v212, 6, v213
	v_lshlrev_b32_e32 v212, 2, v214

.LBB0_1896:
	s_cmp_eq_u32 s40, 0
	s_cbranch_scc1 .Lpeel6
	s_add_u32 s33, s74, s40
	s_addc_u32 s44, s75, s41
	s_add_u32 s56, s33, 0x1d800080
	s_addc_u32 s57, s44, 0
	s_add_u32 s33, s33, 0x1d800100
	s_addc_u32 s52, s44, 0
	v_add_u32_e32 v2, 0x10000, v173
	v_add_u32_e32 v14, 0x14000, v173
	s_and_b64 s[44:45], s[42:43], exec
	ds_read_b128 v[18:21], v2
	ds_read_b128 v[22:25], v2 offset:1024
	ds_read_b128 v[26:29], v2 offset:2048
	ds_read_b128 v[30:33], v2 offset:3072
	ds_read_b128 v[2:5], v14
	ds_read_b128 v[6:9], v14 offset:1024
	ds_read_b128 v[10:13], v14 offset:2048
	ds_read_b128 v[14:17], v14 offset:3072
	s_cselect_b32 s55, s11, s52
	s_cselect_b32 s54, s10, s33
	s_add_u32 s33, s2, s40
	s_addc_u32 s44, s23, s41
	s_and_b64 s[42:43], s[42:43], exec
	s_cselect_b32 s43, s39, s44
	s_cselect_b32 s42, s38, s33
	s_add_u32 s44, s54, 0x80
	s_addc_u32 s45, s55, 0
	s_add_u32 s52, s42, 0x80
	s_addc_u32 s53, s43, 0
	ds_read_b128 v[180:183], v174
	ds_read_b128 v[184:187], v174 offset:1024
	ds_read_b128 v[188:191], v174 offset:2048
	ds_read_b128 v[192:195], v174 offset:3072
	ds_read_b128 v[196:199], v174 offset:4096
	ds_read_b128 v[200:203], v174 offset:5120
	ds_read_b128 v[204:207], v174 offset:6144
	ds_read_b128 v[208:211], v174 offset:7168
	s_mov_b32 s33, m0
	s_mov_b32 m0, s93
	s_nop 0
	global_load_lds_dwordx4 v178, s[56:57]
	s_mov_b32 m0, s33
	s_nop 0
	s_mov_b32 s33, m0
	s_mov_b32 m0, s94
	s_nop 0
	global_load_lds_dwordx4 v177, s[56:57]
	s_mov_b32 m0, s33
	s_waitcnt vmcnt(8)
	s_waitcnt lgkmcnt(0)
	s_barrier
	s_setprio 1
	s_waitcnt lgkmcnt(6)
	v_mfma_f32_16x16x128_f8f6f4 v[158:161], v[18:25], v[180:187], v[158:161]
	v_mfma_f32_16x16x128_f8f6f4 v[154:157], v[26:33], v[180:187], v[154:157]
	s_waitcnt lgkmcnt(4)
	v_mfma_f32_16x16x128_f8f6f4 v[150:153], v[18:25], v[188:195], v[150:153]
	v_mfma_f32_16x16x128_f8f6f4 v[146:149], v[26:33], v[188:195], v[146:149]
	s_waitcnt lgkmcnt(2)
	v_mfma_f32_16x16x128_f8f6f4 v[142:145], v[18:25], v[196:203], v[142:145]
	v_mfma_f32_16x16x128_f8f6f4 v[138:141], v[26:33], v[196:203], v[138:141]
	s_waitcnt lgkmcnt(0)
	v_mfma_f32_16x16x128_f8f6f4 v[134:137], v[18:25], v[204:211], v[134:137]
	v_mfma_f32_16x16x128_f8f6f4 v[130:133], v[26:33], v[204:211], v[130:133]
	s_setprio 0
	s_setprio 1
	v_mfma_f32_16x16x128_f8f6f4 v[126:129], v[2:9], v[180:187], v[126:129]
	v_mfma_f32_16x16x128_f8f6f4 v[122:125], v[10:17], v[180:187], v[122:125]
	v_mfma_f32_16x16x128_f8f6f4 v[118:121], v[2:9], v[188:195], v[118:121]
	v_mfma_f32_16x16x128_f8f6f4 v[114:117], v[10:17], v[188:195], v[114:117]
	v_mfma_f32_16x16x128_f8f6f4 v[110:113], v[2:9], v[196:203], v[110:113]
	v_mfma_f32_16x16x128_f8f6f4 v[106:109], v[10:17], v[196:203], v[106:109]
	v_mfma_f32_16x16x128_f8f6f4 v[102:105], v[2:9], v[204:211], v[102:105]
	v_mfma_f32_16x16x128_f8f6f4 v[98:101], v[10:17], v[204:211], v[98:101]
	s_setprio 0
	s_barrier
	ds_read_b128 v[180:183], v174 offset:16384
	ds_read_b128 v[184:187], v174 offset:17408
	ds_read_b128 v[188:191], v174 offset:18432
	ds_read_b128 v[192:195], v174 offset:19456
	ds_read_b128 v[196:199], v174 offset:20480
	ds_read_b128 v[200:203], v174 offset:21504
	ds_read_b128 v[204:207], v174 offset:22528
	ds_read_b128 v[208:211], v174 offset:23552
	s_mov_b32 s33, m0
	s_mov_b32 m0, s67
	s_nop 0
	global_load_lds_dwordx4 v1, s[42:43]
	s_mov_b32 m0, s33
	s_add_u32 s56, s42, 0x20000
	s_mov_b32 s33, m0
	s_mov_b32 m0, s68
	s_nop 0
	global_load_lds_dwordx4 v163, s[42:43]
	s_mov_b32 m0, s33
	s_addc_u32 s57, s43, 0
	s_mov_b32 s33, m0
	s_mov_b32 m0, s69
	s_nop 0
	global_load_lds_dwordx4 v1, s[56:57]
	s_mov_b32 m0, s33
	s_nop 0
	s_mov_b32 s33, m0
	s_mov_b32 m0, s76
	s_nop 0
	global_load_lds_dwordx4 v163, s[56:57]
	s_mov_b32 m0, s33
	s_nop 0
	s_mov_b32 s33, m0
	s_mov_b32 m0, s15
	s_nop 0
	global_load_lds_dwordx4 v168, s[54:55]
	s_mov_b32 m0, s33
	s_nop 0
	s_mov_b32 s33, m0
	s_mov_b32 m0, s79
	s_nop 0
	global_load_lds_dwordx4 v172, s[54:55]
	s_mov_b32 m0, s33
	s_waitcnt vmcnt(8)
	s_waitcnt lgkmcnt(0)
	s_barrier
	s_setprio 1
	s_waitcnt lgkmcnt(6)
	v_mfma_f32_16x16x128_f8f6f4 v[94:97], v[18:25], v[180:187], v[94:97]
	v_mfma_f32_16x16x128_f8f6f4 v[90:93], v[26:33], v[180:187], v[90:93]
	s_waitcnt lgkmcnt(4)
	v_mfma_f32_16x16x128_f8f6f4 v[86:89], v[18:25], v[188:195], v[86:89]
	v_mfma_f32_16x16x128_f8f6f4 v[82:85], v[26:33], v[188:195], v[82:85]
	s_waitcnt lgkmcnt(2)
	v_mfma_f32_16x16x128_f8f6f4 v[78:81], v[18:25], v[196:203], v[78:81]
	v_mfma_f32_16x16x128_f8f6f4 v[74:77], v[26:33], v[196:203], v[74:77]
	s_waitcnt lgkmcnt(0)
	v_mfma_f32_16x16x128_f8f6f4 v[70:73], v[18:25], v[204:211], v[70:73]
	v_mfma_f32_16x16x128_f8f6f4 v[66:69], v[26:33], v[204:211], v[66:69]
	s_setprio 0
	s_setprio 1
	v_mfma_f32_16x16x128_f8f6f4 v[62:65], v[2:9], v[180:187], v[62:65]
	v_mfma_f32_16x16x128_f8f6f4 v[58:61], v[10:17], v[180:187], v[58:61]
	v_mfma_f32_16x16x128_f8f6f4 v[54:57], v[2:9], v[188:195], v[54:57]
	v_mfma_f32_16x16x128_f8f6f4 v[50:53], v[10:17], v[188:195], v[50:53]
	v_mfma_f32_16x16x128_f8f6f4 v[46:49], v[2:9], v[196:203], v[46:49]
	v_mfma_f32_16x16x128_f8f6f4 v[42:45], v[10:17], v[196:203], v[42:45]
	v_mfma_f32_16x16x128_f8f6f4 v[38:41], v[2:9], v[204:211], v[38:41]
	v_mfma_f32_16x16x128_f8f6f4 v[34:37], v[10:17], v[204:211], v[34:37]
	s_setprio 0
	s_barrier
.Lmid6:
	v_add_u32_e32 v14, 0x18000, v173
	v_add_u32_e32 v30, 0x1c000, v173
	ds_read_b128 v[2:5], v14
	ds_read_b128 v[6:9], v14 offset:1024
	ds_read_b128 v[10:13], v14 offset:2048
	ds_read_b128 v[14:17], v14 offset:3072
	ds_read_b128 v[18:21], v30
	ds_read_b128 v[22:25], v30 offset:1024
	ds_read_b128 v[26:29], v30 offset:2048
	ds_read_b128 v[30:33], v30 offset:3072
	ds_read_b128 v[180:183], v174 offset:32768
	ds_read_b128 v[184:187], v174 offset:33792
	ds_read_b128 v[188:191], v174 offset:34816
	ds_read_b128 v[192:195], v174 offset:35840
	ds_read_b128 v[196:199], v174 offset:36864
	ds_read_b128 v[200:203], v174 offset:37888
	ds_read_b128 v[204:207], v174 offset:38912
	ds_read_b128 v[208:211], v174 offset:39936
	s_mov_b32 s33, m0
	s_mov_b32 m0, s80
	s_nop 0
	global_load_lds_dwordx4 v169, s[54:55]
	s_mov_b32 m0, s33
	s_nop 0
	s_mov_b32 s33, m0
	s_mov_b32 m0, s81
	s_nop 0
	global_load_lds_dwordx4 v175, s[54:55]
	s_mov_b32 m0, s33
	s_waitcnt vmcnt(8)
	s_waitcnt lgkmcnt(0)
	s_barrier
	s_setprio 1
	s_waitcnt lgkmcnt(6)
	v_mfma_f32_16x16x128_f8f6f4 v[158:161], v[2:9], v[180:187], v[158:161]
	v_mfma_f32_16x16x128_f8f6f4 v[154:157], v[10:17], v[180:187], v[154:157]
	s_waitcnt lgkmcnt(4)
	v_mfma_f32_16x16x128_f8f6f4 v[150:153], v[2:9], v[188:195], v[150:153]
	v_mfma_f32_16x16x128_f8f6f4 v[146:149], v[10:17], v[188:195], v[146:149]
	s_waitcnt lgkmcnt(2)
	v_mfma_f32_16x16x128_f8f6f4 v[142:145], v[2:9], v[196:203], v[142:145]
	v_mfma_f32_16x16x128_f8f6f4 v[138:141], v[10:17], v[196:203], v[138:141]
	s_waitcnt lgkmcnt(0)
	v_mfma_f32_16x16x128_f8f6f4 v[134:137], v[2:9], v[204:211], v[134:137]
	v_mfma_f32_16x16x128_f8f6f4 v[130:133], v[10:17], v[204:211], v[130:133]
	s_setprio 0
	s_setprio 1
	v_mfma_f32_16x16x128_f8f6f4 v[126:129], v[18:25], v[180:187], v[126:129]
	v_mfma_f32_16x16x128_f8f6f4 v[122:125], v[26:33], v[180:187], v[122:125]
	v_mfma_f32_16x16x128_f8f6f4 v[118:121], v[18:25], v[188:195], v[118:121]
	v_mfma_f32_16x16x128_f8f6f4 v[114:117], v[26:33], v[188:195], v[114:117]
	v_mfma_f32_16x16x128_f8f6f4 v[110:113], v[18:25], v[196:203], v[110:113]
	v_mfma_f32_16x16x128_f8f6f4 v[106:109], v[26:33], v[196:203], v[106:109]
	v_mfma_f32_16x16x128_f8f6f4 v[102:105], v[18:25], v[204:211], v[102:105]
	v_mfma_f32_16x16x128_f8f6f4 v[98:101], v[26:33], v[204:211], v[98:101]
	s_setprio 0
	s_barrier
	ds_read_b128 v[180:183], v174 offset:49152
	ds_read_b128 v[184:187], v174 offset:50176
	ds_read_b128 v[188:191], v174 offset:51200
	ds_read_b128 v[192:195], v174 offset:52224
	ds_read_b128 v[196:199], v174 offset:53248
	ds_read_b128 v[200:203], v174 offset:54272
	ds_read_b128 v[204:207], v174 offset:55296
	ds_read_b128 v[208:211], v174 offset:56320
	s_mov_b32 s33, m0
	s_mov_b32 m0, s84
	s_nop 0
	global_load_lds_dwordx4 v1, s[52:53]
	s_mov_b32 m0, s33
	s_add_u32 s42, s42, 0x20080
	s_mov_b32 s33, m0
	s_mov_b32 m0, s85
	s_nop 0
	global_load_lds_dwordx4 v163, s[52:53]
	s_mov_b32 m0, s33
	s_addc_u32 s43, s43, 0
	s_mov_b32 s33, m0
	s_mov_b32 m0, s91
	s_nop 0
	global_load_lds_dwordx4 v1, s[42:43]
	s_mov_b32 m0, s33
	s_nop 0
	s_mov_b32 s33, m0
	s_mov_b32 m0, s92
	s_nop 0
	global_load_lds_dwordx4 v163, s[42:43]
	s_mov_b32 m0, s33
	s_nop 0
	s_mov_b32 s33, m0
	s_mov_b32 m0, s86
	s_nop 0
	global_load_lds_dwordx4 v168, s[44:45]
	s_mov_b32 m0, s33
	s_nop 0
	s_mov_b32 s33, m0
	s_mov_b32 m0, s87
	s_nop 0
	global_load_lds_dwordx4 v172, s[44:45]
	s_mov_b32 m0, s33
	s_waitcnt vmcnt(8)
	s_waitcnt lgkmcnt(0)
	s_barrier
	s_setprio 1
	s_waitcnt lgkmcnt(6)
	v_mfma_f32_16x16x128_f8f6f4 v[94:97], v[2:9], v[180:187], v[94:97]
	v_mfma_f32_16x16x128_f8f6f4 v[90:93], v[10:17], v[180:187], v[90:93]
	s_waitcnt lgkmcnt(4)
	v_mfma_f32_16x16x128_f8f6f4 v[86:89], v[2:9], v[188:195], v[86:89]
	v_mfma_f32_16x16x128_f8f6f4 v[82:85], v[10:17], v[188:195], v[82:85]
	s_waitcnt lgkmcnt(2)
	v_mfma_f32_16x16x128_f8f6f4 v[78:81], v[2:9], v[196:203], v[78:81]
	v_mfma_f32_16x16x128_f8f6f4 v[74:77], v[10:17], v[196:203], v[74:77]
	s_waitcnt lgkmcnt(0)
	v_mfma_f32_16x16x128_f8f6f4 v[70:73], v[2:9], v[204:211], v[70:73]
	v_mfma_f32_16x16x128_f8f6f4 v[66:69], v[10:17], v[204:211], v[66:69]
	s_setprio 0
	s_setprio 1
	v_mfma_f32_16x16x128_f8f6f4 v[62:65], v[18:25], v[180:187], v[62:65]
	v_mfma_f32_16x16x128_f8f6f4 v[58:61], v[26:33], v[180:187], v[58:61]
	v_mfma_f32_16x16x128_f8f6f4 v[54:57], v[18:25], v[188:195], v[54:57]
	v_mfma_f32_16x16x128_f8f6f4 v[50:53], v[26:33], v[188:195], v[50:53]
	v_mfma_f32_16x16x128_f8f6f4 v[46:49], v[18:25], v[196:203], v[46:49]
	v_mfma_f32_16x16x128_f8f6f4 v[42:45], v[26:33], v[196:203], v[42:45]
	v_mfma_f32_16x16x128_f8f6f4 v[38:41], v[18:25], v[204:211], v[38:41]
	v_mfma_f32_16x16x128_f8f6f4 v[34:37], v[26:33], v[204:211], v[34:37]
	s_setprio 0
	s_cmp_lt_i32 s9, 4
	s_cbranch_scc1 .Lkb6_do
	s_cmp_lg_u64 s[16:17], 0
	s_cbranch_scc0 .Lkb6_skip

.LBB0_1897:
	s_cmpk_eq_i32 s40, 0x300
	s_cselect_b64 s[42:43], -1, 0
	s_and_b64 vcc, exec, s[6:7]
	s_cbranch_vccnz .LBB0_1895
	s_cmp_lg_u32 s40, 0
	s_cselect_b64 s[44:45], -1, 0
	s_or_b64 s[44:45], s[18:19], s[44:45]
	s_and_b64 vcc, exec, s[44:45]
	s_cbranch_vccnz .LBB0_1900
	v_mov_b32_e32 v2, s8
	ds_read_b32 v2, v2 offset:288
	s_waitcnt lgkmcnt(0)
	v_readfirstlane_b32 s33, v2
	s_lshl_b32 s44, s33, 2
	s_add_i32 s44, s44, 0
	s_add_i32 s44, s44, 0x20240
	v_mov_b32_e32 v2, s44
	ds_read_b32 v2, v2
	s_lshl_b32 s44, s33, 14
	s_ashr_i32 s45, s44, 31
	s_lshl_b64 s[44:45], s[44:45], 2
	s_waitcnt lgkmcnt(0)
	v_readfirstlane_b32 s33, v2
	s_sub_i32 s33, s65, s33
	s_lshl_b32 s52, s33, 8
	s_add_u32 s33, s58, s44
	s_addc_u32 s54, s59, s45
	s_ashr_i32 s53, s52, 31
	s_lshl_b64 s[44:45], s[52:53], 2
	s_add_u32 s44, s33, s44
	s_addc_u32 s45, s54, s45
	s_mov_b32 s33, m0
	s_mov_b32 m0, s25
	s_nop 0
	global_load_lds_dwordx4 v170, s[44:45]
	s_mov_b32 m0, s33

.Lpeel6:
	s_add_u32 s33, s74, s40
	s_addc_u32 s44, s75, s41
	s_add_u32 s56, s33, 0x1d800080
	s_addc_u32 s57, s44, 0
	s_add_u32 s33, s33, 0x1d800100
	s_addc_u32 s52, s44, 0
	v_add_u32_e32 v2, 0x10000, v173
	v_add_u32_e32 v14, 0x14000, v173
	s_and_b64 s[44:45], s[42:43], exec
	ds_read_b128 v[18:21], v2
	ds_read_b128 v[22:25], v2 offset:1024
	ds_read_b128 v[26:29], v2 offset:2048
	ds_read_b128 v[30:33], v2 offset:3072
	ds_read_b128 v[2:5], v14
	ds_read_b128 v[6:9], v14 offset:1024
	ds_read_b128 v[10:13], v14 offset:2048
	ds_read_b128 v[14:17], v14 offset:3072
	s_cselect_b32 s55, s11, s52
	s_cselect_b32 s54, s10, s33
	s_add_u32 s33, s2, s40
	s_addc_u32 s44, s23, s41
	s_and_b64 s[42:43], s[42:43], exec
	s_cselect_b32 s43, s39, s44
	s_cselect_b32 s42, s38, s33
	s_add_u32 s44, s54, 0x80
	s_addc_u32 s45, s55, 0
	s_add_u32 s52, s42, 0x80
	s_addc_u32 s53, s43, 0
	ds_read_b128 v[180:183], v174
	ds_read_b128 v[184:187], v174 offset:1024
	ds_read_b128 v[188:191], v174 offset:2048
	ds_read_b128 v[192:195], v174 offset:3072
	ds_read_b128 v[196:199], v174 offset:4096
	ds_read_b128 v[200:203], v174 offset:5120
	ds_read_b128 v[204:207], v174 offset:6144
	ds_read_b128 v[208:211], v174 offset:7168
	s_mov_b32 s33, m0
	s_mov_b32 m0, s93
	s_nop 0
	global_load_lds_dwordx4 v178, s[56:57]
	s_mov_b32 m0, s33
	s_nop 0
	s_mov_b32 s33, m0
	s_mov_b32 m0, s94
	s_nop 0
	global_load_lds_dwordx4 v177, s[56:57]
	s_mov_b32 m0, s33
	s_waitcnt vmcnt(8)
	s_waitcnt lgkmcnt(0)
	s_barrier
	s_setprio 1
	s_waitcnt lgkmcnt(6)
	v_mfma_f32_16x16x128_f8f6f4 v[158:161], v[18:25], v[180:187], 0
	v_mfma_f32_16x16x128_f8f6f4 v[154:157], v[26:33], v[180:187], 0
	s_waitcnt lgkmcnt(4)
	v_mfma_f32_16x16x128_f8f6f4 v[150:153], v[18:25], v[188:195], 0
	v_mfma_f32_16x16x128_f8f6f4 v[146:149], v[26:33], v[188:195], 0
	s_waitcnt lgkmcnt(2)
	v_mfma_f32_16x16x128_f8f6f4 v[142:145], v[18:25], v[196:203], 0
	v_mfma_f32_16x16x128_f8f6f4 v[138:141], v[26:33], v[196:203], 0
	s_waitcnt lgkmcnt(0)
	v_mfma_f32_16x16x128_f8f6f4 v[134:137], v[18:25], v[204:211], 0
	v_mfma_f32_16x16x128_f8f6f4 v[130:133], v[26:33], v[204:211], 0
	s_setprio 0
	s_setprio 1
	v_mfma_f32_16x16x128_f8f6f4 v[126:129], v[2:9], v[180:187], 0
	v_mfma_f32_16x16x128_f8f6f4 v[122:125], v[10:17], v[180:187], 0
	v_mfma_f32_16x16x128_f8f6f4 v[118:121], v[2:9], v[188:195], 0
	v_mfma_f32_16x16x128_f8f6f4 v[114:117], v[10:17], v[188:195], 0
	v_mfma_f32_16x16x128_f8f6f4 v[110:113], v[2:9], v[196:203], 0
	v_mfma_f32_16x16x128_f8f6f4 v[106:109], v[10:17], v[196:203], 0
	v_mfma_f32_16x16x128_f8f6f4 v[102:105], v[2:9], v[204:211], 0
	v_mfma_f32_16x16x128_f8f6f4 v[98:101], v[10:17], v[204:211], 0
	s_setprio 0
	s_barrier
	ds_read_b128 v[180:183], v174 offset:16384
	ds_read_b128 v[184:187], v174 offset:17408
	ds_read_b128 v[188:191], v174 offset:18432
	ds_read_b128 v[192:195], v174 offset:19456
	ds_read_b128 v[196:199], v174 offset:20480
	ds_read_b128 v[200:203], v174 offset:21504
	ds_read_b128 v[204:207], v174 offset:22528
	ds_read_b128 v[208:211], v174 offset:23552
	s_mov_b32 s33, m0
	s_mov_b32 m0, s67
	s_nop 0
	global_load_lds_dwordx4 v1, s[42:43]
	s_mov_b32 m0, s33
	s_add_u32 s56, s42, 0x20000
	s_mov_b32 s33, m0
	s_mov_b32 m0, s68
	s_nop 0
	global_load_lds_dwordx4 v163, s[42:43]
	s_mov_b32 m0, s33
	s_addc_u32 s57, s43, 0
	s_mov_b32 s33, m0
	s_mov_b32 m0, s69
	s_nop 0
	global_load_lds_dwordx4 v1, s[56:57]
	s_mov_b32 m0, s33
	s_nop 0
	s_mov_b32 s33, m0
	s_mov_b32 m0, s76
	s_nop 0
	global_load_lds_dwordx4 v163, s[56:57]
	s_mov_b32 m0, s33
	s_nop 0
	s_mov_b32 s33, m0
	s_mov_b32 m0, s15
	s_nop 0
	global_load_lds_dwordx4 v168, s[54:55]
	s_mov_b32 m0, s33
	s_nop 0
	s_mov_b32 s33, m0
	s_mov_b32 m0, s79
	s_nop 0
	global_load_lds_dwordx4 v172, s[54:55]
	s_mov_b32 m0, s33
	s_waitcnt vmcnt(8)
	s_waitcnt lgkmcnt(0)
	s_barrier
	s_setprio 1
	s_waitcnt lgkmcnt(6)
	v_mfma_f32_16x16x128_f8f6f4 v[94:97], v[18:25], v[180:187], 0
	v_mfma_f32_16x16x128_f8f6f4 v[90:93], v[26:33], v[180:187], 0
	s_waitcnt lgkmcnt(4)
	v_mfma_f32_16x16x128_f8f6f4 v[86:89], v[18:25], v[188:195], 0
	v_mfma_f32_16x16x128_f8f6f4 v[82:85], v[26:33], v[188:195], 0
	s_waitcnt lgkmcnt(2)
	v_mfma_f32_16x16x128_f8f6f4 v[78:81], v[18:25], v[196:203], 0
	v_mfma_f32_16x16x128_f8f6f4 v[74:77], v[26:33], v[196:203], 0
	s_waitcnt lgkmcnt(0)
	v_mfma_f32_16x16x128_f8f6f4 v[70:73], v[18:25], v[204:211], 0
	v_mfma_f32_16x16x128_f8f6f4 v[66:69], v[26:33], v[204:211], 0
	s_setprio 0
	s_setprio 1
	v_mfma_f32_16x16x128_f8f6f4 v[62:65], v[2:9], v[180:187], 0
	v_mfma_f32_16x16x128_f8f6f4 v[58:61], v[10:17], v[180:187], 0
	v_mfma_f32_16x16x128_f8f6f4 v[54:57], v[2:9], v[188:195], 0
	v_mfma_f32_16x16x128_f8f6f4 v[50:53], v[10:17], v[188:195], 0
	v_mfma_f32_16x16x128_f8f6f4 v[46:49], v[2:9], v[196:203], 0
	v_mfma_f32_16x16x128_f8f6f4 v[42:45], v[10:17], v[196:203], 0
	v_mfma_f32_16x16x128_f8f6f4 v[38:41], v[2:9], v[204:211], 0
	v_mfma_f32_16x16x128_f8f6f4 v[34:37], v[10:17], v[204:211], 0
	s_setprio 0
	s_barrier
	s_branch .Lmid6
.LBB0_1902:
	v_mov_b32_e32 v2, s24
	ds_read_b32 v2, v2 offset:288
	s_mov_b64 s[52:53], -1
	s_waitcnt lgkmcnt(0)
	v_readfirstlane_b32 s44, v2
	s_lshl_b32 s31, s44, 2
	s_add_i32 s31, s31, 0
	s_add_i32 s31, s31, 0x20240
	v_mov_b32_e32 v2, s31
	ds_read_b32 v2, v2
	s_cmp_lt_i32 s66, 2
	s_waitcnt lgkmcnt(0)
	v_readfirstlane_b32 s31, v2
	s_cbranch_scc1 .LBB0_1906
	s_cmp_eq_u32 s66, 2
	s_cbranch_scc0 .LBB0_1905
	s_lshl_b32 s54, s44, 14
	s_sub_i32 s31, s36, s31
	s_ashr_i32 s55, s54, 31
	s_lshl_b32 s52, s31, 8
	s_lshl_b64 s[54:55], s[54:55], 2
	s_add_u32 s31, s60, s54
	s_addc_u32 s33, s61, s55
	s_ashr_i32 s53, s52, 31
	s_lshl_b64 s[52:53], s[52:53], 2
	s_add_u32 s52, s31, s52
	s_addc_u32 s53, s33, s53
	s_mov_b32 s31, m0
	s_mov_b32 m0, s90
	s_nop 0
	global_load_lds_dwordx4 v170, s[52:53]
	s_mov_b32 m0, s31

.LBB0_1906:
	s_andn2_b64 vcc, exec, s[52:53]
	s_mov_b32 s31, s28
	s_cbranch_vccnz .LBB0_1896
	s_cmp_lg_u32 s66, 1
	s_mov_b32 s31, s28
	s_cbranch_scc1 .LBB0_1896
	s_ashr_i32 s45, s44, 31
	s_lshl_b64 s[44:45], s[44:45], 13
	s_add_u32 s44, s77, s44
	s_addc_u32 s45, s78, s45
	s_mov_b32 s31, m0
	s_mov_b32 m0, s29
	s_nop 0
	global_load_lds_dwordx4 v170, s[44:45]
	s_mov_b32 m0, s31
	s_mov_b32 s31, s28
	s_branch .LBB0_1896

.LBB0_1930:
	s_andn2_b64 vcc, exec, s[0:1]
	v_lshlrev_b32_e32 v1, 4, v0
	s_cbranch_vccnz .LBB0_1963
	s_waitcnt vmcnt(0)
	v_lshrrev_b32_e32 v3, 1, v0
	v_bfe_u32 v4, v0, 2, 2
	v_and_or_b32 v3, v3, 24, v4
	v_lshrrev_b32_e32 v4, 3, v0
	v_lshrrev_b32_e32 v6, 5, v0
	v_and_b32_e32 v4, 32, v4
	v_and_b32_e32 v6, 4, v6
	v_and_b32_e32 v2, 32, v0
	v_or3_b32 v4, v6, v4, v3
	v_bitop3_b32 v2, v1, v2, 48 bitop3:0x6c
	v_and_b32_e32 v5, 64, v0
	v_lshlrev_b32_e32 v4, 10, v4
	v_or3_b32 v165, v4, v5, v2
	v_or_b32_e32 v4, 0x2000, v1
	s_lshl_b32 s0, s2, 2
	v_lshrrev_b32_e32 v4, 7, v4
	v_lshrrev_b32_e32 v6, 9, v1
	s_add_i32 s5, s0, 0
	v_and_b32_e32 v4, 0x60, v4
	v_and_b32_e32 v6, 4, v6
	s_add_i32 s5, s5, 0x201c0
	v_or3_b32 v3, v6, v4, v3
	v_mov_b32_e32 v4, s5
	ds_read_b32 v4, v4 offset:288
	s_lshr_b32 s30, s4, 6
	s_ashr_i32 s27, s26, 31
	s_lshl_b32 s7, s30, 10
	s_lshl_b64 s[8:9], s[26:27], 18
	s_waitcnt lgkmcnt(0)
	v_readfirstlane_b32 s0, v4
	s_ashr_i32 s1, s0, 31
	s_lshl_b64 s[0:1], s[0:1], 21
	s_add_u32 s0, s3, s0
	s_addc_u32 s1, s21, s1
	s_add_u32 s38, s0, s8
	v_lshrrev_b32_e32 v5, 4, v1
	s_addc_u32 s39, s1, s9
	s_add_i32 s31, s7, 0
	v_and_b32_e32 v5, 64, v5
	v_lshlrev_b32_e32 v3, 10, v3
	s_add_i32 s34, s31, 0x10000
	s_mov_b32 s0, m0
	s_mov_b32 m0, s34
	s_nop 0
	global_load_lds_dwordx4 v165, s[38:39]
	s_mov_b32 m0, s0
	s_add_i32 s35, s31, 0x12000
	v_or3_b32 v167, v3, v5, v2
	s_mov_b32 s0, m0
	s_mov_b32 m0, s35
	s_nop 0
	global_load_lds_dwordx4 v167, s[38:39]
	s_mov_b32 m0, s0
	s_add_u32 s8, s38, 0x20000
	s_addc_u32 s9, s39, 0
	s_add_i32 s36, s31, 0x14000
	s_mov_b32 s0, m0
	s_mov_b32 m0, s36
	s_nop 0
	global_load_lds_dwordx4 v165, s[8:9]
	s_mov_b32 m0, s0
	s_add_i32 s37, s31, 0x16000
	s_mov_b32 s7, m0
	s_mov_b32 m0, s37
	s_nop 0
	global_load_lds_dwordx4 v167, s[8:9]
	s_mov_b32 m0, s7
	s_cmp_lt_u32 s4, 64
	s_cselect_b64 s[0:1], -1, 0
	s_cmp_gt_u32 s4, 63
	s_cbranch_scc1 .LBB0_1933
	v_mov_b32_e32 v2, s5
	ds_read_b32 v2, v2 offset:288
	v_lshlrev_b32_e32 v3, 4, v218
	s_waitcnt lgkmcnt(0)
	v_readfirstlane_b32 s5, v2
	s_lshl_b32 s7, s5, 2
	s_add_i32 s7, s7, 0
	s_add_i32 s7, s7, 0x20240
	v_mov_b32_e32 v2, s7
	ds_read_b32 v2, v2
	s_lshl_b32 s8, s5, 14
	s_ashr_i32 s9, s8, 31
	s_lshl_b64 s[8:9], s[8:9], 2
	s_waitcnt lgkmcnt(0)
	v_readfirstlane_b32 s5, v2
	s_sub_i32 s5, s2, s5
	s_lshl_b32 s14, s5, 8
	s_add_u32 s5, s58, s8
	s_addc_u32 s7, s59, s9
	s_ashr_i32 s15, s14, 31
	s_lshl_b64 s[8:9], s[14:15], 2
	s_add_u32 s8, s5, s8
	s_addc_u32 s9, s7, s9
	s_add_i32 s5, 0, 0x20800
	s_mov_b32 s7, m0
	s_mov_b32 m0, s5
	s_nop 0
	global_load_lds_dwordx4 v3, s[8:9]
	s_mov_b32 m0, s7
.LBB0_1933:
	v_mov_b32_e32 v2, v0
	s_waitcnt vmcnt(0)
	s_barrier
	s_add_i32 s5, 0, 0x20800
	v_ashrrev_i32_e32 v3, 31, v2
	v_lshrrev_b32_e32 v3, 26, v3
	v_lshlrev_b32_e32 v4, 4, v2
	v_add_u32_e32 v3, v2, v3
	v_bfe_i32 v2, v2, 27, 1
	v_lshrrev_b32_e32 v2, 22, v2
	v_add_u32_e32 v2, v4, v2
	v_and_b32_e32 v2, 0xfffffc00, v2
	v_sub_u32_e32 v2, v4, v2
	v_lshrrev_b32_e32 v5, 4, v2
	v_ashrrev_i32_e32 v6, 31, v2
	v_and_b32_e32 v5, 32, v5
	v_lshrrev_b32_e32 v6, 26, v6
	v_add_u32_e32 v4, 0x2000, v4
	v_xad_u32 v2, v5, v2, v6
	v_ashrrev_i32_e32 v5, 31, v4
	v_lshrrev_b32_e32 v5, 22, v5
	v_add_u32_e32 v5, v4, v5
	v_ashrrev_i32_e32 v5, 10, v5
	v_mul_i32_i24_e32 v6, 0x400, v5
	v_sub_u32_e32 v4, v4, v6
	v_lshrrev_b32_e32 v6, 4, v4
	v_ashrrev_i32_e32 v7, 31, v4
	v_ashrrev_i32_e32 v3, 6, v3
	v_and_b32_e32 v6, 32, v6
	v_lshrrev_b32_e32 v7, 26, v7
	v_lshlrev_b32_e32 v3, 3, v3
	v_lshlrev_b32_e32 v5, 3, v5
	v_xad_u32 v4, v6, v4, v7
	v_and_b32_e32 v3, 0x3ffffff0, v3
	v_ashrrev_i32_e32 v2, 6, v2
	v_and_b32_e32 v5, 0x3ffffff0, v5
	v_ashrrev_i32_e32 v4, 6, v4
	v_add_u32_e32 v2, v2, v3
	v_add_u32_e32 v4, v4, v5
	v_lshl_add_u32 v2, v2, 2, s5
	v_lshl_add_u32 v4, v4, 2, s5
	v_mov_b32_e32 v6, v0
	ds_read2st64_b32 v[2:3], v2 offset1:2
	ds_read2st64_b32 v[4:5], v4 offset1:2
	v_mov_b32_e32 v168, 1
	v_ashrrev_i32_e32 v8, 31, v6
	v_lshrrev_b32_e32 v8, 26, v8
	v_lshlrev_b32_e32 v7, 4, v6
	v_add_u32_e32 v8, v6, v8
	v_bfe_i32 v6, v6, 27, 1
	v_lshrrev_b32_e32 v6, 22, v6
	v_add_u32_e32 v6, v7, v6
	v_and_b32_e32 v6, 0xfffffc00, v6
	v_sub_u32_e32 v6, v7, v6
	v_lshrrev_b32_e32 v9, 4, v6
	v_bitop3_b32 v9, v9, v6, 32 bitop3:0x6c
	v_ashrrev_i32_e32 v6, 31, v6
	v_lshrrev_b32_e32 v6, 26, v6
	v_add_u32_e32 v6, v9, v6
	v_and_b32_e32 v6, 0xc0, v6
	v_sub_u32_e32 v6, v9, v6
	v_lshrrev_b32_e32 v8, 1, v8
	v_ashrrev_i16_sdwa v6, v168, sext(v6) dst_sel:DWORD dst_unused:UNUSED_PAD src0_sel:DWORD src1_sel:BYTE_0
	v_and_b32_e32 v8, 32, v8
	v_bfe_i32 v6, v6, 0, 16
	s_waitcnt lgkmcnt(1)
	v_min_u32_e32 v2, 0x3fff, v2
	v_add_lshl_u32 v6, v8, v6, 1
	v_min_u32_e32 v3, 0x3fff, v3
	v_lshl_add_u32 v171, v2, 10, v6
	v_add_u32_e32 v2, 0x2000, v7
	v_lshl_add_u32 v164, v3, 10, v6
	v_ashrrev_i32_e32 v3, 31, v2
	v_lshrrev_b32_e32 v3, 22, v3
	v_add_u32_e32 v3, v2, v3
	v_ashrrev_i32_e32 v3, 10, v3
	v_mul_i32_i24_e32 v6, 0x400, v3
	v_sub_u32_e32 v2, v2, v6
	v_lshrrev_b32_e32 v6, 4, v2
	v_bitop3_b32 v6, v6, v2, 32 bitop3:0x6c
	v_ashrrev_i32_e32 v2, 31, v2
	v_lshrrev_b32_e32 v2, 26, v2
	v_add_u32_e32 v2, v6, v2
	v_and_b32_e32 v2, 0xc0, v2
	v_sub_u32_e32 v2, v6, v2
	v_lshlrev_b32_e32 v3, 5, v3
	v_ashrrev_i16_sdwa v2, v168, sext(v2) dst_sel:DWORD dst_unused:UNUSED_PAD src0_sel:DWORD src1_sel:BYTE_0
	v_and_b32_e32 v3, 32, v3
	v_bfe_i32 v2, v2, 0, 16
	s_waitcnt lgkmcnt(0)
	v_min_u32_e32 v4, 0x3fff, v4
	v_add_lshl_u32 v2, v3, v2, 1
	s_mov_b32 s7, m0
	s_mov_b32 m0, s31
	s_nop 0
	global_load_lds_dwordx4 v171, s[10:11]
	s_mov_b32 m0, s7
	v_lshl_add_u32 v173, v4, 10, v2
	s_add_i32 s56, s31, 0x2000
	s_mov_b32 s7, m0
	s_mov_b32 m0, s56
	s_nop 0
	global_load_lds_dwordx4 v173, s[10:11]
	s_mov_b32 m0, s7
	v_min_u32_e32 v5, 0x3fff, v5
	s_add_i32 s57, s31, 0x4000
	s_mov_b32 s7, m0
	s_mov_b32 m0, s57
	s_nop 0
	global_load_lds_dwordx4 v164, s[10:11]
	s_mov_b32 m0, s7
	s_lshr_b32 s5, s4, 8
	v_lshl_add_u32 v166, v5, 10, v2
	s_add_i32 s63, s31, 0x6000
	s_mov_b32 s7, m0
	s_mov_b32 m0, s63
	s_nop 0
	global_load_lds_dwordx4 v166, s[10:11]
	s_mov_b32 m0, s7
	s_cmp_eq_u32 s5, 1
	v_writelane_b32 v253, s24, 33
	s_cselect_b64 s[14:15], -1, 0
	s_cmp_lg_u32 s5, 1
	v_writelane_b32 v253, s25, 34
	s_cbranch_scc1 .LBB0_1935
	s_barrier
.LBB0_1935:
	v_and_b32_e32 v169, 15, v0
	v_and_b32_e32 v2, 48, v0
	v_lshlrev_b32_e32 v4, 2, v0
	s_lshl_b32 s64, s5, 6
	v_lshl_or_b32 v3, v169, 6, v2
	s_lshl_b32 s5, s5, 13
	v_and_b32_e32 v4, 32, v4
	v_bitop3_b32 v3, v3, s5, v4 bitop3:0xde
	s_lshl_b32 s5, s30, 5
	s_and_b32 s65, s5, 0x60
	v_lshlrev_b32_e32 v5, 6, v0
	s_movk_i32 s5, 0x3c0
	v_and_or_b32 v2, v5, s5, v2
	s_lshl_b32 s5, s65, 7
	s_add_u32 s16, s38, 0x80
	v_bitop3_b32 v2, s5, v2, v4 bitop3:0xf6
	s_waitcnt vmcnt(2)
	s_barrier
	s_addc_u32 s17, s39, 0
	s_add_i32 s66, s31, 0x18000
	s_mov_b32 s5, m0
	s_mov_b32 m0, s66
	s_nop 0
	global_load_lds_dwordx4 v165, s[16:17]
	s_mov_b32 m0, s5
	s_add_i32 s67, s31, 0x1a000
	s_mov_b32 s5, m0
	s_mov_b32 m0, s67
	s_nop 0
	global_load_lds_dwordx4 v167, s[16:17]
	s_mov_b32 m0, s5
	s_add_u32 s16, s74, 0x1d800080
	s_addc_u32 s17, s75, 0
	s_add_i32 s68, s31, 0x8000
	s_mov_b32 s5, m0
	s_mov_b32 m0, s68
	s_nop 0
	global_load_lds_dwordx4 v171, s[16:17]
	s_mov_b32 m0, s5
	s_add_i32 s69, s31, 0xa000
	s_mov_b32 s5, m0
	s_mov_b32 m0, s69
	s_nop 0
	global_load_lds_dwordx4 v173, s[16:17]
	s_mov_b32 m0, s5
	s_add_u32 s16, s38, 0x20080
	s_addc_u32 s17, s39, 0
	s_add_i32 s76, s31, 0x1c000
	s_mov_b32 s5, m0
	s_mov_b32 m0, s76
	s_nop 0
	global_load_lds_dwordx4 v165, s[16:17]
	s_mov_b32 m0, s5
	s_add_i32 s77, s31, 0x1e000
	s_mov_b32 s5, m0
	s_mov_b32 m0, s77
	s_nop 0
	global_load_lds_dwordx4 v167, s[16:17]
	s_mov_b32 m0, s5
	s_add_i32 s78, s31, 0xc000
	s_waitcnt vmcnt(6)
	s_cmpk_lt_u32 s4, 0x100
	s_cselect_b64 s[16:17], -1, 0
	s_ashr_i32 s7, s6, 31
	v_lshrrev_b32_e32 v170, 4, v218
	s_mov_b32 s8, 0
	v_lshlrev_b32_e32 v172, 4, v218
	s_add_i32 s79, s31, 0xe000
	s_ashr_i32 s80, s90, 31
	s_ashr_i32 s81, s93, 31
	v_mov_b64_e32 v[162:163], s[6:7]
	s_add_i32 s7, 0, 0x201c0
	s_xor_b64 s[18:19], s[0:1], -1
	v_add_u32_e32 v174, 0, v2
	v_add_u32_e32 v175, 0, v3
	s_mov_b32 s82, 0xc0e00000
	s_mov_b32 s20, 0xc01d265f
	v_mov_b32_e32 v176, 0x40e00000
	s_barrier
	s_branch .LBB0_1938

.LBB0_1943:
	s_add_u32 s54, s38, 0x80
	s_addc_u32 s55, s39, 0
	v_add_u32_e32 v2, 0x10000, v174
	v_add_u32_e32 v14, 0x14000, v174
	s_add_u32 s38, s38, 0x100
	ds_read_b128 v[18:21], v2
	ds_read_b128 v[22:25], v2 offset:1024
	ds_read_b128 v[26:29], v2 offset:2048
	ds_read_b128 v[30:33], v2 offset:3072
	ds_read_b128 v[2:5], v14
	ds_read_b128 v[6:9], v14 offset:1024
	ds_read_b128 v[10:13], v14 offset:2048
	ds_read_b128 v[14:17], v14 offset:3072
	s_addc_u32 s39, s39, 0
	s_and_b64 s[40:41], s[40:41], exec
	s_cselect_b32 s52, s10, s38
	s_cselect_b32 s53, s11, s39
	s_cselect_b32 s41, s1, s87
	s_cselect_b32 s40, s0, s86
	s_add_u32 s42, s52, 0x80
	s_addc_u32 s43, s53, 0
	s_add_u32 s44, s40, 0x80
	s_addc_u32 s45, s41, 0
	ds_read_b128 v[180:183], v175
	ds_read_b128 v[184:187], v175 offset:1024
	ds_read_b128 v[188:191], v175 offset:2048
	ds_read_b128 v[192:195], v175 offset:3072
	ds_read_b128 v[196:199], v175 offset:4096
	ds_read_b128 v[200:203], v175 offset:5120
	ds_read_b128 v[204:207], v175 offset:6144
	ds_read_b128 v[208:211], v175 offset:7168
	s_mov_b32 s33, m0
	s_mov_b32 m0, s78
	s_nop 0
	global_load_lds_dwordx4 v164, s[54:55]
	s_mov_b32 m0, s33
	s_nop 0
	s_mov_b32 s33, m0
	s_mov_b32 m0, s79
	s_nop 0
	global_load_lds_dwordx4 v166, s[54:55]
	s_mov_b32 m0, s33
	s_waitcnt vmcnt(8)
	s_waitcnt lgkmcnt(0)
	s_barrier
	s_setprio 1
	s_waitcnt lgkmcnt(6)
	v_mfma_f32_16x16x128_f8f6f4 v[158:161], v[18:25], v[180:187], v[158:161]
	v_mfma_f32_16x16x128_f8f6f4 v[150:153], v[26:33], v[180:187], v[150:153]
	s_waitcnt lgkmcnt(4)
	v_mfma_f32_16x16x128_f8f6f4 v[142:145], v[18:25], v[188:195], v[142:145]
	v_mfma_f32_16x16x128_f8f6f4 v[134:137], v[26:33], v[188:195], v[134:137]
	s_waitcnt lgkmcnt(2)
	v_mfma_f32_16x16x128_f8f6f4 v[126:129], v[18:25], v[196:203], v[126:129]
	v_mfma_f32_16x16x128_f8f6f4 v[118:121], v[26:33], v[196:203], v[118:121]
	s_waitcnt lgkmcnt(0)
	v_mfma_f32_16x16x128_f8f6f4 v[110:113], v[18:25], v[204:211], v[110:113]
	v_mfma_f32_16x16x128_f8f6f4 v[102:105], v[26:33], v[204:211], v[102:105]
	s_setprio 0
	s_setprio 1
	v_mfma_f32_16x16x128_f8f6f4 v[154:157], v[2:9], v[180:187], v[154:157]
	v_mfma_f32_16x16x128_f8f6f4 v[146:149], v[10:17], v[180:187], v[146:149]
	v_mfma_f32_16x16x128_f8f6f4 v[138:141], v[2:9], v[188:195], v[138:141]
	v_mfma_f32_16x16x128_f8f6f4 v[130:133], v[10:17], v[188:195], v[130:133]
	v_mfma_f32_16x16x128_f8f6f4 v[122:125], v[2:9], v[196:203], v[122:125]
	v_mfma_f32_16x16x128_f8f6f4 v[114:117], v[10:17], v[196:203], v[114:117]
	v_mfma_f32_16x16x128_f8f6f4 v[106:109], v[2:9], v[204:211], v[106:109]
	v_mfma_f32_16x16x128_f8f6f4 v[98:101], v[10:17], v[204:211], v[98:101]
	s_setprio 0
	s_barrier
	ds_read_b128 v[180:183], v175 offset:16384
	ds_read_b128 v[184:187], v175 offset:17408
	ds_read_b128 v[188:191], v175 offset:18432
	ds_read_b128 v[192:195], v175 offset:19456
	ds_read_b128 v[196:199], v175 offset:20480
	ds_read_b128 v[200:203], v175 offset:21504
	ds_read_b128 v[204:207], v175 offset:22528
	ds_read_b128 v[208:211], v175 offset:23552
	s_mov_b32 s33, m0
	s_mov_b32 m0, s34
	s_nop 0
	global_load_lds_dwordx4 v165, s[40:41]
	s_mov_b32 m0, s33
	s_add_u32 s54, s40, 0x20000
	s_mov_b32 s33, m0
	s_mov_b32 m0, s35
	s_nop 0
	global_load_lds_dwordx4 v167, s[40:41]
	s_mov_b32 m0, s33
	s_addc_u32 s55, s41, 0
	s_mov_b32 s33, m0
	s_mov_b32 m0, s36
	s_nop 0
	global_load_lds_dwordx4 v165, s[54:55]
	s_mov_b32 m0, s33
	s_nop 0
	s_mov_b32 s33, m0
	s_mov_b32 m0, s37
	s_nop 0
	global_load_lds_dwordx4 v167, s[54:55]
	s_mov_b32 m0, s33
	s_nop 0
	s_mov_b32 s33, m0
	s_mov_b32 m0, s31
	s_nop 0
	global_load_lds_dwordx4 v171, s[52:53]
	s_mov_b32 m0, s33
	s_nop 0
	s_mov_b32 s33, m0
	s_mov_b32 m0, s56
	s_nop 0
	global_load_lds_dwordx4 v173, s[52:53]
	s_mov_b32 m0, s33
	s_waitcnt vmcnt(8)
	s_waitcnt lgkmcnt(0)
	s_barrier
	s_setprio 1
	s_waitcnt lgkmcnt(6)
	v_mfma_f32_16x16x128_f8f6f4 v[94:97], v[18:25], v[180:187], v[94:97]
	v_mfma_f32_16x16x128_f8f6f4 v[86:89], v[26:33], v[180:187], v[86:89]
	s_waitcnt lgkmcnt(4)
	v_mfma_f32_16x16x128_f8f6f4 v[78:81], v[18:25], v[188:195], v[78:81]
	v_mfma_f32_16x16x128_f8f6f4 v[70:73], v[26:33], v[188:195], v[70:73]
	s_waitcnt lgkmcnt(2)
	v_mfma_f32_16x16x128_f8f6f4 v[62:65], v[18:25], v[196:203], v[62:65]
	v_mfma_f32_16x16x128_f8f6f4 v[54:57], v[26:33], v[196:203], v[54:57]
	s_waitcnt lgkmcnt(0)
	v_mfma_f32_16x16x128_f8f6f4 v[46:49], v[18:25], v[204:211], v[46:49]
	v_mfma_f32_16x16x128_f8f6f4 v[38:41], v[26:33], v[204:211], v[38:41]
	s_setprio 0
	s_setprio 1
	v_mfma_f32_16x16x128_f8f6f4 v[90:93], v[2:9], v[180:187], v[90:93]
	v_mfma_f32_16x16x128_f8f6f4 v[82:85], v[10:17], v[180:187], v[82:85]
	v_mfma_f32_16x16x128_f8f6f4 v[74:77], v[2:9], v[188:195], v[74:77]
	v_mfma_f32_16x16x128_f8f6f4 v[66:69], v[10:17], v[188:195], v[66:69]
	v_mfma_f32_16x16x128_f8f6f4 v[58:61], v[2:9], v[196:203], v[58:61]
	v_mfma_f32_16x16x128_f8f6f4 v[50:53], v[10:17], v[196:203], v[50:53]
	v_mfma_f32_16x16x128_f8f6f4 v[42:45], v[2:9], v[204:211], v[42:45]
	v_mfma_f32_16x16x128_f8f6f4 v[34:37], v[10:17], v[204:211], v[34:37]
	s_setprio 0
	s_barrier
	v_add_u32_e32 v14, 0x18000, v174
	v_add_u32_e32 v30, 0x1c000, v174
	ds_read_b128 v[2:5], v14
	ds_read_b128 v[6:9], v14 offset:1024
	ds_read_b128 v[10:13], v14 offset:2048
	ds_read_b128 v[14:17], v14 offset:3072
	ds_read_b128 v[18:21], v30
	ds_read_b128 v[22:25], v30 offset:1024
	ds_read_b128 v[26:29], v30 offset:2048
	ds_read_b128 v[30:33], v30 offset:3072
	ds_read_b128 v[180:183], v175 offset:32768
	ds_read_b128 v[184:187], v175 offset:33792
	ds_read_b128 v[188:191], v175 offset:34816
	ds_read_b128 v[192:195], v175 offset:35840
	ds_read_b128 v[196:199], v175 offset:36864
	ds_read_b128 v[200:203], v175 offset:37888
	ds_read_b128 v[204:207], v175 offset:38912
	ds_read_b128 v[208:211], v175 offset:39936
	s_mov_b32 s33, m0
	s_mov_b32 m0, s57
	s_nop 0
	global_load_lds_dwordx4 v177, s[52:53]
	s_mov_b32 m0, s33
	s_nop 0
	s_mov_b32 s33, m0
	s_mov_b32 m0, s63
	s_nop 0
	global_load_lds_dwordx4 v178, s[52:53]
	s_mov_b32 m0, s33
	s_waitcnt vmcnt(8)
	s_waitcnt lgkmcnt(0)
	s_barrier
	s_setprio 1
	s_waitcnt lgkmcnt(6)
	v_mfma_f32_16x16x128_f8f6f4 v[158:161], v[2:9], v[180:187], v[158:161]
	v_mfma_f32_16x16x128_f8f6f4 v[150:153], v[10:17], v[180:187], v[150:153]
	s_waitcnt lgkmcnt(4)
	v_mfma_f32_16x16x128_f8f6f4 v[142:145], v[2:9], v[188:195], v[142:145]
	v_mfma_f32_16x16x128_f8f6f4 v[134:137], v[10:17], v[188:195], v[134:137]
	s_waitcnt lgkmcnt(2)
	v_mfma_f32_16x16x128_f8f6f4 v[126:129], v[2:9], v[196:203], v[126:129]
	v_mfma_f32_16x16x128_f8f6f4 v[118:121], v[10:17], v[196:203], v[118:121]
	s_waitcnt lgkmcnt(0)
	v_mfma_f32_16x16x128_f8f6f4 v[110:113], v[2:9], v[204:211], v[110:113]
	v_mfma_f32_16x16x128_f8f6f4 v[102:105], v[10:17], v[204:211], v[102:105]
	s_setprio 0
	s_setprio 1
	v_mfma_f32_16x16x128_f8f6f4 v[154:157], v[18:25], v[180:187], v[154:157]
	v_mfma_f32_16x16x128_f8f6f4 v[146:149], v[26:33], v[180:187], v[146:149]
	v_mfma_f32_16x16x128_f8f6f4 v[138:141], v[18:25], v[188:195], v[138:141]
	v_mfma_f32_16x16x128_f8f6f4 v[130:133], v[26:33], v[188:195], v[130:133]
	v_mfma_f32_16x16x128_f8f6f4 v[122:125], v[18:25], v[196:203], v[122:125]
	v_mfma_f32_16x16x128_f8f6f4 v[114:117], v[26:33], v[196:203], v[114:117]
	v_mfma_f32_16x16x128_f8f6f4 v[106:109], v[18:25], v[204:211], v[106:109]
	v_mfma_f32_16x16x128_f8f6f4 v[98:101], v[26:33], v[204:211], v[98:101]
	s_setprio 0
	s_barrier
	ds_read_b128 v[180:183], v175 offset:49152
	ds_read_b128 v[184:187], v175 offset:50176
	ds_read_b128 v[188:191], v175 offset:51200
	ds_read_b128 v[192:195], v175 offset:52224
	ds_read_b128 v[196:199], v175 offset:53248
	ds_read_b128 v[200:203], v175 offset:54272
	ds_read_b128 v[204:207], v175 offset:55296
	ds_read_b128 v[208:211], v175 offset:56320
	s_mov_b32 s33, m0
	s_mov_b32 m0, s66
	s_nop 0
	global_load_lds_dwordx4 v165, s[44:45]
	s_mov_b32 m0, s33
	s_add_u32 s40, s40, 0x20080
	s_mov_b32 s33, m0
	s_mov_b32 m0, s67
	s_nop 0
	global_load_lds_dwordx4 v167, s[44:45]
	s_mov_b32 m0, s33
	s_addc_u32 s41, s41, 0
	s_mov_b32 s33, m0
	s_mov_b32 m0, s76
	s_nop 0
	global_load_lds_dwordx4 v165, s[40:41]
	s_mov_b32 m0, s33
	s_nop 0
	s_mov_b32 s33, m0
	s_mov_b32 m0, s77
	s_nop 0
	global_load_lds_dwordx4 v167, s[40:41]
	s_mov_b32 m0, s33
	s_nop 0
	s_mov_b32 s33, m0
	s_mov_b32 m0, s68
	s_nop 0
	global_load_lds_dwordx4 v171, s[42:43]
	s_mov_b32 m0, s33
	s_nop 0
	s_mov_b32 s33, m0
	s_mov_b32 m0, s69
	s_nop 0
	global_load_lds_dwordx4 v173, s[42:43]
	s_mov_b32 m0, s33
	s_waitcnt vmcnt(8)
	s_waitcnt lgkmcnt(0)
	s_barrier
	s_setprio 1
	s_waitcnt lgkmcnt(6)
	v_mfma_f32_16x16x128_f8f6f4 v[94:97], v[2:9], v[180:187], v[94:97]
	v_mfma_f32_16x16x128_f8f6f4 v[86:89], v[10:17], v[180:187], v[86:89]
	s_waitcnt lgkmcnt(4)
	v_mfma_f32_16x16x128_f8f6f4 v[78:81], v[2:9], v[188:195], v[78:81]
	v_mfma_f32_16x16x128_f8f6f4 v[70:73], v[10:17], v[188:195], v[70:73]
	s_waitcnt lgkmcnt(2)
	v_mfma_f32_16x16x128_f8f6f4 v[62:65], v[2:9], v[196:203], v[62:65]
	v_mfma_f32_16x16x128_f8f6f4 v[54:57], v[10:17], v[196:203], v[54:57]
	s_waitcnt lgkmcnt(0)
	v_mfma_f32_16x16x128_f8f6f4 v[46:49], v[2:9], v[204:211], v[46:49]
	v_mfma_f32_16x16x128_f8f6f4 v[38:41], v[10:17], v[204:211], v[38:41]
	s_setprio 0
	s_setprio 1
	v_mfma_f32_16x16x128_f8f6f4 v[90:93], v[18:25], v[180:187], v[90:93]
	v_mfma_f32_16x16x128_f8f6f4 v[82:85], v[26:33], v[180:187], v[82:85]
	v_mfma_f32_16x16x128_f8f6f4 v[74:77], v[18:25], v[188:195], v[74:77]
	v_mfma_f32_16x16x128_f8f6f4 v[66:69], v[26:33], v[188:195], v[66:69]
	v_mfma_f32_16x16x128_f8f6f4 v[58:61], v[18:25], v[196:203], v[58:61]
	v_mfma_f32_16x16x128_f8f6f4 v[50:53], v[26:33], v[196:203], v[50:53]
	v_mfma_f32_16x16x128_f8f6f4 v[42:45], v[18:25], v[204:211], v[42:45]
	v_mfma_f32_16x16x128_f8f6f4 v[34:37], v[26:33], v[204:211], v[34:37]
	s_setprio 0
	s_barrier
	s_add_i32 s88, s88, 2
	s_add_u32 s86, s86, 0x100
	s_addc_u32 s87, s87, 0
	s_cmp_gt_u32 s88, 5
	s_cbranch_scc1 .LBB0_1957
.LBB0_1944:
	s_cmp_eq_u32 s88, 4
	s_cselect_b64 s[40:41], -1, 0
	s_and_b64 vcc, exec, s[4:5]
	s_cbranch_vccnz .LBB0_1949
	s_cmp_lg_u32 s88, -2
	s_cselect_b64 s[42:43], -1, 0
	s_or_b64 s[42:43], s[18:19], s[42:43]
	s_and_b64 vcc, exec, s[42:43]
	s_cbranch_vccnz .LBB0_1947
	v_mov_b32_e32 v2, s29
	ds_read_b32 v2, v2 offset:288
	s_waitcnt lgkmcnt(0)
	v_readfirstlane_b32 s33, v2
	s_lshl_b32 s42, s33, 2
	s_add_i32 s42, s42, 0
	s_add_i32 s42, s42, 0x20240
	v_mov_b32_e32 v2, s42
	ds_read_b32 v2, v2
	s_lshl_b32 s42, s33, 14
	s_ashr_i32 s43, s42, 31
	s_lshl_b64 s[42:43], s[42:43], 2
	s_waitcnt lgkmcnt(0)
	v_readfirstlane_b32 s33, v2
	s_sub_i32 s33, s84, s33
	s_lshl_b32 s44, s33, 8
	s_add_u32 s33, s58, s42
	s_addc_u32 s52, s59, s43
	s_ashr_i32 s45, s44, 31
	s_lshl_b64 s[42:43], s[44:45], 2
	s_add_u32 s42, s33, s42
	s_addc_u32 s43, s52, s43
	s_mov_b32 s33, m0
	s_mov_b32 m0, s23
	s_nop 0
	global_load_lds_dwordx4 v172, s[42:43]
	s_mov_b32 m0, s33

.LBB0_1949:
	s_cmp_lg_u32 s88, -2
	s_cbranch_scc1 .LBB0_1943
	v_mov_b32_e32 v2, s25
	ds_read_b32 v2, v2 offset:288
	s_mov_b64 s[44:45], -1
	s_waitcnt lgkmcnt(0)
	v_readfirstlane_b32 s42, v2
	s_lshl_b32 s33, s42, 2
	s_add_i32 s33, s33, 0
	s_add_i32 s33, s33, 0x20240
	v_mov_b32_e32 v2, s33
	ds_read_b32 v2, v2
	s_cmp_lt_i32 s30, 2
	s_waitcnt lgkmcnt(0)
	v_readfirstlane_b32 s33, v2
	s_cbranch_scc1 .LBB0_1954
	s_cmp_eq_u32 s30, 2
	s_cbranch_scc0 .LBB0_1953
	s_lshl_b32 s52, s42, 14
	s_sub_i32 s33, s2, s33
	s_ashr_i32 s53, s52, 31
	s_lshl_b32 s44, s33, 8
	s_lshl_b64 s[52:53], s[52:53], 2
	s_add_u32 s33, s60, s52
	s_addc_u32 s43, s61, s53
	s_ashr_i32 s45, s44, 31
	s_lshl_b64 s[44:45], s[44:45], 2
	s_add_u32 s44, s33, s44
	s_addc_u32 s45, s43, s45
	s_mov_b32 s33, m0
	s_mov_b32 m0, s28
	s_nop 0
	global_load_lds_dwordx4 v172, s[44:45]
	s_mov_b32 m0, s33

.LBB0_1954:
	s_andn2_b64 vcc, exec, s[44:45]
	s_mov_b32 s85, s24
	s_cbranch_vccnz .LBB0_1943
	s_cmp_lg_u32 s30, 1
	s_mov_b32 s85, s24
	s_cbranch_scc1 .LBB0_1943
	s_ashr_i32 s43, s42, 31
	s_lshl_b64 s[42:43], s[42:43], 13
	s_add_u32 s42, s8, s42
	s_addc_u32 s43, s9, s43
	s_mov_b32 s33, m0
	s_mov_b32 m0, s27
	s_nop 0
	global_load_lds_dwordx4 v172, s[42:43]
	s_mov_b32 m0, s33
	s_mov_b32 s85, s24
	s_branch .LBB0_1943

.LBB0_2037:
	s_and_b64 vcc, exec, s[0:1]
	s_cbranch_vccnz .LBB0_2100
	s_add_u32 s60, s74, 0x20000
	s_addc_u32 s61, s75, 0
	s_lshl_b32 s1, s22, 2
	s_add_i32 s1, s1, 0
	s_add_i32 s1, s1, 0x202e0
	s_waitcnt vmcnt(1)
	v_mov_b32_e32 v7, s1
	ds_read_b32 v7, v7
	v_lshlrev_b32_e32 v1, 4, v0
	s_waitcnt vmcnt(0)
	v_and_b32_e32 v2, 32, v0
	v_bitop3_b32 v1, v1, v2, 48 bitop3:0x6c
	v_lshrrev_b32_e32 v2, 1, v0
	v_bfe_u32 v3, v0, 2, 2
	v_lshrrev_b32_e32 v4, 3, v0
	s_movk_i32 s0, 0x78
	v_and_or_b32 v5, v2, 24, v3
	v_and_b32_e32 v3, 56, v4
	v_lshrrev_b32_e32 v6, 5, v0
	v_bitop3_b32 v4, v4, s0, 64 bitop3:0xc8
	v_and_or_b32 v2, v0, 64, v1
	v_or_b32_e32 v1, v6, v3
	v_or_b32_e32 v6, v6, v4
	s_movk_i32 s0, 0x64
	v_and_or_b32 v1, v1, 36, v5
	v_and_or_b32 v5, v6, s0, v5
	s_waitcnt lgkmcnt(0)
	v_readfirstlane_b32 s0, v7
	s_lshr_b32 s62, s21, 6
	s_ashr_i32 s1, s0, 31
	s_ashr_i32 s39, s38, 31
	s_lshl_b32 s2, s62, 10
	s_lshl_b64 s[4:5], s[38:39], 18
	s_lshl_b64 s[0:1], s[0:1], 20
	s_add_u32 s0, s35, s0
	s_addc_u32 s1, s54, s1
	s_add_u32 s26, s0, s4
	s_addc_u32 s27, s1, s5
	s_add_i32 s63, s2, 0
	v_lshl_or_b32 v1, v1, 10, v2
	s_add_i32 s64, s63, 0x10000
	s_mov_b32 s0, m0
	s_mov_b32 m0, s64
	s_nop 0
	global_load_lds_dwordx4 v1, s[26:27]
	s_mov_b32 m0, s0
	v_lshl_or_b32 v162, v5, 10, v2
	s_add_i32 s65, s63, 0x12000
	s_mov_b32 s0, m0
	s_mov_b32 m0, s65
	s_nop 0
	global_load_lds_dwordx4 v162, s[26:27]
	s_mov_b32 m0, s0
	s_add_u32 s0, s26, 0x20000
	s_addc_u32 s1, s27, 0
	s_add_i32 s24, s63, 0x14000
	s_mov_b32 s2, m0
	s_mov_b32 m0, s24
	s_nop 0
	global_load_lds_dwordx4 v1, s[0:1]
	s_mov_b32 m0, s2
	s_add_i32 s25, s63, 0x16000
	s_mov_b32 s2, m0
	s_mov_b32 m0, s25
	s_nop 0
	global_load_lds_dwordx4 v162, s[0:1]
	s_mov_b32 m0, s2
	v_cmp_lt_u32_e64 s[0:1], 63, v0
	v_cmp_gt_u32_e64 s[4:5], 64, v0
	s_and_saveexec_b64 s[8:9], s[4:5]
	s_cbranch_execz .LBB0_2053
	s_lshl_b32 s12, s22, 6
	s_ashr_i32 s13, s12, 31
	s_lshl_b64 s[12:13], s[12:13], 2
	s_add_u32 s12, s60, s12
	s_addc_u32 s13, s61, s13
	s_mov_b32 s2, 1
	v_mov_b32_e32 v5, 0
	s_branch .LBB0_2041

.LBB0_2053:
	s_or_b64 exec, exec, s[8:9]
	v_lshrrev_b32_e32 v5, 2, v0
	s_ashr_i32 s23, s22, 31
	s_lshl_b64 s[8:9], s[22:23], 18
	v_and_b32_e32 v5, 15, v5
	s_add_u32 s36, s3, s8
	v_and_or_b32 v3, v3, 48, v5
	s_movk_i32 s2, 0x70
	s_barrier
	s_addc_u32 s37, s34, s9
	v_lshl_or_b32 v163, v3, 10, v2
	v_and_or_b32 v3, v4, s2, v5
	s_mov_b32 s2, m0
	s_mov_b32 m0, s63
	s_nop 0
	global_load_lds_dwordx4 v163, s[36:37]
	s_mov_b32 m0, s2
	s_lshr_b32 s12, s21, 8
	s_add_i32 s2, s63, 0x2000
	v_lshl_or_b32 v164, v3, 10, v2
	s_mov_b32 s8, m0
	s_mov_b32 m0, s2
	s_nop 0
	global_load_lds_dwordx4 v164, s[36:37]
	s_mov_b32 m0, s8
	s_add_u32 s14, s36, 0x20000
	s_addc_u32 s15, s37, 0
	s_add_i32 s23, s63, 0x4000
	s_mov_b32 s8, m0
	s_mov_b32 m0, s23
	s_nop 0
	global_load_lds_dwordx4 v163, s[14:15]
	s_mov_b32 m0, s8
	s_add_i32 s28, s63, 0x6000
	s_mov_b32 s13, m0
	s_mov_b32 m0, s28
	s_nop 0
	global_load_lds_dwordx4 v164, s[14:15]
	s_mov_b32 m0, s13
	s_cmp_eq_u32 s12, 1
	s_mov_b32 s33, 0
	s_cselect_b64 s[8:9], -1, 0
	s_cmp_lg_u32 s12, 1
	s_cbranch_scc1 .LBB0_2055
	s_barrier
.LBB0_2055:
	v_and_b32_e32 v165, 15, v0
	v_and_b32_e32 v2, 48, v0
	v_lshlrev_b32_e32 v4, 2, v0
	s_lshl_b32 s29, s12, 6
	v_lshl_or_b32 v3, v165, 6, v2
	s_lshl_b32 s12, s12, 13
	v_and_b32_e32 v4, 32, v4
	v_bitop3_b32 v3, v3, s12, v4 bitop3:0xde
	s_lshl_b32 s12, s62, 5
	s_and_b32 s66, s12, 0x60
	v_lshlrev_b32_e32 v5, 6, v0
	s_movk_i32 s12, 0x3c0
	v_and_or_b32 v2, v5, s12, v2
	s_lshl_b32 s12, s66, 7
	v_bitop3_b32 v2, s12, v2, v4 bitop3:0xf6
	s_add_u32 s12, s26, 0x80
	s_waitcnt vmcnt(2)
	s_barrier
	s_addc_u32 s13, s27, 0
	s_add_i32 s67, s63, 0x18000
	s_mov_b32 s14, m0
	s_mov_b32 m0, s67
	s_nop 0
	global_load_lds_dwordx4 v1, s[12:13]
	s_mov_b32 m0, s14
	s_add_i32 s68, s63, 0x1a000
	s_mov_b32 s14, m0
	s_mov_b32 m0, s68
	s_nop 0
	global_load_lds_dwordx4 v162, s[12:13]
	s_mov_b32 m0, s14
	s_add_u32 s12, s36, 0x80
	s_addc_u32 s13, s37, 0
	s_add_i32 s69, s63, 0x8000
	s_mov_b32 s14, m0
	s_mov_b32 m0, s69
	s_nop 0
	global_load_lds_dwordx4 v163, s[12:13]
	s_mov_b32 m0, s14
	s_add_i32 s76, s63, 0xa000
	s_mov_b32 s14, m0
	s_mov_b32 m0, s76
	s_nop 0
	global_load_lds_dwordx4 v164, s[12:13]
	s_mov_b32 m0, s14
	s_add_u32 s12, s26, 0x20080
	s_addc_u32 s13, s27, 0
	s_add_i32 s77, s63, 0x1c000
	s_mov_b32 s14, m0
	s_mov_b32 m0, s77
	s_nop 0
	global_load_lds_dwordx4 v1, s[12:13]
	s_mov_b32 m0, s14
	s_add_i32 s78, s63, 0x1e000
	s_add_i32 s79, s63, 0xc000
	s_mov_b32 s14, m0
	s_mov_b32 m0, s78
	s_nop 0
	global_load_lds_dwordx4 v162, s[12:13]
	s_mov_b32 m0, s14
	s_cmpk_lt_u32 s21, 0x100
	s_waitcnt vmcnt(6)
	s_cselect_b64 s[12:13], -1, 0
	s_add_i32 s80, s63, 0xe000
	s_lshr_b32 s14, s20, 5
	s_and_b64 s[6:7], s[6:7], exec
	v_lshrrev_b32_e32 v166, 4, v218
	v_lshlrev_b32_e32 v167, 4, v218
	s_cselect_b32 s81, s14, 0
	s_and_b32 s82, s59, 15
	v_mov_b32_e32 v168, 0
	v_mov_b32_e32 v169, 0
	v_mov_b32_e32 v170, 1
	v_add_u32_e32 v171, 0, v2
	v_add_u32_e32 v172, 0, v3
	s_mov_b32 s83, 0xc3e00000
	v_mov_b32_e32 v173, 0x43e00000
	v_mov_b32_e32 v174, 0
	s_barrier
	s_branch .LBB0_2058

.LBB0_2084:
	s_cmp_lg_u32 s91, 0
	s_cbranch_scc1 .LBB0_2092
	v_mov_b32_e32 v2, s39
	ds_read_b32 v2, v2 offset:288
	s_mov_b64 s[46:47], -1
	s_waitcnt lgkmcnt(0)
	v_readfirstlane_b32 s44, v2
	s_lshl_b32 s33, s44, 2
	s_add_i32 s33, s33, 0
	s_add_i32 s33, s33, 0x20240
	v_mov_b32_e32 v2, s33
	ds_read_b32 v2, v2
	s_cmp_lt_i32 s62, 2
	s_waitcnt lgkmcnt(0)
	v_readfirstlane_b32 s33, v2
	s_cbranch_scc1 .LBB0_2089
	s_cmp_eq_u32 s62, 2
	s_cbranch_scc0 .LBB0_2088
	s_lshl_b32 s48, s44, 14
	s_sub_i32 s33, s22, s33
	s_ashr_i32 s49, s48, 31
	s_lshl_b32 s46, s33, 8
	s_lshl_b64 s[48:49], s[48:49], 2
	s_add_u32 s33, s55, s48
	s_addc_u32 s45, s56, s49
	s_ashr_i32 s47, s46, 31
	s_lshl_b64 s[46:47], s[46:47], 2
	s_add_u32 s46, s33, s46
	s_addc_u32 s47, s45, s47
	s_mov_b32 s33, m0
	s_mov_b32 m0, s88
	s_nop 0
	global_load_lds_dwordx4 v167, s[46:47]
	s_mov_b32 m0, s33

.LBB0_2089:
	s_andn2_b64 vcc, exec, s[46:47]
	s_mov_b32 s85, s86
	s_cbranch_vccnz .LBB0_2092
	s_cmp_lg_u32 s62, 1
	s_mov_b32 s85, s86
	s_cbranch_scc1 .LBB0_2092
	s_ashr_i32 s45, s44, 31
	s_lshl_b64 s[44:45], s[44:45], 12
	s_add_u32 s44, s89, s44
	s_addc_u32 s45, s90, s45
	s_mov_b32 s33, m0
	s_mov_b32 m0, s87
	s_nop 0
	global_load_lds_dwordx4 v167, s[44:45]
	s_mov_b32 m0, s33
	s_mov_b32 s85, s86
.LBB0_2092:
	s_cmp_eq_u32 s91, 0
	s_cbranch_scc1 .Lpeel7
	s_lshl_b32 s33, s91, 7
	s_add_u32 s52, s36, s33
	s_addc_u32 s53, s37, 0
	s_add_u32 s46, s52, 0x100
	s_addc_u32 s47, s53, 0
	s_and_b64 s[44:45], s[42:43], exec
	s_cselect_b32 s49, s15, s47
	s_cselect_b32 s48, s17, s46
	s_add_u32 s33, s26, s33
	v_add_u32_e32 v2, 0x10000, v171
	v_add_u32_e32 v14, 0x14000, v171
	s_addc_u32 s44, s27, 0
	ds_read_b128 v[18:21], v2
	ds_read_b128 v[22:25], v2 offset:1024
	ds_read_b128 v[26:29], v2 offset:2048
	ds_read_b128 v[30:33], v2 offset:3072
	ds_read_b128 v[2:5], v14
	ds_read_b128 v[6:9], v14 offset:1024
	ds_read_b128 v[10:13], v14 offset:2048
	ds_read_b128 v[14:17], v14 offset:3072
	s_add_u32 s33, s33, 0x100
	s_addc_u32 s44, s44, 0
	s_and_b64 s[42:43], s[42:43], exec
	s_cselect_b32 s43, s19, s44
	s_cselect_b32 s42, s18, s33
	s_add_u32 s44, s48, 0x80
	s_addc_u32 s45, s49, 0
	s_add_u32 s46, s42, 0x80
	s_addc_u32 s47, s43, 0
	ds_read_b128 v[176:179], v172
	ds_read_b128 v[180:183], v172 offset:1024
	ds_read_b128 v[184:187], v172 offset:2048
	ds_read_b128 v[188:191], v172 offset:3072
	ds_read_b128 v[192:195], v172 offset:4096
	ds_read_b128 v[196:199], v172 offset:5120
	ds_read_b128 v[200:203], v172 offset:6144
	ds_read_b128 v[204:207], v172 offset:7168
	s_add_u32 s52, s52, 0x20080
	s_addc_u32 s53, s53, 0
	s_mov_b32 s33, m0
	s_mov_b32 m0, s79
	s_nop 0
	global_load_lds_dwordx4 v163, s[52:53]
	s_mov_b32 m0, s33
	s_nop 0
	s_mov_b32 s33, m0
	s_mov_b32 m0, s80
	s_nop 0
	global_load_lds_dwordx4 v164, s[52:53]
	s_mov_b32 m0, s33
	s_waitcnt vmcnt(8)
	s_waitcnt lgkmcnt(0)
	s_barrier
	s_setprio 1
	s_waitcnt lgkmcnt(6)
	v_mfma_f32_16x16x128_f8f6f4 v[158:161], v[18:25], v[176:183], v[158:161]
	v_mfma_f32_16x16x128_f8f6f4 v[154:157], v[26:33], v[176:183], v[154:157]
	s_waitcnt lgkmcnt(4)
	v_mfma_f32_16x16x128_f8f6f4 v[142:145], v[18:25], v[184:191], v[142:145]
	v_mfma_f32_16x16x128_f8f6f4 v[138:141], v[26:33], v[184:191], v[138:141]
	s_waitcnt lgkmcnt(2)
	v_mfma_f32_16x16x128_f8f6f4 v[126:129], v[18:25], v[192:199], v[126:129]
	v_mfma_f32_16x16x128_f8f6f4 v[122:125], v[26:33], v[192:199], v[122:125]
	s_waitcnt lgkmcnt(0)
	v_mfma_f32_16x16x128_f8f6f4 v[110:113], v[18:25], v[200:207], v[110:113]
	v_mfma_f32_16x16x128_f8f6f4 v[106:109], v[26:33], v[200:207], v[106:109]
	s_setprio 0
	s_setprio 1
	v_mfma_f32_16x16x128_f8f6f4 v[150:153], v[2:9], v[176:183], v[150:153]
	v_mfma_f32_16x16x128_f8f6f4 v[146:149], v[10:17], v[176:183], v[146:149]
	v_mfma_f32_16x16x128_f8f6f4 v[134:137], v[2:9], v[184:191], v[134:137]
	v_mfma_f32_16x16x128_f8f6f4 v[130:133], v[10:17], v[184:191], v[130:133]
	v_mfma_f32_16x16x128_f8f6f4 v[118:121], v[2:9], v[192:199], v[118:121]
	v_mfma_f32_16x16x128_f8f6f4 v[114:117], v[10:17], v[192:199], v[114:117]
	v_mfma_f32_16x16x128_f8f6f4 v[102:105], v[2:9], v[200:207], v[102:105]
	v_mfma_f32_16x16x128_f8f6f4 v[98:101], v[10:17], v[200:207], v[98:101]
	s_setprio 0
	s_barrier
	ds_read_b128 v[176:179], v172 offset:16384
	ds_read_b128 v[180:183], v172 offset:17408
	ds_read_b128 v[184:187], v172 offset:18432
	ds_read_b128 v[188:191], v172 offset:19456
	ds_read_b128 v[192:195], v172 offset:20480
	ds_read_b128 v[196:199], v172 offset:21504
	ds_read_b128 v[200:203], v172 offset:22528
	ds_read_b128 v[204:207], v172 offset:23552
	s_mov_b32 s33, m0
	s_mov_b32 m0, s64
	s_nop 0
	global_load_lds_dwordx4 v1, s[42:43]
	s_mov_b32 m0, s33
	s_add_u32 s52, s42, 0x20000
	s_mov_b32 s33, m0
	s_mov_b32 m0, s65
	s_nop 0
	global_load_lds_dwordx4 v162, s[42:43]
	s_mov_b32 m0, s33
	s_addc_u32 s53, s43, 0
	s_mov_b32 s33, m0
	s_mov_b32 m0, s24
	s_nop 0
	global_load_lds_dwordx4 v1, s[52:53]
	s_mov_b32 m0, s33
	s_nop 0
	s_mov_b32 s33, m0
	s_mov_b32 m0, s25
	s_nop 0
	global_load_lds_dwordx4 v162, s[52:53]
	s_mov_b32 m0, s33
	s_nop 0
	s_mov_b32 s33, m0
	s_mov_b32 m0, s63
	s_nop 0
	global_load_lds_dwordx4 v163, s[48:49]
	s_mov_b32 m0, s33
	s_nop 0
	s_mov_b32 s33, m0
	s_mov_b32 m0, s2
	s_nop 0
	global_load_lds_dwordx4 v164, s[48:49]
	s_mov_b32 m0, s33
	s_waitcnt vmcnt(8)
	s_waitcnt lgkmcnt(0)
	s_barrier
	s_setprio 1
	s_waitcnt lgkmcnt(6)
	v_mfma_f32_16x16x128_f8f6f4 v[94:97], v[18:25], v[176:183], v[94:97]
	v_mfma_f32_16x16x128_f8f6f4 v[90:93], v[26:33], v[176:183], v[90:93]
	s_waitcnt lgkmcnt(4)
	v_mfma_f32_16x16x128_f8f6f4 v[78:81], v[18:25], v[184:191], v[78:81]
	v_mfma_f32_16x16x128_f8f6f4 v[74:77], v[26:33], v[184:191], v[74:77]
	s_waitcnt lgkmcnt(2)
	v_mfma_f32_16x16x128_f8f6f4 v[62:65], v[18:25], v[192:199], v[62:65]
	v_mfma_f32_16x16x128_f8f6f4 v[58:61], v[26:33], v[192:199], v[58:61]
	s_waitcnt lgkmcnt(0)
	v_mfma_f32_16x16x128_f8f6f4 v[46:49], v[18:25], v[200:207], v[46:49]
	v_mfma_f32_16x16x128_f8f6f4 v[42:45], v[26:33], v[200:207], v[42:45]
	s_setprio 0
	s_setprio 1
	v_mfma_f32_16x16x128_f8f6f4 v[86:89], v[2:9], v[176:183], v[86:89]
	v_mfma_f32_16x16x128_f8f6f4 v[82:85], v[10:17], v[176:183], v[82:85]
	v_mfma_f32_16x16x128_f8f6f4 v[70:73], v[2:9], v[184:191], v[70:73]
	v_mfma_f32_16x16x128_f8f6f4 v[66:69], v[10:17], v[184:191], v[66:69]
	v_mfma_f32_16x16x128_f8f6f4 v[54:57], v[2:9], v[192:199], v[54:57]
	v_mfma_f32_16x16x128_f8f6f4 v[50:53], v[10:17], v[192:199], v[50:53]
	v_mfma_f32_16x16x128_f8f6f4 v[38:41], v[2:9], v[200:207], v[38:41]
	v_mfma_f32_16x16x128_f8f6f4 v[34:37], v[10:17], v[200:207], v[34:37]
	s_setprio 0
	s_barrier
.Lmid7:
	v_add_u32_e32 v14, 0x18000, v171
	v_add_u32_e32 v30, 0x1c000, v171
	ds_read_b128 v[2:5], v14
	ds_read_b128 v[6:9], v14 offset:1024
	ds_read_b128 v[10:13], v14 offset:2048
	ds_read_b128 v[14:17], v14 offset:3072
	ds_read_b128 v[18:21], v30
	ds_read_b128 v[22:25], v30 offset:1024
	ds_read_b128 v[26:29], v30 offset:2048
	ds_read_b128 v[30:33], v30 offset:3072
	ds_read_b128 v[176:179], v172 offset:32768
	ds_read_b128 v[180:183], v172 offset:33792
	ds_read_b128 v[184:187], v172 offset:34816
	ds_read_b128 v[188:191], v172 offset:35840
	ds_read_b128 v[192:195], v172 offset:36864
	ds_read_b128 v[196:199], v172 offset:37888
	ds_read_b128 v[200:203], v172 offset:38912
	ds_read_b128 v[204:207], v172 offset:39936
	s_add_u32 s48, s48, 0x20000
	s_addc_u32 s49, s49, 0
	s_mov_b32 s33, m0
	s_mov_b32 m0, s23
	s_nop 0
	global_load_lds_dwordx4 v163, s[48:49]
	s_mov_b32 m0, s33
	s_nop 0
	s_mov_b32 s33, m0
	s_mov_b32 m0, s28
	s_nop 0
	global_load_lds_dwordx4 v164, s[48:49]
	s_mov_b32 m0, s33
	s_waitcnt vmcnt(8)
	s_waitcnt lgkmcnt(0)
	s_barrier
	s_setprio 1
	s_waitcnt lgkmcnt(6)
	v_mfma_f32_16x16x128_f8f6f4 v[158:161], v[2:9], v[176:183], v[158:161]
	v_mfma_f32_16x16x128_f8f6f4 v[154:157], v[10:17], v[176:183], v[154:157]
	s_waitcnt lgkmcnt(4)
	v_mfma_f32_16x16x128_f8f6f4 v[142:145], v[2:9], v[184:191], v[142:145]
	v_mfma_f32_16x16x128_f8f6f4 v[138:141], v[10:17], v[184:191], v[138:141]
	s_waitcnt lgkmcnt(2)
	v_mfma_f32_16x16x128_f8f6f4 v[126:129], v[2:9], v[192:199], v[126:129]
	v_mfma_f32_16x16x128_f8f6f4 v[122:125], v[10:17], v[192:199], v[122:125]
	s_waitcnt lgkmcnt(0)
	v_mfma_f32_16x16x128_f8f6f4 v[110:113], v[2:9], v[200:207], v[110:113]
	v_mfma_f32_16x16x128_f8f6f4 v[106:109], v[10:17], v[200:207], v[106:109]
	s_setprio 0
	s_setprio 1
	v_mfma_f32_16x16x128_f8f6f4 v[150:153], v[18:25], v[176:183], v[150:153]
	v_mfma_f32_16x16x128_f8f6f4 v[146:149], v[26:33], v[176:183], v[146:149]
	v_mfma_f32_16x16x128_f8f6f4 v[134:137], v[18:25], v[184:191], v[134:137]
	v_mfma_f32_16x16x128_f8f6f4 v[130:133], v[26:33], v[184:191], v[130:133]
	v_mfma_f32_16x16x128_f8f6f4 v[118:121], v[18:25], v[192:199], v[118:121]
	v_mfma_f32_16x16x128_f8f6f4 v[114:117], v[26:33], v[192:199], v[114:117]
	v_mfma_f32_16x16x128_f8f6f4 v[102:105], v[18:25], v[200:207], v[102:105]
	v_mfma_f32_16x16x128_f8f6f4 v[98:101], v[26:33], v[200:207], v[98:101]
	s_setprio 0
	s_barrier
	ds_read_b128 v[176:179], v172 offset:49152
	ds_read_b128 v[180:183], v172 offset:50176
	ds_read_b128 v[184:187], v172 offset:51200
	ds_read_b128 v[188:191], v172 offset:52224
	ds_read_b128 v[192:195], v172 offset:53248
	ds_read_b128 v[196:199], v172 offset:54272
	ds_read_b128 v[200:203], v172 offset:55296
	ds_read_b128 v[204:207], v172 offset:56320
	s_mov_b32 s33, m0
	s_mov_b32 m0, s67
	s_nop 0
	global_load_lds_dwordx4 v1, s[46:47]
	s_mov_b32 m0, s33
	s_add_u32 s42, s42, 0x20080
	s_mov_b32 s33, m0
	s_mov_b32 m0, s68
	s_nop 0
	global_load_lds_dwordx4 v162, s[46:47]
	s_mov_b32 m0, s33
	s_addc_u32 s43, s43, 0
	s_mov_b32 s33, m0
	s_mov_b32 m0, s77
	s_nop 0
	global_load_lds_dwordx4 v1, s[42:43]
	s_mov_b32 m0, s33
	s_nop 0
	s_mov_b32 s33, m0
	s_mov_b32 m0, s78
	s_nop 0
	global_load_lds_dwordx4 v162, s[42:43]
	s_mov_b32 m0, s33
	s_nop 0
	s_mov_b32 s33, m0
	s_mov_b32 m0, s69
	s_nop 0
	global_load_lds_dwordx4 v163, s[44:45]
	s_mov_b32 m0, s33
	s_nop 0
	s_mov_b32 s33, m0
	s_mov_b32 m0, s76
	s_nop 0
	global_load_lds_dwordx4 v164, s[44:45]
	s_mov_b32 m0, s33
	s_waitcnt vmcnt(8)
	s_waitcnt lgkmcnt(0)
	s_barrier
	s_setprio 1
	s_waitcnt lgkmcnt(6)
	v_mfma_f32_16x16x128_f8f6f4 v[94:97], v[2:9], v[176:183], v[94:97]
	v_mfma_f32_16x16x128_f8f6f4 v[90:93], v[10:17], v[176:183], v[90:93]
	s_waitcnt lgkmcnt(4)
	v_mfma_f32_16x16x128_f8f6f4 v[78:81], v[2:9], v[184:191], v[78:81]
	v_mfma_f32_16x16x128_f8f6f4 v[74:77], v[10:17], v[184:191], v[74:77]
	s_waitcnt lgkmcnt(2)
	v_mfma_f32_16x16x128_f8f6f4 v[62:65], v[2:9], v[192:199], v[62:65]
	v_mfma_f32_16x16x128_f8f6f4 v[58:61], v[10:17], v[192:199], v[58:61]
	s_waitcnt lgkmcnt(0)
	v_mfma_f32_16x16x128_f8f6f4 v[46:49], v[2:9], v[200:207], v[46:49]
	v_mfma_f32_16x16x128_f8f6f4 v[42:45], v[10:17], v[200:207], v[42:45]
	s_setprio 0
	s_setprio 1
	v_mfma_f32_16x16x128_f8f6f4 v[86:89], v[18:25], v[176:183], v[86:89]
	v_mfma_f32_16x16x128_f8f6f4 v[82:85], v[26:33], v[176:183], v[82:85]
	v_mfma_f32_16x16x128_f8f6f4 v[70:73], v[18:25], v[184:191], v[70:73]
	v_mfma_f32_16x16x128_f8f6f4 v[66:69], v[26:33], v[184:191], v[66:69]
	v_mfma_f32_16x16x128_f8f6f4 v[54:57], v[18:25], v[192:199], v[54:57]
	v_mfma_f32_16x16x128_f8f6f4 v[50:53], v[26:33], v[192:199], v[50:53]
	v_mfma_f32_16x16x128_f8f6f4 v[38:41], v[18:25], v[200:207], v[38:41]
	v_mfma_f32_16x16x128_f8f6f4 v[34:37], v[26:33], v[200:207], v[34:37]
	s_setprio 0
	s_cmp_lt_u32 s91, 6
	s_cbranch_scc1 .Lkb7_do
	s_cmp_lg_u64 s[12:13], 0
	s_cbranch_scc0 .Lkb7_skip

.Lpeel7:
	s_lshl_b32 s33, s91, 7
	s_add_u32 s52, s36, s33
	s_addc_u32 s53, s37, 0
	s_add_u32 s46, s52, 0x100
	s_addc_u32 s47, s53, 0
	s_and_b64 s[44:45], s[42:43], exec
	s_cselect_b32 s49, s15, s47
	s_cselect_b32 s48, s17, s46
	s_add_u32 s33, s26, s33
	v_add_u32_e32 v2, 0x10000, v171
	v_add_u32_e32 v14, 0x14000, v171
	s_addc_u32 s44, s27, 0
	ds_read_b128 v[18:21], v2
	ds_read_b128 v[22:25], v2 offset:1024
	ds_read_b128 v[26:29], v2 offset:2048
	ds_read_b128 v[30:33], v2 offset:3072
	ds_read_b128 v[2:5], v14
	ds_read_b128 v[6:9], v14 offset:1024
	ds_read_b128 v[10:13], v14 offset:2048
	ds_read_b128 v[14:17], v14 offset:3072
	s_add_u32 s33, s33, 0x100
	s_addc_u32 s44, s44, 0
	s_and_b64 s[42:43], s[42:43], exec
	s_cselect_b32 s43, s19, s44
	s_cselect_b32 s42, s18, s33
	s_add_u32 s44, s48, 0x80
	s_addc_u32 s45, s49, 0
	s_add_u32 s46, s42, 0x80
	s_addc_u32 s47, s43, 0
	ds_read_b128 v[176:179], v172
	ds_read_b128 v[180:183], v172 offset:1024
	ds_read_b128 v[184:187], v172 offset:2048
	ds_read_b128 v[188:191], v172 offset:3072
	ds_read_b128 v[192:195], v172 offset:4096
	ds_read_b128 v[196:199], v172 offset:5120
	ds_read_b128 v[200:203], v172 offset:6144
	ds_read_b128 v[204:207], v172 offset:7168
	s_add_u32 s52, s52, 0x20080
	s_addc_u32 s53, s53, 0
	s_mov_b32 s33, m0
	s_mov_b32 m0, s79
	s_nop 0
	global_load_lds_dwordx4 v163, s[52:53]
	s_mov_b32 m0, s33
	s_nop 0
	s_mov_b32 s33, m0
	s_mov_b32 m0, s80
	s_nop 0
	global_load_lds_dwordx4 v164, s[52:53]
	s_mov_b32 m0, s33
	s_waitcnt vmcnt(8)
	s_waitcnt lgkmcnt(0)
	s_barrier
	s_setprio 1
	s_waitcnt lgkmcnt(6)
	v_mfma_f32_16x16x128_f8f6f4 v[158:161], v[18:25], v[176:183], 0
	v_mfma_f32_16x16x128_f8f6f4 v[154:157], v[26:33], v[176:183], 0
	s_waitcnt lgkmcnt(4)
	v_mfma_f32_16x16x128_f8f6f4 v[142:145], v[18:25], v[184:191], 0
	v_mfma_f32_16x16x128_f8f6f4 v[138:141], v[26:33], v[184:191], 0
	s_waitcnt lgkmcnt(2)
	v_mfma_f32_16x16x128_f8f6f4 v[126:129], v[18:25], v[192:199], 0
	v_mfma_f32_16x16x128_f8f6f4 v[122:125], v[26:33], v[192:199], 0
	s_waitcnt lgkmcnt(0)
	v_mfma_f32_16x16x128_f8f6f4 v[110:113], v[18:25], v[200:207], 0
	v_mfma_f32_16x16x128_f8f6f4 v[106:109], v[26:33], v[200:207], 0
	s_setprio 0
	s_setprio 1
	v_mfma_f32_16x16x128_f8f6f4 v[150:153], v[2:9], v[176:183], 0
	v_mfma_f32_16x16x128_f8f6f4 v[146:149], v[10:17], v[176:183], 0
	v_mfma_f32_16x16x128_f8f6f4 v[134:137], v[2:9], v[184:191], 0
	v_mfma_f32_16x16x128_f8f6f4 v[130:133], v[10:17], v[184:191], 0
	v_mfma_f32_16x16x128_f8f6f4 v[118:121], v[2:9], v[192:199], 0
	v_mfma_f32_16x16x128_f8f6f4 v[114:117], v[10:17], v[192:199], 0
	v_mfma_f32_16x16x128_f8f6f4 v[102:105], v[2:9], v[200:207], 0
	v_mfma_f32_16x16x128_f8f6f4 v[98:101], v[10:17], v[200:207], 0
	s_setprio 0
	s_barrier
	ds_read_b128 v[176:179], v172 offset:16384
	ds_read_b128 v[180:183], v172 offset:17408
	ds_read_b128 v[184:187], v172 offset:18432
	ds_read_b128 v[188:191], v172 offset:19456
	ds_read_b128 v[192:195], v172 offset:20480
	ds_read_b128 v[196:199], v172 offset:21504
	ds_read_b128 v[200:203], v172 offset:22528
	ds_read_b128 v[204:207], v172 offset:23552
	s_mov_b32 s33, m0
	s_mov_b32 m0, s64
	s_nop 0
	global_load_lds_dwordx4 v1, s[42:43]
	s_mov_b32 m0, s33
	s_add_u32 s52, s42, 0x20000
	s_mov_b32 s33, m0
	s_mov_b32 m0, s65
	s_nop 0
	global_load_lds_dwordx4 v162, s[42:43]
	s_mov_b32 m0, s33
	s_addc_u32 s53, s43, 0
	s_mov_b32 s33, m0
	s_mov_b32 m0, s24
	s_nop 0
	global_load_lds_dwordx4 v1, s[52:53]
	s_mov_b32 m0, s33
	s_nop 0
	s_mov_b32 s33, m0
	s_mov_b32 m0, s25
	s_nop 0
	global_load_lds_dwordx4 v162, s[52:53]
	s_mov_b32 m0, s33
	s_nop 0
	s_mov_b32 s33, m0
	s_mov_b32 m0, s63
	s_nop 0
	global_load_lds_dwordx4 v163, s[48:49]
	s_mov_b32 m0, s33
	s_nop 0
	s_mov_b32 s33, m0
	s_mov_b32 m0, s2
	s_nop 0
	global_load_lds_dwordx4 v164, s[48:49]
	s_mov_b32 m0, s33
	s_waitcnt vmcnt(8)
	s_waitcnt lgkmcnt(0)
	s_barrier
	s_setprio 1
	s_waitcnt lgkmcnt(6)
	v_mfma_f32_16x16x128_f8f6f4 v[94:97], v[18:25], v[176:183], 0
	v_mfma_f32_16x16x128_f8f6f4 v[90:93], v[26:33], v[176:183], 0
	s_waitcnt lgkmcnt(4)
	v_mfma_f32_16x16x128_f8f6f4 v[78:81], v[18:25], v[184:191], 0
	v_mfma_f32_16x16x128_f8f6f4 v[74:77], v[26:33], v[184:191], 0
	s_waitcnt lgkmcnt(2)
	v_mfma_f32_16x16x128_f8f6f4 v[62:65], v[18:25], v[192:199], 0
	v_mfma_f32_16x16x128_f8f6f4 v[58:61], v[26:33], v[192:199], 0
	s_waitcnt lgkmcnt(0)
	v_mfma_f32_16x16x128_f8f6f4 v[46:49], v[18:25], v[200:207], 0
	v_mfma_f32_16x16x128_f8f6f4 v[42:45], v[26:33], v[200:207], 0
	s_setprio 0
	s_setprio 1
	v_mfma_f32_16x16x128_f8f6f4 v[86:89], v[2:9], v[176:183], 0
	v_mfma_f32_16x16x128_f8f6f4 v[82:85], v[10:17], v[176:183], 0
	v_mfma_f32_16x16x128_f8f6f4 v[70:73], v[2:9], v[184:191], 0
	v_mfma_f32_16x16x128_f8f6f4 v[66:69], v[10:17], v[184:191], 0
	v_mfma_f32_16x16x128_f8f6f4 v[54:57], v[2:9], v[192:199], 0
	v_mfma_f32_16x16x128_f8f6f4 v[50:53], v[10:17], v[192:199], 0
	v_mfma_f32_16x16x128_f8f6f4 v[38:41], v[2:9], v[200:207], 0
	v_mfma_f32_16x16x128_f8f6f4 v[34:37], v[10:17], v[200:207], 0
	s_setprio 0
	s_barrier
	s_branch .Lmid7

.LBB0_2107:
	v_lshlrev_b32_e32 v1, 4, v0
	s_waitcnt vmcnt(0)
	v_and_b32_e32 v2, 32, v0
	v_bitop3_b32 v1, v1, v2, 48 bitop3:0x6c
	v_lshrrev_b32_e32 v2, 1, v0
	v_bfe_u32 v4, v0, 2, 2
	v_bfe_u32 v3, v0, 2, 4
	v_and_or_b32 v2, v2, 24, v4
	v_lshrrev_b32_e32 v4, 3, v0
	v_lshrrev_b32_e32 v6, 5, v0
	v_and_or_b32 v5, v4, 48, v3
	v_and_or_b32 v4, v4, 32, v6
	v_and_or_b32 v4, v4, 36, v2
	v_and_or_b32 v1, v0, 64, v1
	v_lshl_or_b32 v163, v4, 10, v1
	v_bfe_u32 v4, v0, 3, 25
	v_or_b32_e32 v4, 64, v4
	s_movk_i32 s5, 0x70
	v_and_or_b32 v3, v4, s5, v3
	s_movk_i32 s5, 0x60
	v_and_or_b32 v4, v4, s5, v6
	s_movk_i32 s5, 0x64
	v_and_or_b32 v2, v4, s5, v2
	s_add_i32 s5, s6, s4
	s_ashr_i32 s4, s5, 31
	s_lshr_b32 s4, s4, 27
	s_add_i32 s6, s5, s4
	s_ashr_i32 s4, s6, 5
	s_lshl_b32 s7, s4, 3
	s_sub_i32 s4, s57, s7
	s_min_i32 s9, s4, 8
	s_abs_i32 s12, s9
	v_lshl_or_b32 v164, v3, 10, v1
	v_cvt_f32_u32_e32 v3, s12
	s_sub_i32 s14, 0, s12
	s_andn2_b32 s6, s6, 31
	s_sub_i32 s5, s5, s6
	v_rcp_iflag_f32_e32 v3, v3
	s_abs_i32 s13, s5
	s_lshr_b32 s30, s8, 6
	s_xor_b32 s6, s5, s9
	v_mul_f32_e32 v3, 0x4f7ffffe, v3
	v_cvt_u32_f32_e32 v3, v3
	s_lshr_b32 s4, s8, 8
	s_lshl_b32 s16, s30, 10
	s_ashr_i32 s6, s6, 31
	v_readfirstlane_b32 s15, v3
	s_mul_i32 s14, s14, s15
	s_mul_hi_u32 s14, s15, s14
	s_add_i32 s15, s15, s14
	s_mul_hi_u32 s14, s13, s15
	s_mul_i32 s15, s14, s12
	s_sub_i32 s13, s13, s15
	s_add_i32 s15, s14, 1
	s_sub_i32 s17, s13, s12
	s_cmp_ge_u32 s13, s12
	s_cselect_b32 s14, s15, s14
	s_cselect_b32 s13, s17, s13
	s_add_i32 s15, s14, 1
	s_cmp_ge_u32 s13, s12
	s_cselect_b32 s12, s15, s14
	s_xor_b32 s12, s12, s6
	s_sub_i32 s26, s12, s6
	s_mul_i32 s6, s26, s9
	s_sub_i32 s5, s5, s6
	s_add_i32 s20, s7, s5
	s_lshl_b32 s5, s20, 2
	s_add_i32 s5, s5, 0
	s_add_i32 s5, s5, 0x202e0
	v_mov_b32_e32 v3, s5
	ds_read_b32 v3, v3
	s_ashr_i32 s21, s20, 31
	s_ashr_i32 s27, s26, 31
	s_lshl_b64 s[6:7], s[20:21], 18
	s_lshl_b64 s[14:15], s[26:27], 18
	s_waitcnt lgkmcnt(0)
	v_readfirstlane_b32 s12, v3
	s_ashr_i32 s13, s12, 31
	s_lshl_b64 s[12:13], s[12:13], 20
	s_add_u32 s5, s35, s12
	s_addc_u32 s9, s54, s13
	s_add_u32 s36, s5, s14
	s_addc_u32 s37, s9, s15
	s_add_i32 s21, s16, 0
	s_add_i32 s31, s21, 0x10000
	s_mov_b32 s5, m0
	s_mov_b32 m0, s31
	s_nop 0
	global_load_lds_dwordx4 v163, s[36:37]
	s_mov_b32 m0, s5
	s_add_i32 s44, s21, 0x12000
	v_lshl_or_b32 v165, v2, 10, v1
	s_mov_b32 s5, m0
	s_mov_b32 m0, s44
	s_nop 0
	global_load_lds_dwordx4 v165, s[36:37]
	s_mov_b32 m0, s5
	s_add_u32 s12, s36, 0x20000
	s_addc_u32 s13, s37, 0
	s_add_i32 s45, s21, 0x14000
	s_mov_b32 s5, m0
	s_mov_b32 m0, s45
	s_nop 0
	global_load_lds_dwordx4 v163, s[12:13]
	s_mov_b32 m0, s5
	s_add_i32 s46, s21, 0x16000
	s_mov_b32 s5, m0
	s_mov_b32 m0, s46
	s_nop 0
	global_load_lds_dwordx4 v165, s[12:13]
	s_mov_b32 m0, s5
	s_add_u32 s22, s3, s6
	v_lshl_or_b32 v162, v5, 10, v1
	s_addc_u32 s23, s34, s7
	s_mov_b32 s5, m0
	s_mov_b32 m0, s21
	s_nop 0
	global_load_lds_dwordx4 v162, s[22:23]
	s_mov_b32 m0, s5
	s_add_i32 s47, s21, 0x2000
	s_mov_b32 s5, m0
	s_mov_b32 m0, s47
	s_nop 0
	global_load_lds_dwordx4 v164, s[22:23]
	s_mov_b32 m0, s5
	s_add_u32 s12, s22, 0x20000
	s_addc_u32 s13, s23, 0
	s_add_i32 s48, s21, 0x4000
	s_mov_b32 s5, m0
	s_mov_b32 m0, s48
	s_nop 0
	global_load_lds_dwordx4 v162, s[12:13]
	s_mov_b32 m0, s5
	s_add_i32 s49, s21, 0x6000
	s_mov_b32 s5, m0
	s_mov_b32 m0, s49
	s_nop 0
	global_load_lds_dwordx4 v164, s[12:13]
	s_mov_b32 m0, s5
	s_cmp_eq_u32 s4, 1
	s_mov_b32 s33, 0
	s_cselect_b64 s[6:7], -1, 0
	s_cmp_lg_u32 s4, 1
	s_cbranch_scc1 .LBB0_2109
	s_barrier
.LBB0_2109:
	v_and_b32_e32 v166, 15, v0
	v_and_b32_e32 v1, 48, v0
	v_lshlrev_b32_e32 v3, 2, v0
	s_lshl_b32 s52, s4, 6
	v_lshl_or_b32 v2, v166, 6, v1
	s_lshl_b32 s4, s4, 13
	v_and_b32_e32 v3, 32, v3
	v_bitop3_b32 v2, v2, s4, v3 bitop3:0xde
	s_lshl_b32 s4, s30, 5
	s_and_b32 s53, s4, 0x60
	v_lshlrev_b32_e32 v0, 6, v0
	s_movk_i32 s4, 0x3c0
	v_and_or_b32 v0, v0, s4, v1
	s_lshl_b32 s4, s53, 7
	v_bitop3_b32 v0, s4, v0, v3 bitop3:0xf6
	s_add_u32 s4, s36, 0x80
	s_waitcnt vmcnt(2)
	s_barrier
	s_addc_u32 s5, s37, 0
	s_add_i32 s58, s21, 0x18000
	s_mov_b32 s9, m0
	s_mov_b32 m0, s58
	s_nop 0
	global_load_lds_dwordx4 v163, s[4:5]
	s_mov_b32 m0, s9
	s_add_i32 s59, s21, 0x1a000
	s_mov_b32 s9, m0
	s_mov_b32 m0, s59
	s_nop 0
	global_load_lds_dwordx4 v165, s[4:5]
	s_mov_b32 m0, s9
	s_add_u32 s4, s22, 0x80
	s_addc_u32 s5, s23, 0
	s_add_i32 s60, s21, 0x8000
	s_mov_b32 s9, m0
	s_mov_b32 m0, s60
	s_nop 0
	global_load_lds_dwordx4 v162, s[4:5]
	s_mov_b32 m0, s9
	s_add_i32 s61, s21, 0xa000
	s_mov_b32 s9, m0
	s_mov_b32 m0, s61
	s_nop 0
	global_load_lds_dwordx4 v164, s[4:5]
	s_mov_b32 m0, s9
	s_add_u32 s4, s36, 0x20080
	s_addc_u32 s5, s37, 0
	s_add_i32 s62, s21, 0x1c000
	s_mov_b32 s9, m0
	s_mov_b32 m0, s62
	s_nop 0
	global_load_lds_dwordx4 v163, s[4:5]
	s_mov_b32 m0, s9
	s_add_i32 s63, s21, 0x1e000
	s_mov_b32 s9, m0
	s_mov_b32 m0, s63
	s_nop 0
	global_load_lds_dwordx4 v165, s[4:5]
	s_mov_b32 m0, s9
	s_waitcnt vmcnt(6)
	s_add_i32 s64, s21, 0xc000
	s_cmpk_lt_u32 s8, 0x100
	v_lshrrev_b32_e32 v167, 4, v218
	v_lshlrev_b32_e32 v168, 4, v218
	s_cselect_b64 s[8:9], -1, 0
	s_add_i32 s65, s21, 0xe000
	s_ashr_i32 s66, s90, 31
	v_mov_b64_e32 v[160:161], s[0:1]
	v_add_u32_e32 v169, 0, v0
	v_add_u32_e32 v170, 0, v2
	s_mov_b32 s67, 0xc3e00000
	v_mov_b32_e32 v171, 0x43e00000
	s_barrier
	s_branch .LBB0_2112

.LBB0_2121:
	v_mov_b32_e32 v0, s5
	ds_read_b32 v0, v0 offset:288
	s_mov_b64 s[36:37], -1
	s_waitcnt lgkmcnt(0)
	v_readfirstlane_b32 s26, v0
	s_lshl_b32 s27, s26, 2
	s_add_i32 s27, s27, 0
	s_add_i32 s27, s27, 0x20240
	v_mov_b32_e32 v0, s27
	ds_read_b32 v0, v0
	s_cmp_lt_i32 s30, 2
	s_waitcnt lgkmcnt(0)
	v_readfirstlane_b32 s27, v0
	s_cbranch_scc1 .LBB0_2125
	s_cmp_eq_u32 s30, 2
	s_cbranch_scc0 .LBB0_2124
	s_lshl_b32 s38, s26, 14
	s_sub_i32 s27, s20, s27
	s_ashr_i32 s39, s38, 31
	s_lshl_b32 s36, s27, 8
	s_lshl_b64 s[38:39], s[38:39], 2
	s_add_u32 s27, s55, s38
	s_addc_u32 s33, s56, s39
	s_ashr_i32 s37, s36, 31
	s_lshl_b64 s[36:37], s[36:37], 2
	s_add_u32 s36, s27, s36
	s_addc_u32 s37, s33, s37
	s_mov_b32 s27, m0
	s_mov_b32 m0, s78
	s_nop 0
	global_load_lds_dwordx4 v168, s[36:37]
	s_mov_b32 m0, s27

.LBB0_2125:
	s_andn2_b64 vcc, exec, s[36:37]
	s_mov_b32 s69, s76
	s_cbranch_vccnz .LBB0_2128
	s_cmp_lg_u32 s30, 1
	s_mov_b32 s69, s76
	s_cbranch_scc1 .LBB0_2128
	s_ashr_i32 s27, s26, 31
	s_lshl_b64 s[26:27], s[26:27], 12
	s_add_u32 s26, s79, s26
	s_addc_u32 s27, s80, s27
	s_mov_b32 s33, m0
	s_mov_b32 m0, s77
	s_nop 0
	global_load_lds_dwordx4 v168, s[26:27]
	s_mov_b32 m0, s33
	s_mov_b32 s69, s76
.LBB0_2128:
	v_add_u32_e32 v0, 0x10000, v169
	v_add_u32_e32 v12, 0x14000, v169
	s_add_u32 s26, s22, 0x100
	ds_read_b128 v[16:19], v0
	ds_read_b128 v[20:23], v0 offset:1024
	ds_read_b128 v[24:27], v0 offset:2048
	ds_read_b128 v[28:31], v0 offset:3072
	ds_read_b128 v[0:3], v12
	ds_read_b128 v[4:7], v12 offset:1024
	ds_read_b128 v[8:11], v12 offset:2048
	ds_read_b128 v[12:15], v12 offset:3072
	s_addc_u32 s27, s23, 0
	s_cmp_eq_u32 s83, 4
	s_cselect_b32 s42, s15, s26
	s_cselect_b32 s43, s13, s27
	s_cselect_b32 s37, s17, s82
	s_cselect_b32 s36, s16, s81
	s_add_u32 s38, s42, 0x80
	s_addc_u32 s39, s43, 0
	s_add_u32 s40, s36, 0x80
	s_addc_u32 s41, s37, 0
	ds_read_b128 v[172:175], v170
	ds_read_b128 v[176:179], v170 offset:1024
	ds_read_b128 v[180:183], v170 offset:2048
	ds_read_b128 v[184:187], v170 offset:3072
	ds_read_b128 v[188:191], v170 offset:4096
	ds_read_b128 v[192:195], v170 offset:5120
	ds_read_b128 v[196:199], v170 offset:6144
	ds_read_b128 v[200:203], v170 offset:7168
	s_add_u32 s22, s22, 0x20080
	s_addc_u32 s23, s23, 0
	s_mov_b32 s33, m0
	s_mov_b32 m0, s64
	s_nop 0
	global_load_lds_dwordx4 v162, s[22:23]
	s_mov_b32 m0, s33
	s_nop 0
	s_mov_b32 s33, m0
	s_mov_b32 m0, s65
	s_nop 0
	global_load_lds_dwordx4 v164, s[22:23]
	s_mov_b32 m0, s33
	s_waitcnt vmcnt(8)
	s_waitcnt lgkmcnt(0)
	s_barrier
	s_setprio 1
	s_waitcnt lgkmcnt(6)
	v_mfma_f32_16x16x128_f8f6f4 v[156:159], v[16:23], v[172:179], v[156:159]
	v_mfma_f32_16x16x128_f8f6f4 v[152:155], v[24:31], v[172:179], v[152:155]
	s_waitcnt lgkmcnt(4)
	v_mfma_f32_16x16x128_f8f6f4 v[140:143], v[16:23], v[180:187], v[140:143]
	v_mfma_f32_16x16x128_f8f6f4 v[136:139], v[24:31], v[180:187], v[136:139]
	s_waitcnt lgkmcnt(2)
	v_mfma_f32_16x16x128_f8f6f4 v[124:127], v[16:23], v[188:195], v[124:127]
	v_mfma_f32_16x16x128_f8f6f4 v[120:123], v[24:31], v[188:195], v[120:123]
	s_waitcnt lgkmcnt(0)
	v_mfma_f32_16x16x128_f8f6f4 v[108:111], v[16:23], v[196:203], v[108:111]
	v_mfma_f32_16x16x128_f8f6f4 v[104:107], v[24:31], v[196:203], v[104:107]
	s_setprio 0
	s_setprio 1
	v_mfma_f32_16x16x128_f8f6f4 v[148:151], v[0:7], v[172:179], v[148:151]
	v_mfma_f32_16x16x128_f8f6f4 v[144:147], v[8:15], v[172:179], v[144:147]
	v_mfma_f32_16x16x128_f8f6f4 v[132:135], v[0:7], v[180:187], v[132:135]
	v_mfma_f32_16x16x128_f8f6f4 v[128:131], v[8:15], v[180:187], v[128:131]
	v_mfma_f32_16x16x128_f8f6f4 v[116:119], v[0:7], v[188:195], v[116:119]
	v_mfma_f32_16x16x128_f8f6f4 v[112:115], v[8:15], v[188:195], v[112:115]
	v_mfma_f32_16x16x128_f8f6f4 v[100:103], v[0:7], v[196:203], v[100:103]
	v_mfma_f32_16x16x128_f8f6f4 v[96:99], v[8:15], v[196:203], v[96:99]
	s_setprio 0
	s_barrier
	ds_read_b128 v[172:175], v170 offset:16384
	ds_read_b128 v[176:179], v170 offset:17408
	ds_read_b128 v[180:183], v170 offset:18432
	ds_read_b128 v[184:187], v170 offset:19456
	ds_read_b128 v[188:191], v170 offset:20480
	ds_read_b128 v[192:195], v170 offset:21504
	ds_read_b128 v[196:199], v170 offset:22528
	ds_read_b128 v[200:203], v170 offset:23552
	s_mov_b32 s22, m0
	s_mov_b32 m0, s31
	s_nop 0
	global_load_lds_dwordx4 v163, s[36:37]
	s_mov_b32 m0, s22
	s_nop 0
	s_mov_b32 s22, m0
	s_mov_b32 m0, s44
	s_nop 0
	global_load_lds_dwordx4 v165, s[36:37]
	s_mov_b32 m0, s22
	s_add_u32 s22, s36, 0x20000
	s_addc_u32 s23, s37, 0
	s_mov_b32 s33, m0
	s_mov_b32 m0, s45
	s_nop 0
	global_load_lds_dwordx4 v163, s[22:23]
	s_mov_b32 m0, s33
	s_nop 0
	s_mov_b32 s33, m0
	s_mov_b32 m0, s46
	s_nop 0
	global_load_lds_dwordx4 v165, s[22:23]
	s_mov_b32 m0, s33
	s_mov_b32 s22, m0
	s_mov_b32 m0, s21
	s_nop 0
	global_load_lds_dwordx4 v162, s[42:43]
	s_mov_b32 m0, s22
	s_nop 0
	s_mov_b32 s22, m0
	s_mov_b32 m0, s47
	s_nop 0
	global_load_lds_dwordx4 v164, s[42:43]
	s_mov_b32 m0, s22
	s_waitcnt vmcnt(8)
	s_waitcnt lgkmcnt(0)
	s_barrier
	s_setprio 1
	s_waitcnt lgkmcnt(6)
	v_mfma_f32_16x16x128_f8f6f4 v[92:95], v[16:23], v[172:179], v[92:95]
	v_mfma_f32_16x16x128_f8f6f4 v[88:91], v[24:31], v[172:179], v[88:91]
	s_waitcnt lgkmcnt(4)
	v_mfma_f32_16x16x128_f8f6f4 v[76:79], v[16:23], v[180:187], v[76:79]
	v_mfma_f32_16x16x128_f8f6f4 v[72:75], v[24:31], v[180:187], v[72:75]
	s_waitcnt lgkmcnt(2)
	v_mfma_f32_16x16x128_f8f6f4 v[60:63], v[16:23], v[188:195], v[60:63]
	v_mfma_f32_16x16x128_f8f6f4 v[56:59], v[24:31], v[188:195], v[56:59]
	s_waitcnt lgkmcnt(0)
	v_mfma_f32_16x16x128_f8f6f4 v[44:47], v[16:23], v[196:203], v[44:47]
	v_mfma_f32_16x16x128_f8f6f4 v[40:43], v[24:31], v[196:203], v[40:43]
	s_setprio 0
	s_setprio 1
	v_mfma_f32_16x16x128_f8f6f4 v[84:87], v[0:7], v[172:179], v[84:87]
	v_mfma_f32_16x16x128_f8f6f4 v[80:83], v[8:15], v[172:179], v[80:83]
	v_mfma_f32_16x16x128_f8f6f4 v[68:71], v[0:7], v[180:187], v[68:71]
	v_mfma_f32_16x16x128_f8f6f4 v[64:67], v[8:15], v[180:187], v[64:67]
	v_mfma_f32_16x16x128_f8f6f4 v[52:55], v[0:7], v[188:195], v[52:55]
	v_mfma_f32_16x16x128_f8f6f4 v[48:51], v[8:15], v[188:195], v[48:51]
	v_mfma_f32_16x16x128_f8f6f4 v[36:39], v[0:7], v[196:203], v[36:39]
	v_mfma_f32_16x16x128_f8f6f4 v[32:35], v[8:15], v[196:203], v[32:35]
	s_setprio 0
	s_barrier
	v_add_u32_e32 v12, 0x18000, v169
	v_add_u32_e32 v28, 0x1c000, v169
	ds_read_b128 v[0:3], v12
	ds_read_b128 v[4:7], v12 offset:1024
	ds_read_b128 v[8:11], v12 offset:2048
	ds_read_b128 v[12:15], v12 offset:3072
	ds_read_b128 v[16:19], v28
	ds_read_b128 v[20:23], v28 offset:1024
	ds_read_b128 v[24:27], v28 offset:2048
	ds_read_b128 v[28:31], v28 offset:3072
	ds_read_b128 v[172:175], v170 offset:32768
	ds_read_b128 v[176:179], v170 offset:33792
	ds_read_b128 v[180:183], v170 offset:34816
	ds_read_b128 v[184:187], v170 offset:35840
	ds_read_b128 v[188:191], v170 offset:36864
	ds_read_b128 v[192:195], v170 offset:37888
	ds_read_b128 v[196:199], v170 offset:38912
	ds_read_b128 v[200:203], v170 offset:39936
	s_add_u32 s22, s42, 0x20000
	s_addc_u32 s23, s43, 0
	s_mov_b32 s33, m0
	s_mov_b32 m0, s48
	s_nop 0
	global_load_lds_dwordx4 v162, s[22:23]
	s_mov_b32 m0, s33
	s_nop 0
	s_mov_b32 s33, m0
	s_mov_b32 m0, s49
	s_nop 0
	global_load_lds_dwordx4 v164, s[22:23]
	s_mov_b32 m0, s33
	s_waitcnt vmcnt(8)
	s_waitcnt lgkmcnt(0)
	s_barrier
	s_setprio 1
	s_waitcnt lgkmcnt(6)
	v_mfma_f32_16x16x128_f8f6f4 v[156:159], v[0:7], v[172:179], v[156:159]
	v_mfma_f32_16x16x128_f8f6f4 v[152:155], v[8:15], v[172:179], v[152:155]
	s_waitcnt lgkmcnt(4)
	v_mfma_f32_16x16x128_f8f6f4 v[140:143], v[0:7], v[180:187], v[140:143]
	v_mfma_f32_16x16x128_f8f6f4 v[136:139], v[8:15], v[180:187], v[136:139]
	s_waitcnt lgkmcnt(2)
	v_mfma_f32_16x16x128_f8f6f4 v[124:127], v[0:7], v[188:195], v[124:127]
	v_mfma_f32_16x16x128_f8f6f4 v[120:123], v[8:15], v[188:195], v[120:123]
	s_waitcnt lgkmcnt(0)
	v_mfma_f32_16x16x128_f8f6f4 v[108:111], v[0:7], v[196:203], v[108:111]
	v_mfma_f32_16x16x128_f8f6f4 v[104:107], v[8:15], v[196:203], v[104:107]
	s_setprio 0
	s_setprio 1
	v_mfma_f32_16x16x128_f8f6f4 v[148:151], v[16:23], v[172:179], v[148:151]
	v_mfma_f32_16x16x128_f8f6f4 v[144:147], v[24:31], v[172:179], v[144:147]
	v_mfma_f32_16x16x128_f8f6f4 v[132:135], v[16:23], v[180:187], v[132:135]
	v_mfma_f32_16x16x128_f8f6f4 v[128:131], v[24:31], v[180:187], v[128:131]
	v_mfma_f32_16x16x128_f8f6f4 v[116:119], v[16:23], v[188:195], v[116:119]
	v_mfma_f32_16x16x128_f8f6f4 v[112:115], v[24:31], v[188:195], v[112:115]
	v_mfma_f32_16x16x128_f8f6f4 v[100:103], v[16:23], v[196:203], v[100:103]
	v_mfma_f32_16x16x128_f8f6f4 v[96:99], v[24:31], v[196:203], v[96:99]
	s_setprio 0
	s_barrier
	ds_read_b128 v[172:175], v170 offset:49152
	ds_read_b128 v[176:179], v170 offset:50176
	ds_read_b128 v[180:183], v170 offset:51200
	ds_read_b128 v[184:187], v170 offset:52224
	ds_read_b128 v[188:191], v170 offset:53248
	ds_read_b128 v[192:195], v170 offset:54272
	ds_read_b128 v[196:199], v170 offset:55296
	ds_read_b128 v[200:203], v170 offset:56320
	s_mov_b32 s22, m0
	s_mov_b32 m0, s58
	s_nop 0
	global_load_lds_dwordx4 v163, s[40:41]
	s_mov_b32 m0, s22
	s_nop 0
	s_mov_b32 s22, m0
	s_mov_b32 m0, s59
	s_nop 0
	global_load_lds_dwordx4 v165, s[40:41]
	s_mov_b32 m0, s22
	s_add_u32 s22, s36, 0x20080
	s_addc_u32 s23, s37, 0
	s_mov_b32 s33, m0
	s_mov_b32 m0, s62
	s_nop 0
	global_load_lds_dwordx4 v163, s[22:23]
	s_mov_b32 m0, s33
	s_nop 0
	s_mov_b32 s33, m0
	s_mov_b32 m0, s63
	s_nop 0
	global_load_lds_dwordx4 v165, s[22:23]
	s_mov_b32 m0, s33
	s_mov_b32 s22, m0
	s_mov_b32 m0, s60
	s_nop 0
	global_load_lds_dwordx4 v162, s[38:39]
	s_mov_b32 m0, s22
	s_nop 0
	s_mov_b32 s22, m0
	s_mov_b32 m0, s61
	s_nop 0
	global_load_lds_dwordx4 v164, s[38:39]
	s_mov_b32 m0, s22
	s_waitcnt vmcnt(8)
	s_waitcnt lgkmcnt(0)
	s_barrier
	s_setprio 1
	s_waitcnt lgkmcnt(6)
	v_mfma_f32_16x16x128_f8f6f4 v[92:95], v[0:7], v[172:179], v[92:95]
	v_mfma_f32_16x16x128_f8f6f4 v[88:91], v[8:15], v[172:179], v[88:91]
	s_waitcnt lgkmcnt(4)
	v_mfma_f32_16x16x128_f8f6f4 v[76:79], v[0:7], v[180:187], v[76:79]
	v_mfma_f32_16x16x128_f8f6f4 v[72:75], v[8:15], v[180:187], v[72:75]
	s_waitcnt lgkmcnt(2)
	v_mfma_f32_16x16x128_f8f6f4 v[60:63], v[0:7], v[188:195], v[60:63]
	v_mfma_f32_16x16x128_f8f6f4 v[56:59], v[8:15], v[188:195], v[56:59]
	s_waitcnt lgkmcnt(0)
	v_mfma_f32_16x16x128_f8f6f4 v[44:47], v[0:7], v[196:203], v[44:47]
	v_mfma_f32_16x16x128_f8f6f4 v[40:43], v[8:15], v[196:203], v[40:43]
	s_setprio 0
	s_setprio 1
	v_mfma_f32_16x16x128_f8f6f4 v[84:87], v[16:23], v[172:179], v[84:87]
	v_mfma_f32_16x16x128_f8f6f4 v[80:83], v[24:31], v[172:179], v[80:83]
	v_mfma_f32_16x16x128_f8f6f4 v[68:71], v[16:23], v[180:187], v[68:71]
	v_mfma_f32_16x16x128_f8f6f4 v[64:67], v[24:31], v[180:187], v[64:67]
	v_mfma_f32_16x16x128_f8f6f4 v[52:55], v[16:23], v[188:195], v[52:55]
	v_mfma_f32_16x16x128_f8f6f4 v[48:51], v[24:31], v[188:195], v[48:51]
	v_mfma_f32_16x16x128_f8f6f4 v[36:39], v[16:23], v[196:203], v[36:39]
	v_mfma_f32_16x16x128_f8f6f4 v[32:35], v[24:31], v[196:203], v[32:35]
	s_setprio 0
	s_barrier
	s_add_i32 s83, s83, 2
	s_add_u32 s81, s81, 0x100
	s_addc_u32 s82, s82, 0
	s_cmp_gt_u32 s83, 5
	s_cbranch_scc1 .LBB0_2130
	s_mov_b64 s[22:23], s[26:27]
	s_cmp_lg_u32 s83, -2
	s_cbranch_scc0 .LBB0_2121
	s_branch .LBB0_2128
